# packed-math GU epilogue, removed redundant MFMA-hazard nops, MFMA runs placed at 4 mod 8
# speedup vs baseline: 1.0264x; 1.0011x over previous
.LBB0_233:
	s_add_u32 s30, s28, 0x100
	ds_read_b128 v[158:161], v141
	ds_read_b128 v[162:165], v142
	ds_read_b128 v[166:169], v149
	ds_read_b128 v[170:173], v150
	s_addc_u32 s31, s29, 0
	s_and_b32 s62, s30, 0x700
	s_add_u32 s63, s16, s62
	s_addc_u32 s64, s17, 0
	s_cmp_eq_u32 s61, 12
	s_cselect_b64 s[36:37], -1, 0
	s_and_b64 s[34:35], s[36:37], exec
	s_cselect_b32 s35, s21, s64
	s_cselect_b32 s34, s23, s63
	s_cselect_b32 s63, 0, 0
	s_cselect_b32 s62, 0, s62
	s_add_u32 s28, s18, s28
	s_addc_u32 s29, s19, s29
	s_add_u32 s28, s28, 0x40080
	s_addc_u32 s29, s29, 0
	ds_read_b128 v[174:177], v157
	ds_read_b128 v[178:181], v157 offset:1024
	ds_read_b128 v[182:185], v157 offset:2048
	ds_read_b128 v[186:189], v157 offset:3072
	ds_read_b128 v[190:193], v157 offset:4096
	ds_read_b128 v[194:197], v157 offset:5120
	ds_read_b128 v[198:201], v157 offset:6144
	ds_read_b128 v[202:205], v157 offset:7168
	s_add_i32 m0, s15, 0xc000
	s_nop 0
	global_load_lds_dwordx4 v134, s[28:29]
	s_add_i32 m0, s15, 0xe000
	s_nop 0
	global_load_lds_dwordx4 v130, s[28:29]
	s_waitcnt lgkmcnt(8)
	s_barrier
	s_waitcnt lgkmcnt(0)
	s_setprio 1
	s_waitcnt lgkmcnt(0)
	v_mfma_f32_16x16x32_bf16 v[124:127], v[158:161], v[174:177], v[124:127]
	v_mfma_f32_16x16x32_bf16 v[120:123], v[166:169], v[174:177], v[120:123]
	v_mfma_f32_16x16x32_bf16 v[116:119], v[158:161], v[182:185], v[116:119]
	v_mfma_f32_16x16x32_bf16 v[112:115], v[166:169], v[182:185], v[112:115]
	v_mfma_f32_16x16x32_bf16 v[100:103], v[158:161], v[190:193], v[100:103]
	v_mfma_f32_16x16x32_bf16 v[96:99], v[166:169], v[190:193], v[96:99]
	v_mfma_f32_16x16x32_bf16 v[84:87], v[158:161], v[198:201], v[84:87]
	v_mfma_f32_16x16x32_bf16 v[80:83], v[166:169], v[198:201], v[80:83]
	v_mfma_f32_16x16x32_bf16 v[124:127], v[162:165], v[178:181], v[124:127]
	v_mfma_f32_16x16x32_bf16 v[120:123], v[170:173], v[178:181], v[120:123]
	v_mfma_f32_16x16x32_bf16 v[116:119], v[162:165], v[186:189], v[116:119]
	v_mfma_f32_16x16x32_bf16 v[112:115], v[170:173], v[186:189], v[112:115]
	v_mfma_f32_16x16x32_bf16 v[100:103], v[162:165], v[194:197], v[100:103]
	v_mfma_f32_16x16x32_bf16 v[96:99], v[170:173], v[194:197], v[96:99]
	v_mfma_f32_16x16x32_bf16 v[84:87], v[162:165], v[202:205], v[84:87]
	v_mfma_f32_16x16x32_bf16 v[80:83], v[170:173], v[202:205], v[80:83]
	s_setprio 0
	s_barrier
	s_mov_b64 s[28:29], s[34:35]
	s_mov_b32 m0, s44
	ds_read_b128 v[210:213], v143
	ds_read_b128 v[214:217], v144
	ds_read_b128 v[218:221], v151
	ds_read_b128 v[222:225], v152
	s_nop 0
	global_load_lds_dwordx4 v132, s[28:29]
	s_mov_b32 m0, s45
	s_nop 0
	global_load_lds_dwordx4 v128, s[28:29]
	s_nop 0
	s_barrier
	s_waitcnt lgkmcnt(0)
	s_setprio 1
	s_waitcnt lgkmcnt(0)
	v_mfma_f32_16x16x32_bf16 v[108:111], v[210:213], v[174:177], v[108:111]
	v_mfma_f32_16x16x32_bf16 v[104:107], v[218:221], v[174:177], v[104:107]
	v_mfma_f32_16x16x32_bf16 v[92:95], v[210:213], v[182:185], v[92:95]
	v_mfma_f32_16x16x32_bf16 v[88:91], v[218:221], v[182:185], v[88:91]
	v_mfma_f32_16x16x32_bf16 v[76:79], v[210:213], v[190:193], v[76:79]
	v_mfma_f32_16x16x32_bf16 v[72:75], v[218:221], v[190:193], v[72:75]
	v_mfma_f32_16x16x32_bf16 v[68:71], v[210:213], v[198:201], v[68:71]
	v_mfma_f32_16x16x32_bf16 v[64:67], v[218:221], v[198:201], v[64:67]
	v_mfma_f32_16x16x32_bf16 v[108:111], v[214:217], v[178:181], v[108:111]
	v_mfma_f32_16x16x32_bf16 v[104:107], v[222:225], v[178:181], v[104:107]
	v_mfma_f32_16x16x32_bf16 v[92:95], v[214:217], v[186:189], v[92:95]
	v_mfma_f32_16x16x32_bf16 v[88:91], v[222:225], v[186:189], v[88:91]
	v_mfma_f32_16x16x32_bf16 v[76:79], v[214:217], v[194:197], v[76:79]
	v_mfma_f32_16x16x32_bf16 v[72:75], v[222:225], v[194:197], v[72:75]
	v_mfma_f32_16x16x32_bf16 v[68:71], v[214:217], v[202:205], v[68:71]
	v_mfma_f32_16x16x32_bf16 v[64:67], v[222:225], v[202:205], v[64:67]
	s_setprio 0
	s_and_b64 s[28:29], s[6:7], s[36:37]
	s_and_b64 s[28:29], s[28:29], exec
	s_cselect_b32 s28, s24, s18
	s_cselect_b32 s29, s25, s19
	s_add_u32 s28, s28, s62
	s_addc_u32 s29, s29, s63
	s_mov_b64 s[36:37], s[28:29]
	s_mov_b32 m0, s15
	s_barrier
	ds_read_b128 v[174:177], v157 offset:16384
	ds_read_b128 v[178:181], v157 offset:17408
	ds_read_b128 v[182:185], v157 offset:18432
	ds_read_b128 v[186:189], v157 offset:19456
	ds_read_b128 v[190:193], v157 offset:20480
	ds_read_b128 v[194:197], v157 offset:21504
	ds_read_b128 v[198:201], v157 offset:22528
	ds_read_b128 v[202:205], v157 offset:23552
	s_nop 0
	global_load_lds_dwordx4 v134, s[36:37]
	s_mov_b32 m0, s46
	s_nop 0
	global_load_lds_dwordx4 v130, s[36:37]
	s_nop 0
	s_barrier
	s_waitcnt lgkmcnt(0)
	s_setprio 1
	s_waitcnt lgkmcnt(0)
	v_mfma_f32_16x16x32_bf16 v[60:63], v[158:161], v[174:177], v[60:63]
	v_mfma_f32_16x16x32_bf16 v[56:59], v[166:169], v[174:177], v[56:59]
	v_mfma_f32_16x16x32_bf16 v[52:55], v[158:161], v[182:185], v[52:55]
	v_mfma_f32_16x16x32_bf16 v[48:51], v[166:169], v[182:185], v[48:51]
	v_mfma_f32_16x16x32_bf16 v[36:39], v[158:161], v[190:193], v[36:39]
	v_mfma_f32_16x16x32_bf16 v[32:35], v[166:169], v[190:193], v[32:35]
	v_mfma_f32_16x16x32_bf16 v[20:23], v[158:161], v[198:201], v[20:23]
	v_mfma_f32_16x16x32_bf16 v[16:19], v[166:169], v[198:201], v[16:19]
	v_mfma_f32_16x16x32_bf16 v[60:63], v[162:165], v[178:181], v[60:63]
	v_mfma_f32_16x16x32_bf16 v[56:59], v[170:173], v[178:181], v[56:59]
	v_mfma_f32_16x16x32_bf16 v[52:55], v[162:165], v[186:189], v[52:55]
	v_mfma_f32_16x16x32_bf16 v[48:51], v[170:173], v[186:189], v[48:51]
	v_mfma_f32_16x16x32_bf16 v[36:39], v[162:165], v[194:197], v[36:39]
	v_mfma_f32_16x16x32_bf16 v[32:35], v[170:173], v[194:197], v[32:35]
	v_mfma_f32_16x16x32_bf16 v[20:23], v[162:165], v[202:205], v[20:23]
	v_mfma_f32_16x16x32_bf16 v[16:19], v[170:173], v[202:205], v[16:19]
	s_setprio 0
	s_barrier
	s_add_u32 s36, s34, 0x40000
	s_addc_u32 s37, s35, 0
	s_mov_b32 m0, s47
	s_nop 0
	global_load_lds_dwordx4 v132, s[36:37]
	s_mov_b32 m0, s48
	s_nop 0
	global_load_lds_dwordx4 v128, s[36:37]
	s_waitcnt vmcnt(6)
	s_barrier
	s_setprio 1
	v_mfma_f32_16x16x32_bf16 v[44:47], v[210:213], v[174:177], v[44:47]
	v_mfma_f32_16x16x32_bf16 v[40:43], v[218:221], v[174:177], v[40:43]
	v_mfma_f32_16x16x32_bf16 v[28:31], v[210:213], v[182:185], v[28:31]
	v_mfma_f32_16x16x32_bf16 v[24:27], v[218:221], v[182:185], v[24:27]
	v_mfma_f32_16x16x32_bf16 v[12:15], v[210:213], v[190:193], v[12:15]
	v_mfma_f32_16x16x32_bf16 v[8:11], v[218:221], v[190:193], v[8:11]
	v_mfma_f32_16x16x32_bf16 v[4:7], v[210:213], v[198:201], v[4:7]
	v_mfma_f32_16x16x32_bf16 v[0:3], v[218:221], v[198:201], v[0:3]
	v_mfma_f32_16x16x32_bf16 v[44:47], v[214:217], v[178:181], v[44:47]
	v_mfma_f32_16x16x32_bf16 v[40:43], v[222:225], v[178:181], v[40:43]
	v_mfma_f32_16x16x32_bf16 v[28:31], v[214:217], v[186:189], v[28:31]
	v_mfma_f32_16x16x32_bf16 v[24:27], v[222:225], v[186:189], v[24:27]
	v_mfma_f32_16x16x32_bf16 v[12:15], v[214:217], v[194:197], v[12:15]
	v_mfma_f32_16x16x32_bf16 v[8:11], v[222:225], v[194:197], v[8:11]
	v_mfma_f32_16x16x32_bf16 v[4:7], v[214:217], v[202:205], v[4:7]
	v_mfma_f32_16x16x32_bf16 v[0:3], v[222:225], v[202:205], v[0:3]
	s_setprio 0
	s_barrier
	ds_read_b128 v[158:161], v145
	ds_read_b128 v[162:165], v146
	ds_read_b128 v[166:169], v153
	ds_read_b128 v[170:173], v154
	s_add_u32 s36, s28, 0x40000
	s_addc_u32 s37, s29, 0
	s_mov_b32 m0, s49
	ds_read_b128 v[174:177], v157 offset:32768
	ds_read_b128 v[178:181], v157 offset:33792
	ds_read_b128 v[182:185], v157 offset:34816
	ds_read_b128 v[186:189], v157 offset:35840
	ds_read_b128 v[190:193], v157 offset:36864
	ds_read_b128 v[194:197], v157 offset:37888
	ds_read_b128 v[198:201], v157 offset:38912
	ds_read_b128 v[202:205], v157 offset:39936
	s_nop 0
	global_load_lds_dwordx4 v134, s[36:37]
	s_mov_b32 m0, s50
	s_nop 0
	global_load_lds_dwordx4 v130, s[36:37]
	s_waitcnt lgkmcnt(8)
	s_barrier
	s_waitcnt lgkmcnt(0)
	s_setprio 1
	s_waitcnt lgkmcnt(0)
	v_mfma_f32_16x16x32_bf16 v[124:127], v[158:161], v[174:177], v[124:127]
	v_mfma_f32_16x16x32_bf16 v[120:123], v[166:169], v[174:177], v[120:123]
	v_mfma_f32_16x16x32_bf16 v[116:119], v[158:161], v[182:185], v[116:119]
	v_mfma_f32_16x16x32_bf16 v[112:115], v[166:169], v[182:185], v[112:115]
	v_mfma_f32_16x16x32_bf16 v[100:103], v[158:161], v[190:193], v[100:103]
	v_mfma_f32_16x16x32_bf16 v[96:99], v[166:169], v[190:193], v[96:99]
	v_mfma_f32_16x16x32_bf16 v[84:87], v[158:161], v[198:201], v[84:87]
	v_mfma_f32_16x16x32_bf16 v[80:83], v[166:169], v[198:201], v[80:83]
	v_mfma_f32_16x16x32_bf16 v[124:127], v[162:165], v[178:181], v[124:127]
	v_mfma_f32_16x16x32_bf16 v[120:123], v[170:173], v[178:181], v[120:123]
	v_mfma_f32_16x16x32_bf16 v[116:119], v[162:165], v[186:189], v[116:119]
	v_mfma_f32_16x16x32_bf16 v[112:115], v[170:173], v[186:189], v[112:115]
	v_mfma_f32_16x16x32_bf16 v[100:103], v[162:165], v[194:197], v[100:103]
	v_mfma_f32_16x16x32_bf16 v[96:99], v[170:173], v[194:197], v[96:99]
	v_mfma_f32_16x16x32_bf16 v[84:87], v[162:165], v[202:205], v[84:87]
	v_mfma_f32_16x16x32_bf16 v[80:83], v[170:173], v[202:205], v[80:83]
	s_setprio 0
	s_barrier
	s_add_u32 s36, s34, 0x80
	s_addc_u32 s37, s35, 0
	s_mov_b32 m0, s52
	ds_read_b128 v[210:213], v147
	ds_read_b128 v[214:217], v148
	ds_read_b128 v[218:221], v155
	ds_read_b128 v[222:225], v156
	s_nop 0
	global_load_lds_dwordx4 v132, s[36:37]
	s_mov_b32 m0, s53
	s_nop 0
	global_load_lds_dwordx4 v128, s[36:37]
	s_nop 0
	s_barrier
	s_waitcnt lgkmcnt(0)
	s_setprio 1
	s_waitcnt lgkmcnt(0)
	v_mfma_f32_16x16x32_bf16 v[108:111], v[210:213], v[174:177], v[108:111]
	v_mfma_f32_16x16x32_bf16 v[104:107], v[218:221], v[174:177], v[104:107]
	v_mfma_f32_16x16x32_bf16 v[92:95], v[210:213], v[182:185], v[92:95]
	v_mfma_f32_16x16x32_bf16 v[88:91], v[218:221], v[182:185], v[88:91]
	v_mfma_f32_16x16x32_bf16 v[76:79], v[210:213], v[190:193], v[76:79]
	v_mfma_f32_16x16x32_bf16 v[72:75], v[218:221], v[190:193], v[72:75]
	v_mfma_f32_16x16x32_bf16 v[68:71], v[210:213], v[198:201], v[68:71]
	v_mfma_f32_16x16x32_bf16 v[64:67], v[218:221], v[198:201], v[64:67]
	v_mfma_f32_16x16x32_bf16 v[108:111], v[214:217], v[178:181], v[108:111]
	v_mfma_f32_16x16x32_bf16 v[104:107], v[222:225], v[178:181], v[104:107]
	v_mfma_f32_16x16x32_bf16 v[92:95], v[214:217], v[186:189], v[92:95]
	v_mfma_f32_16x16x32_bf16 v[88:91], v[222:225], v[186:189], v[88:91]
	v_mfma_f32_16x16x32_bf16 v[76:79], v[214:217], v[194:197], v[76:79]
	v_mfma_f32_16x16x32_bf16 v[72:75], v[222:225], v[194:197], v[72:75]
	v_mfma_f32_16x16x32_bf16 v[68:71], v[214:217], v[202:205], v[68:71]
	v_mfma_f32_16x16x32_bf16 v[64:67], v[222:225], v[202:205], v[64:67]
	s_setprio 0
	s_add_u32 s28, s28, 0x80
	s_addc_u32 s29, s29, 0
	s_mov_b32 m0, s54
	s_barrier
	ds_read_b128 v[174:177], v157 offset:49152
	ds_read_b128 v[178:181], v157 offset:50176
	ds_read_b128 v[182:185], v157 offset:51200
	ds_read_b128 v[186:189], v157 offset:52224
	ds_read_b128 v[190:193], v157 offset:53248
	ds_read_b128 v[194:197], v157 offset:54272
	ds_read_b128 v[198:201], v157 offset:55296
	ds_read_b128 v[202:205], v157 offset:56320
	s_nop 0
	global_load_lds_dwordx4 v134, s[28:29]
	s_mov_b32 m0, s55
	s_nop 0
	global_load_lds_dwordx4 v130, s[28:29]
	s_nop 0
	s_barrier
	s_waitcnt lgkmcnt(0)
	s_setprio 1
	s_waitcnt lgkmcnt(0)
	v_mfma_f32_16x16x32_bf16 v[60:63], v[158:161], v[174:177], v[60:63]
	v_mfma_f32_16x16x32_bf16 v[56:59], v[166:169], v[174:177], v[56:59]
	v_mfma_f32_16x16x32_bf16 v[52:55], v[158:161], v[182:185], v[52:55]
	v_mfma_f32_16x16x32_bf16 v[48:51], v[166:169], v[182:185], v[48:51]
	v_mfma_f32_16x16x32_bf16 v[36:39], v[158:161], v[190:193], v[36:39]
	v_mfma_f32_16x16x32_bf16 v[32:35], v[166:169], v[190:193], v[32:35]
	v_mfma_f32_16x16x32_bf16 v[20:23], v[158:161], v[198:201], v[20:23]
	v_mfma_f32_16x16x32_bf16 v[16:19], v[166:169], v[198:201], v[16:19]
	v_mfma_f32_16x16x32_bf16 v[60:63], v[162:165], v[178:181], v[60:63]
	v_mfma_f32_16x16x32_bf16 v[56:59], v[170:173], v[178:181], v[56:59]
	v_mfma_f32_16x16x32_bf16 v[52:55], v[162:165], v[186:189], v[52:55]
	v_mfma_f32_16x16x32_bf16 v[48:51], v[170:173], v[186:189], v[48:51]
	v_mfma_f32_16x16x32_bf16 v[36:39], v[162:165], v[194:197], v[36:39]
	v_mfma_f32_16x16x32_bf16 v[32:35], v[170:173], v[194:197], v[32:35]
	v_mfma_f32_16x16x32_bf16 v[20:23], v[162:165], v[202:205], v[20:23]
	v_mfma_f32_16x16x32_bf16 v[16:19], v[170:173], v[202:205], v[16:19]
	s_setprio 0
	s_barrier
	s_add_u32 s28, s34, 0x40080
	s_addc_u32 s29, s35, 0
	s_mov_b32 m0, s56
	s_nop 0
	global_load_lds_dwordx4 v132, s[28:29]
	s_mov_b32 m0, s57
	s_nop 0
	global_load_lds_dwordx4 v128, s[28:29]
	s_waitcnt vmcnt(6)
	s_barrier
	s_setprio 1
	v_mfma_f32_16x16x32_bf16 v[44:47], v[210:213], v[174:177], v[44:47]
	v_mfma_f32_16x16x32_bf16 v[40:43], v[218:221], v[174:177], v[40:43]
	v_mfma_f32_16x16x32_bf16 v[28:31], v[210:213], v[182:185], v[28:31]
	v_mfma_f32_16x16x32_bf16 v[24:27], v[218:221], v[182:185], v[24:27]
	v_mfma_f32_16x16x32_bf16 v[12:15], v[210:213], v[190:193], v[12:15]
	v_mfma_f32_16x16x32_bf16 v[8:11], v[218:221], v[190:193], v[8:11]
	v_mfma_f32_16x16x32_bf16 v[4:7], v[210:213], v[198:201], v[4:7]
	v_mfma_f32_16x16x32_bf16 v[0:3], v[218:221], v[198:201], v[0:3]
	v_mfma_f32_16x16x32_bf16 v[44:47], v[214:217], v[178:181], v[44:47]
	v_mfma_f32_16x16x32_bf16 v[40:43], v[222:225], v[178:181], v[40:43]
	v_mfma_f32_16x16x32_bf16 v[28:31], v[214:217], v[186:189], v[28:31]
	v_mfma_f32_16x16x32_bf16 v[24:27], v[222:225], v[186:189], v[24:27]
	v_mfma_f32_16x16x32_bf16 v[12:15], v[214:217], v[194:197], v[12:15]
	v_mfma_f32_16x16x32_bf16 v[8:11], v[222:225], v[194:197], v[8:11]
	v_mfma_f32_16x16x32_bf16 v[4:7], v[214:217], v[202:205], v[4:7]
	v_mfma_f32_16x16x32_bf16 v[0:3], v[222:225], v[202:205], v[0:3]
	s_setprio 0
	s_add_i32 s61, s61, 2
	s_cmp_gt_u32 s61, 13
	s_mov_b64 s[28:29], s[30:31]
	s_barrier
	s_cbranch_scc0 .LBB0_233
	v_mov_b32_e32 v158, v140
	v_mov_b64_e32 v[160:161], s[2:3]
	v_ashrrev_i32_e32 v159, 2, v158
	v_and_b32_e32 v159, 0xffffffc0, v159
	v_lshl_add_u32 v159, s14, 8, v159
	v_and_or_b32 v164, v158, 15, v159
	v_lshrrev_b32_e32 v158, 1, v158
	v_and_b32_e32 v158, 0x78, v158
	v_lshl_or_b32 v158, s60, 8, v158
	v_ashrrev_i32_e32 v159, 31, v158
	v_cvt_pk_bf16_f32 v68, v68, v69
	v_cvt_pk_bf16_f32 v69, v70, v71
	v_cvt_pk_bf16_f32 v70, v64, v65
	v_add_u32_e32 v64, 0x80, v164
	v_mad_i64_i32 v[162:163], s[6:7], v164, s59, v[160:161]
	v_lshlrev_b64 v[158:159], 1, v[158:159]
	v_cvt_pk_bf16_f32 v108, v108, v109
	v_cvt_pk_bf16_f32 v109, v110, v111
	v_cvt_pk_bf16_f32 v110, v104, v105
	v_or_b32_e32 v104, 16, v164
	v_mad_i64_i32 v[64:65], s[6:7], v64, s59, v[160:161]
	v_cvt_pk_bf16_f32 v44, v44, v45
	v_cvt_pk_bf16_f32 v45, v46, v47
	v_cvt_pk_bf16_f32 v46, v40, v41
	v_add_u32_e32 v40, 0x90, v164
	v_lshl_add_u64 v[162:163], v[162:163], 0, v[158:159]
	v_cvt_pk_bf16_f32 v111, v106, v107
	v_mad_i64_i32 v[104:105], s[6:7], v104, s59, v[160:161]
	v_cvt_pk_bf16_f32 v92, v92, v93
	v_cvt_pk_bf16_f32 v93, v94, v95
	v_cvt_pk_bf16_f32 v94, v88, v89
	v_or_b32_e32 v88, 32, v164
	v_lshl_add_u64 v[64:65], v[64:65], 0, v[158:159]
	v_cvt_pk_bf16_f32 v47, v42, v43
	v_mad_i64_i32 v[40:41], s[6:7], v40, s59, v[160:161]
	v_cvt_pk_bf16_f32 v28, v28, v29
	v_cvt_pk_bf16_f32 v29, v30, v31
	v_cvt_pk_bf16_f32 v30, v24, v25
	v_add_u32_e32 v24, 0xa0, v164
	global_store_dwordx4 v[162:163], v[108:111], off offset:256
	v_cvt_pk_bf16_f32 v95, v90, v91
	v_mad_i64_i32 v[88:89], s[6:7], v88, s59, v[160:161]
	v_lshl_add_u64 v[108:109], v[104:105], 0, v[158:159]
	v_cvt_pk_bf16_f32 v76, v76, v77
	v_cvt_pk_bf16_f32 v77, v78, v79
	v_cvt_pk_bf16_f32 v78, v72, v73
	v_or_b32_e32 v72, 48, v164
	global_store_dwordx4 v[64:65], v[44:47], off offset:256
	v_cvt_pk_bf16_f32 v31, v26, v27
	v_mad_i64_i32 v[24:25], s[6:7], v24, s59, v[160:161]
	v_lshl_add_u64 v[44:45], v[40:41], 0, v[158:159]
	v_cvt_pk_bf16_f32 v12, v12, v13
	v_cvt_pk_bf16_f32 v13, v14, v15
	v_cvt_pk_bf16_f32 v14, v8, v9
	v_add_u32_e32 v8, 0xb0, v164
	global_store_dwordx4 v[108:109], v[92:95], off offset:256
	v_cvt_pk_bf16_f32 v79, v74, v75
	v_mad_i64_i32 v[72:73], s[6:7], v72, s59, v[160:161]
	v_lshl_add_u64 v[92:93], v[88:89], 0, v[158:159]
	global_store_dwordx4 v[44:45], v[28:31], off offset:256
	v_cvt_pk_bf16_f32 v15, v10, v11
	v_mad_i64_i32 v[8:9], s[6:7], v8, s59, v[160:161]
	v_lshl_add_u64 v[28:29], v[24:25], 0, v[158:159]
	v_cvt_pk_bf16_f32 v124, v124, v125
	v_cvt_pk_bf16_f32 v125, v126, v127
	v_cvt_pk_bf16_f32 v126, v120, v121
	v_cvt_pk_bf16_f32 v127, v122, v123
	v_cvt_pk_bf16_f32 v104, v116, v117
	v_cvt_pk_bf16_f32 v105, v118, v119
	v_cvt_pk_bf16_f32 v106, v112, v113
	v_cvt_pk_bf16_f32 v107, v114, v115
	v_cvt_pk_bf16_f32 v88, v100, v101
	v_cvt_pk_bf16_f32 v89, v102, v103
	v_cvt_pk_bf16_f32 v90, v96, v97
	v_cvt_pk_bf16_f32 v91, v98, v99
	global_store_dwordx4 v[92:93], v[76:79], off offset:256
	v_cvt_pk_bf16_f32 v74, v80, v81
	v_cvt_pk_bf16_f32 v75, v82, v83
	v_lshl_add_u64 v[76:77], v[72:73], 0, v[158:159]
	v_cvt_pk_bf16_f32 v72, v84, v85
	v_cvt_pk_bf16_f32 v73, v86, v87
	v_cvt_pk_bf16_f32 v71, v66, v67
	v_cvt_pk_bf16_f32 v60, v60, v61
	v_cvt_pk_bf16_f32 v61, v62, v63
	v_cvt_pk_bf16_f32 v62, v56, v57
	v_cvt_pk_bf16_f32 v63, v58, v59
	v_cvt_pk_bf16_f32 v40, v52, v53
	v_cvt_pk_bf16_f32 v41, v54, v55
	v_cvt_pk_bf16_f32 v42, v48, v49
	v_cvt_pk_bf16_f32 v43, v50, v51
	v_cvt_pk_bf16_f32 v24, v36, v37
	v_cvt_pk_bf16_f32 v25, v38, v39
	v_cvt_pk_bf16_f32 v26, v32, v33
	v_cvt_pk_bf16_f32 v27, v34, v35
	global_store_dwordx4 v[28:29], v[12:15], off offset:256
	v_cvt_pk_bf16_f32 v10, v16, v17
	v_cvt_pk_bf16_f32 v11, v18, v19
	v_lshl_add_u64 v[12:13], v[8:9], 0, v[158:159]
	v_cvt_pk_bf16_f32 v8, v20, v21
	v_cvt_pk_bf16_f32 v9, v22, v23
	v_cvt_pk_bf16_f32 v4, v4, v5
	v_cvt_pk_bf16_f32 v5, v6, v7
	v_cvt_pk_bf16_f32 v6, v0, v1
	v_cvt_pk_bf16_f32 v7, v2, v3
	s_and_b64 vcc, exec, s[4:5]
	s_mov_b32 s60, s20
	s_mov_b32 s14, s22
	s_mov_b64 s[16:17], s[26:27]
	s_mov_b64 s[18:19], s[24:25]
	global_store_dwordx4 v[162:163], v[124:127], off
	global_store_dwordx4 v[108:109], v[104:107], off
	global_store_dwordx4 v[92:93], v[88:91], off
	global_store_dwordx4 v[76:77], v[72:75], off
	global_store_dwordx4 v[76:77], v[68:71], off offset:256
	global_store_dwordx4 v[64:65], v[60:63], off
	global_store_dwordx4 v[44:45], v[40:43], off
	global_store_dwordx4 v[28:29], v[24:27], off
	global_store_dwordx4 v[12:13], v[8:11], off
	global_store_dwordx4 v[12:13], v[4:7], off offset:256
	s_cbranch_vccz .LBB0_230
	s_waitcnt vmcnt(0)
	s_cmpk_gt_u32 s33, 0xff
	s_cbranch_scc1 .LBB0_237
	s_barrier

.LBB0_558:
	s_add_u32 s40, s38, 0x100
	ds_read_b128 v[88:91], v163
	ds_read_b128 v[92:95], v164
	ds_read_b128 v[104:107], v171
	ds_read_b128 v[108:111], v172
	s_addc_u32 s41, s39, 0
	s_and_b32 s25, s40, 0x700
	s_add_u32 s27, s34, s25
	s_addc_u32 s33, s35, 0
	s_cmp_eq_u32 s20, 12
	s_cselect_b64 s[44:45], -1, 0
	s_and_b64 s[42:43], s[44:45], exec
	s_cselect_b32 s43, s1, s33
	s_cselect_b32 s42, s3, s27
	s_cselect_b32 s27, 0, 0
	s_cselect_b32 s25, 0, s25
	s_add_u32 s33, s36, s38
	s_addc_u32 s39, s37, s39
	s_add_u32 s38, s33, 0x40080
	s_addc_u32 s39, s39, 0
	ds_read_b128 v[158:161], v179
	ds_read_b128 v[180:183], v179 offset:1024
	ds_read_b128 v[184:187], v179 offset:2048
	ds_read_b128 v[188:191], v179 offset:3072
	ds_read_b128 v[192:195], v179 offset:4096
	ds_read_b128 v[196:199], v179 offset:5120
	ds_read_b128 v[200:203], v179 offset:6144
	ds_read_b128 v[204:207], v179 offset:7168
	s_add_i32 m0, s51, 0xc000
	s_nop 0
	global_load_lds_dwordx4 v144, s[38:39]
	s_add_i32 m0, s51, 0xe000
	s_nop 0
	global_load_lds_dwordx4 v148, s[38:39]
	s_waitcnt lgkmcnt(8)
	s_nop 0
	s_barrier
	s_waitcnt lgkmcnt(0)
	s_setprio 1
	s_waitcnt lgkmcnt(0)
	v_mfma_f32_16x16x32_bf16 v[140:143], v[88:91], v[158:161], v[140:143]
	v_mfma_f32_16x16x32_bf16 v[136:139], v[104:107], v[158:161], v[136:139]
	v_mfma_f32_16x16x32_bf16 v[124:127], v[88:91], v[184:187], v[124:127]
	v_mfma_f32_16x16x32_bf16 v[120:123], v[104:107], v[184:187], v[120:123]
	v_mfma_f32_16x16x32_bf16 v[100:103], v[88:91], v[192:195], v[100:103]
	v_mfma_f32_16x16x32_bf16 v[96:99], v[104:107], v[192:195], v[96:99]
	v_mfma_f32_16x16x32_bf16 v[76:79], v[88:91], v[200:203], v[76:79]
	v_mfma_f32_16x16x32_bf16 v[72:75], v[104:107], v[200:203], v[72:75]
	v_mfma_f32_16x16x32_bf16 v[140:143], v[92:95], v[180:183], v[140:143]
	v_mfma_f32_16x16x32_bf16 v[136:139], v[108:111], v[180:183], v[136:139]
	v_mfma_f32_16x16x32_bf16 v[124:127], v[92:95], v[188:191], v[124:127]
	v_mfma_f32_16x16x32_bf16 v[120:123], v[108:111], v[188:191], v[120:123]
	v_mfma_f32_16x16x32_bf16 v[100:103], v[92:95], v[196:199], v[100:103]
	v_mfma_f32_16x16x32_bf16 v[96:99], v[108:111], v[196:199], v[96:99]
	v_mfma_f32_16x16x32_bf16 v[76:79], v[92:95], v[204:207], v[76:79]
	v_mfma_f32_16x16x32_bf16 v[72:75], v[108:111], v[204:207], v[72:75]
	s_setprio 0
	s_barrier
	s_mov_b64 s[38:39], s[42:43]
	s_mov_b32 m0, s52
	ds_read_b128 v[210:213], v165
	ds_read_b128 v[214:217], v166
	ds_read_b128 v[218:221], v173
	ds_read_b128 v[222:225], v174
	s_nop 0
	global_load_lds_dwordx4 v146, s[38:39]
	s_mov_b32 m0, s53
	s_nop 0
	global_load_lds_dwordx4 v150, s[38:39]
	s_nop 0
	s_barrier
	s_waitcnt lgkmcnt(0)
	s_setprio 1
	s_waitcnt lgkmcnt(0)
	v_mfma_f32_16x16x32_bf16 v[132:135], v[210:213], v[158:161], v[132:135]
	v_mfma_f32_16x16x32_bf16 v[128:131], v[218:221], v[158:161], v[128:131]
	v_mfma_f32_16x16x32_bf16 v[116:119], v[210:213], v[184:187], v[116:119]
	v_mfma_f32_16x16x32_bf16 v[112:115], v[218:221], v[184:187], v[112:115]
	v_mfma_f32_16x16x32_bf16 v[84:87], v[210:213], v[192:195], v[84:87]
	v_mfma_f32_16x16x32_bf16 v[80:83], v[218:221], v[192:195], v[80:83]
	v_mfma_f32_16x16x32_bf16 v[68:71], v[210:213], v[200:203], v[68:71]
	v_mfma_f32_16x16x32_bf16 v[64:67], v[218:221], v[200:203], v[64:67]
	v_mfma_f32_16x16x32_bf16 v[132:135], v[214:217], v[180:183], v[132:135]
	v_mfma_f32_16x16x32_bf16 v[128:131], v[222:225], v[180:183], v[128:131]
	v_mfma_f32_16x16x32_bf16 v[116:119], v[214:217], v[188:191], v[116:119]
	v_mfma_f32_16x16x32_bf16 v[112:115], v[222:225], v[188:191], v[112:115]
	v_mfma_f32_16x16x32_bf16 v[84:87], v[214:217], v[196:199], v[84:87]
	v_mfma_f32_16x16x32_bf16 v[80:83], v[222:225], v[196:199], v[80:83]
	v_mfma_f32_16x16x32_bf16 v[68:71], v[214:217], v[204:207], v[68:71]
	v_mfma_f32_16x16x32_bf16 v[64:67], v[222:225], v[204:207], v[64:67]
	s_setprio 0
	s_and_b64 s[38:39], s[8:9], s[44:45]
	s_and_b64 s[38:39], s[38:39], exec
	s_cselect_b32 s38, s28, s36
	s_cselect_b32 s33, s29, s37
	s_add_u32 s38, s38, s25
	s_addc_u32 s39, s33, s27
	s_mov_b64 s[44:45], s[38:39]
	s_mov_b32 m0, s51
	s_barrier
	ds_read_b128 v[158:161], v179 offset:16384
	ds_read_b128 v[180:183], v179 offset:17408
	ds_read_b128 v[184:187], v179 offset:18432
	ds_read_b128 v[188:191], v179 offset:19456
	ds_read_b128 v[192:195], v179 offset:20480
	ds_read_b128 v[196:199], v179 offset:21504
	ds_read_b128 v[200:203], v179 offset:22528
	ds_read_b128 v[204:207], v179 offset:23552
	s_nop 0
	global_load_lds_dwordx4 v144, s[44:45]
	s_mov_b32 m0, s54
	s_nop 0
	global_load_lds_dwordx4 v148, s[44:45]
	s_nop 0
	s_barrier
	s_waitcnt lgkmcnt(0)
	s_setprio 1
	s_waitcnt lgkmcnt(0)
	v_mfma_f32_16x16x32_bf16 v[60:63], v[88:91], v[158:161], v[60:63]
	v_mfma_f32_16x16x32_bf16 v[56:59], v[104:107], v[158:161], v[56:59]
	v_mfma_f32_16x16x32_bf16 v[44:47], v[88:91], v[184:187], v[44:47]
	v_mfma_f32_16x16x32_bf16 v[40:43], v[104:107], v[184:187], v[40:43]
	v_mfma_f32_16x16x32_bf16 v[28:31], v[88:91], v[192:195], v[28:31]
	v_mfma_f32_16x16x32_bf16 v[24:27], v[104:107], v[192:195], v[24:27]
	v_mfma_f32_16x16x32_bf16 v[12:15], v[88:91], v[200:203], v[12:15]
	v_mfma_f32_16x16x32_bf16 v[8:11], v[104:107], v[200:203], v[8:11]
	v_mfma_f32_16x16x32_bf16 v[60:63], v[92:95], v[180:183], v[60:63]
	v_mfma_f32_16x16x32_bf16 v[56:59], v[108:111], v[180:183], v[56:59]
	v_mfma_f32_16x16x32_bf16 v[44:47], v[92:95], v[188:191], v[44:47]
	v_mfma_f32_16x16x32_bf16 v[40:43], v[108:111], v[188:191], v[40:43]
	v_mfma_f32_16x16x32_bf16 v[28:31], v[92:95], v[196:199], v[28:31]
	v_mfma_f32_16x16x32_bf16 v[24:27], v[108:111], v[196:199], v[24:27]
	v_mfma_f32_16x16x32_bf16 v[12:15], v[92:95], v[204:207], v[12:15]
	v_mfma_f32_16x16x32_bf16 v[8:11], v[108:111], v[204:207], v[8:11]
	s_setprio 0
	s_barrier
	s_add_u32 s44, s42, 0x40000
	s_addc_u32 s45, s43, 0
	s_mov_b32 m0, s55
	s_nop 0
	global_load_lds_dwordx4 v146, s[44:45]
	s_mov_b32 m0, s56
	s_nop 0
	global_load_lds_dwordx4 v150, s[44:45]
	s_waitcnt vmcnt(6)
	s_barrier
	s_setprio 1
	v_mfma_f32_16x16x32_bf16 v[52:55], v[210:213], v[158:161], v[52:55]
	v_mfma_f32_16x16x32_bf16 v[48:51], v[218:221], v[158:161], v[48:51]
	v_mfma_f32_16x16x32_bf16 v[36:39], v[210:213], v[184:187], v[36:39]
	v_mfma_f32_16x16x32_bf16 v[32:35], v[218:221], v[184:187], v[32:35]
	v_mfma_f32_16x16x32_bf16 v[20:23], v[210:213], v[192:195], v[20:23]
	v_mfma_f32_16x16x32_bf16 v[16:19], v[218:221], v[192:195], v[16:19]
	v_mfma_f32_16x16x32_bf16 v[4:7], v[210:213], v[200:203], v[4:7]
	v_mfma_f32_16x16x32_bf16 v[0:3], v[218:221], v[200:203], v[0:3]
	v_mfma_f32_16x16x32_bf16 v[52:55], v[214:217], v[180:183], v[52:55]
	v_mfma_f32_16x16x32_bf16 v[48:51], v[222:225], v[180:183], v[48:51]
	v_mfma_f32_16x16x32_bf16 v[36:39], v[214:217], v[188:191], v[36:39]
	v_mfma_f32_16x16x32_bf16 v[32:35], v[222:225], v[188:191], v[32:35]
	v_mfma_f32_16x16x32_bf16 v[20:23], v[214:217], v[196:199], v[20:23]
	v_mfma_f32_16x16x32_bf16 v[16:19], v[222:225], v[196:199], v[16:19]
	v_mfma_f32_16x16x32_bf16 v[4:7], v[214:217], v[204:207], v[4:7]
	v_mfma_f32_16x16x32_bf16 v[0:3], v[222:225], v[204:207], v[0:3]
	s_setprio 0
	s_barrier
	ds_read_b128 v[88:91], v167
	ds_read_b128 v[92:95], v168
	ds_read_b128 v[104:107], v175
	ds_read_b128 v[108:111], v176
	s_add_u32 s44, s38, 0x40000
	s_addc_u32 s45, s39, 0
	s_mov_b32 m0, s57
	ds_read_b128 v[158:161], v179 offset:32768
	ds_read_b128 v[180:183], v179 offset:33792
	ds_read_b128 v[184:187], v179 offset:34816
	ds_read_b128 v[188:191], v179 offset:35840
	ds_read_b128 v[192:195], v179 offset:36864
	ds_read_b128 v[196:199], v179 offset:37888
	ds_read_b128 v[200:203], v179 offset:38912
	ds_read_b128 v[204:207], v179 offset:39936
	s_nop 0
	global_load_lds_dwordx4 v144, s[44:45]
	s_mov_b32 m0, s58
	s_nop 0
	global_load_lds_dwordx4 v148, s[44:45]
	s_waitcnt lgkmcnt(8)
	s_barrier
	s_waitcnt lgkmcnt(0)
	s_setprio 1
	s_waitcnt lgkmcnt(0)
	v_mfma_f32_16x16x32_bf16 v[140:143], v[88:91], v[158:161], v[140:143]
	v_mfma_f32_16x16x32_bf16 v[136:139], v[104:107], v[158:161], v[136:139]
	v_mfma_f32_16x16x32_bf16 v[124:127], v[88:91], v[184:187], v[124:127]
	v_mfma_f32_16x16x32_bf16 v[120:123], v[104:107], v[184:187], v[120:123]
	v_mfma_f32_16x16x32_bf16 v[100:103], v[88:91], v[192:195], v[100:103]
	v_mfma_f32_16x16x32_bf16 v[96:99], v[104:107], v[192:195], v[96:99]
	v_mfma_f32_16x16x32_bf16 v[76:79], v[88:91], v[200:203], v[76:79]
	v_mfma_f32_16x16x32_bf16 v[72:75], v[104:107], v[200:203], v[72:75]
	v_mfma_f32_16x16x32_bf16 v[140:143], v[92:95], v[180:183], v[140:143]
	v_mfma_f32_16x16x32_bf16 v[136:139], v[108:111], v[180:183], v[136:139]
	v_mfma_f32_16x16x32_bf16 v[124:127], v[92:95], v[188:191], v[124:127]
	v_mfma_f32_16x16x32_bf16 v[120:123], v[108:111], v[188:191], v[120:123]
	v_mfma_f32_16x16x32_bf16 v[100:103], v[92:95], v[196:199], v[100:103]
	v_mfma_f32_16x16x32_bf16 v[96:99], v[108:111], v[196:199], v[96:99]
	v_mfma_f32_16x16x32_bf16 v[76:79], v[92:95], v[204:207], v[76:79]
	v_mfma_f32_16x16x32_bf16 v[72:75], v[108:111], v[204:207], v[72:75]
	s_setprio 0
	s_barrier
	s_add_u32 s44, s42, 0x80
	s_addc_u32 s45, s43, 0
	s_mov_b32 m0, s61
	ds_read_b128 v[210:213], v169
	ds_read_b128 v[214:217], v170
	ds_read_b128 v[218:221], v177
	ds_read_b128 v[222:225], v178
	s_nop 0
	global_load_lds_dwordx4 v146, s[44:45]
	s_mov_b32 m0, s62
	s_nop 0
	global_load_lds_dwordx4 v150, s[44:45]
	s_nop 0
	s_barrier
	s_waitcnt lgkmcnt(0)
	s_setprio 1
	s_waitcnt lgkmcnt(0)
	v_mfma_f32_16x16x32_bf16 v[132:135], v[210:213], v[158:161], v[132:135]
	v_mfma_f32_16x16x32_bf16 v[128:131], v[218:221], v[158:161], v[128:131]
	v_mfma_f32_16x16x32_bf16 v[116:119], v[210:213], v[184:187], v[116:119]
	v_mfma_f32_16x16x32_bf16 v[112:115], v[218:221], v[184:187], v[112:115]
	v_mfma_f32_16x16x32_bf16 v[84:87], v[210:213], v[192:195], v[84:87]
	v_mfma_f32_16x16x32_bf16 v[80:83], v[218:221], v[192:195], v[80:83]
	v_mfma_f32_16x16x32_bf16 v[68:71], v[210:213], v[200:203], v[68:71]
	v_mfma_f32_16x16x32_bf16 v[64:67], v[218:221], v[200:203], v[64:67]
	v_mfma_f32_16x16x32_bf16 v[132:135], v[214:217], v[180:183], v[132:135]
	v_mfma_f32_16x16x32_bf16 v[128:131], v[222:225], v[180:183], v[128:131]
	v_mfma_f32_16x16x32_bf16 v[116:119], v[214:217], v[188:191], v[116:119]
	v_mfma_f32_16x16x32_bf16 v[112:115], v[222:225], v[188:191], v[112:115]
	v_mfma_f32_16x16x32_bf16 v[84:87], v[214:217], v[196:199], v[84:87]
	v_mfma_f32_16x16x32_bf16 v[80:83], v[222:225], v[196:199], v[80:83]
	v_mfma_f32_16x16x32_bf16 v[68:71], v[214:217], v[204:207], v[68:71]
	v_mfma_f32_16x16x32_bf16 v[64:67], v[222:225], v[204:207], v[64:67]
	s_setprio 0
	s_add_u32 s38, s38, 0x80
	s_addc_u32 s39, s39, 0
	s_mov_b32 m0, s63
	s_barrier
	ds_read_b128 v[158:161], v179 offset:49152
	ds_read_b128 v[180:183], v179 offset:50176
	ds_read_b128 v[184:187], v179 offset:51200
	ds_read_b128 v[188:191], v179 offset:52224
	ds_read_b128 v[192:195], v179 offset:53248
	ds_read_b128 v[196:199], v179 offset:54272
	ds_read_b128 v[200:203], v179 offset:55296
	ds_read_b128 v[204:207], v179 offset:56320
	s_nop 0
	global_load_lds_dwordx4 v144, s[38:39]
	s_mov_b32 m0, s64
	s_nop 0
	global_load_lds_dwordx4 v148, s[38:39]
	s_nop 0
	s_barrier
	s_waitcnt lgkmcnt(0)
	s_setprio 1
	s_waitcnt lgkmcnt(0)
	v_mfma_f32_16x16x32_bf16 v[60:63], v[88:91], v[158:161], v[60:63]
	v_mfma_f32_16x16x32_bf16 v[56:59], v[104:107], v[158:161], v[56:59]
	v_mfma_f32_16x16x32_bf16 v[44:47], v[88:91], v[184:187], v[44:47]
	v_mfma_f32_16x16x32_bf16 v[40:43], v[104:107], v[184:187], v[40:43]
	v_mfma_f32_16x16x32_bf16 v[28:31], v[88:91], v[192:195], v[28:31]
	v_mfma_f32_16x16x32_bf16 v[24:27], v[104:107], v[192:195], v[24:27]
	v_mfma_f32_16x16x32_bf16 v[12:15], v[88:91], v[200:203], v[12:15]
	v_mfma_f32_16x16x32_bf16 v[8:11], v[104:107], v[200:203], v[8:11]
	v_mfma_f32_16x16x32_bf16 v[60:63], v[92:95], v[180:183], v[60:63]
	v_mfma_f32_16x16x32_bf16 v[56:59], v[108:111], v[180:183], v[56:59]
	v_mfma_f32_16x16x32_bf16 v[44:47], v[92:95], v[188:191], v[44:47]
	v_mfma_f32_16x16x32_bf16 v[40:43], v[108:111], v[188:191], v[40:43]
	v_mfma_f32_16x16x32_bf16 v[28:31], v[92:95], v[196:199], v[28:31]
	v_mfma_f32_16x16x32_bf16 v[24:27], v[108:111], v[196:199], v[24:27]
	v_mfma_f32_16x16x32_bf16 v[12:15], v[92:95], v[204:207], v[12:15]
	v_mfma_f32_16x16x32_bf16 v[8:11], v[108:111], v[204:207], v[8:11]
	s_setprio 0
	s_barrier
	s_add_u32 s38, s42, 0x40080
	s_addc_u32 s39, s43, 0
	s_mov_b32 m0, s65
	s_nop 0
	global_load_lds_dwordx4 v146, s[38:39]
	s_mov_b32 m0, s66
	s_nop 0
	global_load_lds_dwordx4 v150, s[38:39]
	s_waitcnt vmcnt(6)
	s_barrier
	s_setprio 1
	v_mfma_f32_16x16x32_bf16 v[52:55], v[210:213], v[158:161], v[52:55]
	v_mfma_f32_16x16x32_bf16 v[48:51], v[218:221], v[158:161], v[48:51]
	v_mfma_f32_16x16x32_bf16 v[36:39], v[210:213], v[184:187], v[36:39]
	v_mfma_f32_16x16x32_bf16 v[32:35], v[218:221], v[184:187], v[32:35]
	v_mfma_f32_16x16x32_bf16 v[20:23], v[210:213], v[192:195], v[20:23]
	v_mfma_f32_16x16x32_bf16 v[16:19], v[218:221], v[192:195], v[16:19]
	v_mfma_f32_16x16x32_bf16 v[4:7], v[210:213], v[200:203], v[4:7]
	v_mfma_f32_16x16x32_bf16 v[0:3], v[218:221], v[200:203], v[0:3]
	v_mfma_f32_16x16x32_bf16 v[52:55], v[214:217], v[180:183], v[52:55]
	v_mfma_f32_16x16x32_bf16 v[48:51], v[222:225], v[180:183], v[48:51]
	v_mfma_f32_16x16x32_bf16 v[36:39], v[214:217], v[188:191], v[36:39]
	v_mfma_f32_16x16x32_bf16 v[32:35], v[222:225], v[188:191], v[32:35]
	v_mfma_f32_16x16x32_bf16 v[20:23], v[214:217], v[196:199], v[20:23]
	v_mfma_f32_16x16x32_bf16 v[16:19], v[222:225], v[196:199], v[16:19]
	v_mfma_f32_16x16x32_bf16 v[4:7], v[214:217], v[204:207], v[4:7]
	v_mfma_f32_16x16x32_bf16 v[0:3], v[222:225], v[204:207], v[0:3]
	s_setprio 0
	s_add_i32 s20, s20, 2
	s_cmp_gt_u32 s20, 13
	s_mov_b64 s[38:39], s[40:41]
	s_barrier
	s_cbranch_scc0 .LBB0_558
	s_cmpk_gt_i32 s2, 0x7f
	s_cselect_b64 s[34:35], -1, 0
	v_mov_b32_e32 v88, v162
	s_mov_b64 s[8:9], 0xc000
	s_and_b64 vcc, exec, s[34:35]
	s_cbranch_vccnz .LBB0_561
	s_ashr_i32 s1, s2, 31
	s_lshr_b32 s1, s1, 28
	s_add_i32 s1, s2, s1
	s_ashr_i32 s1, s1, 4
	s_mul_hi_i32 s9, s1, 0x1800
	s_mul_i32 s8, s1, 0x1800

.LBB0_994:
	v_mov_b32_e32 v0, v209
	s_mov_b32 s98, 0x44800000
	s_mov_b32 s100, 0xbd38aa3b
	s_ashr_i32 s2, s0, 31
	v_ashrrev_i32_e32 v1, 2, v0
	v_and_b32_e32 v1, 0xffffffc0, v1
	v_lshl_add_u32 v1, s33, 8, v1
	v_and_or_b32 v4, v0, 15, v1
	v_lshrrev_b32_e32 v2, 1, v0
	s_lshr_b32 s2, s2, 29
	s_add_i32 s2, s0, s2
	s_and_b32 s2, s2, 0x1fffff8
	s_sub_i32 s0, s0, s2
	v_and_b32_e32 v2, 0x78, v2
	v_ashrrev_i32_e32 v5, 31, v4
	v_lshl_or_b32 v2, s0, 7, v2
	v_lshlrev_b64 v[0:1], 10, v[4:5]
	v_ashrrev_i32_e32 v3, 31, v2
	v_lshl_add_u64 v[0:1], s[14:15], 0, v[0:1]
	v_lshl_add_u64 v[0:1], v[0:1], 0, v[2:3]
	v_pk_mul_f32 v[10:11], v[188:189], s[100:101] op_sel_hi:[1,0]
	v_pk_mul_f32 v[12:13], v[190:191], s[100:101] op_sel_hi:[1,0]
	v_pk_mul_f32 v[14:15], v[180:181], s[100:101] op_sel_hi:[1,0]
	v_pk_mul_f32 v[16:17], v[182:183], s[100:101] op_sel_hi:[1,0]
	v_exp_f32_e32 v10, v10
	v_exp_f32_e32 v11, v11
	v_exp_f32_e32 v12, v12
	v_exp_f32_e32 v13, v13
	v_exp_f32_e32 v14, v14
	v_exp_f32_e32 v15, v15
	v_exp_f32_e32 v16, v16
	v_exp_f32_e32 v17, v17
	v_pk_fma_f32 v[10:11], v[10:11], s[98:99], s[98:99] op_sel_hi:[1,0,0]
	v_pk_fma_f32 v[12:13], v[12:13], s[98:99], s[98:99] op_sel_hi:[1,0,0]
	v_pk_fma_f32 v[14:15], v[14:15], s[98:99], s[98:99] op_sel_hi:[1,0,0]
	v_pk_fma_f32 v[16:17], v[16:17], s[98:99], s[98:99] op_sel_hi:[1,0,0]
	v_rcp_f32_e32 v10, v10
	v_rcp_f32_e32 v11, v11
	v_rcp_f32_e32 v12, v12
	v_rcp_f32_e32 v13, v13
	v_rcp_f32_e32 v14, v14
	v_rcp_f32_e32 v15, v15
	v_rcp_f32_e32 v16, v16
	v_rcp_f32_e32 v17, v17
	v_pk_mul_f32 v[10:11], v[188:189], v[10:11]
	v_pk_mul_f32 v[12:13], v[190:191], v[12:13]
	v_pk_mul_f32 v[14:15], v[180:181], v[14:15]
	v_pk_mul_f32 v[16:17], v[182:183], v[16:17]
	v_pk_mul_f32 v[10:11], v[10:11], v[184:185]
	v_pk_mul_f32 v[12:13], v[12:13], v[186:187]
	v_pk_mul_f32 v[14:15], v[14:15], v[176:177]
	v_pk_mul_f32 v[16:17], v[16:17], v[178:179]
	v_cvt_pk_fp8_f32 v18, v10, v11
	v_cvt_pk_fp8_f32 v19, v14, v15
	v_cvt_pk_fp8_f32 v18, v12, v13 op_sel:[0,0,1]
	v_cvt_pk_fp8_f32 v19, v16, v17 op_sel:[0,0,1]
	s_nop 0
	global_store_dwordx2 v[0:1], v[18:19], off
	v_or_b32_e32 v8, 16, v4
	v_ashrrev_i32_e32 v9, 31, v8
	v_lshlrev_b64 v[8:9], 10, v[8:9]
	v_lshl_add_u64 v[8:9], s[14:15], 0, v[8:9]
	v_lshl_add_u64 v[8:9], v[8:9], 0, v[2:3]
	v_pk_mul_f32 v[10:11], v[172:173], s[100:101] op_sel_hi:[1,0]
	v_pk_mul_f32 v[12:13], v[174:175], s[100:101] op_sel_hi:[1,0]
	v_pk_mul_f32 v[14:15], v[164:165], s[100:101] op_sel_hi:[1,0]
	v_pk_mul_f32 v[16:17], v[166:167], s[100:101] op_sel_hi:[1,0]
	v_exp_f32_e32 v10, v10
	v_exp_f32_e32 v11, v11
	v_exp_f32_e32 v12, v12
	v_exp_f32_e32 v13, v13
	v_exp_f32_e32 v14, v14
	v_exp_f32_e32 v15, v15
	v_exp_f32_e32 v16, v16
	v_exp_f32_e32 v17, v17
	v_pk_fma_f32 v[10:11], v[10:11], s[98:99], s[98:99] op_sel_hi:[1,0,0]
	v_pk_fma_f32 v[12:13], v[12:13], s[98:99], s[98:99] op_sel_hi:[1,0,0]
	v_pk_fma_f32 v[14:15], v[14:15], s[98:99], s[98:99] op_sel_hi:[1,0,0]
	v_pk_fma_f32 v[16:17], v[16:17], s[98:99], s[98:99] op_sel_hi:[1,0,0]
	v_rcp_f32_e32 v10, v10
	v_rcp_f32_e32 v11, v11
	v_rcp_f32_e32 v12, v12
	v_rcp_f32_e32 v13, v13
	v_rcp_f32_e32 v14, v14
	v_rcp_f32_e32 v15, v15
	v_rcp_f32_e32 v16, v16
	v_rcp_f32_e32 v17, v17
	v_pk_mul_f32 v[10:11], v[172:173], v[10:11]
	v_pk_mul_f32 v[12:13], v[174:175], v[12:13]
	v_pk_mul_f32 v[14:15], v[164:165], v[14:15]
	v_pk_mul_f32 v[16:17], v[166:167], v[16:17]
	v_pk_mul_f32 v[10:11], v[10:11], v[168:169]
	v_pk_mul_f32 v[12:13], v[12:13], v[170:171]
	v_pk_mul_f32 v[14:15], v[14:15], v[160:161]
	v_pk_mul_f32 v[16:17], v[16:17], v[162:163]
	v_cvt_pk_fp8_f32 v18, v10, v11
	v_cvt_pk_fp8_f32 v19, v14, v15
	v_cvt_pk_fp8_f32 v18, v12, v13 op_sel:[0,0,1]
	v_cvt_pk_fp8_f32 v19, v16, v17 op_sel:[0,0,1]
	s_nop 0
	global_store_dwordx2 v[8:9], v[18:19], off
	v_or_b32_e32 v8, 32, v4
	v_ashrrev_i32_e32 v9, 31, v8
	v_or_b32_e32 v4, 48, v4
	v_lshlrev_b64 v[6:7], 10, v[8:9]
	v_lshl_add_u64 v[6:7], s[14:15], 0, v[6:7]
	v_lshl_add_u64 v[6:7], v[6:7], 0, v[2:3]
	v_pk_mul_f32 v[10:11], v[156:157], s[100:101] op_sel_hi:[1,0]
	v_pk_mul_f32 v[12:13], v[158:159], s[100:101] op_sel_hi:[1,0]
	v_pk_mul_f32 v[14:15], v[148:149], s[100:101] op_sel_hi:[1,0]
	v_pk_mul_f32 v[16:17], v[150:151], s[100:101] op_sel_hi:[1,0]
	v_exp_f32_e32 v10, v10
	v_exp_f32_e32 v11, v11
	v_exp_f32_e32 v12, v12
	v_exp_f32_e32 v13, v13
	v_exp_f32_e32 v14, v14
	v_exp_f32_e32 v15, v15
	v_exp_f32_e32 v16, v16
	v_exp_f32_e32 v17, v17
	v_pk_fma_f32 v[10:11], v[10:11], s[98:99], s[98:99] op_sel_hi:[1,0,0]
	v_pk_fma_f32 v[12:13], v[12:13], s[98:99], s[98:99] op_sel_hi:[1,0,0]
	v_pk_fma_f32 v[14:15], v[14:15], s[98:99], s[98:99] op_sel_hi:[1,0,0]
	v_pk_fma_f32 v[16:17], v[16:17], s[98:99], s[98:99] op_sel_hi:[1,0,0]
	v_rcp_f32_e32 v10, v10
	v_rcp_f32_e32 v11, v11
	v_rcp_f32_e32 v12, v12
	v_rcp_f32_e32 v13, v13
	v_rcp_f32_e32 v14, v14
	v_rcp_f32_e32 v15, v15
	v_rcp_f32_e32 v16, v16
	v_rcp_f32_e32 v17, v17
	v_pk_mul_f32 v[10:11], v[156:157], v[10:11]
	v_pk_mul_f32 v[12:13], v[158:159], v[12:13]
	v_pk_mul_f32 v[14:15], v[148:149], v[14:15]
	v_pk_mul_f32 v[16:17], v[150:151], v[16:17]
	v_pk_mul_f32 v[10:11], v[10:11], v[152:153]
	v_pk_mul_f32 v[12:13], v[12:13], v[154:155]
	v_pk_mul_f32 v[14:15], v[14:15], v[144:145]
	v_pk_mul_f32 v[16:17], v[16:17], v[146:147]
	v_cvt_pk_fp8_f32 v18, v10, v11
	v_cvt_pk_fp8_f32 v19, v14, v15
	v_cvt_pk_fp8_f32 v18, v12, v13 op_sel:[0,0,1]
	v_cvt_pk_fp8_f32 v19, v16, v17 op_sel:[0,0,1]
	s_nop 0
	global_store_dwordx2 v[6:7], v[18:19], off
	v_ashrrev_i32_e32 v5, 31, v4
	v_lshlrev_b64 v[4:5], 10, v[4:5]
	v_lshl_add_u64 v[4:5], s[14:15], 0, v[4:5]
	v_lshl_add_u64 v[2:3], v[4:5], 0, v[2:3]
	s_mov_b32 s33, s52
	v_pk_mul_f32 v[10:11], v[140:141], s[100:101] op_sel_hi:[1,0]
	v_pk_mul_f32 v[12:13], v[142:143], s[100:101] op_sel_hi:[1,0]
	v_pk_mul_f32 v[14:15], v[132:133], s[100:101] op_sel_hi:[1,0]
	v_pk_mul_f32 v[16:17], v[134:135], s[100:101] op_sel_hi:[1,0]
	v_exp_f32_e32 v10, v10
	v_exp_f32_e32 v11, v11
	v_exp_f32_e32 v12, v12
	v_exp_f32_e32 v13, v13
	v_exp_f32_e32 v14, v14
	v_exp_f32_e32 v15, v15
	v_exp_f32_e32 v16, v16
	v_exp_f32_e32 v17, v17
	v_pk_fma_f32 v[10:11], v[10:11], s[98:99], s[98:99] op_sel_hi:[1,0,0]
	v_pk_fma_f32 v[12:13], v[12:13], s[98:99], s[98:99] op_sel_hi:[1,0,0]
	v_pk_fma_f32 v[14:15], v[14:15], s[98:99], s[98:99] op_sel_hi:[1,0,0]
	v_pk_fma_f32 v[16:17], v[16:17], s[98:99], s[98:99] op_sel_hi:[1,0,0]
	v_rcp_f32_e32 v10, v10
	v_rcp_f32_e32 v11, v11
	v_rcp_f32_e32 v12, v12
	v_rcp_f32_e32 v13, v13
	v_rcp_f32_e32 v14, v14
	v_rcp_f32_e32 v15, v15
	v_rcp_f32_e32 v16, v16
	v_rcp_f32_e32 v17, v17
	v_pk_mul_f32 v[10:11], v[140:141], v[10:11]
	v_pk_mul_f32 v[12:13], v[142:143], v[12:13]
	v_pk_mul_f32 v[14:15], v[132:133], v[14:15]
	v_pk_mul_f32 v[16:17], v[134:135], v[16:17]
	v_pk_mul_f32 v[10:11], v[10:11], v[136:137]
	v_pk_mul_f32 v[12:13], v[12:13], v[138:139]
	v_pk_mul_f32 v[14:15], v[14:15], v[128:129]
	v_pk_mul_f32 v[16:17], v[16:17], v[130:131]
	v_cvt_pk_fp8_f32 v18, v10, v11
	v_cvt_pk_fp8_f32 v19, v14, v15
	v_cvt_pk_fp8_f32 v18, v12, v13 op_sel:[0,0,1]
	v_cvt_pk_fp8_f32 v19, v16, v17 op_sel:[0,0,1]
	s_nop 0
	global_store_dwordx2 v[2:3], v[18:19], off
	s_mov_b32 s0, s18
	v_add_co_u32_e32 v6, vcc, s49, v0
	v_addc_co_u32_e32 v7, vcc, 0, v1, vcc
	v_pk_mul_f32 v[10:11], v[124:125], s[100:101] op_sel_hi:[1,0]
	v_pk_mul_f32 v[12:13], v[126:127], s[100:101] op_sel_hi:[1,0]
	v_pk_mul_f32 v[14:15], v[116:117], s[100:101] op_sel_hi:[1,0]
	v_pk_mul_f32 v[16:17], v[118:119], s[100:101] op_sel_hi:[1,0]
	v_exp_f32_e32 v10, v10
	v_exp_f32_e32 v11, v11
	v_exp_f32_e32 v12, v12
	v_exp_f32_e32 v13, v13
	v_exp_f32_e32 v14, v14
	v_exp_f32_e32 v15, v15
	v_exp_f32_e32 v16, v16
	v_exp_f32_e32 v17, v17
	v_pk_fma_f32 v[10:11], v[10:11], s[98:99], s[98:99] op_sel_hi:[1,0,0]
	v_pk_fma_f32 v[12:13], v[12:13], s[98:99], s[98:99] op_sel_hi:[1,0,0]
	v_pk_fma_f32 v[14:15], v[14:15], s[98:99], s[98:99] op_sel_hi:[1,0,0]
	v_pk_fma_f32 v[16:17], v[16:17], s[98:99], s[98:99] op_sel_hi:[1,0,0]
	v_rcp_f32_e32 v10, v10
	v_rcp_f32_e32 v11, v11
	v_rcp_f32_e32 v12, v12
	v_rcp_f32_e32 v13, v13
	v_rcp_f32_e32 v14, v14
	v_rcp_f32_e32 v15, v15
	v_rcp_f32_e32 v16, v16
	v_rcp_f32_e32 v17, v17
	v_pk_mul_f32 v[10:11], v[124:125], v[10:11]
	v_pk_mul_f32 v[12:13], v[126:127], v[12:13]
	v_pk_mul_f32 v[14:15], v[116:117], v[14:15]
	v_pk_mul_f32 v[16:17], v[118:119], v[16:17]
	v_pk_mul_f32 v[10:11], v[10:11], v[120:121]
	v_pk_mul_f32 v[12:13], v[12:13], v[122:123]
	v_pk_mul_f32 v[14:15], v[14:15], v[112:113]
	v_pk_mul_f32 v[16:17], v[16:17], v[114:115]
	v_cvt_pk_fp8_f32 v18, v10, v11
	v_cvt_pk_fp8_f32 v19, v14, v15
	v_cvt_pk_fp8_f32 v18, v12, v13 op_sel:[0,0,1]
	v_cvt_pk_fp8_f32 v19, v16, v17 op_sel:[0,0,1]
	s_nop 0
	global_store_dwordx2 v[6:7], v[18:19], off
	v_add_co_u32_e32 v6, vcc, s50, v0
	v_addc_co_u32_e32 v7, vcc, 0, v1, vcc
	v_pk_mul_f32 v[10:11], v[108:109], s[100:101] op_sel_hi:[1,0]
	v_pk_mul_f32 v[12:13], v[110:111], s[100:101] op_sel_hi:[1,0]
	v_pk_mul_f32 v[14:15], v[100:101], s[100:101] op_sel_hi:[1,0]
	v_pk_mul_f32 v[16:17], v[102:103], s[100:101] op_sel_hi:[1,0]
	v_exp_f32_e32 v10, v10
	v_exp_f32_e32 v11, v11
	v_exp_f32_e32 v12, v12
	v_exp_f32_e32 v13, v13
	v_exp_f32_e32 v14, v14
	v_exp_f32_e32 v15, v15
	v_exp_f32_e32 v16, v16
	v_exp_f32_e32 v17, v17
	v_pk_fma_f32 v[10:11], v[10:11], s[98:99], s[98:99] op_sel_hi:[1,0,0]
	v_pk_fma_f32 v[12:13], v[12:13], s[98:99], s[98:99] op_sel_hi:[1,0,0]
	v_pk_fma_f32 v[14:15], v[14:15], s[98:99], s[98:99] op_sel_hi:[1,0,0]
	v_pk_fma_f32 v[16:17], v[16:17], s[98:99], s[98:99] op_sel_hi:[1,0,0]
	v_rcp_f32_e32 v10, v10
	v_rcp_f32_e32 v11, v11
	v_rcp_f32_e32 v12, v12
	v_rcp_f32_e32 v13, v13
	v_rcp_f32_e32 v14, v14
	v_rcp_f32_e32 v15, v15
	v_rcp_f32_e32 v16, v16
	v_rcp_f32_e32 v17, v17
	v_pk_mul_f32 v[10:11], v[108:109], v[10:11]
	v_pk_mul_f32 v[12:13], v[110:111], v[12:13]
	v_pk_mul_f32 v[14:15], v[100:101], v[14:15]
	v_pk_mul_f32 v[16:17], v[102:103], v[16:17]
	v_pk_mul_f32 v[10:11], v[10:11], v[104:105]
	v_pk_mul_f32 v[12:13], v[12:13], v[106:107]
	v_pk_mul_f32 v[14:15], v[14:15], v[96:97]
	v_pk_mul_f32 v[16:17], v[16:17], v[98:99]
	v_cvt_pk_fp8_f32 v18, v10, v11
	v_cvt_pk_fp8_f32 v19, v14, v15
	v_cvt_pk_fp8_f32 v18, v12, v13 op_sel:[0,0,1]
	v_cvt_pk_fp8_f32 v19, v16, v17 op_sel:[0,0,1]
	s_nop 0
	global_store_dwordx2 v[6:7], v[18:19], off
	v_add_co_u32_e32 v6, vcc, s51, v0
	v_addc_co_u32_e32 v7, vcc, 0, v1, vcc
	v_pk_mul_f32 v[10:11], v[92:93], s[100:101] op_sel_hi:[1,0]
	v_pk_mul_f32 v[12:13], v[94:95], s[100:101] op_sel_hi:[1,0]
	v_pk_mul_f32 v[14:15], v[84:85], s[100:101] op_sel_hi:[1,0]
	v_pk_mul_f32 v[16:17], v[86:87], s[100:101] op_sel_hi:[1,0]
	v_exp_f32_e32 v10, v10
	v_exp_f32_e32 v11, v11
	v_exp_f32_e32 v12, v12
	v_exp_f32_e32 v13, v13
	v_exp_f32_e32 v14, v14
	v_exp_f32_e32 v15, v15
	v_exp_f32_e32 v16, v16
	v_exp_f32_e32 v17, v17
	v_pk_fma_f32 v[10:11], v[10:11], s[98:99], s[98:99] op_sel_hi:[1,0,0]
	v_pk_fma_f32 v[12:13], v[12:13], s[98:99], s[98:99] op_sel_hi:[1,0,0]
	v_pk_fma_f32 v[14:15], v[14:15], s[98:99], s[98:99] op_sel_hi:[1,0,0]
	v_pk_fma_f32 v[16:17], v[16:17], s[98:99], s[98:99] op_sel_hi:[1,0,0]
	v_rcp_f32_e32 v10, v10
	v_rcp_f32_e32 v11, v11
	v_rcp_f32_e32 v12, v12
	v_rcp_f32_e32 v13, v13
	v_rcp_f32_e32 v14, v14
	v_rcp_f32_e32 v15, v15
	v_rcp_f32_e32 v16, v16
	v_rcp_f32_e32 v17, v17
	v_pk_mul_f32 v[10:11], v[92:93], v[10:11]
	v_pk_mul_f32 v[12:13], v[94:95], v[12:13]
	v_pk_mul_f32 v[14:15], v[84:85], v[14:15]
	v_pk_mul_f32 v[16:17], v[86:87], v[16:17]
	v_pk_mul_f32 v[10:11], v[10:11], v[88:89]
	v_pk_mul_f32 v[12:13], v[12:13], v[90:91]
	v_pk_mul_f32 v[14:15], v[14:15], v[80:81]
	v_pk_mul_f32 v[16:17], v[16:17], v[82:83]
	v_cvt_pk_fp8_f32 v18, v10, v11
	v_cvt_pk_fp8_f32 v19, v14, v15
	v_cvt_pk_fp8_f32 v18, v12, v13 op_sel:[0,0,1]
	v_cvt_pk_fp8_f32 v19, v16, v17 op_sel:[0,0,1]
	s_nop 0
	global_store_dwordx2 v[6:7], v[18:19], off
	v_add_co_u32_e32 v0, vcc, 0x2c000, v0
	s_mov_b64 s[2:3], s[20:21]
	s_nop 0
	v_addc_co_u32_e32 v1, vcc, 0, v1, vcc
	s_and_b64 vcc, exec, s[6:7]
	v_pk_mul_f32 v[10:11], v[76:77], s[100:101] op_sel_hi:[1,0]
	v_pk_mul_f32 v[12:13], v[78:79], s[100:101] op_sel_hi:[1,0]
	v_pk_mul_f32 v[14:15], v[68:69], s[100:101] op_sel_hi:[1,0]
	v_pk_mul_f32 v[16:17], v[70:71], s[100:101] op_sel_hi:[1,0]
	v_exp_f32_e32 v10, v10
	v_exp_f32_e32 v11, v11
	v_exp_f32_e32 v12, v12
	v_exp_f32_e32 v13, v13
	v_exp_f32_e32 v14, v14
	v_exp_f32_e32 v15, v15
	v_exp_f32_e32 v16, v16
	v_exp_f32_e32 v17, v17
	v_pk_fma_f32 v[10:11], v[10:11], s[98:99], s[98:99] op_sel_hi:[1,0,0]
	v_pk_fma_f32 v[12:13], v[12:13], s[98:99], s[98:99] op_sel_hi:[1,0,0]
	v_pk_fma_f32 v[14:15], v[14:15], s[98:99], s[98:99] op_sel_hi:[1,0,0]
	v_pk_fma_f32 v[16:17], v[16:17], s[98:99], s[98:99] op_sel_hi:[1,0,0]
	v_rcp_f32_e32 v10, v10
	v_rcp_f32_e32 v11, v11
	v_rcp_f32_e32 v12, v12
	v_rcp_f32_e32 v13, v13
	v_rcp_f32_e32 v14, v14
	v_rcp_f32_e32 v15, v15
	v_rcp_f32_e32 v16, v16
	v_rcp_f32_e32 v17, v17
	v_pk_mul_f32 v[10:11], v[76:77], v[10:11]
	v_pk_mul_f32 v[12:13], v[78:79], v[12:13]
	v_pk_mul_f32 v[14:15], v[68:69], v[14:15]
	v_pk_mul_f32 v[16:17], v[70:71], v[16:17]
	v_pk_mul_f32 v[10:11], v[10:11], v[72:73]
	v_pk_mul_f32 v[12:13], v[12:13], v[74:75]
	v_pk_mul_f32 v[14:15], v[14:15], v[64:65]
	v_pk_mul_f32 v[16:17], v[16:17], v[66:67]
	v_cvt_pk_fp8_f32 v18, v10, v11
	v_cvt_pk_fp8_f32 v19, v14, v15
	v_cvt_pk_fp8_f32 v18, v12, v13 op_sel:[0,0,1]
	v_cvt_pk_fp8_f32 v19, v16, v17 op_sel:[0,0,1]
	s_nop 0
	global_store_dwordx2 v[0:1], v[18:19], off
	s_cbranch_vccnz .LBB0_1001

.LBB0_998:
	s_add_i32 s22, s4, 0xf2401100
	s_and_b32 s55, s22, 0x300
	s_add_u32 s24, s2, s55
	s_addc_u32 s25, s3, 0
	s_and_b64 s[22:23], s[26:27], exec
	s_cselect_b32 s23, s19, s25
	s_cselect_b32 s22, s53, s24
	s_mov_b64 s[24:25], s[22:23]
	s_mov_b32 m0, s34
	ds_read_b128 v[16:19], v217
	ds_read_b128 v[20:23], v218
	ds_read_b128 v[24:27], v225
	ds_read_b128 v[28:31], v226
	v_mov_b32_e32 v203, v197
	global_load_lds_dwordx4 v194, s[24:25]
	v_lshl_add_u64 v[236:237], s[24:25], 0, v[192:193]
	s_mov_b32 m0, s35
	s_add_u32 s24, s22, 0x80
	global_load_lds_dwordx4 v[236:237], off
	s_barrier
	s_waitcnt lgkmcnt(0)
	s_addc_u32 s25, s23, 0
	s_and_b64 s[26:27], s[26:27], exec
	s_cselect_b32 s27, 0, 0
	s_cselect_b32 s26, 0, s55
	s_setprio 1
	s_waitcnt lgkmcnt(0)
	v_mfma_scale_f32_16x16x128_f8f6f4 v[184:187], v[16:23], v[56:63], v[184:187], v212, v212 op_sel_hi:[0,0,0]
	v_mfma_scale_f32_16x16x128_f8f6f4 v[176:179], v[24:31], v[56:63], v[176:179], v212, v212 op_sel_hi:[0,0,0]
	v_mfma_scale_f32_16x16x128_f8f6f4 v[168:171], v[16:23], v[48:55], v[168:171], v212, v212 op_sel_hi:[0,0,0]
	v_mfma_scale_f32_16x16x128_f8f6f4 v[160:163], v[24:31], v[48:55], v[160:163], v212, v212 op_sel_hi:[0,0,0]
	v_mfma_scale_f32_16x16x128_f8f6f4 v[152:155], v[16:23], v[40:47], v[152:155], v212, v212 op_sel_hi:[0,0,0]
	v_mfma_scale_f32_16x16x128_f8f6f4 v[144:147], v[24:31], v[40:47], v[144:147], v212, v212 op_sel_hi:[0,0,0]
	v_mfma_scale_f32_16x16x128_f8f6f4 v[136:139], v[16:23], v[32:39], v[136:139], v212, v212 op_sel_hi:[0,0,0]
	v_mfma_scale_f32_16x16x128_f8f6f4 v[128:131], v[24:31], v[32:39], v[128:131], v212, v212 op_sel_hi:[0,0,0]
	s_setprio 0
	s_add_u32 s26, s12, s26
	s_addc_u32 s27, s13, s27
	s_mov_b64 s[56:57], s[26:27]
	s_mov_b32 m0, s1
	s_barrier
	ds_read_b128 v[32:35], v231 offset:16384
	ds_read_b128 v[40:43], v231 offset:18432
	ds_read_b128 v[36:39], v232 offset:16384
	ds_read_b128 v[44:47], v232 offset:18432
	ds_read_b128 v[48:51], v231 offset:20480
	ds_read_b128 v[56:59], v231 offset:22528
	ds_read_b128 v[52:55], v232 offset:20480
	ds_read_b128 v[60:63], v232 offset:22528
	s_nop 0
	global_load_lds_dwordx4 v198, s[56:57]
	s_mov_b32 m0, s36
	s_nop 0
	global_load_lds_dwordx4 v200, s[56:57]
	s_nop 0
	s_barrier
	s_waitcnt lgkmcnt(0)
	s_setprio 1
	s_waitcnt lgkmcnt(0)
	v_mfma_scale_f32_16x16x128_f8f6f4 v[124:127], v[0:7], v[32:39], v[124:127], v212, v212 op_sel_hi:[0,0,0]
	v_mfma_scale_f32_16x16x128_f8f6f4 v[116:119], v[8:15], v[32:39], v[116:119], v212, v212 op_sel_hi:[0,0,0]
	v_mfma_scale_f32_16x16x128_f8f6f4 v[108:111], v[0:7], v[40:47], v[108:111], v212, v212 op_sel_hi:[0,0,0]
	v_mfma_scale_f32_16x16x128_f8f6f4 v[100:103], v[8:15], v[40:47], v[100:103], v212, v212 op_sel_hi:[0,0,0]
	v_mfma_scale_f32_16x16x128_f8f6f4 v[92:95], v[0:7], v[48:55], v[92:95], v212, v212 op_sel_hi:[0,0,0]
	v_mfma_scale_f32_16x16x128_f8f6f4 v[84:87], v[8:15], v[48:55], v[84:87], v212, v212 op_sel_hi:[0,0,0]
	v_mfma_scale_f32_16x16x128_f8f6f4 v[76:79], v[0:7], v[56:63], v[76:79], v212, v212 op_sel_hi:[0,0,0]
	v_mfma_scale_f32_16x16x128_f8f6f4 v[68:71], v[8:15], v[56:63], v[68:71], v212, v212 op_sel_hi:[0,0,0]
	s_setprio 0
	s_barrier
	s_add_u32 s56, s22, 0x20000
	s_addc_u32 s57, s23, 0
	s_mov_b32 m0, s37
	s_nop 0
	global_load_lds_dwordx4 v194, s[56:57]
	s_mov_b32 m0, s38
	s_nop 0
	global_load_lds_dwordx4 v192, s[56:57]
	s_waitcnt vmcnt(6)
	s_barrier
	s_setprio 1
	v_mfma_scale_f32_16x16x128_f8f6f4 v[120:123], v[16:23], v[32:39], v[120:123], v212, v212 op_sel_hi:[0,0,0]
	v_mfma_scale_f32_16x16x128_f8f6f4 v[112:115], v[24:31], v[32:39], v[112:115], v212, v212 op_sel_hi:[0,0,0]
	v_mfma_scale_f32_16x16x128_f8f6f4 v[104:107], v[16:23], v[40:47], v[104:107], v212, v212 op_sel_hi:[0,0,0]
	v_mfma_scale_f32_16x16x128_f8f6f4 v[96:99], v[24:31], v[40:47], v[96:99], v212, v212 op_sel_hi:[0,0,0]
	v_mfma_scale_f32_16x16x128_f8f6f4 v[88:91], v[16:23], v[48:55], v[88:91], v212, v212 op_sel_hi:[0,0,0]
	v_mfma_scale_f32_16x16x128_f8f6f4 v[80:83], v[24:31], v[48:55], v[80:83], v212, v212 op_sel_hi:[0,0,0]
	v_mfma_scale_f32_16x16x128_f8f6f4 v[72:75], v[16:23], v[56:63], v[72:75], v212, v212 op_sel_hi:[0,0,0]
	v_mfma_scale_f32_16x16x128_f8f6f4 v[64:67], v[24:31], v[56:63], v[64:67], v212, v212 op_sel_hi:[0,0,0]
	s_setprio 0
	s_barrier
	ds_read_b128 v[0:3], v219
	ds_read_b128 v[4:7], v220
	ds_read_b128 v[8:11], v227
	ds_read_b128 v[12:15], v228
	s_mov_b64 s[56:57], s[26:27]
	s_mov_b32 m0, s39
	ds_read_b128 v[16:19], v231 offset:32768
	ds_read_b128 v[24:27], v231 offset:34816
	ds_read_b128 v[20:23], v232 offset:32768
	ds_read_b128 v[28:31], v232 offset:34816
	ds_read_b128 v[32:35], v231 offset:36864
	ds_read_b128 v[40:43], v231 offset:38912
	ds_read_b128 v[36:39], v232 offset:36864
	ds_read_b128 v[44:47], v232 offset:38912
	s_nop 0
	global_load_lds_dwordx4 v196, s[56:57]
	s_mov_b32 m0, s40
	s_nop 0
	global_load_lds_dwordx4 v202, s[56:57]
	s_waitcnt lgkmcnt(8)
	s_barrier
	s_waitcnt lgkmcnt(0)
	s_setprio 1
	s_waitcnt lgkmcnt(0)
	v_mfma_scale_f32_16x16x128_f8f6f4 v[188:191], v[0:7], v[16:23], v[188:191], v212, v212 op_sel_hi:[0,0,0]
	v_mfma_scale_f32_16x16x128_f8f6f4 v[180:183], v[8:15], v[16:23], v[180:183], v212, v212 op_sel_hi:[0,0,0]
	v_mfma_scale_f32_16x16x128_f8f6f4 v[172:175], v[0:7], v[24:31], v[172:175], v212, v212 op_sel_hi:[0,0,0]
	v_mfma_scale_f32_16x16x128_f8f6f4 v[164:167], v[8:15], v[24:31], v[164:167], v212, v212 op_sel_hi:[0,0,0]
	v_mfma_scale_f32_16x16x128_f8f6f4 v[156:159], v[0:7], v[32:39], v[156:159], v212, v212 op_sel_hi:[0,0,0]
	v_mfma_scale_f32_16x16x128_f8f6f4 v[148:151], v[8:15], v[32:39], v[148:151], v212, v212 op_sel_hi:[0,0,0]
	v_mfma_scale_f32_16x16x128_f8f6f4 v[140:143], v[0:7], v[40:47], v[140:143], v212, v212 op_sel_hi:[0,0,0]
	v_mfma_scale_f32_16x16x128_f8f6f4 v[132:135], v[8:15], v[40:47], v[132:135], v212, v212 op_sel_hi:[0,0,0]
	s_setprio 0
	s_barrier
	s_mov_b32 m0, s42
	ds_read_b128 v[48:51], v221
	ds_read_b128 v[52:55], v222
	ds_read_b128 v[56:59], v229
	ds_read_b128 v[60:63], v230
	s_nop 0
	global_load_lds_dwordx4 v194, s[24:25]
	s_mov_b32 m0, s43
	s_nop 0
	global_load_lds_dwordx4 v192, s[24:25]
	s_barrier
	s_waitcnt lgkmcnt(0)
	s_setprio 1
	s_waitcnt lgkmcnt(0)
	v_mfma_scale_f32_16x16x128_f8f6f4 v[184:187], v[48:55], v[16:23], v[184:187], v212, v212 op_sel_hi:[0,0,0]
	v_mfma_scale_f32_16x16x128_f8f6f4 v[176:179], v[56:63], v[16:23], v[176:179], v212, v212 op_sel_hi:[0,0,0]
	v_mfma_scale_f32_16x16x128_f8f6f4 v[168:171], v[48:55], v[24:31], v[168:171], v212, v212 op_sel_hi:[0,0,0]
	v_mfma_scale_f32_16x16x128_f8f6f4 v[160:163], v[56:63], v[24:31], v[160:163], v212, v212 op_sel_hi:[0,0,0]
	v_mfma_scale_f32_16x16x128_f8f6f4 v[152:155], v[48:55], v[32:39], v[152:155], v212, v212 op_sel_hi:[0,0,0]
	v_mfma_scale_f32_16x16x128_f8f6f4 v[144:147], v[56:63], v[32:39], v[144:147], v212, v212 op_sel_hi:[0,0,0]
	v_mfma_scale_f32_16x16x128_f8f6f4 v[136:139], v[48:55], v[40:47], v[136:139], v212, v212 op_sel_hi:[0,0,0]
	v_mfma_scale_f32_16x16x128_f8f6f4 v[128:131], v[56:63], v[40:47], v[128:131], v212, v212 op_sel_hi:[0,0,0]
	s_setprio 0
	s_add_u32 s24, s26, 0x80
	s_addc_u32 s25, s27, 0
	s_mov_b32 m0, s44
	s_barrier
	ds_read_b128 v[16:19], v231 offset:49152
	ds_read_b128 v[24:27], v231 offset:51200
	ds_read_b128 v[20:23], v232 offset:49152
	ds_read_b128 v[28:31], v232 offset:51200
	ds_read_b128 v[32:35], v231 offset:53248
	ds_read_b128 v[40:43], v231 offset:55296
	ds_read_b128 v[36:39], v232 offset:53248
	ds_read_b128 v[44:47], v232 offset:55296
	s_nop 0
	global_load_lds_dwordx4 v198, s[24:25]
	s_mov_b32 m0, s45
	s_nop 0
	global_load_lds_dwordx4 v200, s[24:25]
	s_nop 0
	s_barrier
	s_waitcnt lgkmcnt(0)
	s_setprio 1
	s_waitcnt lgkmcnt(0)
	v_mfma_scale_f32_16x16x128_f8f6f4 v[124:127], v[0:7], v[16:23], v[124:127], v212, v212 op_sel_hi:[0,0,0]
	v_mfma_scale_f32_16x16x128_f8f6f4 v[116:119], v[8:15], v[16:23], v[116:119], v212, v212 op_sel_hi:[0,0,0]
	v_mfma_scale_f32_16x16x128_f8f6f4 v[108:111], v[0:7], v[24:31], v[108:111], v212, v212 op_sel_hi:[0,0,0]
	v_mfma_scale_f32_16x16x128_f8f6f4 v[100:103], v[8:15], v[24:31], v[100:103], v212, v212 op_sel_hi:[0,0,0]
	v_mfma_scale_f32_16x16x128_f8f6f4 v[92:95], v[0:7], v[32:39], v[92:95], v212, v212 op_sel_hi:[0,0,0]
	v_mfma_scale_f32_16x16x128_f8f6f4 v[84:87], v[8:15], v[32:39], v[84:87], v212, v212 op_sel_hi:[0,0,0]
	v_mfma_scale_f32_16x16x128_f8f6f4 v[76:79], v[0:7], v[40:47], v[76:79], v212, v212 op_sel_hi:[0,0,0]
	v_mfma_scale_f32_16x16x128_f8f6f4 v[68:71], v[8:15], v[40:47], v[68:71], v212, v212 op_sel_hi:[0,0,0]
	s_setprio 0
	s_barrier
	s_add_u32 s22, s22, 0x20080
	s_addc_u32 s23, s23, 0
	s_mov_b32 m0, s46
	s_nop 0
	global_load_lds_dwordx4 v194, s[22:23]
	s_mov_b32 m0, s47
	s_nop 0
	global_load_lds_dwordx4 v192, s[22:23]
	s_waitcnt vmcnt(6)
	s_barrier
	s_setprio 1
	v_mfma_scale_f32_16x16x128_f8f6f4 v[120:123], v[48:55], v[16:23], v[120:123], v212, v212 op_sel_hi:[0,0,0]
	v_mfma_scale_f32_16x16x128_f8f6f4 v[112:115], v[56:63], v[16:23], v[112:115], v212, v212 op_sel_hi:[0,0,0]
	v_mfma_scale_f32_16x16x128_f8f6f4 v[104:107], v[48:55], v[24:31], v[104:107], v212, v212 op_sel_hi:[0,0,0]
	v_mfma_scale_f32_16x16x128_f8f6f4 v[96:99], v[56:63], v[24:31], v[96:99], v212, v212 op_sel_hi:[0,0,0]
	v_mfma_scale_f32_16x16x128_f8f6f4 v[88:91], v[48:55], v[32:39], v[88:91], v212, v212 op_sel_hi:[0,0,0]
	v_mfma_scale_f32_16x16x128_f8f6f4 v[80:83], v[56:63], v[32:39], v[80:83], v212, v212 op_sel_hi:[0,0,0]
	v_mfma_scale_f32_16x16x128_f8f6f4 v[72:75], v[48:55], v[40:47], v[72:75], v212, v212 op_sel_hi:[0,0,0]
	v_mfma_scale_f32_16x16x128_f8f6f4 v[64:67], v[56:63], v[40:47], v[64:67], v212, v212 op_sel_hi:[0,0,0]
	s_setprio 0
	s_add_i32 s54, s54, 2
	s_add_u32 s4, s4, 0x100
	s_addc_u32 s5, s5, 0
	s_cmp_gt_u32 s54, 5
	s_barrier
	s_cbranch_scc1 .LBB0_994

.LBB0_1063:
	s_add_u32 s26, s30, 0x100
	ds_read_b128 v[0:3], v174
	ds_read_b128 v[4:7], v175
	ds_read_b128 v[8:11], v182
	ds_read_b128 v[12:15], v183
	s_addc_u32 s27, s31, 0
	s_and_b32 s60, s26, 0x300
	s_add_u32 s59, s4, s60
	s_addc_u32 s61, s5, 0
	s_cmp_eq_u32 s33, 4
	s_cselect_b64 s[34:35], -1, 0
	s_and_b64 s[28:29], s[34:35], exec
	s_cselect_b32 s29, s17, s61
	s_cselect_b32 s28, s19, s59
	s_cselect_b32 s59, 0, 0
	s_cselect_b32 s60, 0, s60
	s_add_u32 s30, s24, s30
	s_addc_u32 s31, s25, s31
	s_add_u32 s30, s30, 0x20080
	s_addc_u32 s31, s31, 0
	ds_read_b128 v[194:197], v190
	ds_read_b128 v[210:213], v190 offset:2048
	ds_read_b128 v[198:201], v191
	ds_read_b128 v[214:217], v191 offset:2048
	ds_read_b128 v[218:221], v190 offset:4096
	ds_read_b128 v[226:229], v190 offset:6144
	ds_read_b128 v[222:225], v191 offset:4096
	ds_read_b128 v[230:233], v191 offset:6144
	s_add_i32 m0, s1, 0xc000
	s_nop 0
	global_load_lds_dwordx4 v166, s[30:31]
	s_add_i32 m0, s1, 0xe000
	s_nop 0
	global_load_lds_dwordx4 v162, s[30:31]
	s_waitcnt lgkmcnt(8)
	s_barrier
	s_waitcnt lgkmcnt(0)
	s_setprio 1
	s_waitcnt lgkmcnt(0)
	v_mfma_scale_f32_16x16x128_f8f6f4 v[156:159], v[0:7], v[194:201], v[156:159], v173, v173 op_sel_hi:[0,0,0]
	v_mfma_scale_f32_16x16x128_f8f6f4 v[152:155], v[8:15], v[194:201], v[152:155], v173, v173 op_sel_hi:[0,0,0]
	v_mfma_scale_f32_16x16x128_f8f6f4 v[140:143], v[0:7], v[210:217], v[140:143], v173, v173 op_sel_hi:[0,0,0]
	v_mfma_scale_f32_16x16x128_f8f6f4 v[136:139], v[8:15], v[210:217], v[136:139], v173, v173 op_sel_hi:[0,0,0]
	v_mfma_scale_f32_16x16x128_f8f6f4 v[124:127], v[0:7], v[218:225], v[124:127], v173, v173 op_sel_hi:[0,0,0]
	v_mfma_scale_f32_16x16x128_f8f6f4 v[120:123], v[8:15], v[218:225], v[120:123], v173, v173 op_sel_hi:[0,0,0]
	v_mfma_scale_f32_16x16x128_f8f6f4 v[108:111], v[0:7], v[226:233], v[108:111], v173, v173 op_sel_hi:[0,0,0]
	v_mfma_scale_f32_16x16x128_f8f6f4 v[104:107], v[8:15], v[226:233], v[104:107], v173, v173 op_sel_hi:[0,0,0]
	s_setprio 0
	s_barrier
	s_mov_b64 s[30:31], s[28:29]
	s_mov_b32 m0, s3
	ds_read_b128 v[16:19], v176
	ds_read_b128 v[20:23], v177
	ds_read_b128 v[24:27], v184
	ds_read_b128 v[28:31], v185
	s_nop 0
	global_load_lds_dwordx4 v164, s[30:31]
	s_mov_b32 m0, s43
	s_nop 0
	global_load_lds_dwordx4 v160, s[30:31]
	s_nop 0
	s_barrier
	s_waitcnt lgkmcnt(0)
	s_setprio 1
	s_waitcnt lgkmcnt(0)
	v_mfma_scale_f32_16x16x128_f8f6f4 v[148:151], v[16:23], v[194:201], v[148:151], v173, v173 op_sel_hi:[0,0,0]
	v_mfma_scale_f32_16x16x128_f8f6f4 v[144:147], v[24:31], v[194:201], v[144:147], v173, v173 op_sel_hi:[0,0,0]
	v_mfma_scale_f32_16x16x128_f8f6f4 v[132:135], v[16:23], v[210:217], v[132:135], v173, v173 op_sel_hi:[0,0,0]
	v_mfma_scale_f32_16x16x128_f8f6f4 v[128:131], v[24:31], v[210:217], v[128:131], v173, v173 op_sel_hi:[0,0,0]
	v_mfma_scale_f32_16x16x128_f8f6f4 v[116:119], v[16:23], v[218:225], v[116:119], v173, v173 op_sel_hi:[0,0,0]
	v_mfma_scale_f32_16x16x128_f8f6f4 v[112:115], v[24:31], v[218:225], v[112:115], v173, v173 op_sel_hi:[0,0,0]
	v_mfma_scale_f32_16x16x128_f8f6f4 v[100:103], v[16:23], v[226:233], v[100:103], v173, v173 op_sel_hi:[0,0,0]
	v_mfma_scale_f32_16x16x128_f8f6f4 v[96:99], v[24:31], v[226:233], v[96:99], v173, v173 op_sel_hi:[0,0,0]
	s_setprio 0
	s_and_b64 s[30:31], s[8:9], s[34:35]
	s_and_b64 s[30:31], s[30:31], exec
	s_cselect_b32 s30, s20, s24
	s_cselect_b32 s31, s21, s25
	s_add_u32 s30, s30, s60
	s_addc_u32 s31, s31, s59
	s_mov_b64 s[34:35], s[30:31]
	s_mov_b32 m0, s1
	s_barrier
	ds_read_b128 v[194:197], v190 offset:16384
	ds_read_b128 v[210:213], v190 offset:18432
	ds_read_b128 v[198:201], v191 offset:16384
	ds_read_b128 v[214:217], v191 offset:18432
	ds_read_b128 v[218:221], v190 offset:20480
	ds_read_b128 v[226:229], v190 offset:22528
	ds_read_b128 v[222:225], v191 offset:20480
	ds_read_b128 v[230:233], v191 offset:22528
	s_nop 0
	global_load_lds_dwordx4 v166, s[34:35]
	s_mov_b32 m0, s44
	s_nop 0
	global_load_lds_dwordx4 v162, s[34:35]
	s_nop 0
	s_barrier
	s_waitcnt lgkmcnt(0)
	s_setprio 1
	s_waitcnt lgkmcnt(0)
	v_mfma_scale_f32_16x16x128_f8f6f4 v[92:95], v[0:7], v[194:201], v[92:95], v173, v173 op_sel_hi:[0,0,0]
	v_mfma_scale_f32_16x16x128_f8f6f4 v[88:91], v[8:15], v[194:201], v[88:91], v173, v173 op_sel_hi:[0,0,0]
	v_mfma_scale_f32_16x16x128_f8f6f4 v[76:79], v[0:7], v[210:217], v[76:79], v173, v173 op_sel_hi:[0,0,0]
	v_mfma_scale_f32_16x16x128_f8f6f4 v[72:75], v[8:15], v[210:217], v[72:75], v173, v173 op_sel_hi:[0,0,0]
	v_mfma_scale_f32_16x16x128_f8f6f4 v[60:63], v[0:7], v[218:225], v[60:63], v173, v173 op_sel_hi:[0,0,0]
	v_mfma_scale_f32_16x16x128_f8f6f4 v[56:59], v[8:15], v[218:225], v[56:59], v173, v173 op_sel_hi:[0,0,0]
	v_mfma_scale_f32_16x16x128_f8f6f4 v[44:47], v[0:7], v[226:233], v[44:47], v173, v173 op_sel_hi:[0,0,0]
	v_mfma_scale_f32_16x16x128_f8f6f4 v[40:43], v[8:15], v[226:233], v[40:43], v173, v173 op_sel_hi:[0,0,0]
	s_setprio 0
	s_barrier
	s_add_u32 s34, s28, 0x20000
	s_addc_u32 s35, s29, 0
	s_mov_b32 m0, s45
	s_nop 0
	global_load_lds_dwordx4 v164, s[34:35]
	s_mov_b32 m0, s46
	s_nop 0
	global_load_lds_dwordx4 v160, s[34:35]
	s_waitcnt vmcnt(6)
	s_barrier
	s_setprio 1
	v_mfma_scale_f32_16x16x128_f8f6f4 v[84:87], v[16:23], v[194:201], v[84:87], v173, v173 op_sel_hi:[0,0,0]
	v_mfma_scale_f32_16x16x128_f8f6f4 v[80:83], v[24:31], v[194:201], v[80:83], v173, v173 op_sel_hi:[0,0,0]
	v_mfma_scale_f32_16x16x128_f8f6f4 v[68:71], v[16:23], v[210:217], v[68:71], v173, v173 op_sel_hi:[0,0,0]
	v_mfma_scale_f32_16x16x128_f8f6f4 v[64:67], v[24:31], v[210:217], v[64:67], v173, v173 op_sel_hi:[0,0,0]
	v_mfma_scale_f32_16x16x128_f8f6f4 v[52:55], v[16:23], v[218:225], v[52:55], v173, v173 op_sel_hi:[0,0,0]
	v_mfma_scale_f32_16x16x128_f8f6f4 v[48:51], v[24:31], v[218:225], v[48:51], v173, v173 op_sel_hi:[0,0,0]
	v_mfma_scale_f32_16x16x128_f8f6f4 v[36:39], v[16:23], v[226:233], v[36:39], v173, v173 op_sel_hi:[0,0,0]
	v_mfma_scale_f32_16x16x128_f8f6f4 v[32:35], v[24:31], v[226:233], v[32:35], v173, v173 op_sel_hi:[0,0,0]
	s_setprio 0
	s_barrier
	ds_read_b128 v[0:3], v178
	ds_read_b128 v[4:7], v179
	ds_read_b128 v[8:11], v186
	ds_read_b128 v[12:15], v187
	s_add_u32 s34, s30, 0x20000
	s_addc_u32 s35, s31, 0
	s_mov_b32 m0, s47
	ds_read_b128 v[16:19], v190 offset:32768
	ds_read_b128 v[24:27], v190 offset:34816
	ds_read_b128 v[20:23], v191 offset:32768
	ds_read_b128 v[28:31], v191 offset:34816
	ds_read_b128 v[194:197], v190 offset:36864
	ds_read_b128 v[210:213], v190 offset:38912
	ds_read_b128 v[198:201], v191 offset:36864
	ds_read_b128 v[214:217], v191 offset:38912
	s_nop 0
	global_load_lds_dwordx4 v166, s[34:35]
	s_mov_b32 m0, s48
	s_nop 0
	global_load_lds_dwordx4 v162, s[34:35]
	s_waitcnt lgkmcnt(8)
	s_barrier
	s_waitcnt lgkmcnt(0)
	s_setprio 1
	s_waitcnt lgkmcnt(0)
	v_mfma_scale_f32_16x16x128_f8f6f4 v[156:159], v[0:7], v[16:23], v[156:159], v173, v173 op_sel_hi:[0,0,0]
	v_mfma_scale_f32_16x16x128_f8f6f4 v[152:155], v[8:15], v[16:23], v[152:155], v173, v173 op_sel_hi:[0,0,0]
	v_mfma_scale_f32_16x16x128_f8f6f4 v[140:143], v[0:7], v[24:31], v[140:143], v173, v173 op_sel_hi:[0,0,0]
	v_mfma_scale_f32_16x16x128_f8f6f4 v[136:139], v[8:15], v[24:31], v[136:139], v173, v173 op_sel_hi:[0,0,0]
	v_mfma_scale_f32_16x16x128_f8f6f4 v[124:127], v[0:7], v[194:201], v[124:127], v173, v173 op_sel_hi:[0,0,0]
	v_mfma_scale_f32_16x16x128_f8f6f4 v[120:123], v[8:15], v[194:201], v[120:123], v173, v173 op_sel_hi:[0,0,0]
	v_mfma_scale_f32_16x16x128_f8f6f4 v[108:111], v[0:7], v[210:217], v[108:111], v173, v173 op_sel_hi:[0,0,0]
	v_mfma_scale_f32_16x16x128_f8f6f4 v[104:107], v[8:15], v[210:217], v[104:107], v173, v173 op_sel_hi:[0,0,0]
	s_setprio 0
	s_barrier
	s_add_u32 s34, s28, 0x80
	s_addc_u32 s35, s29, 0
	s_mov_b32 m0, s50
	ds_read_b128 v[218:221], v180
	ds_read_b128 v[222:225], v181
	ds_read_b128 v[226:229], v188
	ds_read_b128 v[230:233], v189
	s_nop 0
	global_load_lds_dwordx4 v164, s[34:35]
	s_mov_b32 m0, s51
	s_nop 0
	global_load_lds_dwordx4 v160, s[34:35]
	s_nop 0
	s_barrier
	s_waitcnt lgkmcnt(0)
	s_setprio 1
	s_waitcnt lgkmcnt(0)
	v_mfma_scale_f32_16x16x128_f8f6f4 v[148:151], v[218:225], v[16:23], v[148:151], v173, v173 op_sel_hi:[0,0,0]
	v_mfma_scale_f32_16x16x128_f8f6f4 v[144:147], v[226:233], v[16:23], v[144:147], v173, v173 op_sel_hi:[0,0,0]
	v_mfma_scale_f32_16x16x128_f8f6f4 v[132:135], v[218:225], v[24:31], v[132:135], v173, v173 op_sel_hi:[0,0,0]
	v_mfma_scale_f32_16x16x128_f8f6f4 v[128:131], v[226:233], v[24:31], v[128:131], v173, v173 op_sel_hi:[0,0,0]
	v_mfma_scale_f32_16x16x128_f8f6f4 v[116:119], v[218:225], v[194:201], v[116:119], v173, v173 op_sel_hi:[0,0,0]
	v_mfma_scale_f32_16x16x128_f8f6f4 v[112:115], v[226:233], v[194:201], v[112:115], v173, v173 op_sel_hi:[0,0,0]
	v_mfma_scale_f32_16x16x128_f8f6f4 v[100:103], v[218:225], v[210:217], v[100:103], v173, v173 op_sel_hi:[0,0,0]
	v_mfma_scale_f32_16x16x128_f8f6f4 v[96:99], v[226:233], v[210:217], v[96:99], v173, v173 op_sel_hi:[0,0,0]
	s_setprio 0
	s_add_u32 s30, s30, 0x80
	s_addc_u32 s31, s31, 0
	s_mov_b32 m0, s52
	s_barrier
	ds_read_b128 v[16:19], v190 offset:49152
	ds_read_b128 v[24:27], v190 offset:51200
	ds_read_b128 v[20:23], v191 offset:49152
	ds_read_b128 v[28:31], v191 offset:51200
	ds_read_b128 v[194:197], v190 offset:53248
	ds_read_b128 v[210:213], v190 offset:55296
	ds_read_b128 v[198:201], v191 offset:53248
	ds_read_b128 v[214:217], v191 offset:55296
	s_nop 0
	global_load_lds_dwordx4 v166, s[30:31]
	s_mov_b32 m0, s53
	s_nop 0
	global_load_lds_dwordx4 v162, s[30:31]
	s_nop 0
	s_barrier
	s_waitcnt lgkmcnt(0)
	s_setprio 1
	s_waitcnt lgkmcnt(0)
	v_mfma_scale_f32_16x16x128_f8f6f4 v[92:95], v[0:7], v[16:23], v[92:95], v173, v173 op_sel_hi:[0,0,0]
	v_mfma_scale_f32_16x16x128_f8f6f4 v[88:91], v[8:15], v[16:23], v[88:91], v173, v173 op_sel_hi:[0,0,0]
	v_mfma_scale_f32_16x16x128_f8f6f4 v[76:79], v[0:7], v[24:31], v[76:79], v173, v173 op_sel_hi:[0,0,0]
	v_mfma_scale_f32_16x16x128_f8f6f4 v[72:75], v[8:15], v[24:31], v[72:75], v173, v173 op_sel_hi:[0,0,0]
	v_mfma_scale_f32_16x16x128_f8f6f4 v[60:63], v[0:7], v[194:201], v[60:63], v173, v173 op_sel_hi:[0,0,0]
	v_mfma_scale_f32_16x16x128_f8f6f4 v[56:59], v[8:15], v[194:201], v[56:59], v173, v173 op_sel_hi:[0,0,0]
	v_mfma_scale_f32_16x16x128_f8f6f4 v[44:47], v[0:7], v[210:217], v[44:47], v173, v173 op_sel_hi:[0,0,0]
	v_mfma_scale_f32_16x16x128_f8f6f4 v[40:43], v[8:15], v[210:217], v[40:43], v173, v173 op_sel_hi:[0,0,0]
	s_setprio 0
	s_barrier
	s_add_u32 s28, s28, 0x20080
	s_addc_u32 s29, s29, 0
	s_mov_b32 m0, s54
	s_nop 0
	global_load_lds_dwordx4 v164, s[28:29]
	s_mov_b32 m0, s55
	s_nop 0
	global_load_lds_dwordx4 v160, s[28:29]
	s_waitcnt vmcnt(6)
	s_barrier
	s_setprio 1
	v_mfma_scale_f32_16x16x128_f8f6f4 v[84:87], v[218:225], v[16:23], v[84:87], v173, v173 op_sel_hi:[0,0,0]
	v_mfma_scale_f32_16x16x128_f8f6f4 v[80:83], v[226:233], v[16:23], v[80:83], v173, v173 op_sel_hi:[0,0,0]
	v_mfma_scale_f32_16x16x128_f8f6f4 v[68:71], v[218:225], v[24:31], v[68:71], v173, v173 op_sel_hi:[0,0,0]
	v_mfma_scale_f32_16x16x128_f8f6f4 v[64:67], v[226:233], v[24:31], v[64:67], v173, v173 op_sel_hi:[0,0,0]
	v_mfma_scale_f32_16x16x128_f8f6f4 v[52:55], v[218:225], v[194:201], v[52:55], v173, v173 op_sel_hi:[0,0,0]
	v_mfma_scale_f32_16x16x128_f8f6f4 v[48:51], v[226:233], v[194:201], v[48:51], v173, v173 op_sel_hi:[0,0,0]
	v_mfma_scale_f32_16x16x128_f8f6f4 v[36:39], v[218:225], v[210:217], v[36:39], v173, v173 op_sel_hi:[0,0,0]
	v_mfma_scale_f32_16x16x128_f8f6f4 v[32:35], v[226:233], v[210:217], v[32:35], v173, v173 op_sel_hi:[0,0,0]
	s_setprio 0
	s_add_i32 s33, s33, 2
	s_cmp_gt_u32 s33, 5
	s_mov_b64 s[30:31], s[26:27]
	s_barrier
	s_cbranch_scc0 .LBB0_1063
	v_mov_b32_e32 v2, v172
	v_mov_b32_e32 v8, 0
	v_ashrrev_i32_e32 v0, 2, v2
	v_and_b32_e32 v0, 0xffffffc0, v0
	v_lshl_add_u32 v0, s2, 8, v0
	v_and_or_b32 v6, v2, 15, v0
	v_ashrrev_i32_e32 v7, 31, v6
	v_lshl_add_u64 v[0:1], v[6:7], 2, s[10:11]
	global_load_dword v14, v[0:1], off
	global_load_dword v194, v[0:1], off offset:64
	global_load_dword v195, v[0:1], off offset:128
	global_load_dword v196, v[0:1], off offset:192
	global_load_dword v197, v[0:1], off offset:512
	global_load_dword v198, v[0:1], off offset:576
	global_load_dword v199, v[0:1], off offset:640
	global_load_dword v200, v[0:1], off offset:704
	s_ashr_i32 s2, s0, 31
	s_lshr_b32 s2, s2, 30
	s_add_i32 s2, s0, s2
	v_lshrrev_b32_e32 v2, 1, v2
	s_and_b32 s2, s2, 0xfffffc
	v_and_b32_e32 v2, 0x78, v2
	s_sub_i32 s0, s0, s2
	v_lshl_or_b32 v4, s0, 8, v2
	v_lshlrev_b64 v[2:3], 10, v[6:7]
	v_mov_b32_e32 v9, 0
	v_mov_b32_e32 v10, 0
	v_mov_b32_e32 v11, 0
	v_ashrrev_i32_e32 v5, 31, v4
	v_or_b32_e32 v12, 16, v6
	v_lshl_add_u64 v[2:3], s[14:15], 0, v[2:3]
	v_ashrrev_i32_e32 v13, 31, v12
	v_lshl_add_u64 v[2:3], v[2:3], 0, v[4:5]
	s_mov_b32 s0, 0x20000
	s_mov_b64 s[4:5], 0x20000
	s_mov_b64 s[24:25], s[20:21]
	s_mov_b32 s2, s16
	s_waitcnt vmcnt(0)
	v_mul_f32_e32 v7, 0x3d000000, v14
	v_mul_f32_e32 v14, 0x42000000, v7
	v_pk_mul_f32 v[18:19], v[156:157], v[14:15] op_sel_hi:[1,0]
	v_pk_mul_f32 v[22:23], v[152:153], v[14:15] op_sel_hi:[1,0]
	v_pk_mul_f32 v[16:17], v[158:159], v[14:15] op_sel_hi:[1,0]
	v_pk_mul_f32 v[20:21], v[154:155], v[14:15] op_sel_hi:[1,0]
	v_pk_mul_f32 v[24:25], v[150:151], v[14:15] op_sel_hi:[1,0]
	v_pk_mul_f32 v[26:27], v[148:149], v[14:15] op_sel_hi:[1,0]
	v_pk_mul_f32 v[28:29], v[146:147], v[14:15] op_sel_hi:[1,0]
	v_pk_mul_f32 v[14:15], v[144:145], v[14:15] op_sel_hi:[1,0]
	v_med3_f32 v7, v18, s57, v192
	v_med3_f32 v18, v22, s57, v192
	v_med3_f32 v19, v19, s57, v192
	v_med3_f32 v22, v23, s57, v192
	v_med3_f32 v23, v26, s57, v192
	v_med3_f32 v14, v14, s57, v192
	v_med3_f32 v26, v27, s57, v192
	v_med3_f32 v15, v15, s57, v192
	v_cvt_pk_fp8_f32 v8, v7, v19
	v_cvt_pk_fp8_f32 v9, v18, v22
	v_cvt_pk_fp8_f32 v10, v23, v26
	v_cvt_pk_fp8_f32 v11, v14, v15
	v_med3_f32 v16, v16, s57, v192
	v_med3_f32 v20, v20, s57, v192
	v_med3_f32 v17, v17, s57, v192
	v_med3_f32 v21, v21, s57, v192
	v_med3_f32 v24, v24, s57, v192
	v_med3_f32 v27, v28, s57, v192
	v_med3_f32 v25, v25, s57, v192
	v_med3_f32 v28, v29, s57, v192
	v_cvt_pk_fp8_f32 v8, v16, v17 op_sel:[0,0,1]
	v_cvt_pk_fp8_f32 v9, v20, v21 op_sel:[0,0,1]
	v_cvt_pk_fp8_f32 v10, v24, v25 op_sel:[0,0,1]
	v_cvt_pk_fp8_f32 v11, v27, v28 op_sel:[0,0,1]
	v_lshl_add_u64 v[14:15], v[12:13], 2, s[10:11]
	global_store_dwordx2 v[2:3], v[8:9], off
	global_store_dwordx2 v[2:3], v[10:11], off offset:128
	v_mov_b32_e32 v8, 0
	v_mov_b32_e32 v9, 0
	v_mov_b32_e32 v10, 0
	v_mov_b32_e32 v11, 0
	v_lshlrev_b64 v[12:13], 10, v[12:13]
	v_or_b32_e32 v14, 32, v6
	v_lshl_add_u64 v[12:13], s[14:15], 0, v[12:13]
	v_ashrrev_i32_e32 v15, 31, v14
	v_lshl_add_u64 v[12:13], v[12:13], 0, v[4:5]
	v_lshl_add_u64 v[16:17], v[14:15], 2, s[10:11]
	v_or_b32_e32 v6, 48, v6
	v_mul_f32_e32 v7, 0x3d000000, v194
	v_mul_f32_e32 v18, 0x42000000, v7
	v_pk_mul_f32 v[22:23], v[140:141], v[18:19] op_sel_hi:[1,0]
	v_pk_mul_f32 v[26:27], v[136:137], v[18:19] op_sel_hi:[1,0]
	v_pk_mul_f32 v[20:21], v[142:143], v[18:19] op_sel_hi:[1,0]
	v_pk_mul_f32 v[24:25], v[138:139], v[18:19] op_sel_hi:[1,0]
	v_pk_mul_f32 v[28:29], v[134:135], v[18:19] op_sel_hi:[1,0]
	v_pk_mul_f32 v[30:31], v[132:133], v[18:19] op_sel_hi:[1,0]
	v_pk_mul_f32 v[130:131], v[130:131], v[18:19] op_sel_hi:[1,0]
	v_pk_mul_f32 v[18:19], v[128:129], v[18:19] op_sel_hi:[1,0]
	v_med3_f32 v7, v22, s57, v192
	v_med3_f32 v22, v26, s57, v192
	v_med3_f32 v23, v23, s57, v192
	v_med3_f32 v26, v27, s57, v192
	v_med3_f32 v27, v30, s57, v192
	v_med3_f32 v18, v18, s57, v192
	v_med3_f32 v30, v31, s57, v192
	v_med3_f32 v19, v19, s57, v192
	v_cvt_pk_fp8_f32 v8, v7, v23
	v_cvt_pk_fp8_f32 v9, v22, v26
	v_cvt_pk_fp8_f32 v10, v27, v30
	v_cvt_pk_fp8_f32 v11, v18, v19
	v_med3_f32 v20, v20, s57, v192
	v_med3_f32 v24, v24, s57, v192
	v_med3_f32 v21, v21, s57, v192
	v_med3_f32 v25, v25, s57, v192
	v_med3_f32 v28, v28, s57, v192
	v_med3_f32 v31, v130, s57, v192
	v_med3_f32 v29, v29, s57, v192
	v_med3_f32 v128, v131, s57, v192
	v_cvt_pk_fp8_f32 v8, v20, v21 op_sel:[0,0,1]
	v_cvt_pk_fp8_f32 v9, v24, v25 op_sel:[0,0,1]
	v_cvt_pk_fp8_f32 v10, v28, v29 op_sel:[0,0,1]
	v_cvt_pk_fp8_f32 v11, v31, v128 op_sel:[0,0,1]
	global_store_dwordx2 v[12:13], v[8:9], off
	global_store_dwordx2 v[12:13], v[10:11], off offset:128
	v_mov_b32_e32 v8, 0
	v_mov_b32_e32 v9, 0
	v_mov_b32_e32 v10, 0
	v_mov_b32_e32 v11, 0
	v_lshlrev_b64 v[12:13], 10, v[14:15]
	v_lshl_add_u64 v[12:13], s[14:15], 0, v[12:13]
	v_ashrrev_i32_e32 v7, 31, v6
	v_lshl_add_u64 v[12:13], v[12:13], 0, v[4:5]
	v_lshl_add_u64 v[14:15], v[6:7], 2, s[10:11]
	v_lshlrev_b64 v[6:7], 10, v[6:7]
	v_lshl_add_u64 v[6:7], s[14:15], 0, v[6:7]
	v_lshl_add_u64 v[4:5], v[6:7], 0, v[4:5]
	v_mov_b32_e32 v6, 0
	v_mov_b32_e32 v7, 0
	v_mul_f32_e32 v16, 0x3d000000, v195
	v_mul_f32_e32 v16, 0x42000000, v16
	v_pk_mul_f32 v[20:21], v[124:125], v[16:17] op_sel_hi:[1,0]
	v_pk_mul_f32 v[24:25], v[120:121], v[16:17] op_sel_hi:[1,0]
	v_pk_mul_f32 v[18:19], v[126:127], v[16:17] op_sel_hi:[1,0]
	v_pk_mul_f32 v[22:23], v[122:123], v[16:17] op_sel_hi:[1,0]
	v_pk_mul_f32 v[26:27], v[118:119], v[16:17] op_sel_hi:[1,0]
	v_pk_mul_f32 v[28:29], v[116:117], v[16:17] op_sel_hi:[1,0]
	v_pk_mul_f32 v[30:31], v[114:115], v[16:17] op_sel_hi:[1,0]
	v_pk_mul_f32 v[16:17], v[112:113], v[16:17] op_sel_hi:[1,0]
	v_med3_f32 v20, v20, s57, v192
	v_med3_f32 v24, v24, s57, v192
	v_med3_f32 v21, v21, s57, v192
	v_med3_f32 v25, v25, s57, v192
	v_med3_f32 v28, v28, s57, v192
	v_med3_f32 v16, v16, s57, v192
	v_med3_f32 v29, v29, s57, v192
	v_med3_f32 v17, v17, s57, v192
	v_cvt_pk_fp8_f32 v8, v20, v21
	v_cvt_pk_fp8_f32 v9, v24, v25
	v_cvt_pk_fp8_f32 v10, v28, v29
	v_cvt_pk_fp8_f32 v11, v16, v17
	v_med3_f32 v18, v18, s57, v192
	v_med3_f32 v22, v22, s57, v192
	v_med3_f32 v19, v19, s57, v192
	v_med3_f32 v23, v23, s57, v192
	v_med3_f32 v26, v26, s57, v192
	v_med3_f32 v30, v30, s57, v192
	v_med3_f32 v27, v27, s57, v192
	v_med3_f32 v31, v31, s57, v192
	v_cvt_pk_fp8_f32 v8, v18, v19 op_sel:[0,0,1]
	v_cvt_pk_fp8_f32 v9, v22, v23 op_sel:[0,0,1]
	v_cvt_pk_fp8_f32 v10, v26, v27 op_sel:[0,0,1]
	v_cvt_pk_fp8_f32 v11, v30, v31 op_sel:[0,0,1]
	global_store_dwordx2 v[12:13], v[8:9], off
	global_store_dwordx2 v[12:13], v[10:11], off offset:128
	v_mov_b32_e32 v8, 0
	v_mov_b32_e32 v9, 0
	v_mov_b32_e32 v10, 0
	v_mov_b32_e32 v11, 0
	v_mul_f32_e32 v12, 0x3d000000, v196
	v_mul_f32_e32 v12, 0x42000000, v12
	v_pk_mul_f32 v[16:17], v[108:109], v[12:13] op_sel_hi:[1,0]
	v_pk_mul_f32 v[20:21], v[104:105], v[12:13] op_sel_hi:[1,0]
	v_pk_mul_f32 v[14:15], v[110:111], v[12:13] op_sel_hi:[1,0]
	v_pk_mul_f32 v[18:19], v[106:107], v[12:13] op_sel_hi:[1,0]
	v_pk_mul_f32 v[22:23], v[102:103], v[12:13] op_sel_hi:[1,0]
	v_pk_mul_f32 v[24:25], v[100:101], v[12:13] op_sel_hi:[1,0]
	v_pk_mul_f32 v[26:27], v[98:99], v[12:13] op_sel_hi:[1,0]
	v_pk_mul_f32 v[12:13], v[96:97], v[12:13] op_sel_hi:[1,0]
	v_med3_f32 v16, v16, s57, v192
	v_med3_f32 v20, v20, s57, v192
	v_med3_f32 v17, v17, s57, v192
	v_med3_f32 v21, v21, s57, v192
	v_med3_f32 v24, v24, s57, v192
	v_med3_f32 v12, v12, s57, v192
	v_med3_f32 v25, v25, s57, v192
	v_med3_f32 v13, v13, s57, v192
	v_cvt_pk_fp8_f32 v8, v16, v17
	v_cvt_pk_fp8_f32 v9, v20, v21
	v_cvt_pk_fp8_f32 v10, v24, v25
	v_cvt_pk_fp8_f32 v11, v12, v13
	v_med3_f32 v14, v14, s57, v192
	v_med3_f32 v18, v18, s57, v192
	v_med3_f32 v15, v15, s57, v192
	v_med3_f32 v19, v19, s57, v192
	v_med3_f32 v22, v22, s57, v192
	v_med3_f32 v26, v26, s57, v192
	v_med3_f32 v23, v23, s57, v192
	v_med3_f32 v27, v27, s57, v192
	v_cvt_pk_fp8_f32 v8, v14, v15 op_sel:[0,0,1]
	v_cvt_pk_fp8_f32 v9, v18, v19 op_sel:[0,0,1]
	v_cvt_pk_fp8_f32 v10, v22, v23 op_sel:[0,0,1]
	v_cvt_pk_fp8_f32 v11, v26, v27 op_sel:[0,0,1]
	global_store_dwordx2 v[4:5], v[8:9], off
	global_store_dwordx2 v[4:5], v[10:11], off offset:128
	v_mov_b32_e32 v4, 0
	v_mov_b32_e32 v5, 0
	v_lshl_add_u64 v[8:9], v[2:3], 0, s[4:5]
	s_mov_b64 s[4:5], 0x24000
	v_mul_f32_e32 v10, 0x3d000000, v197
	v_mul_f32_e32 v10, 0x42000000, v10
	v_pk_mul_f32 v[14:15], v[92:93], v[10:11] op_sel_hi:[1,0]
	v_pk_mul_f32 v[18:19], v[88:89], v[10:11] op_sel_hi:[1,0]
	v_pk_mul_f32 v[12:13], v[94:95], v[10:11] op_sel_hi:[1,0]
	v_pk_mul_f32 v[16:17], v[90:91], v[10:11] op_sel_hi:[1,0]
	v_pk_mul_f32 v[20:21], v[86:87], v[10:11] op_sel_hi:[1,0]
	v_pk_mul_f32 v[22:23], v[84:85], v[10:11] op_sel_hi:[1,0]
	v_pk_mul_f32 v[24:25], v[82:83], v[10:11] op_sel_hi:[1,0]
	v_pk_mul_f32 v[10:11], v[80:81], v[10:11] op_sel_hi:[1,0]
	v_med3_f32 v14, v14, s57, v192
	v_med3_f32 v18, v18, s57, v192
	v_med3_f32 v15, v15, s57, v192
	v_med3_f32 v19, v19, s57, v192
	v_med3_f32 v22, v22, s57, v192
	v_med3_f32 v10, v10, s57, v192
	v_med3_f32 v23, v23, s57, v192
	v_med3_f32 v11, v11, s57, v192
	v_cvt_pk_fp8_f32 v4, v14, v15
	v_cvt_pk_fp8_f32 v5, v18, v19
	v_cvt_pk_fp8_f32 v6, v22, v23
	v_cvt_pk_fp8_f32 v7, v10, v11
	v_med3_f32 v12, v12, s57, v192
	v_med3_f32 v16, v16, s57, v192
	v_med3_f32 v13, v13, s57, v192
	v_med3_f32 v17, v17, s57, v192
	v_med3_f32 v20, v20, s57, v192
	v_med3_f32 v24, v24, s57, v192
	v_med3_f32 v21, v21, s57, v192
	v_med3_f32 v25, v25, s57, v192
	v_cvt_pk_fp8_f32 v4, v12, v13 op_sel:[0,0,1]
	v_cvt_pk_fp8_f32 v5, v16, v17 op_sel:[0,0,1]
	v_cvt_pk_fp8_f32 v6, v20, v21 op_sel:[0,0,1]
	v_cvt_pk_fp8_f32 v7, v24, v25 op_sel:[0,0,1]
	v_add_co_u32_e32 v10, vcc, s0, v2
	s_mov_b32 s0, 0x24000
	s_nop 0
	v_addc_co_u32_e32 v11, vcc, 0, v3, vcc
	global_store_dwordx2 v[10:11], v[4:5], off
	global_store_dwordx2 v[8:9], v[6:7], off offset:128
	v_mov_b32_e32 v4, 0
	v_mov_b32_e32 v5, 0
	v_mov_b32_e32 v6, 0
	v_mov_b32_e32 v7, 0
	v_lshl_add_u64 v[8:9], v[2:3], 0, s[4:5]
	s_mov_b64 s[4:5], 0x28000
	v_mul_f32_e32 v10, 0x3d000000, v198
	v_mul_f32_e32 v10, 0x42000000, v10
	v_pk_mul_f32 v[14:15], v[76:77], v[10:11] op_sel_hi:[1,0]
	v_pk_mul_f32 v[18:19], v[72:73], v[10:11] op_sel_hi:[1,0]
	v_pk_mul_f32 v[12:13], v[78:79], v[10:11] op_sel_hi:[1,0]
	v_pk_mul_f32 v[16:17], v[74:75], v[10:11] op_sel_hi:[1,0]
	v_pk_mul_f32 v[20:21], v[70:71], v[10:11] op_sel_hi:[1,0]
	v_pk_mul_f32 v[22:23], v[68:69], v[10:11] op_sel_hi:[1,0]
	v_pk_mul_f32 v[24:25], v[66:67], v[10:11] op_sel_hi:[1,0]
	v_pk_mul_f32 v[10:11], v[64:65], v[10:11] op_sel_hi:[1,0]
	v_med3_f32 v14, v14, s57, v192
	v_med3_f32 v18, v18, s57, v192
	v_med3_f32 v15, v15, s57, v192
	v_med3_f32 v19, v19, s57, v192
	v_med3_f32 v22, v22, s57, v192
	v_med3_f32 v10, v10, s57, v192
	v_med3_f32 v23, v23, s57, v192
	v_med3_f32 v11, v11, s57, v192
	v_cvt_pk_fp8_f32 v4, v14, v15
	v_cvt_pk_fp8_f32 v5, v18, v19
	v_cvt_pk_fp8_f32 v6, v22, v23
	v_cvt_pk_fp8_f32 v7, v10, v11
	v_med3_f32 v12, v12, s57, v192
	v_med3_f32 v16, v16, s57, v192
	v_med3_f32 v13, v13, s57, v192
	v_med3_f32 v17, v17, s57, v192
	v_med3_f32 v20, v20, s57, v192
	v_med3_f32 v24, v24, s57, v192
	v_med3_f32 v21, v21, s57, v192
	v_med3_f32 v25, v25, s57, v192
	v_cvt_pk_fp8_f32 v4, v12, v13 op_sel:[0,0,1]
	v_cvt_pk_fp8_f32 v5, v16, v17 op_sel:[0,0,1]
	v_cvt_pk_fp8_f32 v6, v20, v21 op_sel:[0,0,1]
	v_cvt_pk_fp8_f32 v7, v24, v25 op_sel:[0,0,1]
	v_add_co_u32_e32 v10, vcc, s0, v2
	s_mov_b32 s0, 0x28000
	s_nop 0
	v_addc_co_u32_e32 v11, vcc, 0, v3, vcc
	global_store_dwordx2 v[10:11], v[4:5], off
	global_store_dwordx2 v[8:9], v[6:7], off offset:128
	v_mov_b32_e32 v4, 0
	v_mov_b32_e32 v5, 0
	v_mov_b32_e32 v6, 0
	v_mov_b32_e32 v7, 0
	v_lshl_add_u64 v[8:9], v[2:3], 0, s[4:5]
	s_mov_b64 s[4:5], s[22:23]
	v_mul_f32_e32 v10, 0x3d000000, v199
	v_mul_f32_e32 v10, 0x42000000, v10
	v_pk_mul_f32 v[14:15], v[60:61], v[10:11] op_sel_hi:[1,0]
	v_pk_mul_f32 v[18:19], v[56:57], v[10:11] op_sel_hi:[1,0]
	v_pk_mul_f32 v[12:13], v[62:63], v[10:11] op_sel_hi:[1,0]
	v_pk_mul_f32 v[16:17], v[58:59], v[10:11] op_sel_hi:[1,0]
	v_pk_mul_f32 v[20:21], v[54:55], v[10:11] op_sel_hi:[1,0]
	v_pk_mul_f32 v[22:23], v[52:53], v[10:11] op_sel_hi:[1,0]
	v_pk_mul_f32 v[24:25], v[50:51], v[10:11] op_sel_hi:[1,0]
	v_pk_mul_f32 v[10:11], v[48:49], v[10:11] op_sel_hi:[1,0]
	v_med3_f32 v14, v14, s57, v192
	v_med3_f32 v18, v18, s57, v192
	v_med3_f32 v15, v15, s57, v192
	v_med3_f32 v19, v19, s57, v192
	v_med3_f32 v22, v22, s57, v192
	v_med3_f32 v10, v10, s57, v192
	v_med3_f32 v23, v23, s57, v192
	v_med3_f32 v11, v11, s57, v192
	v_cvt_pk_fp8_f32 v4, v14, v15
	v_cvt_pk_fp8_f32 v5, v18, v19
	v_cvt_pk_fp8_f32 v6, v22, v23
	v_cvt_pk_fp8_f32 v7, v10, v11
	v_med3_f32 v12, v12, s57, v192
	v_med3_f32 v16, v16, s57, v192
	v_med3_f32 v13, v13, s57, v192
	v_med3_f32 v17, v17, s57, v192
	v_med3_f32 v20, v20, s57, v192
	v_med3_f32 v24, v24, s57, v192
	v_med3_f32 v21, v21, s57, v192
	v_med3_f32 v25, v25, s57, v192
	v_cvt_pk_fp8_f32 v4, v12, v13 op_sel:[0,0,1]
	v_cvt_pk_fp8_f32 v5, v16, v17 op_sel:[0,0,1]
	v_cvt_pk_fp8_f32 v6, v20, v21 op_sel:[0,0,1]
	v_cvt_pk_fp8_f32 v7, v24, v25 op_sel:[0,0,1]
	v_add_co_u32_e32 v10, vcc, s0, v2
	s_mov_b32 s0, s18
	s_nop 0
	v_addc_co_u32_e32 v11, vcc, 0, v3, vcc
	global_store_dwordx2 v[10:11], v[4:5], off
	global_store_dwordx2 v[8:9], v[6:7], off offset:128
	v_mov_b32_e32 v0, 0
	v_mov_b32_e32 v1, 0
	v_mov_b32_e32 v4, 0
	v_mov_b32_e32 v5, 0
	s_and_b64 vcc, exec, s[6:7]
	s_mov_b64 s[6:7], 0x2c000
	v_lshl_add_u64 v[6:7], v[2:3], 0, s[6:7]
	v_add_co_u32_e64 v2, s[6:7], s58, v2
	v_mul_f32_e32 v8, 0x3d000000, v200
	v_mul_f32_e32 v8, 0x42000000, v8
	v_pk_mul_f32 v[12:13], v[44:45], v[8:9] op_sel_hi:[1,0]
	v_pk_mul_f32 v[16:17], v[40:41], v[8:9] op_sel_hi:[1,0]
	v_pk_mul_f32 v[10:11], v[46:47], v[8:9] op_sel_hi:[1,0]
	v_pk_mul_f32 v[14:15], v[42:43], v[8:9] op_sel_hi:[1,0]
	v_pk_mul_f32 v[18:19], v[38:39], v[8:9] op_sel_hi:[1,0]
	v_pk_mul_f32 v[20:21], v[36:37], v[8:9] op_sel_hi:[1,0]
	v_pk_mul_f32 v[22:23], v[34:35], v[8:9] op_sel_hi:[1,0]
	v_pk_mul_f32 v[8:9], v[32:33], v[8:9] op_sel_hi:[1,0]
	v_med3_f32 v12, v12, s57, v192
	v_med3_f32 v16, v16, s57, v192
	v_med3_f32 v13, v13, s57, v192
	v_med3_f32 v17, v17, s57, v192
	v_med3_f32 v20, v20, s57, v192
	v_med3_f32 v8, v8, s57, v192
	v_med3_f32 v21, v21, s57, v192
	v_med3_f32 v9, v9, s57, v192
	v_cvt_pk_fp8_f32 v0, v12, v13
	v_cvt_pk_fp8_f32 v1, v16, v17
	v_cvt_pk_fp8_f32 v4, v20, v21
	v_cvt_pk_fp8_f32 v5, v8, v9
	v_med3_f32 v10, v10, s57, v192
	v_med3_f32 v14, v14, s57, v192
	v_med3_f32 v11, v11, s57, v192
	v_med3_f32 v15, v15, s57, v192
	v_med3_f32 v18, v18, s57, v192
	v_med3_f32 v22, v22, s57, v192
	v_med3_f32 v19, v19, s57, v192
	v_med3_f32 v23, v23, s57, v192
	v_cvt_pk_fp8_f32 v0, v10, v11 op_sel:[0,0,1]
	v_cvt_pk_fp8_f32 v1, v14, v15 op_sel:[0,0,1]
	v_cvt_pk_fp8_f32 v4, v18, v19 op_sel:[0,0,1]
	v_cvt_pk_fp8_f32 v5, v22, v23 op_sel:[0,0,1]
	v_addc_co_u32_e64 v3, s[6:7], 0, v3, s[6:7]
	global_store_dwordx2 v[2:3], v[0:1], off
	global_store_dwordx2 v[6:7], v[4:5], off offset:128
	s_cbranch_vccz .LBB0_1060
	s_waitcnt vmcnt(0)
	v_readlane_b32 s54, v242, 34
	s_cmpk_gt_u32 s36, 0xff
	v_readlane_b32 s55, v242, 35
	s_cbranch_scc1 .LBB0_1067
	s_barrier

.LBB0_1204:
	s_add_u32 s30, s28, 0x100
	ds_read_b128 v[158:161], v141
	ds_read_b128 v[162:165], v142
	ds_read_b128 v[166:169], v149
	ds_read_b128 v[170:173], v150
	s_addc_u32 s31, s29, 0
	s_and_b32 s61, s30, 0x700
	s_add_u32 s62, s16, s61
	s_addc_u32 s63, s17, 0
	s_cmp_eq_u32 s60, 12
	s_cselect_b64 s[36:37], -1, 0
	s_and_b64 s[34:35], s[36:37], exec
	s_cselect_b32 s35, s19, s63
	s_cselect_b32 s34, s21, s62
	s_cselect_b32 s62, 0, 0
	s_cselect_b32 s61, 0, s61
	s_add_u32 s28, s22, s28
	s_addc_u32 s29, s23, s29
	s_add_u32 s28, s28, 0x40080
	s_addc_u32 s29, s29, 0
	ds_read_b128 v[174:177], v157
	ds_read_b128 v[178:181], v157 offset:1024
	ds_read_b128 v[182:185], v157 offset:2048
	ds_read_b128 v[186:189], v157 offset:3072
	ds_read_b128 v[190:193], v157 offset:4096
	ds_read_b128 v[194:197], v157 offset:5120
	ds_read_b128 v[198:201], v157 offset:6144
	ds_read_b128 v[202:205], v157 offset:7168
	s_add_i32 m0, s3, 0xc000
	s_nop 0
	global_load_lds_dwordx4 v134, s[28:29]
	s_add_i32 m0, s3, 0xe000
	s_nop 0
	global_load_lds_dwordx4 v130, s[28:29]
	s_waitcnt lgkmcnt(8)
	s_barrier
	s_waitcnt lgkmcnt(0)
	s_setprio 1
	s_waitcnt lgkmcnt(0)
	v_mfma_f32_16x16x32_bf16 v[124:127], v[158:161], v[174:177], v[124:127]
	v_mfma_f32_16x16x32_bf16 v[120:123], v[166:169], v[174:177], v[120:123]
	v_mfma_f32_16x16x32_bf16 v[116:119], v[158:161], v[182:185], v[116:119]
	v_mfma_f32_16x16x32_bf16 v[108:111], v[166:169], v[182:185], v[108:111]
	v_mfma_f32_16x16x32_bf16 v[100:103], v[158:161], v[190:193], v[100:103]
	v_mfma_f32_16x16x32_bf16 v[92:95], v[166:169], v[190:193], v[92:95]
	v_mfma_f32_16x16x32_bf16 v[84:87], v[158:161], v[198:201], v[84:87]
	v_mfma_f32_16x16x32_bf16 v[76:79], v[166:169], v[198:201], v[76:79]
	v_mfma_f32_16x16x32_bf16 v[124:127], v[162:165], v[178:181], v[124:127]
	v_mfma_f32_16x16x32_bf16 v[120:123], v[170:173], v[178:181], v[120:123]
	v_mfma_f32_16x16x32_bf16 v[116:119], v[162:165], v[186:189], v[116:119]
	v_mfma_f32_16x16x32_bf16 v[108:111], v[170:173], v[186:189], v[108:111]
	v_mfma_f32_16x16x32_bf16 v[100:103], v[162:165], v[194:197], v[100:103]
	v_mfma_f32_16x16x32_bf16 v[92:95], v[170:173], v[194:197], v[92:95]
	v_mfma_f32_16x16x32_bf16 v[84:87], v[162:165], v[202:205], v[84:87]
	v_mfma_f32_16x16x32_bf16 v[76:79], v[170:173], v[202:205], v[76:79]
	s_setprio 0
	s_barrier
	s_mov_b64 s[28:29], s[34:35]
	s_mov_b32 m0, s44
	ds_read_b128 v[210:213], v143
	ds_read_b128 v[214:217], v144
	ds_read_b128 v[218:221], v151
	ds_read_b128 v[222:225], v152
	s_nop 0
	global_load_lds_dwordx4 v132, s[28:29]
	s_mov_b32 m0, s45
	s_nop 0
	global_load_lds_dwordx4 v128, s[28:29]
	s_nop 0
	s_barrier
	s_waitcnt lgkmcnt(0)
	s_setprio 1
	s_waitcnt lgkmcnt(0)
	v_mfma_f32_16x16x32_bf16 v[112:115], v[210:213], v[174:177], v[112:115]
	v_mfma_f32_16x16x32_bf16 v[104:107], v[218:221], v[174:177], v[104:107]
	v_mfma_f32_16x16x32_bf16 v[96:99], v[210:213], v[182:185], v[96:99]
	v_mfma_f32_16x16x32_bf16 v[88:91], v[218:221], v[182:185], v[88:91]
	v_mfma_f32_16x16x32_bf16 v[80:83], v[210:213], v[190:193], v[80:83]
	v_mfma_f32_16x16x32_bf16 v[72:75], v[218:221], v[190:193], v[72:75]
	v_mfma_f32_16x16x32_bf16 v[68:71], v[210:213], v[198:201], v[68:71]
	v_mfma_f32_16x16x32_bf16 v[64:67], v[218:221], v[198:201], v[64:67]
	v_mfma_f32_16x16x32_bf16 v[112:115], v[214:217], v[178:181], v[112:115]
	v_mfma_f32_16x16x32_bf16 v[104:107], v[222:225], v[178:181], v[104:107]
	v_mfma_f32_16x16x32_bf16 v[96:99], v[214:217], v[186:189], v[96:99]
	v_mfma_f32_16x16x32_bf16 v[88:91], v[222:225], v[186:189], v[88:91]
	v_mfma_f32_16x16x32_bf16 v[80:83], v[214:217], v[194:197], v[80:83]
	v_mfma_f32_16x16x32_bf16 v[72:75], v[222:225], v[194:197], v[72:75]
	v_mfma_f32_16x16x32_bf16 v[68:71], v[214:217], v[202:205], v[68:71]
	v_mfma_f32_16x16x32_bf16 v[64:67], v[222:225], v[202:205], v[64:67]
	s_setprio 0
	s_and_b64 s[28:29], s[12:13], s[36:37]
	s_and_b64 s[28:29], s[28:29], exec
	s_cselect_b32 s28, s24, s22
	s_cselect_b32 s29, s25, s23
	s_add_u32 s28, s28, s61
	s_addc_u32 s29, s29, s62
	s_mov_b64 s[36:37], s[28:29]
	s_mov_b32 m0, s3
	s_barrier
	ds_read_b128 v[174:177], v157 offset:16384
	ds_read_b128 v[178:181], v157 offset:17408
	ds_read_b128 v[182:185], v157 offset:18432
	ds_read_b128 v[186:189], v157 offset:19456
	ds_read_b128 v[190:193], v157 offset:20480
	ds_read_b128 v[194:197], v157 offset:21504
	ds_read_b128 v[198:201], v157 offset:22528
	ds_read_b128 v[202:205], v157 offset:23552
	s_nop 0
	global_load_lds_dwordx4 v134, s[36:37]
	s_mov_b32 m0, s46
	s_nop 0
	global_load_lds_dwordx4 v130, s[36:37]
	s_nop 0
	s_barrier
	s_waitcnt lgkmcnt(0)
	s_setprio 1
	s_waitcnt lgkmcnt(0)
	v_mfma_f32_16x16x32_bf16 v[60:63], v[158:161], v[174:177], v[60:63]
	v_mfma_f32_16x16x32_bf16 v[56:59], v[166:169], v[174:177], v[56:59]
	v_mfma_f32_16x16x32_bf16 v[52:55], v[158:161], v[182:185], v[52:55]
	v_mfma_f32_16x16x32_bf16 v[48:51], v[166:169], v[182:185], v[48:51]
	v_mfma_f32_16x16x32_bf16 v[36:39], v[158:161], v[190:193], v[36:39]
	v_mfma_f32_16x16x32_bf16 v[32:35], v[166:169], v[190:193], v[32:35]
	v_mfma_f32_16x16x32_bf16 v[20:23], v[158:161], v[198:201], v[20:23]
	v_mfma_f32_16x16x32_bf16 v[16:19], v[166:169], v[198:201], v[16:19]
	v_mfma_f32_16x16x32_bf16 v[60:63], v[162:165], v[178:181], v[60:63]
	v_mfma_f32_16x16x32_bf16 v[56:59], v[170:173], v[178:181], v[56:59]
	v_mfma_f32_16x16x32_bf16 v[52:55], v[162:165], v[186:189], v[52:55]
	v_mfma_f32_16x16x32_bf16 v[48:51], v[170:173], v[186:189], v[48:51]
	v_mfma_f32_16x16x32_bf16 v[36:39], v[162:165], v[194:197], v[36:39]
	v_mfma_f32_16x16x32_bf16 v[32:35], v[170:173], v[194:197], v[32:35]
	v_mfma_f32_16x16x32_bf16 v[20:23], v[162:165], v[202:205], v[20:23]
	v_mfma_f32_16x16x32_bf16 v[16:19], v[170:173], v[202:205], v[16:19]
	s_setprio 0
	s_barrier
	s_add_u32 s36, s34, 0x40000
	s_addc_u32 s37, s35, 0
	s_mov_b32 m0, s47
	s_nop 0
	global_load_lds_dwordx4 v132, s[36:37]
	s_mov_b32 m0, s48
	s_nop 0
	global_load_lds_dwordx4 v128, s[36:37]
	s_waitcnt vmcnt(6)
	s_barrier
	s_setprio 1
	v_mfma_f32_16x16x32_bf16 v[44:47], v[210:213], v[174:177], v[44:47]
	v_mfma_f32_16x16x32_bf16 v[40:43], v[218:221], v[174:177], v[40:43]
	v_mfma_f32_16x16x32_bf16 v[28:31], v[210:213], v[182:185], v[28:31]
	v_mfma_f32_16x16x32_bf16 v[24:27], v[218:221], v[182:185], v[24:27]
	v_mfma_f32_16x16x32_bf16 v[12:15], v[210:213], v[190:193], v[12:15]
	v_mfma_f32_16x16x32_bf16 v[8:11], v[218:221], v[190:193], v[8:11]
	v_mfma_f32_16x16x32_bf16 v[4:7], v[210:213], v[198:201], v[4:7]
	v_mfma_f32_16x16x32_bf16 v[0:3], v[218:221], v[198:201], v[0:3]
	v_mfma_f32_16x16x32_bf16 v[44:47], v[214:217], v[178:181], v[44:47]
	v_mfma_f32_16x16x32_bf16 v[40:43], v[222:225], v[178:181], v[40:43]
	v_mfma_f32_16x16x32_bf16 v[28:31], v[214:217], v[186:189], v[28:31]
	v_mfma_f32_16x16x32_bf16 v[24:27], v[222:225], v[186:189], v[24:27]
	v_mfma_f32_16x16x32_bf16 v[12:15], v[214:217], v[194:197], v[12:15]
	v_mfma_f32_16x16x32_bf16 v[8:11], v[222:225], v[194:197], v[8:11]
	v_mfma_f32_16x16x32_bf16 v[4:7], v[214:217], v[202:205], v[4:7]
	v_mfma_f32_16x16x32_bf16 v[0:3], v[222:225], v[202:205], v[0:3]
	s_setprio 0
	s_barrier
	ds_read_b128 v[158:161], v145
	ds_read_b128 v[162:165], v146
	ds_read_b128 v[166:169], v153
	ds_read_b128 v[170:173], v154
	s_add_u32 s36, s28, 0x40000
	s_addc_u32 s37, s29, 0
	s_mov_b32 m0, s49
	ds_read_b128 v[174:177], v157 offset:32768
	ds_read_b128 v[178:181], v157 offset:33792
	ds_read_b128 v[182:185], v157 offset:34816
	ds_read_b128 v[186:189], v157 offset:35840
	ds_read_b128 v[190:193], v157 offset:36864
	ds_read_b128 v[194:197], v157 offset:37888
	ds_read_b128 v[198:201], v157 offset:38912
	ds_read_b128 v[202:205], v157 offset:39936
	s_nop 0
	global_load_lds_dwordx4 v134, s[36:37]
	s_mov_b32 m0, s50
	s_nop 0
	global_load_lds_dwordx4 v130, s[36:37]
	s_waitcnt lgkmcnt(8)
	s_barrier
	s_waitcnt lgkmcnt(0)
	s_setprio 1
	s_waitcnt lgkmcnt(0)
	v_mfma_f32_16x16x32_bf16 v[124:127], v[158:161], v[174:177], v[124:127]
	v_mfma_f32_16x16x32_bf16 v[120:123], v[166:169], v[174:177], v[120:123]
	v_mfma_f32_16x16x32_bf16 v[116:119], v[158:161], v[182:185], v[116:119]
	v_mfma_f32_16x16x32_bf16 v[108:111], v[166:169], v[182:185], v[108:111]
	v_mfma_f32_16x16x32_bf16 v[100:103], v[158:161], v[190:193], v[100:103]
	v_mfma_f32_16x16x32_bf16 v[92:95], v[166:169], v[190:193], v[92:95]
	v_mfma_f32_16x16x32_bf16 v[84:87], v[158:161], v[198:201], v[84:87]
	v_mfma_f32_16x16x32_bf16 v[76:79], v[166:169], v[198:201], v[76:79]
	v_mfma_f32_16x16x32_bf16 v[124:127], v[162:165], v[178:181], v[124:127]
	v_mfma_f32_16x16x32_bf16 v[120:123], v[170:173], v[178:181], v[120:123]
	v_mfma_f32_16x16x32_bf16 v[116:119], v[162:165], v[186:189], v[116:119]
	v_mfma_f32_16x16x32_bf16 v[108:111], v[170:173], v[186:189], v[108:111]
	v_mfma_f32_16x16x32_bf16 v[100:103], v[162:165], v[194:197], v[100:103]
	v_mfma_f32_16x16x32_bf16 v[92:95], v[170:173], v[194:197], v[92:95]
	v_mfma_f32_16x16x32_bf16 v[84:87], v[162:165], v[202:205], v[84:87]
	v_mfma_f32_16x16x32_bf16 v[76:79], v[170:173], v[202:205], v[76:79]
	s_setprio 0
	s_barrier
	s_add_u32 s36, s34, 0x80
	s_addc_u32 s37, s35, 0
	s_mov_b32 m0, s52
	ds_read_b128 v[210:213], v147
	ds_read_b128 v[214:217], v148
	ds_read_b128 v[218:221], v155
	ds_read_b128 v[222:225], v156
	s_nop 0
	global_load_lds_dwordx4 v132, s[36:37]
	s_mov_b32 m0, s53
	s_nop 0
	global_load_lds_dwordx4 v128, s[36:37]
	s_nop 0
	s_barrier
	s_waitcnt lgkmcnt(0)
	s_setprio 1
	s_waitcnt lgkmcnt(0)
	v_mfma_f32_16x16x32_bf16 v[112:115], v[210:213], v[174:177], v[112:115]
	v_mfma_f32_16x16x32_bf16 v[104:107], v[218:221], v[174:177], v[104:107]
	v_mfma_f32_16x16x32_bf16 v[96:99], v[210:213], v[182:185], v[96:99]
	v_mfma_f32_16x16x32_bf16 v[88:91], v[218:221], v[182:185], v[88:91]
	v_mfma_f32_16x16x32_bf16 v[80:83], v[210:213], v[190:193], v[80:83]
	v_mfma_f32_16x16x32_bf16 v[72:75], v[218:221], v[190:193], v[72:75]
	v_mfma_f32_16x16x32_bf16 v[68:71], v[210:213], v[198:201], v[68:71]
	v_mfma_f32_16x16x32_bf16 v[64:67], v[218:221], v[198:201], v[64:67]
	v_mfma_f32_16x16x32_bf16 v[112:115], v[214:217], v[178:181], v[112:115]
	v_mfma_f32_16x16x32_bf16 v[104:107], v[222:225], v[178:181], v[104:107]
	v_mfma_f32_16x16x32_bf16 v[96:99], v[214:217], v[186:189], v[96:99]
	v_mfma_f32_16x16x32_bf16 v[88:91], v[222:225], v[186:189], v[88:91]
	v_mfma_f32_16x16x32_bf16 v[80:83], v[214:217], v[194:197], v[80:83]
	v_mfma_f32_16x16x32_bf16 v[72:75], v[222:225], v[194:197], v[72:75]
	v_mfma_f32_16x16x32_bf16 v[68:71], v[214:217], v[202:205], v[68:71]
	v_mfma_f32_16x16x32_bf16 v[64:67], v[222:225], v[202:205], v[64:67]
	s_setprio 0
	s_add_u32 s28, s28, 0x80
	s_addc_u32 s29, s29, 0
	s_mov_b32 m0, s54
	s_barrier
	ds_read_b128 v[174:177], v157 offset:49152
	ds_read_b128 v[178:181], v157 offset:50176
	ds_read_b128 v[182:185], v157 offset:51200
	ds_read_b128 v[186:189], v157 offset:52224
	ds_read_b128 v[190:193], v157 offset:53248
	ds_read_b128 v[194:197], v157 offset:54272
	ds_read_b128 v[198:201], v157 offset:55296
	ds_read_b128 v[202:205], v157 offset:56320
	s_nop 0
	global_load_lds_dwordx4 v134, s[28:29]
	s_mov_b32 m0, s55
	s_nop 0
	global_load_lds_dwordx4 v130, s[28:29]
	s_nop 0
	s_barrier
	s_waitcnt lgkmcnt(0)
	s_setprio 1
	s_waitcnt lgkmcnt(0)
	v_mfma_f32_16x16x32_bf16 v[60:63], v[158:161], v[174:177], v[60:63]
	v_mfma_f32_16x16x32_bf16 v[56:59], v[166:169], v[174:177], v[56:59]
	v_mfma_f32_16x16x32_bf16 v[52:55], v[158:161], v[182:185], v[52:55]
	v_mfma_f32_16x16x32_bf16 v[48:51], v[166:169], v[182:185], v[48:51]
	v_mfma_f32_16x16x32_bf16 v[36:39], v[158:161], v[190:193], v[36:39]
	v_mfma_f32_16x16x32_bf16 v[32:35], v[166:169], v[190:193], v[32:35]
	v_mfma_f32_16x16x32_bf16 v[20:23], v[158:161], v[198:201], v[20:23]
	v_mfma_f32_16x16x32_bf16 v[16:19], v[166:169], v[198:201], v[16:19]
	v_mfma_f32_16x16x32_bf16 v[60:63], v[162:165], v[178:181], v[60:63]
	v_mfma_f32_16x16x32_bf16 v[56:59], v[170:173], v[178:181], v[56:59]
	v_mfma_f32_16x16x32_bf16 v[52:55], v[162:165], v[186:189], v[52:55]
	v_mfma_f32_16x16x32_bf16 v[48:51], v[170:173], v[186:189], v[48:51]
	v_mfma_f32_16x16x32_bf16 v[36:39], v[162:165], v[194:197], v[36:39]
	v_mfma_f32_16x16x32_bf16 v[32:35], v[170:173], v[194:197], v[32:35]
	v_mfma_f32_16x16x32_bf16 v[20:23], v[162:165], v[202:205], v[20:23]
	v_mfma_f32_16x16x32_bf16 v[16:19], v[170:173], v[202:205], v[16:19]
	s_setprio 0
	s_barrier
	s_add_u32 s28, s34, 0x40080
	s_addc_u32 s29, s35, 0
	s_mov_b32 m0, s56
	s_nop 0
	global_load_lds_dwordx4 v132, s[28:29]
	s_mov_b32 m0, s57
	s_nop 0
	global_load_lds_dwordx4 v128, s[28:29]
	s_waitcnt vmcnt(6)
	s_barrier
	s_setprio 1
	v_mfma_f32_16x16x32_bf16 v[44:47], v[210:213], v[174:177], v[44:47]
	v_mfma_f32_16x16x32_bf16 v[40:43], v[218:221], v[174:177], v[40:43]
	v_mfma_f32_16x16x32_bf16 v[28:31], v[210:213], v[182:185], v[28:31]
	v_mfma_f32_16x16x32_bf16 v[24:27], v[218:221], v[182:185], v[24:27]
	v_mfma_f32_16x16x32_bf16 v[12:15], v[210:213], v[190:193], v[12:15]
	v_mfma_f32_16x16x32_bf16 v[8:11], v[218:221], v[190:193], v[8:11]
	v_mfma_f32_16x16x32_bf16 v[4:7], v[210:213], v[198:201], v[4:7]
	v_mfma_f32_16x16x32_bf16 v[0:3], v[218:221], v[198:201], v[0:3]
	v_mfma_f32_16x16x32_bf16 v[44:47], v[214:217], v[178:181], v[44:47]
	v_mfma_f32_16x16x32_bf16 v[40:43], v[222:225], v[178:181], v[40:43]
	v_mfma_f32_16x16x32_bf16 v[28:31], v[214:217], v[186:189], v[28:31]
	v_mfma_f32_16x16x32_bf16 v[24:27], v[222:225], v[186:189], v[24:27]
	v_mfma_f32_16x16x32_bf16 v[12:15], v[214:217], v[194:197], v[12:15]
	v_mfma_f32_16x16x32_bf16 v[8:11], v[222:225], v[194:197], v[8:11]
	v_mfma_f32_16x16x32_bf16 v[4:7], v[214:217], v[202:205], v[4:7]
	v_mfma_f32_16x16x32_bf16 v[0:3], v[222:225], v[202:205], v[0:3]
	s_setprio 0
	s_add_i32 s60, s60, 2
	s_cmp_gt_u32 s60, 13
	s_mov_b64 s[28:29], s[30:31]
	s_barrier
	s_cbranch_scc0 .LBB0_1204
	v_mov_b32_e32 v159, v140
	s_mov_b64 s[12:13], 0x80000
	v_ashrrev_i32_e32 v158, 2, v159
	v_and_b32_e32 v158, 0xffffffc0, v158
	v_lshl_add_u32 v158, s2, 8, v158
	v_and_or_b32 v158, v159, 15, v158
	v_lshrrev_b32_e32 v159, 1, v159
	v_and_b32_e32 v159, 0x78, v159
	v_lshl_or_b32 v160, s59, 8, v159
	v_ashrrev_i32_e32 v159, 31, v158
	v_ashrrev_i32_e32 v161, 31, v160
	v_lshlrev_b64 v[162:163], 12, v[158:159]
	v_lshl_add_u64 v[162:163], s[0:1], 0, v[162:163]
	v_lshlrev_b64 v[160:161], 1, v[160:161]
	v_lshl_add_u64 v[162:163], v[162:163], 0, v[160:161]
	s_mov_b32 s2, 0x80000
	v_cvt_pk_bf16_f32 v60, v60, v61
	v_cvt_pk_bf16_f32 v61, v62, v63
	v_cvt_pk_bf16_f32 v62, v56, v57
	v_add_co_u32_e32 v56, vcc, s2, v162
	v_cvt_pk_bf16_f32 v68, v68, v69
	v_cvt_pk_bf16_f32 v69, v70, v71
	v_cvt_pk_bf16_f32 v70, v64, v65
	v_lshl_add_u64 v[64:65], v[162:163], 0, s[12:13]
	v_addc_co_u32_e32 v57, vcc, 0, v163, vcc
	v_cvt_pk_bf16_f32 v44, v44, v45
	v_cvt_pk_bf16_f32 v45, v46, v47
	v_cvt_pk_bf16_f32 v46, v40, v41
	v_cvt_pk_bf16_f32 v47, v42, v43
	s_mov_b32 s2, 0x90000
	v_cvt_pk_bf16_f32 v112, v112, v113
	v_cvt_pk_bf16_f32 v113, v114, v115
	v_cvt_pk_bf16_f32 v114, v104, v105
	v_or_b32_e32 v104, 16, v158
	global_store_dwordx4 v[64:65], v[44:47], off offset:256
	s_mov_b64 s[12:13], 0x90000
	v_ashrrev_i32_e32 v105, 31, v104
	v_add_co_u32_e32 v46, vcc, s2, v162
	v_cvt_pk_bf16_f32 v96, v96, v97
	v_cvt_pk_bf16_f32 v97, v98, v99
	v_cvt_pk_bf16_f32 v98, v88, v89
	v_or_b32_e32 v88, 32, v158
	v_lshl_add_u64 v[44:45], v[162:163], 0, s[12:13]
	v_addc_co_u32_e32 v47, vcc, 0, v163, vcc
	v_cvt_pk_bf16_f32 v28, v28, v29
	v_cvt_pk_bf16_f32 v29, v30, v31
	v_cvt_pk_bf16_f32 v30, v24, v25
	v_cvt_pk_bf16_f32 v31, v26, v27
	s_mov_b32 s2, 0xa0000
	v_lshlrev_b64 v[104:105], 12, v[104:105]
	v_ashrrev_i32_e32 v89, 31, v88
	v_cvt_pk_bf16_f32 v80, v80, v81
	v_cvt_pk_bf16_f32 v81, v82, v83
	v_cvt_pk_bf16_f32 v82, v72, v73
	v_or_b32_e32 v72, 48, v158
	global_store_dwordx4 v[44:45], v[28:31], off offset:256
	s_mov_b64 s[12:13], 0xa0000
	v_cvt_pk_bf16_f32 v115, v106, v107
	v_add_co_u32_e32 v30, vcc, s2, v162
	v_lshl_add_u64 v[104:105], s[0:1], 0, v[104:105]
	v_lshlrev_b64 v[88:89], 12, v[88:89]
	v_ashrrev_i32_e32 v73, 31, v72
	v_lshl_add_u64 v[28:29], v[162:163], 0, s[12:13]
	v_addc_co_u32_e32 v31, vcc, 0, v163, vcc
	v_cvt_pk_bf16_f32 v12, v12, v13
	v_cvt_pk_bf16_f32 v13, v14, v15
	v_cvt_pk_bf16_f32 v14, v8, v9
	v_cvt_pk_bf16_f32 v15, v10, v11
	s_mov_b32 s2, 0xb0000
	global_store_dwordx4 v[162:163], v[112:115], off offset:256
	v_cvt_pk_bf16_f32 v99, v90, v91
	v_lshl_add_u64 v[88:89], s[0:1], 0, v[88:89]
	v_lshl_add_u64 v[112:113], v[104:105], 0, v[160:161]
	v_lshlrev_b64 v[72:73], 12, v[72:73]
	global_store_dwordx4 v[28:29], v[12:15], off offset:256
	global_store_dwordx4 v[112:113], v[96:99], off offset:256
	v_cvt_pk_bf16_f32 v83, v74, v75
	v_add_co_u32_e32 v14, vcc, s2, v162
	v_lshl_add_u64 v[96:97], v[88:89], 0, v[160:161]
	v_lshl_add_u64 v[72:73], s[0:1], 0, v[72:73]
	s_mov_b64 s[12:13], 0xb0000
	v_addc_co_u32_e32 v15, vcc, 0, v163, vcc
	v_cvt_pk_bf16_f32 v124, v124, v125
	v_cvt_pk_bf16_f32 v125, v126, v127
	v_cvt_pk_bf16_f32 v126, v120, v121
	v_cvt_pk_bf16_f32 v127, v122, v123
	v_cvt_pk_bf16_f32 v104, v116, v117
	v_cvt_pk_bf16_f32 v105, v118, v119
	v_cvt_pk_bf16_f32 v106, v108, v109
	v_cvt_pk_bf16_f32 v107, v110, v111
	v_cvt_pk_bf16_f32 v88, v100, v101
	v_cvt_pk_bf16_f32 v89, v102, v103
	v_cvt_pk_bf16_f32 v90, v92, v93
	v_cvt_pk_bf16_f32 v91, v94, v95
	global_store_dwordx4 v[96:97], v[80:83], off offset:256
	v_cvt_pk_bf16_f32 v74, v76, v77
	v_cvt_pk_bf16_f32 v75, v78, v79
	v_lshl_add_u64 v[80:81], v[72:73], 0, v[160:161]
	v_cvt_pk_bf16_f32 v72, v84, v85
	v_cvt_pk_bf16_f32 v73, v86, v87
	v_cvt_pk_bf16_f32 v71, v66, v67
	v_cvt_pk_bf16_f32 v63, v58, v59
	v_cvt_pk_bf16_f32 v40, v52, v53
	v_cvt_pk_bf16_f32 v41, v54, v55
	v_cvt_pk_bf16_f32 v42, v48, v49
	v_cvt_pk_bf16_f32 v43, v50, v51
	v_cvt_pk_bf16_f32 v24, v36, v37
	v_cvt_pk_bf16_f32 v25, v38, v39
	v_cvt_pk_bf16_f32 v26, v32, v33
	v_cvt_pk_bf16_f32 v27, v34, v35
	v_lshl_add_u64 v[12:13], v[162:163], 0, s[12:13]
	v_cvt_pk_bf16_f32 v8, v20, v21
	v_cvt_pk_bf16_f32 v9, v22, v23
	v_cvt_pk_bf16_f32 v10, v16, v17
	v_cvt_pk_bf16_f32 v11, v18, v19
	v_cvt_pk_bf16_f32 v4, v4, v5
	v_cvt_pk_bf16_f32 v5, v6, v7
	v_cvt_pk_bf16_f32 v6, v0, v1
	v_cvt_pk_bf16_f32 v7, v2, v3
	s_and_b64 vcc, exec, s[6:7]
	s_mov_b32 s59, s18
	s_mov_b32 s2, s20
	s_mov_b64 s[16:17], s[26:27]
	s_mov_b64 s[22:23], s[24:25]
	global_store_dwordx4 v[162:163], v[124:127], off
	global_store_dwordx4 v[112:113], v[104:107], off
	global_store_dwordx4 v[96:97], v[88:91], off
	global_store_dwordx4 v[80:81], v[72:75], off
	global_store_dwordx4 v[80:81], v[68:71], off offset:256
	global_store_dwordx4 v[56:57], v[60:63], off
	global_store_dwordx4 v[46:47], v[40:43], off
	global_store_dwordx4 v[30:31], v[24:27], off
	global_store_dwordx4 v[14:15], v[8:11], off
	global_store_dwordx4 v[12:13], v[4:7], off offset:256
	s_cbranch_vccz .LBB0_1201
	s_waitcnt vmcnt(0)
	v_readlane_b32 s54, v242, 34
	s_cmpk_gt_u32 s33, 0xff
	v_readlane_b32 s55, v242, 35
	s_cbranch_scc1 .LBB0_1208
	s_barrier

.LBB0_1558:
	s_add_u32 s36, s34, 0x100
	ds_read_b128 v[32:35], v167
	ds_read_b128 v[36:39], v168
	ds_read_b128 v[48:51], v175
	ds_read_b128 v[52:55], v176
	s_addc_u32 s37, s35, 0
	s_and_b32 s25, s36, 0x700
	s_add_u32 s33, s4, s25
	s_addc_u32 s65, s5, 0
	s_cmp_eq_u32 s23, 12
	s_cselect_b64 s[40:41], -1, 0
	s_and_b64 s[38:39], s[40:41], exec
	s_cselect_b32 s39, s1, s65
	s_cselect_b32 s38, s10, s33
	s_cselect_b32 s33, 0, 0
	s_cselect_b32 s25, 0, s25
	s_add_u32 s34, s30, s34
	s_addc_u32 s35, s31, s35
	s_add_u32 s34, s34, 0x40080
	s_addc_u32 s35, s35, 0
	ds_read_b128 v[158:161], v183
	ds_read_b128 v[162:165], v183 offset:1024
	ds_read_b128 v[184:187], v183 offset:2048
	ds_read_b128 v[188:191], v183 offset:3072
	ds_read_b128 v[192:195], v183 offset:4096
	ds_read_b128 v[196:199], v183 offset:5120
	ds_read_b128 v[200:203], v183 offset:6144
	ds_read_b128 v[204:207], v183 offset:7168
	s_add_i32 m0, s3, 0xc000
	s_nop 0
	global_load_lds_dwordx4 v144, s[34:35]
	s_add_i32 m0, s3, 0xe000
	s_nop 0
	global_load_lds_dwordx4 v148, s[34:35]
	s_waitcnt lgkmcnt(8)
	s_nop 0
	s_barrier
	s_waitcnt lgkmcnt(0)
	s_setprio 1
	s_waitcnt lgkmcnt(0)
	v_mfma_f32_16x16x32_bf16 v[140:143], v[32:35], v[158:161], v[140:143]
	v_mfma_f32_16x16x32_bf16 v[136:139], v[48:51], v[158:161], v[136:139]
	v_mfma_f32_16x16x32_bf16 v[124:127], v[32:35], v[184:187], v[124:127]
	v_mfma_f32_16x16x32_bf16 v[120:123], v[48:51], v[184:187], v[120:123]
	v_mfma_f32_16x16x32_bf16 v[108:111], v[32:35], v[192:195], v[108:111]
	v_mfma_f32_16x16x32_bf16 v[104:107], v[48:51], v[192:195], v[104:107]
	v_mfma_f32_16x16x32_bf16 v[92:95], v[32:35], v[200:203], v[92:95]
	v_mfma_f32_16x16x32_bf16 v[88:91], v[48:51], v[200:203], v[88:91]
	v_mfma_f32_16x16x32_bf16 v[140:143], v[36:39], v[162:165], v[140:143]
	v_mfma_f32_16x16x32_bf16 v[136:139], v[52:55], v[162:165], v[136:139]
	v_mfma_f32_16x16x32_bf16 v[124:127], v[36:39], v[188:191], v[124:127]
	v_mfma_f32_16x16x32_bf16 v[120:123], v[52:55], v[188:191], v[120:123]
	v_mfma_f32_16x16x32_bf16 v[108:111], v[36:39], v[196:199], v[108:111]
	v_mfma_f32_16x16x32_bf16 v[104:107], v[52:55], v[196:199], v[104:107]
	v_mfma_f32_16x16x32_bf16 v[92:95], v[36:39], v[204:207], v[92:95]
	v_mfma_f32_16x16x32_bf16 v[88:91], v[52:55], v[204:207], v[88:91]
	s_setprio 0
	s_barrier
	s_mov_b64 s[34:35], s[38:39]
	s_mov_b32 m0, s47
	ds_read_b128 v[210:213], v169
	ds_read_b128 v[214:217], v170
	ds_read_b128 v[218:221], v177
	ds_read_b128 v[222:225], v178
	s_nop 0
	global_load_lds_dwordx4 v146, s[34:35]
	s_mov_b32 m0, s48
	s_nop 0
	global_load_lds_dwordx4 v150, s[34:35]
	s_nop 0
	s_barrier
	s_waitcnt lgkmcnt(0)
	s_setprio 1
	s_waitcnt lgkmcnt(0)
	v_mfma_f32_16x16x32_bf16 v[132:135], v[210:213], v[158:161], v[132:135]
	v_mfma_f32_16x16x32_bf16 v[128:131], v[218:221], v[158:161], v[128:131]
	v_mfma_f32_16x16x32_bf16 v[116:119], v[210:213], v[184:187], v[116:119]
	v_mfma_f32_16x16x32_bf16 v[112:115], v[218:221], v[184:187], v[112:115]
	v_mfma_f32_16x16x32_bf16 v[100:103], v[210:213], v[192:195], v[100:103]
	v_mfma_f32_16x16x32_bf16 v[96:99], v[218:221], v[192:195], v[96:99]
	v_mfma_f32_16x16x32_bf16 v[84:87], v[210:213], v[200:203], v[84:87]
	v_mfma_f32_16x16x32_bf16 v[80:83], v[218:221], v[200:203], v[80:83]
	v_mfma_f32_16x16x32_bf16 v[132:135], v[214:217], v[162:165], v[132:135]
	v_mfma_f32_16x16x32_bf16 v[128:131], v[222:225], v[162:165], v[128:131]
	v_mfma_f32_16x16x32_bf16 v[116:119], v[214:217], v[188:191], v[116:119]
	v_mfma_f32_16x16x32_bf16 v[112:115], v[222:225], v[188:191], v[112:115]
	v_mfma_f32_16x16x32_bf16 v[100:103], v[214:217], v[196:199], v[100:103]
	v_mfma_f32_16x16x32_bf16 v[96:99], v[222:225], v[196:199], v[96:99]
	v_mfma_f32_16x16x32_bf16 v[84:87], v[214:217], v[204:207], v[84:87]
	v_mfma_f32_16x16x32_bf16 v[80:83], v[222:225], v[204:207], v[80:83]
	s_setprio 0
	s_and_b64 s[34:35], s[14:15], s[40:41]
	s_and_b64 s[34:35], s[34:35], exec
	s_cselect_b32 s34, s26, s30
	s_cselect_b32 s35, s27, s31
	s_add_u32 s34, s34, s25
	s_addc_u32 s35, s35, s33
	s_mov_b64 s[40:41], s[34:35]
	s_mov_b32 m0, s3
	s_barrier
	ds_read_b128 v[158:161], v183 offset:16384
	ds_read_b128 v[162:165], v183 offset:17408
	ds_read_b128 v[184:187], v183 offset:18432
	ds_read_b128 v[188:191], v183 offset:19456
	ds_read_b128 v[192:195], v183 offset:20480
	ds_read_b128 v[196:199], v183 offset:21504
	ds_read_b128 v[200:203], v183 offset:22528
	ds_read_b128 v[204:207], v183 offset:23552
	s_nop 0
	global_load_lds_dwordx4 v144, s[40:41]
	s_mov_b32 m0, s49
	s_nop 0
	global_load_lds_dwordx4 v148, s[40:41]
	s_nop 0
	s_barrier
	s_waitcnt lgkmcnt(0)
	s_setprio 1
	s_waitcnt lgkmcnt(0)
	v_mfma_f32_16x16x32_bf16 v[76:79], v[32:35], v[158:161], v[76:79]
	v_mfma_f32_16x16x32_bf16 v[72:75], v[48:51], v[158:161], v[72:75]
	v_mfma_f32_16x16x32_bf16 v[60:63], v[32:35], v[184:187], v[60:63]
	v_mfma_f32_16x16x32_bf16 v[56:59], v[48:51], v[184:187], v[56:59]
	v_mfma_f32_16x16x32_bf16 v[28:31], v[32:35], v[192:195], v[28:31]
	v_mfma_f32_16x16x32_bf16 v[24:27], v[48:51], v[192:195], v[24:27]
	v_mfma_f32_16x16x32_bf16 v[12:15], v[32:35], v[200:203], v[12:15]
	v_mfma_f32_16x16x32_bf16 v[8:11], v[48:51], v[200:203], v[8:11]
	v_mfma_f32_16x16x32_bf16 v[76:79], v[36:39], v[162:165], v[76:79]
	v_mfma_f32_16x16x32_bf16 v[72:75], v[52:55], v[162:165], v[72:75]
	v_mfma_f32_16x16x32_bf16 v[60:63], v[36:39], v[188:191], v[60:63]
	v_mfma_f32_16x16x32_bf16 v[56:59], v[52:55], v[188:191], v[56:59]
	v_mfma_f32_16x16x32_bf16 v[28:31], v[36:39], v[196:199], v[28:31]
	v_mfma_f32_16x16x32_bf16 v[24:27], v[52:55], v[196:199], v[24:27]
	v_mfma_f32_16x16x32_bf16 v[12:15], v[36:39], v[204:207], v[12:15]
	v_mfma_f32_16x16x32_bf16 v[8:11], v[52:55], v[204:207], v[8:11]
	s_setprio 0
	s_barrier
	s_add_u32 s40, s38, 0x40000
	s_addc_u32 s41, s39, 0
	s_mov_b32 m0, s50
	s_nop 0
	global_load_lds_dwordx4 v146, s[40:41]
	s_mov_b32 m0, s51
	s_nop 0
	global_load_lds_dwordx4 v150, s[40:41]
	s_waitcnt vmcnt(6)
	s_barrier
	s_setprio 1
	v_mfma_f32_16x16x32_bf16 v[44:47], v[210:213], v[184:187], v[44:47]
	v_mfma_f32_16x16x32_bf16 v[40:43], v[218:221], v[184:187], v[40:43]
	v_mfma_f32_16x16x32_bf16 v[20:23], v[210:213], v[192:195], v[20:23]
	v_mfma_f32_16x16x32_bf16 v[16:19], v[218:221], v[192:195], v[16:19]
	v_mfma_f32_16x16x32_bf16 v[4:7], v[210:213], v[200:203], v[4:7]
	v_mfma_f32_16x16x32_bf16 v[0:3], v[218:221], v[200:203], v[0:3]
	v_mfma_f32_16x16x32_bf16 v[32:35], v[210:213], v[158:161], v[68:71]
	v_mfma_f32_16x16x32_bf16 v[36:39], v[218:221], v[158:161], v[64:67]
	v_mfma_f32_16x16x32_bf16 v[44:47], v[214:217], v[188:191], v[44:47]
	v_mfma_f32_16x16x32_bf16 v[40:43], v[222:225], v[188:191], v[40:43]
	v_mfma_f32_16x16x32_bf16 v[20:23], v[214:217], v[196:199], v[20:23]
	v_mfma_f32_16x16x32_bf16 v[16:19], v[222:225], v[196:199], v[16:19]
	v_mfma_f32_16x16x32_bf16 v[4:7], v[214:217], v[204:207], v[4:7]
	v_mfma_f32_16x16x32_bf16 v[0:3], v[222:225], v[204:207], v[0:3]
	v_mfma_f32_16x16x32_bf16 v[32:35], v[214:217], v[162:165], v[32:35]
	v_mfma_f32_16x16x32_bf16 v[36:39], v[222:225], v[162:165], v[36:39]
	s_setprio 0
	s_barrier
	ds_read_b128 v[48:51], v171
	ds_read_b128 v[52:55], v172
	ds_read_b128 v[64:67], v179
	ds_read_b128 v[68:71], v180
	s_add_u32 s40, s34, 0x40000
	s_addc_u32 s41, s35, 0
	s_mov_b32 m0, s52
	ds_read_b128 v[158:161], v183 offset:32768
	ds_read_b128 v[162:165], v183 offset:33792
	ds_read_b128 v[184:187], v183 offset:34816
	ds_read_b128 v[188:191], v183 offset:35840
	ds_read_b128 v[192:195], v183 offset:36864
	ds_read_b128 v[196:199], v183 offset:37888
	ds_read_b128 v[200:203], v183 offset:38912
	ds_read_b128 v[204:207], v183 offset:39936
	s_nop 0
	global_load_lds_dwordx4 v144, s[40:41]
	s_mov_b32 m0, s53
	s_nop 0
	global_load_lds_dwordx4 v148, s[40:41]
	s_waitcnt lgkmcnt(8)
	s_barrier
	s_waitcnt lgkmcnt(0)
	s_setprio 1
	s_waitcnt lgkmcnt(0)
	v_mfma_f32_16x16x32_bf16 v[140:143], v[48:51], v[158:161], v[140:143]
	v_mfma_f32_16x16x32_bf16 v[136:139], v[64:67], v[158:161], v[136:139]
	v_mfma_f32_16x16x32_bf16 v[124:127], v[48:51], v[184:187], v[124:127]
	v_mfma_f32_16x16x32_bf16 v[120:123], v[64:67], v[184:187], v[120:123]
	v_mfma_f32_16x16x32_bf16 v[108:111], v[48:51], v[192:195], v[108:111]
	v_mfma_f32_16x16x32_bf16 v[104:107], v[64:67], v[192:195], v[104:107]
	v_mfma_f32_16x16x32_bf16 v[92:95], v[48:51], v[200:203], v[92:95]
	v_mfma_f32_16x16x32_bf16 v[88:91], v[64:67], v[200:203], v[88:91]
	v_mfma_f32_16x16x32_bf16 v[140:143], v[52:55], v[162:165], v[140:143]
	v_mfma_f32_16x16x32_bf16 v[136:139], v[68:71], v[162:165], v[136:139]
	v_mfma_f32_16x16x32_bf16 v[124:127], v[52:55], v[188:191], v[124:127]
	v_mfma_f32_16x16x32_bf16 v[120:123], v[68:71], v[188:191], v[120:123]
	v_mfma_f32_16x16x32_bf16 v[108:111], v[52:55], v[196:199], v[108:111]
	v_mfma_f32_16x16x32_bf16 v[104:107], v[68:71], v[196:199], v[104:107]
	v_mfma_f32_16x16x32_bf16 v[92:95], v[52:55], v[204:207], v[92:95]
	v_mfma_f32_16x16x32_bf16 v[88:91], v[68:71], v[204:207], v[88:91]
	s_setprio 0
	s_barrier
	s_add_u32 s40, s38, 0x80
	s_addc_u32 s41, s39, 0
	s_mov_b32 m0, s56
	ds_read_b128 v[210:213], v173
	ds_read_b128 v[214:217], v174
	ds_read_b128 v[218:221], v181
	ds_read_b128 v[222:225], v182
	s_nop 0
	global_load_lds_dwordx4 v146, s[40:41]
	s_mov_b32 m0, s57
	s_nop 0
	global_load_lds_dwordx4 v150, s[40:41]
	s_nop 0
	s_barrier
	s_waitcnt lgkmcnt(0)
	s_setprio 1
	s_waitcnt lgkmcnt(0)
	v_mfma_f32_16x16x32_bf16 v[132:135], v[210:213], v[158:161], v[132:135]
	v_mfma_f32_16x16x32_bf16 v[128:131], v[218:221], v[158:161], v[128:131]
	v_mfma_f32_16x16x32_bf16 v[116:119], v[210:213], v[184:187], v[116:119]
	v_mfma_f32_16x16x32_bf16 v[112:115], v[218:221], v[184:187], v[112:115]
	v_mfma_f32_16x16x32_bf16 v[100:103], v[210:213], v[192:195], v[100:103]
	v_mfma_f32_16x16x32_bf16 v[96:99], v[218:221], v[192:195], v[96:99]
	v_mfma_f32_16x16x32_bf16 v[84:87], v[210:213], v[200:203], v[84:87]
	v_mfma_f32_16x16x32_bf16 v[80:83], v[218:221], v[200:203], v[80:83]
	v_mfma_f32_16x16x32_bf16 v[132:135], v[214:217], v[162:165], v[132:135]
	v_mfma_f32_16x16x32_bf16 v[128:131], v[222:225], v[162:165], v[128:131]
	v_mfma_f32_16x16x32_bf16 v[116:119], v[214:217], v[188:191], v[116:119]
	v_mfma_f32_16x16x32_bf16 v[112:115], v[222:225], v[188:191], v[112:115]
	v_mfma_f32_16x16x32_bf16 v[100:103], v[214:217], v[196:199], v[100:103]
	v_mfma_f32_16x16x32_bf16 v[96:99], v[222:225], v[196:199], v[96:99]
	v_mfma_f32_16x16x32_bf16 v[84:87], v[214:217], v[204:207], v[84:87]
	v_mfma_f32_16x16x32_bf16 v[80:83], v[222:225], v[204:207], v[80:83]
	s_setprio 0
	s_add_u32 s34, s34, 0x80
	s_addc_u32 s35, s35, 0
	s_mov_b32 m0, s58
	s_barrier
	ds_read_b128 v[158:161], v183 offset:49152
	ds_read_b128 v[162:165], v183 offset:50176
	ds_read_b128 v[184:187], v183 offset:51200
	ds_read_b128 v[188:191], v183 offset:52224
	ds_read_b128 v[192:195], v183 offset:53248
	ds_read_b128 v[196:199], v183 offset:54272
	ds_read_b128 v[200:203], v183 offset:55296
	ds_read_b128 v[204:207], v183 offset:56320
	s_nop 0
	global_load_lds_dwordx4 v144, s[34:35]
	s_mov_b32 m0, s59
	s_nop 0
	global_load_lds_dwordx4 v148, s[34:35]
	s_nop 0
	s_barrier
	s_waitcnt lgkmcnt(0)
	s_setprio 1
	s_waitcnt lgkmcnt(0)
	v_mfma_f32_16x16x32_bf16 v[76:79], v[48:51], v[158:161], v[76:79]
	v_mfma_f32_16x16x32_bf16 v[72:75], v[64:67], v[158:161], v[72:75]
	v_mfma_f32_16x16x32_bf16 v[60:63], v[48:51], v[184:187], v[60:63]
	v_mfma_f32_16x16x32_bf16 v[56:59], v[64:67], v[184:187], v[56:59]
	v_mfma_f32_16x16x32_bf16 v[28:31], v[48:51], v[192:195], v[28:31]
	v_mfma_f32_16x16x32_bf16 v[24:27], v[64:67], v[192:195], v[24:27]
	v_mfma_f32_16x16x32_bf16 v[12:15], v[48:51], v[200:203], v[12:15]
	v_mfma_f32_16x16x32_bf16 v[8:11], v[64:67], v[200:203], v[8:11]
	v_mfma_f32_16x16x32_bf16 v[76:79], v[52:55], v[162:165], v[76:79]
	v_mfma_f32_16x16x32_bf16 v[72:75], v[68:71], v[162:165], v[72:75]
	v_mfma_f32_16x16x32_bf16 v[60:63], v[52:55], v[188:191], v[60:63]
	v_mfma_f32_16x16x32_bf16 v[56:59], v[68:71], v[188:191], v[56:59]
	v_mfma_f32_16x16x32_bf16 v[28:31], v[52:55], v[196:199], v[28:31]
	v_mfma_f32_16x16x32_bf16 v[24:27], v[68:71], v[196:199], v[24:27]
	v_mfma_f32_16x16x32_bf16 v[12:15], v[52:55], v[204:207], v[12:15]
	v_mfma_f32_16x16x32_bf16 v[8:11], v[68:71], v[204:207], v[8:11]
	s_setprio 0
	s_barrier
	s_add_u32 s34, s38, 0x40080
	s_addc_u32 s35, s39, 0
	s_mov_b32 m0, s60
	s_nop 0
	global_load_lds_dwordx4 v146, s[34:35]
	s_mov_b32 m0, s61
	s_nop 0
	global_load_lds_dwordx4 v150, s[34:35]
	s_waitcnt vmcnt(6)
	s_barrier
	s_setprio 1
	v_mfma_f32_16x16x32_bf16 v[32:35], v[210:213], v[158:161], v[32:35]
	v_mfma_f32_16x16x32_bf16 v[68:71], v[214:217], v[162:165], v[32:35]
	v_mfma_f32_16x16x32_bf16 v[32:35], v[218:221], v[158:161], v[36:39]
	v_mfma_f32_16x16x32_bf16 v[64:67], v[222:225], v[162:165], v[32:35]
	v_mfma_f32_16x16x32_bf16 v[32:35], v[210:213], v[184:187], v[44:47]
	v_mfma_f32_16x16x32_bf16 v[44:47], v[214:217], v[188:191], v[32:35]
	v_mfma_f32_16x16x32_bf16 v[32:35], v[218:221], v[184:187], v[40:43]
	v_mfma_f32_16x16x32_bf16 v[20:23], v[210:213], v[192:195], v[20:23]
	v_mfma_f32_16x16x32_bf16 v[16:19], v[218:221], v[192:195], v[16:19]
	v_mfma_f32_16x16x32_bf16 v[4:7], v[210:213], v[200:203], v[4:7]
	v_mfma_f32_16x16x32_bf16 v[0:3], v[218:221], v[200:203], v[0:3]
	v_mfma_f32_16x16x32_bf16 v[40:43], v[222:225], v[188:191], v[32:35]
	v_mfma_f32_16x16x32_bf16 v[20:23], v[214:217], v[196:199], v[20:23]
	v_mfma_f32_16x16x32_bf16 v[16:19], v[222:225], v[196:199], v[16:19]
	v_mfma_f32_16x16x32_bf16 v[4:7], v[214:217], v[204:207], v[4:7]
	v_mfma_f32_16x16x32_bf16 v[0:3], v[222:225], v[204:207], v[0:3]
	s_setprio 0
	s_add_i32 s23, s23, 2
	s_cmp_gt_u32 s23, 13
	s_mov_b64 s[34:35], s[36:37]
	s_barrier
	s_cbranch_scc0 .LBB0_1558
	v_mov_b32_e32 v32, v166
	s_cmpk_gt_i32 s2, 0x7f
	s_mov_b64 s[4:5], 0xc000
	s_cbranch_scc1 .LBB0_1561
	s_ashr_i32 s1, s2, 31
	s_lshr_b32 s1, s1, 28
	s_add_i32 s1, s2, s1
	s_ashr_i32 s1, s1, 4
	s_mul_hi_i32 s5, s1, 0x1800
	s_mul_i32 s4, s1, 0x1800

.LBB0_1990:
	v_mov_b32_e32 v0, v209
	s_mov_b32 s98, 0x44800000
	s_mov_b32 s100, 0xbd38aa3b
	s_ashr_i32 s2, s0, 31
	v_ashrrev_i32_e32 v1, 2, v0
	v_and_b32_e32 v1, 0xffffffc0, v1
	v_lshl_add_u32 v1, s33, 8, v1
	v_and_or_b32 v4, v0, 15, v1
	v_lshrrev_b32_e32 v2, 1, v0
	s_lshr_b32 s2, s2, 29
	s_add_i32 s2, s0, s2
	s_and_b32 s2, s2, 0x1fffff8
	s_sub_i32 s0, s0, s2
	v_and_b32_e32 v2, 0x78, v2
	v_ashrrev_i32_e32 v5, 31, v4
	v_lshl_or_b32 v2, s0, 7, v2
	v_lshlrev_b64 v[0:1], 10, v[4:5]
	v_ashrrev_i32_e32 v3, 31, v2
	v_lshl_add_u64 v[0:1], s[10:11], 0, v[0:1]
	v_lshl_add_u64 v[0:1], v[0:1], 0, v[2:3]
	v_pk_mul_f32 v[10:11], v[188:189], s[100:101] op_sel_hi:[1,0]
	v_pk_mul_f32 v[12:13], v[190:191], s[100:101] op_sel_hi:[1,0]
	v_pk_mul_f32 v[14:15], v[180:181], s[100:101] op_sel_hi:[1,0]
	v_pk_mul_f32 v[16:17], v[182:183], s[100:101] op_sel_hi:[1,0]
	v_exp_f32_e32 v10, v10
	v_exp_f32_e32 v11, v11
	v_exp_f32_e32 v12, v12
	v_exp_f32_e32 v13, v13
	v_exp_f32_e32 v14, v14
	v_exp_f32_e32 v15, v15
	v_exp_f32_e32 v16, v16
	v_exp_f32_e32 v17, v17
	v_pk_fma_f32 v[10:11], v[10:11], s[98:99], s[98:99] op_sel_hi:[1,0,0]
	v_pk_fma_f32 v[12:13], v[12:13], s[98:99], s[98:99] op_sel_hi:[1,0,0]
	v_pk_fma_f32 v[14:15], v[14:15], s[98:99], s[98:99] op_sel_hi:[1,0,0]
	v_pk_fma_f32 v[16:17], v[16:17], s[98:99], s[98:99] op_sel_hi:[1,0,0]
	v_rcp_f32_e32 v10, v10
	v_rcp_f32_e32 v11, v11
	v_rcp_f32_e32 v12, v12
	v_rcp_f32_e32 v13, v13
	v_rcp_f32_e32 v14, v14
	v_rcp_f32_e32 v15, v15
	v_rcp_f32_e32 v16, v16
	v_rcp_f32_e32 v17, v17
	v_pk_mul_f32 v[10:11], v[188:189], v[10:11]
	v_pk_mul_f32 v[12:13], v[190:191], v[12:13]
	v_pk_mul_f32 v[14:15], v[180:181], v[14:15]
	v_pk_mul_f32 v[16:17], v[182:183], v[16:17]
	v_pk_mul_f32 v[10:11], v[10:11], v[184:185]
	v_pk_mul_f32 v[12:13], v[12:13], v[186:187]
	v_pk_mul_f32 v[14:15], v[14:15], v[176:177]
	v_pk_mul_f32 v[16:17], v[16:17], v[178:179]
	v_cvt_pk_fp8_f32 v18, v10, v11
	v_cvt_pk_fp8_f32 v19, v14, v15
	v_cvt_pk_fp8_f32 v18, v12, v13 op_sel:[0,0,1]
	v_cvt_pk_fp8_f32 v19, v16, v17 op_sel:[0,0,1]
	s_nop 0
	global_store_dwordx2 v[0:1], v[18:19], off
	v_or_b32_e32 v8, 16, v4
	v_ashrrev_i32_e32 v9, 31, v8
	v_lshlrev_b64 v[8:9], 10, v[8:9]
	v_lshl_add_u64 v[8:9], s[10:11], 0, v[8:9]
	v_lshl_add_u64 v[8:9], v[8:9], 0, v[2:3]
	v_pk_mul_f32 v[10:11], v[172:173], s[100:101] op_sel_hi:[1,0]
	v_pk_mul_f32 v[12:13], v[174:175], s[100:101] op_sel_hi:[1,0]
	v_pk_mul_f32 v[14:15], v[164:165], s[100:101] op_sel_hi:[1,0]
	v_pk_mul_f32 v[16:17], v[166:167], s[100:101] op_sel_hi:[1,0]
	v_exp_f32_e32 v10, v10
	v_exp_f32_e32 v11, v11
	v_exp_f32_e32 v12, v12
	v_exp_f32_e32 v13, v13
	v_exp_f32_e32 v14, v14
	v_exp_f32_e32 v15, v15
	v_exp_f32_e32 v16, v16
	v_exp_f32_e32 v17, v17
	v_pk_fma_f32 v[10:11], v[10:11], s[98:99], s[98:99] op_sel_hi:[1,0,0]
	v_pk_fma_f32 v[12:13], v[12:13], s[98:99], s[98:99] op_sel_hi:[1,0,0]
	v_pk_fma_f32 v[14:15], v[14:15], s[98:99], s[98:99] op_sel_hi:[1,0,0]
	v_pk_fma_f32 v[16:17], v[16:17], s[98:99], s[98:99] op_sel_hi:[1,0,0]
	v_rcp_f32_e32 v10, v10
	v_rcp_f32_e32 v11, v11
	v_rcp_f32_e32 v12, v12
	v_rcp_f32_e32 v13, v13
	v_rcp_f32_e32 v14, v14
	v_rcp_f32_e32 v15, v15
	v_rcp_f32_e32 v16, v16
	v_rcp_f32_e32 v17, v17
	v_pk_mul_f32 v[10:11], v[172:173], v[10:11]
	v_pk_mul_f32 v[12:13], v[174:175], v[12:13]
	v_pk_mul_f32 v[14:15], v[164:165], v[14:15]
	v_pk_mul_f32 v[16:17], v[166:167], v[16:17]
	v_pk_mul_f32 v[10:11], v[10:11], v[168:169]
	v_pk_mul_f32 v[12:13], v[12:13], v[170:171]
	v_pk_mul_f32 v[14:15], v[14:15], v[160:161]
	v_pk_mul_f32 v[16:17], v[16:17], v[162:163]
	v_cvt_pk_fp8_f32 v18, v10, v11
	v_cvt_pk_fp8_f32 v19, v14, v15
	v_cvt_pk_fp8_f32 v18, v12, v13 op_sel:[0,0,1]
	v_cvt_pk_fp8_f32 v19, v16, v17 op_sel:[0,0,1]
	s_nop 0
	global_store_dwordx2 v[8:9], v[18:19], off
	v_or_b32_e32 v8, 32, v4
	v_ashrrev_i32_e32 v9, 31, v8
	v_or_b32_e32 v4, 48, v4
	v_lshlrev_b64 v[6:7], 10, v[8:9]
	v_lshl_add_u64 v[6:7], s[10:11], 0, v[6:7]
	v_lshl_add_u64 v[6:7], v[6:7], 0, v[2:3]
	v_pk_mul_f32 v[10:11], v[156:157], s[100:101] op_sel_hi:[1,0]
	v_pk_mul_f32 v[12:13], v[158:159], s[100:101] op_sel_hi:[1,0]
	v_pk_mul_f32 v[14:15], v[148:149], s[100:101] op_sel_hi:[1,0]
	v_pk_mul_f32 v[16:17], v[150:151], s[100:101] op_sel_hi:[1,0]
	v_exp_f32_e32 v10, v10
	v_exp_f32_e32 v11, v11
	v_exp_f32_e32 v12, v12
	v_exp_f32_e32 v13, v13
	v_exp_f32_e32 v14, v14
	v_exp_f32_e32 v15, v15
	v_exp_f32_e32 v16, v16
	v_exp_f32_e32 v17, v17
	v_pk_fma_f32 v[10:11], v[10:11], s[98:99], s[98:99] op_sel_hi:[1,0,0]
	v_pk_fma_f32 v[12:13], v[12:13], s[98:99], s[98:99] op_sel_hi:[1,0,0]
	v_pk_fma_f32 v[14:15], v[14:15], s[98:99], s[98:99] op_sel_hi:[1,0,0]
	v_pk_fma_f32 v[16:17], v[16:17], s[98:99], s[98:99] op_sel_hi:[1,0,0]
	v_rcp_f32_e32 v10, v10
	v_rcp_f32_e32 v11, v11
	v_rcp_f32_e32 v12, v12
	v_rcp_f32_e32 v13, v13
	v_rcp_f32_e32 v14, v14
	v_rcp_f32_e32 v15, v15
	v_rcp_f32_e32 v16, v16
	v_rcp_f32_e32 v17, v17
	v_pk_mul_f32 v[10:11], v[156:157], v[10:11]
	v_pk_mul_f32 v[12:13], v[158:159], v[12:13]
	v_pk_mul_f32 v[14:15], v[148:149], v[14:15]
	v_pk_mul_f32 v[16:17], v[150:151], v[16:17]
	v_pk_mul_f32 v[10:11], v[10:11], v[152:153]
	v_pk_mul_f32 v[12:13], v[12:13], v[154:155]
	v_pk_mul_f32 v[14:15], v[14:15], v[144:145]
	v_pk_mul_f32 v[16:17], v[16:17], v[146:147]
	v_cvt_pk_fp8_f32 v18, v10, v11
	v_cvt_pk_fp8_f32 v19, v14, v15
	v_cvt_pk_fp8_f32 v18, v12, v13 op_sel:[0,0,1]
	v_cvt_pk_fp8_f32 v19, v16, v17 op_sel:[0,0,1]
	s_nop 0
	global_store_dwordx2 v[6:7], v[18:19], off
	v_ashrrev_i32_e32 v5, 31, v4
	v_lshlrev_b64 v[4:5], 10, v[4:5]
	v_lshl_add_u64 v[4:5], s[10:11], 0, v[4:5]
	v_lshl_add_u64 v[2:3], v[4:5], 0, v[2:3]
	s_mov_b32 s0, 0x20000
	v_pk_mul_f32 v[10:11], v[140:141], s[100:101] op_sel_hi:[1,0]
	v_pk_mul_f32 v[12:13], v[142:143], s[100:101] op_sel_hi:[1,0]
	v_pk_mul_f32 v[14:15], v[132:133], s[100:101] op_sel_hi:[1,0]
	v_pk_mul_f32 v[16:17], v[134:135], s[100:101] op_sel_hi:[1,0]
	v_exp_f32_e32 v10, v10
	v_exp_f32_e32 v11, v11
	v_exp_f32_e32 v12, v12
	v_exp_f32_e32 v13, v13
	v_exp_f32_e32 v14, v14
	v_exp_f32_e32 v15, v15
	v_exp_f32_e32 v16, v16
	v_exp_f32_e32 v17, v17
	v_pk_fma_f32 v[10:11], v[10:11], s[98:99], s[98:99] op_sel_hi:[1,0,0]
	v_pk_fma_f32 v[12:13], v[12:13], s[98:99], s[98:99] op_sel_hi:[1,0,0]
	v_pk_fma_f32 v[14:15], v[14:15], s[98:99], s[98:99] op_sel_hi:[1,0,0]
	v_pk_fma_f32 v[16:17], v[16:17], s[98:99], s[98:99] op_sel_hi:[1,0,0]
	v_rcp_f32_e32 v10, v10
	v_rcp_f32_e32 v11, v11
	v_rcp_f32_e32 v12, v12
	v_rcp_f32_e32 v13, v13
	v_rcp_f32_e32 v14, v14
	v_rcp_f32_e32 v15, v15
	v_rcp_f32_e32 v16, v16
	v_rcp_f32_e32 v17, v17
	v_pk_mul_f32 v[10:11], v[140:141], v[10:11]
	v_pk_mul_f32 v[12:13], v[142:143], v[12:13]
	v_pk_mul_f32 v[14:15], v[132:133], v[14:15]
	v_pk_mul_f32 v[16:17], v[134:135], v[16:17]
	v_pk_mul_f32 v[10:11], v[10:11], v[136:137]
	v_pk_mul_f32 v[12:13], v[12:13], v[138:139]
	v_pk_mul_f32 v[14:15], v[14:15], v[128:129]
	v_pk_mul_f32 v[16:17], v[16:17], v[130:131]
	v_cvt_pk_fp8_f32 v18, v10, v11
	v_cvt_pk_fp8_f32 v19, v14, v15
	v_cvt_pk_fp8_f32 v18, v12, v13 op_sel:[0,0,1]
	v_cvt_pk_fp8_f32 v19, v16, v17 op_sel:[0,0,1]
	s_nop 0
	global_store_dwordx2 v[2:3], v[18:19], off
	s_mov_b32 s33, s49
	v_add_co_u32_e32 v6, vcc, s0, v0
	v_addc_co_u32_e32 v7, vcc, 0, v1, vcc
	v_pk_mul_f32 v[10:11], v[124:125], s[100:101] op_sel_hi:[1,0]
	v_pk_mul_f32 v[12:13], v[126:127], s[100:101] op_sel_hi:[1,0]
	v_pk_mul_f32 v[14:15], v[116:117], s[100:101] op_sel_hi:[1,0]
	v_pk_mul_f32 v[16:17], v[118:119], s[100:101] op_sel_hi:[1,0]
	v_exp_f32_e32 v10, v10
	v_exp_f32_e32 v11, v11
	v_exp_f32_e32 v12, v12
	v_exp_f32_e32 v13, v13
	v_exp_f32_e32 v14, v14
	v_exp_f32_e32 v15, v15
	v_exp_f32_e32 v16, v16
	v_exp_f32_e32 v17, v17
	v_pk_fma_f32 v[10:11], v[10:11], s[98:99], s[98:99] op_sel_hi:[1,0,0]
	v_pk_fma_f32 v[12:13], v[12:13], s[98:99], s[98:99] op_sel_hi:[1,0,0]
	v_pk_fma_f32 v[14:15], v[14:15], s[98:99], s[98:99] op_sel_hi:[1,0,0]
	v_pk_fma_f32 v[16:17], v[16:17], s[98:99], s[98:99] op_sel_hi:[1,0,0]
	v_rcp_f32_e32 v10, v10
	v_rcp_f32_e32 v11, v11
	v_rcp_f32_e32 v12, v12
	v_rcp_f32_e32 v13, v13
	v_rcp_f32_e32 v14, v14
	v_rcp_f32_e32 v15, v15
	v_rcp_f32_e32 v16, v16
	v_rcp_f32_e32 v17, v17
	v_pk_mul_f32 v[10:11], v[124:125], v[10:11]
	v_pk_mul_f32 v[12:13], v[126:127], v[12:13]
	v_pk_mul_f32 v[14:15], v[116:117], v[14:15]
	v_pk_mul_f32 v[16:17], v[118:119], v[16:17]
	v_pk_mul_f32 v[10:11], v[10:11], v[120:121]
	v_pk_mul_f32 v[12:13], v[12:13], v[122:123]
	v_pk_mul_f32 v[14:15], v[14:15], v[112:113]
	v_pk_mul_f32 v[16:17], v[16:17], v[114:115]
	v_cvt_pk_fp8_f32 v18, v10, v11
	v_cvt_pk_fp8_f32 v19, v14, v15
	v_cvt_pk_fp8_f32 v18, v12, v13 op_sel:[0,0,1]
	v_cvt_pk_fp8_f32 v19, v16, v17 op_sel:[0,0,1]
	s_nop 0
	global_store_dwordx2 v[6:7], v[18:19], off
	s_mov_b32 s0, 0x24000
	v_add_co_u32_e32 v6, vcc, s0, v0
	v_addc_co_u32_e32 v7, vcc, 0, v1, vcc
	v_pk_mul_f32 v[10:11], v[108:109], s[100:101] op_sel_hi:[1,0]
	v_pk_mul_f32 v[12:13], v[110:111], s[100:101] op_sel_hi:[1,0]
	v_pk_mul_f32 v[14:15], v[100:101], s[100:101] op_sel_hi:[1,0]
	v_pk_mul_f32 v[16:17], v[102:103], s[100:101] op_sel_hi:[1,0]
	v_exp_f32_e32 v10, v10
	v_exp_f32_e32 v11, v11
	v_exp_f32_e32 v12, v12
	v_exp_f32_e32 v13, v13
	v_exp_f32_e32 v14, v14
	v_exp_f32_e32 v15, v15
	v_exp_f32_e32 v16, v16
	v_exp_f32_e32 v17, v17
	v_pk_fma_f32 v[10:11], v[10:11], s[98:99], s[98:99] op_sel_hi:[1,0,0]
	v_pk_fma_f32 v[12:13], v[12:13], s[98:99], s[98:99] op_sel_hi:[1,0,0]
	v_pk_fma_f32 v[14:15], v[14:15], s[98:99], s[98:99] op_sel_hi:[1,0,0]
	v_pk_fma_f32 v[16:17], v[16:17], s[98:99], s[98:99] op_sel_hi:[1,0,0]
	v_rcp_f32_e32 v10, v10
	v_rcp_f32_e32 v11, v11
	v_rcp_f32_e32 v12, v12
	v_rcp_f32_e32 v13, v13
	v_rcp_f32_e32 v14, v14
	v_rcp_f32_e32 v15, v15
	v_rcp_f32_e32 v16, v16
	v_rcp_f32_e32 v17, v17
	v_pk_mul_f32 v[10:11], v[108:109], v[10:11]
	v_pk_mul_f32 v[12:13], v[110:111], v[12:13]
	v_pk_mul_f32 v[14:15], v[100:101], v[14:15]
	v_pk_mul_f32 v[16:17], v[102:103], v[16:17]
	v_pk_mul_f32 v[10:11], v[10:11], v[104:105]
	v_pk_mul_f32 v[12:13], v[12:13], v[106:107]
	v_pk_mul_f32 v[14:15], v[14:15], v[96:97]
	v_pk_mul_f32 v[16:17], v[16:17], v[98:99]
	v_cvt_pk_fp8_f32 v18, v10, v11
	v_cvt_pk_fp8_f32 v19, v14, v15
	v_cvt_pk_fp8_f32 v18, v12, v13 op_sel:[0,0,1]
	v_cvt_pk_fp8_f32 v19, v16, v17 op_sel:[0,0,1]
	s_nop 0
	global_store_dwordx2 v[6:7], v[18:19], off
	s_mov_b32 s0, 0x28000
	v_add_co_u32_e32 v6, vcc, s0, v0
	v_addc_co_u32_e32 v7, vcc, 0, v1, vcc
	v_pk_mul_f32 v[10:11], v[92:93], s[100:101] op_sel_hi:[1,0]
	v_pk_mul_f32 v[12:13], v[94:95], s[100:101] op_sel_hi:[1,0]
	v_pk_mul_f32 v[14:15], v[84:85], s[100:101] op_sel_hi:[1,0]
	v_pk_mul_f32 v[16:17], v[86:87], s[100:101] op_sel_hi:[1,0]
	v_exp_f32_e32 v10, v10
	v_exp_f32_e32 v11, v11
	v_exp_f32_e32 v12, v12
	v_exp_f32_e32 v13, v13
	v_exp_f32_e32 v14, v14
	v_exp_f32_e32 v15, v15
	v_exp_f32_e32 v16, v16
	v_exp_f32_e32 v17, v17
	v_pk_fma_f32 v[10:11], v[10:11], s[98:99], s[98:99] op_sel_hi:[1,0,0]
	v_pk_fma_f32 v[12:13], v[12:13], s[98:99], s[98:99] op_sel_hi:[1,0,0]
	v_pk_fma_f32 v[14:15], v[14:15], s[98:99], s[98:99] op_sel_hi:[1,0,0]
	v_pk_fma_f32 v[16:17], v[16:17], s[98:99], s[98:99] op_sel_hi:[1,0,0]
	v_rcp_f32_e32 v10, v10
	v_rcp_f32_e32 v11, v11
	v_rcp_f32_e32 v12, v12
	v_rcp_f32_e32 v13, v13
	v_rcp_f32_e32 v14, v14
	v_rcp_f32_e32 v15, v15
	v_rcp_f32_e32 v16, v16
	v_rcp_f32_e32 v17, v17
	v_pk_mul_f32 v[10:11], v[92:93], v[10:11]
	v_pk_mul_f32 v[12:13], v[94:95], v[12:13]
	v_pk_mul_f32 v[14:15], v[84:85], v[14:15]
	v_pk_mul_f32 v[16:17], v[86:87], v[16:17]
	v_pk_mul_f32 v[10:11], v[10:11], v[88:89]
	v_pk_mul_f32 v[12:13], v[12:13], v[90:91]
	v_pk_mul_f32 v[14:15], v[14:15], v[80:81]
	v_pk_mul_f32 v[16:17], v[16:17], v[82:83]
	v_cvt_pk_fp8_f32 v18, v10, v11
	v_cvt_pk_fp8_f32 v19, v14, v15
	v_cvt_pk_fp8_f32 v18, v12, v13 op_sel:[0,0,1]
	v_cvt_pk_fp8_f32 v19, v16, v17 op_sel:[0,0,1]
	s_nop 0
	global_store_dwordx2 v[6:7], v[18:19], off
	v_add_co_u32_e32 v0, vcc, 0x2c000, v0
	s_mov_b32 s0, s20
	s_nop 0
	v_addc_co_u32_e32 v1, vcc, 0, v1, vcc
	s_and_b64 vcc, exec, s[14:15]
	s_mov_b64 s[2:3], s[12:13]
	v_pk_mul_f32 v[10:11], v[76:77], s[100:101] op_sel_hi:[1,0]
	v_pk_mul_f32 v[12:13], v[78:79], s[100:101] op_sel_hi:[1,0]
	v_pk_mul_f32 v[14:15], v[68:69], s[100:101] op_sel_hi:[1,0]
	v_pk_mul_f32 v[16:17], v[70:71], s[100:101] op_sel_hi:[1,0]
	v_exp_f32_e32 v10, v10
	v_exp_f32_e32 v11, v11
	v_exp_f32_e32 v12, v12
	v_exp_f32_e32 v13, v13
	v_exp_f32_e32 v14, v14
	v_exp_f32_e32 v15, v15
	v_exp_f32_e32 v16, v16
	v_exp_f32_e32 v17, v17
	v_pk_fma_f32 v[10:11], v[10:11], s[98:99], s[98:99] op_sel_hi:[1,0,0]
	v_pk_fma_f32 v[12:13], v[12:13], s[98:99], s[98:99] op_sel_hi:[1,0,0]
	v_pk_fma_f32 v[14:15], v[14:15], s[98:99], s[98:99] op_sel_hi:[1,0,0]
	v_pk_fma_f32 v[16:17], v[16:17], s[98:99], s[98:99] op_sel_hi:[1,0,0]
	v_rcp_f32_e32 v10, v10
	v_rcp_f32_e32 v11, v11
	v_rcp_f32_e32 v12, v12
	v_rcp_f32_e32 v13, v13
	v_rcp_f32_e32 v14, v14
	v_rcp_f32_e32 v15, v15
	v_rcp_f32_e32 v16, v16
	v_rcp_f32_e32 v17, v17
	v_pk_mul_f32 v[10:11], v[76:77], v[10:11]
	v_pk_mul_f32 v[12:13], v[78:79], v[12:13]
	v_pk_mul_f32 v[14:15], v[68:69], v[14:15]
	v_pk_mul_f32 v[16:17], v[70:71], v[16:17]
	v_pk_mul_f32 v[10:11], v[10:11], v[72:73]
	v_pk_mul_f32 v[12:13], v[12:13], v[74:75]
	v_pk_mul_f32 v[14:15], v[14:15], v[64:65]
	v_pk_mul_f32 v[16:17], v[16:17], v[66:67]
	v_cvt_pk_fp8_f32 v18, v10, v11
	v_cvt_pk_fp8_f32 v19, v14, v15
	v_cvt_pk_fp8_f32 v18, v12, v13 op_sel:[0,0,1]
	v_cvt_pk_fp8_f32 v19, v16, v17 op_sel:[0,0,1]
	s_nop 0
	global_store_dwordx2 v[0:1], v[18:19], off
	s_cbranch_vccnz .LBB0_1997

.LBB0_1994:
	s_add_i32 s22, s4, 0xf2401100
	s_and_b32 s52, s22, 0x300
	s_add_u32 s24, s2, s52
	s_addc_u32 s25, s3, 0
	s_and_b64 s[22:23], s[26:27], exec
	s_cselect_b32 s23, s21, s25
	s_cselect_b32 s22, s50, s24
	s_mov_b64 s[24:25], s[22:23]
	s_mov_b32 m0, s34
	ds_read_b128 v[16:19], v217
	ds_read_b128 v[20:23], v218
	ds_read_b128 v[24:27], v225
	ds_read_b128 v[28:31], v226
	v_mov_b32_e32 v203, v197
	global_load_lds_dwordx4 v194, s[24:25]
	v_lshl_add_u64 v[236:237], s[24:25], 0, v[192:193]
	s_mov_b32 m0, s35
	s_add_u32 s24, s22, 0x80
	global_load_lds_dwordx4 v[236:237], off
	s_nop 0
	s_barrier
	s_waitcnt lgkmcnt(0)
	s_addc_u32 s25, s23, 0
	s_and_b64 s[26:27], s[26:27], exec
	s_cselect_b32 s27, 0, 0
	s_cselect_b32 s26, 0, s52
	s_setprio 1
	s_waitcnt lgkmcnt(0)
	v_mfma_scale_f32_16x16x128_f8f6f4 v[184:187], v[16:23], v[56:63], v[184:187], v212, v212 op_sel_hi:[0,0,0]
	v_mfma_scale_f32_16x16x128_f8f6f4 v[176:179], v[24:31], v[56:63], v[176:179], v212, v212 op_sel_hi:[0,0,0]
	v_mfma_scale_f32_16x16x128_f8f6f4 v[168:171], v[16:23], v[48:55], v[168:171], v212, v212 op_sel_hi:[0,0,0]
	v_mfma_scale_f32_16x16x128_f8f6f4 v[160:163], v[24:31], v[48:55], v[160:163], v212, v212 op_sel_hi:[0,0,0]
	v_mfma_scale_f32_16x16x128_f8f6f4 v[152:155], v[16:23], v[40:47], v[152:155], v212, v212 op_sel_hi:[0,0,0]
	v_mfma_scale_f32_16x16x128_f8f6f4 v[144:147], v[24:31], v[40:47], v[144:147], v212, v212 op_sel_hi:[0,0,0]
	v_mfma_scale_f32_16x16x128_f8f6f4 v[136:139], v[16:23], v[32:39], v[136:139], v212, v212 op_sel_hi:[0,0,0]
	v_mfma_scale_f32_16x16x128_f8f6f4 v[128:131], v[24:31], v[32:39], v[128:131], v212, v212 op_sel_hi:[0,0,0]
	s_setprio 0
	s_add_u32 s26, s6, s26
	s_addc_u32 s27, s7, s27
	s_mov_b64 s[52:53], s[26:27]
	s_mov_b32 m0, s1
	s_barrier
	ds_read_b128 v[32:35], v231 offset:16384
	ds_read_b128 v[40:43], v231 offset:18432
	ds_read_b128 v[36:39], v232 offset:16384
	ds_read_b128 v[44:47], v232 offset:18432
	ds_read_b128 v[48:51], v231 offset:20480
	ds_read_b128 v[56:59], v231 offset:22528
	ds_read_b128 v[52:55], v232 offset:20480
	ds_read_b128 v[60:63], v232 offset:22528
	s_nop 0
	global_load_lds_dwordx4 v198, s[52:53]
	s_mov_b32 m0, s36
	s_nop 0
	global_load_lds_dwordx4 v200, s[52:53]
	s_nop 0
	s_barrier
	s_waitcnt lgkmcnt(0)
	s_setprio 1
	s_waitcnt lgkmcnt(0)
	v_mfma_scale_f32_16x16x128_f8f6f4 v[124:127], v[0:7], v[32:39], v[124:127], v212, v212 op_sel_hi:[0,0,0]
	v_mfma_scale_f32_16x16x128_f8f6f4 v[116:119], v[8:15], v[32:39], v[116:119], v212, v212 op_sel_hi:[0,0,0]
	v_mfma_scale_f32_16x16x128_f8f6f4 v[108:111], v[0:7], v[40:47], v[108:111], v212, v212 op_sel_hi:[0,0,0]
	v_mfma_scale_f32_16x16x128_f8f6f4 v[100:103], v[8:15], v[40:47], v[100:103], v212, v212 op_sel_hi:[0,0,0]
	v_mfma_scale_f32_16x16x128_f8f6f4 v[92:95], v[0:7], v[48:55], v[92:95], v212, v212 op_sel_hi:[0,0,0]
	v_mfma_scale_f32_16x16x128_f8f6f4 v[84:87], v[8:15], v[48:55], v[84:87], v212, v212 op_sel_hi:[0,0,0]
	v_mfma_scale_f32_16x16x128_f8f6f4 v[76:79], v[0:7], v[56:63], v[76:79], v212, v212 op_sel_hi:[0,0,0]
	v_mfma_scale_f32_16x16x128_f8f6f4 v[68:71], v[8:15], v[56:63], v[68:71], v212, v212 op_sel_hi:[0,0,0]
	s_setprio 0
	s_barrier
	s_add_u32 s52, s22, 0x20000
	s_addc_u32 s53, s23, 0
	s_mov_b32 m0, s37
	s_nop 0
	global_load_lds_dwordx4 v194, s[52:53]
	s_mov_b32 m0, s38
	s_nop 0
	global_load_lds_dwordx4 v192, s[52:53]
	s_waitcnt vmcnt(6)
	s_barrier
	s_setprio 1
	v_mfma_scale_f32_16x16x128_f8f6f4 v[120:123], v[16:23], v[32:39], v[120:123], v212, v212 op_sel_hi:[0,0,0]
	v_mfma_scale_f32_16x16x128_f8f6f4 v[112:115], v[24:31], v[32:39], v[112:115], v212, v212 op_sel_hi:[0,0,0]
	v_mfma_scale_f32_16x16x128_f8f6f4 v[104:107], v[16:23], v[40:47], v[104:107], v212, v212 op_sel_hi:[0,0,0]
	v_mfma_scale_f32_16x16x128_f8f6f4 v[96:99], v[24:31], v[40:47], v[96:99], v212, v212 op_sel_hi:[0,0,0]
	v_mfma_scale_f32_16x16x128_f8f6f4 v[88:91], v[16:23], v[48:55], v[88:91], v212, v212 op_sel_hi:[0,0,0]
	v_mfma_scale_f32_16x16x128_f8f6f4 v[80:83], v[24:31], v[48:55], v[80:83], v212, v212 op_sel_hi:[0,0,0]
	v_mfma_scale_f32_16x16x128_f8f6f4 v[72:75], v[16:23], v[56:63], v[72:75], v212, v212 op_sel_hi:[0,0,0]
	v_mfma_scale_f32_16x16x128_f8f6f4 v[64:67], v[24:31], v[56:63], v[64:67], v212, v212 op_sel_hi:[0,0,0]
	s_setprio 0
	s_barrier
	ds_read_b128 v[0:3], v219
	ds_read_b128 v[4:7], v220
	ds_read_b128 v[8:11], v227
	ds_read_b128 v[12:15], v228
	s_mov_b64 s[52:53], s[26:27]
	s_mov_b32 m0, s39
	ds_read_b128 v[16:19], v231 offset:32768
	ds_read_b128 v[24:27], v231 offset:34816
	ds_read_b128 v[20:23], v232 offset:32768
	ds_read_b128 v[28:31], v232 offset:34816
	ds_read_b128 v[32:35], v231 offset:36864
	ds_read_b128 v[40:43], v231 offset:38912
	ds_read_b128 v[36:39], v232 offset:36864
	ds_read_b128 v[44:47], v232 offset:38912
	s_nop 0
	global_load_lds_dwordx4 v196, s[52:53]
	s_mov_b32 m0, s40
	s_nop 0
	global_load_lds_dwordx4 v202, s[52:53]
	s_waitcnt lgkmcnt(8)
	s_barrier
	s_waitcnt lgkmcnt(0)
	s_setprio 1
	s_waitcnt lgkmcnt(0)
	v_mfma_scale_f32_16x16x128_f8f6f4 v[188:191], v[0:7], v[16:23], v[188:191], v212, v212 op_sel_hi:[0,0,0]
	v_mfma_scale_f32_16x16x128_f8f6f4 v[180:183], v[8:15], v[16:23], v[180:183], v212, v212 op_sel_hi:[0,0,0]
	v_mfma_scale_f32_16x16x128_f8f6f4 v[172:175], v[0:7], v[24:31], v[172:175], v212, v212 op_sel_hi:[0,0,0]
	v_mfma_scale_f32_16x16x128_f8f6f4 v[164:167], v[8:15], v[24:31], v[164:167], v212, v212 op_sel_hi:[0,0,0]
	v_mfma_scale_f32_16x16x128_f8f6f4 v[156:159], v[0:7], v[32:39], v[156:159], v212, v212 op_sel_hi:[0,0,0]
	v_mfma_scale_f32_16x16x128_f8f6f4 v[148:151], v[8:15], v[32:39], v[148:151], v212, v212 op_sel_hi:[0,0,0]
	v_mfma_scale_f32_16x16x128_f8f6f4 v[140:143], v[0:7], v[40:47], v[140:143], v212, v212 op_sel_hi:[0,0,0]
	v_mfma_scale_f32_16x16x128_f8f6f4 v[132:135], v[8:15], v[40:47], v[132:135], v212, v212 op_sel_hi:[0,0,0]
	s_setprio 0
	s_barrier
	s_mov_b32 m0, s42
	ds_read_b128 v[48:51], v221
	ds_read_b128 v[52:55], v222
	ds_read_b128 v[56:59], v229
	ds_read_b128 v[60:63], v230
	s_nop 0
	global_load_lds_dwordx4 v194, s[24:25]
	s_mov_b32 m0, s43
	s_nop 0
	global_load_lds_dwordx4 v192, s[24:25]
	s_barrier
	s_waitcnt lgkmcnt(0)
	s_setprio 1
	s_waitcnt lgkmcnt(0)
	v_mfma_scale_f32_16x16x128_f8f6f4 v[184:187], v[48:55], v[16:23], v[184:187], v212, v212 op_sel_hi:[0,0,0]
	v_mfma_scale_f32_16x16x128_f8f6f4 v[176:179], v[56:63], v[16:23], v[176:179], v212, v212 op_sel_hi:[0,0,0]
	v_mfma_scale_f32_16x16x128_f8f6f4 v[168:171], v[48:55], v[24:31], v[168:171], v212, v212 op_sel_hi:[0,0,0]
	v_mfma_scale_f32_16x16x128_f8f6f4 v[160:163], v[56:63], v[24:31], v[160:163], v212, v212 op_sel_hi:[0,0,0]
	v_mfma_scale_f32_16x16x128_f8f6f4 v[152:155], v[48:55], v[32:39], v[152:155], v212, v212 op_sel_hi:[0,0,0]
	v_mfma_scale_f32_16x16x128_f8f6f4 v[144:147], v[56:63], v[32:39], v[144:147], v212, v212 op_sel_hi:[0,0,0]
	v_mfma_scale_f32_16x16x128_f8f6f4 v[136:139], v[48:55], v[40:47], v[136:139], v212, v212 op_sel_hi:[0,0,0]
	v_mfma_scale_f32_16x16x128_f8f6f4 v[128:131], v[56:63], v[40:47], v[128:131], v212, v212 op_sel_hi:[0,0,0]
	s_setprio 0
	s_add_u32 s24, s26, 0x80
	s_addc_u32 s25, s27, 0
	s_mov_b32 m0, s44
	s_barrier
	ds_read_b128 v[16:19], v231 offset:49152
	ds_read_b128 v[24:27], v231 offset:51200
	ds_read_b128 v[20:23], v232 offset:49152
	ds_read_b128 v[28:31], v232 offset:51200
	ds_read_b128 v[32:35], v231 offset:53248
	ds_read_b128 v[40:43], v231 offset:55296
	ds_read_b128 v[36:39], v232 offset:53248
	ds_read_b128 v[44:47], v232 offset:55296
	s_nop 0
	global_load_lds_dwordx4 v198, s[24:25]
	s_mov_b32 m0, s45
	s_nop 0
	global_load_lds_dwordx4 v200, s[24:25]
	s_nop 0
	s_barrier
	s_waitcnt lgkmcnt(0)
	s_setprio 1
	s_waitcnt lgkmcnt(0)
	v_mfma_scale_f32_16x16x128_f8f6f4 v[124:127], v[0:7], v[16:23], v[124:127], v212, v212 op_sel_hi:[0,0,0]
	v_mfma_scale_f32_16x16x128_f8f6f4 v[116:119], v[8:15], v[16:23], v[116:119], v212, v212 op_sel_hi:[0,0,0]
	v_mfma_scale_f32_16x16x128_f8f6f4 v[108:111], v[0:7], v[24:31], v[108:111], v212, v212 op_sel_hi:[0,0,0]
	v_mfma_scale_f32_16x16x128_f8f6f4 v[100:103], v[8:15], v[24:31], v[100:103], v212, v212 op_sel_hi:[0,0,0]
	v_mfma_scale_f32_16x16x128_f8f6f4 v[92:95], v[0:7], v[32:39], v[92:95], v212, v212 op_sel_hi:[0,0,0]
	v_mfma_scale_f32_16x16x128_f8f6f4 v[84:87], v[8:15], v[32:39], v[84:87], v212, v212 op_sel_hi:[0,0,0]
	v_mfma_scale_f32_16x16x128_f8f6f4 v[76:79], v[0:7], v[40:47], v[76:79], v212, v212 op_sel_hi:[0,0,0]
	v_mfma_scale_f32_16x16x128_f8f6f4 v[68:71], v[8:15], v[40:47], v[68:71], v212, v212 op_sel_hi:[0,0,0]
	s_setprio 0
	s_barrier
	s_add_u32 s22, s22, 0x20080
	s_addc_u32 s23, s23, 0
	s_mov_b32 m0, s46
	s_nop 0
	global_load_lds_dwordx4 v194, s[22:23]
	s_mov_b32 m0, s47
	s_nop 0
	global_load_lds_dwordx4 v192, s[22:23]
	s_waitcnt vmcnt(6)
	s_barrier
	s_setprio 1
	v_mfma_scale_f32_16x16x128_f8f6f4 v[120:123], v[48:55], v[16:23], v[120:123], v212, v212 op_sel_hi:[0,0,0]
	v_mfma_scale_f32_16x16x128_f8f6f4 v[112:115], v[56:63], v[16:23], v[112:115], v212, v212 op_sel_hi:[0,0,0]
	v_mfma_scale_f32_16x16x128_f8f6f4 v[104:107], v[48:55], v[24:31], v[104:107], v212, v212 op_sel_hi:[0,0,0]
	v_mfma_scale_f32_16x16x128_f8f6f4 v[96:99], v[56:63], v[24:31], v[96:99], v212, v212 op_sel_hi:[0,0,0]
	v_mfma_scale_f32_16x16x128_f8f6f4 v[88:91], v[48:55], v[32:39], v[88:91], v212, v212 op_sel_hi:[0,0,0]
	v_mfma_scale_f32_16x16x128_f8f6f4 v[80:83], v[56:63], v[32:39], v[80:83], v212, v212 op_sel_hi:[0,0,0]
	v_mfma_scale_f32_16x16x128_f8f6f4 v[72:75], v[48:55], v[40:47], v[72:75], v212, v212 op_sel_hi:[0,0,0]
	v_mfma_scale_f32_16x16x128_f8f6f4 v[64:67], v[56:63], v[40:47], v[64:67], v212, v212 op_sel_hi:[0,0,0]
	s_setprio 0
	s_add_i32 s51, s51, 2
	s_add_u32 s4, s4, 0x100
	s_addc_u32 s5, s5, 0
	s_cmp_gt_u32 s51, 5
	s_barrier
	s_cbranch_scc1 .LBB0_1990

.LBB0_2059:
	s_add_u32 s24, s28, 0x100
	ds_read_b128 v[0:3], v174
	ds_read_b128 v[4:7], v175
	ds_read_b128 v[8:11], v182
	ds_read_b128 v[12:15], v183
	s_addc_u32 s25, s29, 0
	s_and_b32 s57, s24, 0x300
	s_add_u32 s56, s2, s57
	s_addc_u32 s58, s3, 0
	s_cmp_eq_u32 s33, 4
	s_cselect_b64 s[30:31], -1, 0
	s_and_b64 s[26:27], s[30:31], exec
	s_cselect_b32 s27, s13, s58
	s_cselect_b32 s26, s19, s56
	s_cselect_b32 s56, 0, 0
	s_cselect_b32 s57, 0, s57
	s_add_u32 s28, s4, s28
	s_addc_u32 s29, s5, s29
	s_add_u32 s28, s28, 0x20080
	s_addc_u32 s29, s29, 0
	ds_read_b128 v[194:197], v190
	ds_read_b128 v[210:213], v190 offset:2048
	ds_read_b128 v[198:201], v191
	ds_read_b128 v[214:217], v191 offset:2048
	ds_read_b128 v[218:221], v190 offset:4096
	ds_read_b128 v[226:229], v190 offset:6144
	ds_read_b128 v[222:225], v191 offset:4096
	ds_read_b128 v[230:233], v191 offset:6144
	s_add_i32 m0, s1, 0xc000
	s_nop 0
	global_load_lds_dwordx4 v166, s[28:29]
	s_add_i32 m0, s1, 0xe000
	s_nop 0
	global_load_lds_dwordx4 v162, s[28:29]
	s_waitcnt lgkmcnt(8)
	s_barrier
	s_waitcnt lgkmcnt(0)
	s_setprio 1
	s_waitcnt lgkmcnt(0)
	v_mfma_scale_f32_16x16x128_f8f6f4 v[156:159], v[0:7], v[194:201], v[156:159], v173, v173 op_sel_hi:[0,0,0]
	v_mfma_scale_f32_16x16x128_f8f6f4 v[152:155], v[8:15], v[194:201], v[152:155], v173, v173 op_sel_hi:[0,0,0]
	v_mfma_scale_f32_16x16x128_f8f6f4 v[140:143], v[0:7], v[210:217], v[140:143], v173, v173 op_sel_hi:[0,0,0]
	v_mfma_scale_f32_16x16x128_f8f6f4 v[136:139], v[8:15], v[210:217], v[136:139], v173, v173 op_sel_hi:[0,0,0]
	v_mfma_scale_f32_16x16x128_f8f6f4 v[124:127], v[0:7], v[218:225], v[124:127], v173, v173 op_sel_hi:[0,0,0]
	v_mfma_scale_f32_16x16x128_f8f6f4 v[120:123], v[8:15], v[218:225], v[120:123], v173, v173 op_sel_hi:[0,0,0]
	v_mfma_scale_f32_16x16x128_f8f6f4 v[108:111], v[0:7], v[226:233], v[108:111], v173, v173 op_sel_hi:[0,0,0]
	v_mfma_scale_f32_16x16x128_f8f6f4 v[104:107], v[8:15], v[226:233], v[104:107], v173, v173 op_sel_hi:[0,0,0]
	s_setprio 0
	s_barrier
	s_mov_b64 s[28:29], s[26:27]
	s_mov_b32 m0, s23
	ds_read_b128 v[16:19], v176
	ds_read_b128 v[20:23], v177
	ds_read_b128 v[24:27], v184
	ds_read_b128 v[28:31], v185
	s_nop 0
	global_load_lds_dwordx4 v164, s[28:29]
	s_mov_b32 m0, s41
	s_nop 0
	global_load_lds_dwordx4 v160, s[28:29]
	s_nop 0
	s_barrier
	s_waitcnt lgkmcnt(0)
	s_setprio 1
	s_waitcnt lgkmcnt(0)
	v_mfma_scale_f32_16x16x128_f8f6f4 v[148:151], v[16:23], v[194:201], v[148:151], v173, v173 op_sel_hi:[0,0,0]
	v_mfma_scale_f32_16x16x128_f8f6f4 v[144:147], v[24:31], v[194:201], v[144:147], v173, v173 op_sel_hi:[0,0,0]
	v_mfma_scale_f32_16x16x128_f8f6f4 v[132:135], v[16:23], v[210:217], v[132:135], v173, v173 op_sel_hi:[0,0,0]
	v_mfma_scale_f32_16x16x128_f8f6f4 v[128:131], v[24:31], v[210:217], v[128:131], v173, v173 op_sel_hi:[0,0,0]
	v_mfma_scale_f32_16x16x128_f8f6f4 v[116:119], v[16:23], v[218:225], v[116:119], v173, v173 op_sel_hi:[0,0,0]
	v_mfma_scale_f32_16x16x128_f8f6f4 v[112:115], v[24:31], v[218:225], v[112:115], v173, v173 op_sel_hi:[0,0,0]
	v_mfma_scale_f32_16x16x128_f8f6f4 v[100:103], v[16:23], v[226:233], v[100:103], v173, v173 op_sel_hi:[0,0,0]
	v_mfma_scale_f32_16x16x128_f8f6f4 v[96:99], v[24:31], v[226:233], v[96:99], v173, v173 op_sel_hi:[0,0,0]
	s_setprio 0
	s_and_b64 s[28:29], s[16:17], s[30:31]
	s_and_b64 s[28:29], s[28:29], exec
	s_cselect_b32 s28, s6, s4
	s_cselect_b32 s29, s7, s5
	s_add_u32 s28, s28, s57
	s_addc_u32 s29, s29, s56
	s_mov_b64 s[30:31], s[28:29]
	s_mov_b32 m0, s1
	s_barrier
	ds_read_b128 v[194:197], v190 offset:16384
	ds_read_b128 v[210:213], v190 offset:18432
	ds_read_b128 v[198:201], v191 offset:16384
	ds_read_b128 v[214:217], v191 offset:18432
	ds_read_b128 v[218:221], v190 offset:20480
	ds_read_b128 v[226:229], v190 offset:22528
	ds_read_b128 v[222:225], v191 offset:20480
	ds_read_b128 v[230:233], v191 offset:22528
	s_nop 0
	global_load_lds_dwordx4 v166, s[30:31]
	s_mov_b32 m0, s42
	s_nop 0
	global_load_lds_dwordx4 v162, s[30:31]
	s_nop 0
	s_barrier
	s_waitcnt lgkmcnt(0)
	s_setprio 1
	s_waitcnt lgkmcnt(0)
	v_mfma_scale_f32_16x16x128_f8f6f4 v[92:95], v[0:7], v[194:201], v[92:95], v173, v173 op_sel_hi:[0,0,0]
	v_mfma_scale_f32_16x16x128_f8f6f4 v[88:91], v[8:15], v[194:201], v[88:91], v173, v173 op_sel_hi:[0,0,0]
	v_mfma_scale_f32_16x16x128_f8f6f4 v[76:79], v[0:7], v[210:217], v[76:79], v173, v173 op_sel_hi:[0,0,0]
	v_mfma_scale_f32_16x16x128_f8f6f4 v[72:75], v[8:15], v[210:217], v[72:75], v173, v173 op_sel_hi:[0,0,0]
	v_mfma_scale_f32_16x16x128_f8f6f4 v[60:63], v[0:7], v[218:225], v[60:63], v173, v173 op_sel_hi:[0,0,0]
	v_mfma_scale_f32_16x16x128_f8f6f4 v[56:59], v[8:15], v[218:225], v[56:59], v173, v173 op_sel_hi:[0,0,0]
	v_mfma_scale_f32_16x16x128_f8f6f4 v[44:47], v[0:7], v[226:233], v[44:47], v173, v173 op_sel_hi:[0,0,0]
	v_mfma_scale_f32_16x16x128_f8f6f4 v[40:43], v[8:15], v[226:233], v[40:43], v173, v173 op_sel_hi:[0,0,0]
	s_setprio 0
	s_barrier
	s_add_u32 s30, s26, 0x20000
	s_addc_u32 s31, s27, 0
	s_mov_b32 m0, s43
	s_nop 0
	global_load_lds_dwordx4 v164, s[30:31]
	s_mov_b32 m0, s44
	s_nop 0
	global_load_lds_dwordx4 v160, s[30:31]
	s_waitcnt vmcnt(6)
	s_barrier
	s_setprio 1
	v_mfma_scale_f32_16x16x128_f8f6f4 v[84:87], v[16:23], v[194:201], v[84:87], v173, v173 op_sel_hi:[0,0,0]
	v_mfma_scale_f32_16x16x128_f8f6f4 v[80:83], v[24:31], v[194:201], v[80:83], v173, v173 op_sel_hi:[0,0,0]
	v_mfma_scale_f32_16x16x128_f8f6f4 v[68:71], v[16:23], v[210:217], v[68:71], v173, v173 op_sel_hi:[0,0,0]
	v_mfma_scale_f32_16x16x128_f8f6f4 v[64:67], v[24:31], v[210:217], v[64:67], v173, v173 op_sel_hi:[0,0,0]
	v_mfma_scale_f32_16x16x128_f8f6f4 v[52:55], v[16:23], v[218:225], v[52:55], v173, v173 op_sel_hi:[0,0,0]
	v_mfma_scale_f32_16x16x128_f8f6f4 v[48:51], v[24:31], v[218:225], v[48:51], v173, v173 op_sel_hi:[0,0,0]
	v_mfma_scale_f32_16x16x128_f8f6f4 v[36:39], v[16:23], v[226:233], v[36:39], v173, v173 op_sel_hi:[0,0,0]
	v_mfma_scale_f32_16x16x128_f8f6f4 v[32:35], v[24:31], v[226:233], v[32:35], v173, v173 op_sel_hi:[0,0,0]
	s_setprio 0
	s_barrier
	ds_read_b128 v[0:3], v178
	ds_read_b128 v[4:7], v179
	ds_read_b128 v[8:11], v186
	ds_read_b128 v[12:15], v187
	s_add_u32 s30, s28, 0x20000
	s_addc_u32 s31, s29, 0
	s_mov_b32 m0, s45
	ds_read_b128 v[16:19], v190 offset:32768
	ds_read_b128 v[24:27], v190 offset:34816
	ds_read_b128 v[20:23], v191 offset:32768
	ds_read_b128 v[28:31], v191 offset:34816
	ds_read_b128 v[194:197], v190 offset:36864
	ds_read_b128 v[210:213], v190 offset:38912
	ds_read_b128 v[198:201], v191 offset:36864
	ds_read_b128 v[214:217], v191 offset:38912
	s_nop 0
	global_load_lds_dwordx4 v166, s[30:31]
	s_mov_b32 m0, s46
	s_nop 0
	global_load_lds_dwordx4 v162, s[30:31]
	s_waitcnt lgkmcnt(8)
	s_barrier
	s_waitcnt lgkmcnt(0)
	s_setprio 1
	s_waitcnt lgkmcnt(0)
	v_mfma_scale_f32_16x16x128_f8f6f4 v[156:159], v[0:7], v[16:23], v[156:159], v173, v173 op_sel_hi:[0,0,0]
	v_mfma_scale_f32_16x16x128_f8f6f4 v[152:155], v[8:15], v[16:23], v[152:155], v173, v173 op_sel_hi:[0,0,0]
	v_mfma_scale_f32_16x16x128_f8f6f4 v[140:143], v[0:7], v[24:31], v[140:143], v173, v173 op_sel_hi:[0,0,0]
	v_mfma_scale_f32_16x16x128_f8f6f4 v[136:139], v[8:15], v[24:31], v[136:139], v173, v173 op_sel_hi:[0,0,0]
	v_mfma_scale_f32_16x16x128_f8f6f4 v[124:127], v[0:7], v[194:201], v[124:127], v173, v173 op_sel_hi:[0,0,0]
	v_mfma_scale_f32_16x16x128_f8f6f4 v[120:123], v[8:15], v[194:201], v[120:123], v173, v173 op_sel_hi:[0,0,0]
	v_mfma_scale_f32_16x16x128_f8f6f4 v[108:111], v[0:7], v[210:217], v[108:111], v173, v173 op_sel_hi:[0,0,0]
	v_mfma_scale_f32_16x16x128_f8f6f4 v[104:107], v[8:15], v[210:217], v[104:107], v173, v173 op_sel_hi:[0,0,0]
	s_setprio 0
	s_barrier
	s_add_u32 s30, s26, 0x80
	s_addc_u32 s31, s27, 0
	s_mov_b32 m0, s48
	ds_read_b128 v[218:221], v180
	ds_read_b128 v[222:225], v181
	ds_read_b128 v[226:229], v188
	ds_read_b128 v[230:233], v189
	s_nop 0
	global_load_lds_dwordx4 v164, s[30:31]
	s_mov_b32 m0, s49
	s_nop 0
	global_load_lds_dwordx4 v160, s[30:31]
	s_nop 0
	s_barrier
	s_waitcnt lgkmcnt(0)
	s_setprio 1
	s_waitcnt lgkmcnt(0)
	v_mfma_scale_f32_16x16x128_f8f6f4 v[148:151], v[218:225], v[16:23], v[148:151], v173, v173 op_sel_hi:[0,0,0]
	v_mfma_scale_f32_16x16x128_f8f6f4 v[144:147], v[226:233], v[16:23], v[144:147], v173, v173 op_sel_hi:[0,0,0]
	v_mfma_scale_f32_16x16x128_f8f6f4 v[132:135], v[218:225], v[24:31], v[132:135], v173, v173 op_sel_hi:[0,0,0]
	v_mfma_scale_f32_16x16x128_f8f6f4 v[128:131], v[226:233], v[24:31], v[128:131], v173, v173 op_sel_hi:[0,0,0]
	v_mfma_scale_f32_16x16x128_f8f6f4 v[116:119], v[218:225], v[194:201], v[116:119], v173, v173 op_sel_hi:[0,0,0]
	v_mfma_scale_f32_16x16x128_f8f6f4 v[112:115], v[226:233], v[194:201], v[112:115], v173, v173 op_sel_hi:[0,0,0]
	v_mfma_scale_f32_16x16x128_f8f6f4 v[100:103], v[218:225], v[210:217], v[100:103], v173, v173 op_sel_hi:[0,0,0]
	v_mfma_scale_f32_16x16x128_f8f6f4 v[96:99], v[226:233], v[210:217], v[96:99], v173, v173 op_sel_hi:[0,0,0]
	s_setprio 0
	s_add_u32 s28, s28, 0x80
	s_addc_u32 s29, s29, 0
	s_mov_b32 m0, s50
	s_barrier
	ds_read_b128 v[16:19], v190 offset:49152
	ds_read_b128 v[24:27], v190 offset:51200
	ds_read_b128 v[20:23], v191 offset:49152
	ds_read_b128 v[28:31], v191 offset:51200
	ds_read_b128 v[194:197], v190 offset:53248
	ds_read_b128 v[210:213], v190 offset:55296
	ds_read_b128 v[198:201], v191 offset:53248
	ds_read_b128 v[214:217], v191 offset:55296
	s_nop 0
	global_load_lds_dwordx4 v166, s[28:29]
	s_mov_b32 m0, s51
	s_nop 0
	global_load_lds_dwordx4 v162, s[28:29]
	s_nop 0
	s_barrier
	s_waitcnt lgkmcnt(0)
	s_setprio 1
	s_waitcnt lgkmcnt(0)
	v_mfma_scale_f32_16x16x128_f8f6f4 v[92:95], v[0:7], v[16:23], v[92:95], v173, v173 op_sel_hi:[0,0,0]
	v_mfma_scale_f32_16x16x128_f8f6f4 v[88:91], v[8:15], v[16:23], v[88:91], v173, v173 op_sel_hi:[0,0,0]
	v_mfma_scale_f32_16x16x128_f8f6f4 v[76:79], v[0:7], v[24:31], v[76:79], v173, v173 op_sel_hi:[0,0,0]
	v_mfma_scale_f32_16x16x128_f8f6f4 v[72:75], v[8:15], v[24:31], v[72:75], v173, v173 op_sel_hi:[0,0,0]
	v_mfma_scale_f32_16x16x128_f8f6f4 v[60:63], v[0:7], v[194:201], v[60:63], v173, v173 op_sel_hi:[0,0,0]
	v_mfma_scale_f32_16x16x128_f8f6f4 v[56:59], v[8:15], v[194:201], v[56:59], v173, v173 op_sel_hi:[0,0,0]
	v_mfma_scale_f32_16x16x128_f8f6f4 v[44:47], v[0:7], v[210:217], v[44:47], v173, v173 op_sel_hi:[0,0,0]
	v_mfma_scale_f32_16x16x128_f8f6f4 v[40:43], v[8:15], v[210:217], v[40:43], v173, v173 op_sel_hi:[0,0,0]
	s_setprio 0
	s_barrier
	s_add_u32 s26, s26, 0x20080
	s_addc_u32 s27, s27, 0
	s_mov_b32 m0, s52
	s_nop 0
	global_load_lds_dwordx4 v164, s[26:27]
	s_mov_b32 m0, s53
	s_nop 0
	global_load_lds_dwordx4 v160, s[26:27]
	s_waitcnt vmcnt(6)
	s_barrier
	s_setprio 1
	v_mfma_scale_f32_16x16x128_f8f6f4 v[84:87], v[218:225], v[16:23], v[84:87], v173, v173 op_sel_hi:[0,0,0]
	v_mfma_scale_f32_16x16x128_f8f6f4 v[80:83], v[226:233], v[16:23], v[80:83], v173, v173 op_sel_hi:[0,0,0]
	v_mfma_scale_f32_16x16x128_f8f6f4 v[68:71], v[218:225], v[24:31], v[68:71], v173, v173 op_sel_hi:[0,0,0]
	v_mfma_scale_f32_16x16x128_f8f6f4 v[64:67], v[226:233], v[24:31], v[64:67], v173, v173 op_sel_hi:[0,0,0]
	v_mfma_scale_f32_16x16x128_f8f6f4 v[52:55], v[218:225], v[194:201], v[52:55], v173, v173 op_sel_hi:[0,0,0]
	v_mfma_scale_f32_16x16x128_f8f6f4 v[48:51], v[226:233], v[194:201], v[48:51], v173, v173 op_sel_hi:[0,0,0]
	v_mfma_scale_f32_16x16x128_f8f6f4 v[36:39], v[218:225], v[210:217], v[36:39], v173, v173 op_sel_hi:[0,0,0]
	v_mfma_scale_f32_16x16x128_f8f6f4 v[32:35], v[226:233], v[210:217], v[32:35], v173, v173 op_sel_hi:[0,0,0]
	s_setprio 0
	s_add_i32 s33, s33, 2
	s_cmp_gt_u32 s33, 5
	s_mov_b64 s[28:29], s[24:25]
	s_barrier
	s_cbranch_scc0 .LBB0_2059
	v_mov_b32_e32 v0, v172
	s_ashr_i32 s2, s0, 31
	v_ashrrev_i32_e32 v1, 2, v0
	v_and_b32_e32 v1, 0xffffffc0, v1
	v_lshl_add_u32 v1, s22, 8, v1
	v_and_or_b32 v6, v0, 15, v1
	v_ashrrev_i32_e32 v7, 31, v6
	v_lshl_add_u64 v[2:3], v[6:7], 2, s[8:9]
	global_load_dword v14, v[2:3], off
	global_load_dword v194, v[2:3], off offset:64
	global_load_dword v195, v[2:3], off offset:128
	global_load_dword v196, v[2:3], off offset:192
	global_load_dword v197, v[2:3], off offset:512
	global_load_dword v198, v[2:3], off offset:576
	global_load_dword v199, v[2:3], off offset:640
	global_load_dword v200, v[2:3], off offset:704
	s_lshr_b32 s2, s2, 30
	s_add_i32 s2, s0, s2
	v_lshrrev_b32_e32 v0, 1, v0
	s_and_b32 s2, s2, 0xfffffc
	v_and_b32_e32 v0, 0x78, v0
	s_sub_i32 s0, s0, s2
	v_lshl_or_b32 v4, s0, 8, v0
	v_lshlrev_b64 v[0:1], 10, v[6:7]
	v_mov_b32_e32 v8, 0
	v_mov_b32_e32 v9, 0
	v_mov_b32_e32 v10, 0
	v_mov_b32_e32 v11, 0
	v_ashrrev_i32_e32 v5, 31, v4
	v_or_b32_e32 v12, 16, v6
	v_lshl_add_u64 v[0:1], s[10:11], 0, v[0:1]
	v_ashrrev_i32_e32 v13, 31, v12
	v_lshl_add_u64 v[0:1], v[0:1], 0, v[4:5]
	s_mov_b32 s0, 0x20000
	s_mov_b64 s[2:3], 0x20000
	s_mov_b64 s[4:5], s[6:7]
	s_mov_b64 s[6:7], 0x2c000
	s_mov_b32 s13, 0x2c000
	s_mov_b32 s22, s12
	s_waitcnt vmcnt(0)
	v_mul_f32_e32 v7, 0x3d000000, v14
	v_mul_f32_e32 v14, 0x42000000, v7
	v_pk_mul_f32 v[18:19], v[156:157], v[14:15] op_sel_hi:[1,0]
	v_pk_mul_f32 v[22:23], v[152:153], v[14:15] op_sel_hi:[1,0]
	v_pk_mul_f32 v[16:17], v[158:159], v[14:15] op_sel_hi:[1,0]
	v_pk_mul_f32 v[20:21], v[154:155], v[14:15] op_sel_hi:[1,0]
	v_pk_mul_f32 v[24:25], v[150:151], v[14:15] op_sel_hi:[1,0]
	v_pk_mul_f32 v[26:27], v[148:149], v[14:15] op_sel_hi:[1,0]
	v_pk_mul_f32 v[28:29], v[146:147], v[14:15] op_sel_hi:[1,0]
	v_pk_mul_f32 v[14:15], v[144:145], v[14:15] op_sel_hi:[1,0]
	v_med3_f32 v7, v18, s55, v192
	v_med3_f32 v18, v22, s55, v192
	v_med3_f32 v19, v19, s55, v192
	v_med3_f32 v22, v23, s55, v192
	v_med3_f32 v23, v26, s55, v192
	v_med3_f32 v14, v14, s55, v192
	v_med3_f32 v26, v27, s55, v192
	v_med3_f32 v15, v15, s55, v192
	v_cvt_pk_fp8_f32 v8, v7, v19
	v_cvt_pk_fp8_f32 v9, v18, v22
	v_cvt_pk_fp8_f32 v10, v23, v26
	v_cvt_pk_fp8_f32 v11, v14, v15
	v_med3_f32 v16, v16, s55, v192
	v_med3_f32 v20, v20, s55, v192
	v_med3_f32 v17, v17, s55, v192
	v_med3_f32 v21, v21, s55, v192
	v_med3_f32 v24, v24, s55, v192
	v_med3_f32 v27, v28, s55, v192
	v_med3_f32 v25, v25, s55, v192
	v_med3_f32 v28, v29, s55, v192
	v_cvt_pk_fp8_f32 v8, v16, v17 op_sel:[0,0,1]
	v_cvt_pk_fp8_f32 v9, v20, v21 op_sel:[0,0,1]
	v_cvt_pk_fp8_f32 v10, v24, v25 op_sel:[0,0,1]
	v_cvt_pk_fp8_f32 v11, v27, v28 op_sel:[0,0,1]
	v_lshl_add_u64 v[14:15], v[12:13], 2, s[8:9]
	global_store_dwordx2 v[0:1], v[8:9], off
	global_store_dwordx2 v[0:1], v[10:11], off offset:128
	v_mov_b32_e32 v8, 0
	v_mov_b32_e32 v9, 0
	v_mov_b32_e32 v10, 0
	v_mov_b32_e32 v11, 0
	v_lshlrev_b64 v[12:13], 10, v[12:13]
	v_or_b32_e32 v14, 32, v6
	v_lshl_add_u64 v[12:13], s[10:11], 0, v[12:13]
	v_ashrrev_i32_e32 v15, 31, v14
	v_lshl_add_u64 v[12:13], v[12:13], 0, v[4:5]
	v_lshl_add_u64 v[16:17], v[14:15], 2, s[8:9]
	v_or_b32_e32 v6, 48, v6
	v_mul_f32_e32 v7, 0x3d000000, v194
	v_mul_f32_e32 v18, 0x42000000, v7
	v_pk_mul_f32 v[22:23], v[140:141], v[18:19] op_sel_hi:[1,0]
	v_pk_mul_f32 v[26:27], v[136:137], v[18:19] op_sel_hi:[1,0]
	v_pk_mul_f32 v[20:21], v[142:143], v[18:19] op_sel_hi:[1,0]
	v_pk_mul_f32 v[24:25], v[138:139], v[18:19] op_sel_hi:[1,0]
	v_pk_mul_f32 v[28:29], v[134:135], v[18:19] op_sel_hi:[1,0]
	v_pk_mul_f32 v[30:31], v[132:133], v[18:19] op_sel_hi:[1,0]
	v_pk_mul_f32 v[130:131], v[130:131], v[18:19] op_sel_hi:[1,0]
	v_pk_mul_f32 v[18:19], v[128:129], v[18:19] op_sel_hi:[1,0]
	v_med3_f32 v7, v22, s55, v192
	v_med3_f32 v22, v26, s55, v192
	v_med3_f32 v23, v23, s55, v192
	v_med3_f32 v26, v27, s55, v192
	v_med3_f32 v27, v30, s55, v192
	v_med3_f32 v18, v18, s55, v192
	v_med3_f32 v30, v31, s55, v192
	v_med3_f32 v19, v19, s55, v192
	v_cvt_pk_fp8_f32 v8, v7, v23
	v_cvt_pk_fp8_f32 v9, v22, v26
	v_cvt_pk_fp8_f32 v10, v27, v30
	v_cvt_pk_fp8_f32 v11, v18, v19
	v_med3_f32 v20, v20, s55, v192
	v_med3_f32 v24, v24, s55, v192
	v_med3_f32 v21, v21, s55, v192
	v_med3_f32 v25, v25, s55, v192
	v_med3_f32 v28, v28, s55, v192
	v_med3_f32 v31, v130, s55, v192
	v_med3_f32 v29, v29, s55, v192
	v_med3_f32 v128, v131, s55, v192
	v_cvt_pk_fp8_f32 v8, v20, v21 op_sel:[0,0,1]
	v_cvt_pk_fp8_f32 v9, v24, v25 op_sel:[0,0,1]
	v_cvt_pk_fp8_f32 v10, v28, v29 op_sel:[0,0,1]
	v_cvt_pk_fp8_f32 v11, v31, v128 op_sel:[0,0,1]
	global_store_dwordx2 v[12:13], v[8:9], off
	global_store_dwordx2 v[12:13], v[10:11], off offset:128
	v_mov_b32_e32 v8, 0
	v_mov_b32_e32 v9, 0
	v_mov_b32_e32 v10, 0
	v_mov_b32_e32 v11, 0
	v_lshlrev_b64 v[12:13], 10, v[14:15]
	v_lshl_add_u64 v[12:13], s[10:11], 0, v[12:13]
	v_ashrrev_i32_e32 v7, 31, v6
	v_lshl_add_u64 v[12:13], v[12:13], 0, v[4:5]
	v_lshl_add_u64 v[14:15], v[6:7], 2, s[8:9]
	v_lshlrev_b64 v[6:7], 10, v[6:7]
	v_lshl_add_u64 v[6:7], s[10:11], 0, v[6:7]
	v_lshl_add_u64 v[4:5], v[6:7], 0, v[4:5]
	v_mov_b32_e32 v6, 0
	v_mov_b32_e32 v7, 0
	v_mul_f32_e32 v16, 0x3d000000, v195
	v_mul_f32_e32 v16, 0x42000000, v16
	v_pk_mul_f32 v[20:21], v[124:125], v[16:17] op_sel_hi:[1,0]
	v_pk_mul_f32 v[24:25], v[120:121], v[16:17] op_sel_hi:[1,0]
	v_pk_mul_f32 v[18:19], v[126:127], v[16:17] op_sel_hi:[1,0]
	v_pk_mul_f32 v[22:23], v[122:123], v[16:17] op_sel_hi:[1,0]
	v_pk_mul_f32 v[26:27], v[118:119], v[16:17] op_sel_hi:[1,0]
	v_pk_mul_f32 v[28:29], v[116:117], v[16:17] op_sel_hi:[1,0]
	v_pk_mul_f32 v[30:31], v[114:115], v[16:17] op_sel_hi:[1,0]
	v_pk_mul_f32 v[16:17], v[112:113], v[16:17] op_sel_hi:[1,0]
	v_med3_f32 v20, v20, s55, v192
	v_med3_f32 v24, v24, s55, v192
	v_med3_f32 v21, v21, s55, v192
	v_med3_f32 v25, v25, s55, v192
	v_med3_f32 v28, v28, s55, v192
	v_med3_f32 v16, v16, s55, v192
	v_med3_f32 v29, v29, s55, v192
	v_med3_f32 v17, v17, s55, v192
	v_cvt_pk_fp8_f32 v8, v20, v21
	v_cvt_pk_fp8_f32 v9, v24, v25
	v_cvt_pk_fp8_f32 v10, v28, v29
	v_cvt_pk_fp8_f32 v11, v16, v17
	v_med3_f32 v18, v18, s55, v192
	v_med3_f32 v22, v22, s55, v192
	v_med3_f32 v19, v19, s55, v192
	v_med3_f32 v23, v23, s55, v192
	v_med3_f32 v26, v26, s55, v192
	v_med3_f32 v30, v30, s55, v192
	v_med3_f32 v27, v27, s55, v192
	v_med3_f32 v31, v31, s55, v192
	v_cvt_pk_fp8_f32 v8, v18, v19 op_sel:[0,0,1]
	v_cvt_pk_fp8_f32 v9, v22, v23 op_sel:[0,0,1]
	v_cvt_pk_fp8_f32 v10, v26, v27 op_sel:[0,0,1]
	v_cvt_pk_fp8_f32 v11, v30, v31 op_sel:[0,0,1]
	global_store_dwordx2 v[12:13], v[8:9], off
	global_store_dwordx2 v[12:13], v[10:11], off offset:128
	v_mov_b32_e32 v8, 0
	v_mov_b32_e32 v9, 0
	v_mov_b32_e32 v10, 0
	v_mov_b32_e32 v11, 0
	v_mul_f32_e32 v12, 0x3d000000, v196
	v_mul_f32_e32 v12, 0x42000000, v12
	v_pk_mul_f32 v[16:17], v[108:109], v[12:13] op_sel_hi:[1,0]
	v_pk_mul_f32 v[20:21], v[104:105], v[12:13] op_sel_hi:[1,0]
	v_pk_mul_f32 v[14:15], v[110:111], v[12:13] op_sel_hi:[1,0]
	v_pk_mul_f32 v[18:19], v[106:107], v[12:13] op_sel_hi:[1,0]
	v_pk_mul_f32 v[22:23], v[102:103], v[12:13] op_sel_hi:[1,0]
	v_pk_mul_f32 v[24:25], v[100:101], v[12:13] op_sel_hi:[1,0]
	v_pk_mul_f32 v[26:27], v[98:99], v[12:13] op_sel_hi:[1,0]
	v_pk_mul_f32 v[12:13], v[96:97], v[12:13] op_sel_hi:[1,0]
	v_med3_f32 v16, v16, s55, v192
	v_med3_f32 v20, v20, s55, v192
	v_med3_f32 v17, v17, s55, v192
	v_med3_f32 v21, v21, s55, v192
	v_med3_f32 v24, v24, s55, v192
	v_med3_f32 v12, v12, s55, v192
	v_med3_f32 v25, v25, s55, v192
	v_med3_f32 v13, v13, s55, v192
	v_cvt_pk_fp8_f32 v8, v16, v17
	v_cvt_pk_fp8_f32 v9, v20, v21
	v_cvt_pk_fp8_f32 v10, v24, v25
	v_cvt_pk_fp8_f32 v11, v12, v13
	v_med3_f32 v14, v14, s55, v192
	v_med3_f32 v18, v18, s55, v192
	v_med3_f32 v15, v15, s55, v192
	v_med3_f32 v19, v19, s55, v192
	v_med3_f32 v22, v22, s55, v192
	v_med3_f32 v26, v26, s55, v192
	v_med3_f32 v23, v23, s55, v192
	v_med3_f32 v27, v27, s55, v192
	v_cvt_pk_fp8_f32 v8, v14, v15 op_sel:[0,0,1]
	v_cvt_pk_fp8_f32 v9, v18, v19 op_sel:[0,0,1]
	v_cvt_pk_fp8_f32 v10, v22, v23 op_sel:[0,0,1]
	v_cvt_pk_fp8_f32 v11, v26, v27 op_sel:[0,0,1]
	global_store_dwordx2 v[4:5], v[8:9], off
	global_store_dwordx2 v[4:5], v[10:11], off offset:128
	v_mov_b32_e32 v4, 0
	v_mov_b32_e32 v5, 0
	v_lshl_add_u64 v[8:9], v[0:1], 0, s[2:3]
	s_mov_b64 s[2:3], 0x24000
	v_mul_f32_e32 v10, 0x3d000000, v197
	v_mul_f32_e32 v10, 0x42000000, v10
	v_pk_mul_f32 v[14:15], v[92:93], v[10:11] op_sel_hi:[1,0]
	v_pk_mul_f32 v[18:19], v[88:89], v[10:11] op_sel_hi:[1,0]
	v_pk_mul_f32 v[12:13], v[94:95], v[10:11] op_sel_hi:[1,0]
	v_pk_mul_f32 v[16:17], v[90:91], v[10:11] op_sel_hi:[1,0]
	v_pk_mul_f32 v[20:21], v[86:87], v[10:11] op_sel_hi:[1,0]
	v_pk_mul_f32 v[22:23], v[84:85], v[10:11] op_sel_hi:[1,0]
	v_pk_mul_f32 v[24:25], v[82:83], v[10:11] op_sel_hi:[1,0]
	v_pk_mul_f32 v[10:11], v[80:81], v[10:11] op_sel_hi:[1,0]
	v_med3_f32 v14, v14, s55, v192
	v_med3_f32 v18, v18, s55, v192
	v_med3_f32 v15, v15, s55, v192
	v_med3_f32 v19, v19, s55, v192
	v_med3_f32 v22, v22, s55, v192
	v_med3_f32 v10, v10, s55, v192
	v_med3_f32 v23, v23, s55, v192
	v_med3_f32 v11, v11, s55, v192
	v_cvt_pk_fp8_f32 v4, v14, v15
	v_cvt_pk_fp8_f32 v5, v18, v19
	v_cvt_pk_fp8_f32 v6, v22, v23
	v_cvt_pk_fp8_f32 v7, v10, v11
	v_med3_f32 v12, v12, s55, v192
	v_med3_f32 v16, v16, s55, v192
	v_med3_f32 v13, v13, s55, v192
	v_med3_f32 v17, v17, s55, v192
	v_med3_f32 v20, v20, s55, v192
	v_med3_f32 v24, v24, s55, v192
	v_med3_f32 v21, v21, s55, v192
	v_med3_f32 v25, v25, s55, v192
	v_cvt_pk_fp8_f32 v4, v12, v13 op_sel:[0,0,1]
	v_cvt_pk_fp8_f32 v5, v16, v17 op_sel:[0,0,1]
	v_cvt_pk_fp8_f32 v6, v20, v21 op_sel:[0,0,1]
	v_cvt_pk_fp8_f32 v7, v24, v25 op_sel:[0,0,1]
	v_add_co_u32_e32 v10, vcc, s0, v0
	s_mov_b32 s0, 0x24000
	s_nop 0
	v_addc_co_u32_e32 v11, vcc, 0, v1, vcc
	global_store_dwordx2 v[10:11], v[4:5], off
	global_store_dwordx2 v[8:9], v[6:7], off offset:128
	v_mov_b32_e32 v4, 0
	v_mov_b32_e32 v5, 0
	v_mov_b32_e32 v6, 0
	v_mov_b32_e32 v7, 0
	v_lshl_add_u64 v[8:9], v[0:1], 0, s[2:3]
	s_mov_b64 s[2:3], 0x28000
	v_mul_f32_e32 v10, 0x3d000000, v198
	v_mul_f32_e32 v10, 0x42000000, v10
	v_pk_mul_f32 v[14:15], v[76:77], v[10:11] op_sel_hi:[1,0]
	v_pk_mul_f32 v[18:19], v[72:73], v[10:11] op_sel_hi:[1,0]
	v_pk_mul_f32 v[12:13], v[78:79], v[10:11] op_sel_hi:[1,0]
	v_pk_mul_f32 v[16:17], v[74:75], v[10:11] op_sel_hi:[1,0]
	v_pk_mul_f32 v[20:21], v[70:71], v[10:11] op_sel_hi:[1,0]
	v_pk_mul_f32 v[22:23], v[68:69], v[10:11] op_sel_hi:[1,0]
	v_pk_mul_f32 v[24:25], v[66:67], v[10:11] op_sel_hi:[1,0]
	v_pk_mul_f32 v[10:11], v[64:65], v[10:11] op_sel_hi:[1,0]
	v_med3_f32 v14, v14, s55, v192
	v_med3_f32 v18, v18, s55, v192
	v_med3_f32 v15, v15, s55, v192
	v_med3_f32 v19, v19, s55, v192
	v_med3_f32 v22, v22, s55, v192
	v_med3_f32 v10, v10, s55, v192
	v_med3_f32 v23, v23, s55, v192
	v_med3_f32 v11, v11, s55, v192
	v_cvt_pk_fp8_f32 v4, v14, v15
	v_cvt_pk_fp8_f32 v5, v18, v19
	v_cvt_pk_fp8_f32 v6, v22, v23
	v_cvt_pk_fp8_f32 v7, v10, v11
	v_med3_f32 v12, v12, s55, v192
	v_med3_f32 v16, v16, s55, v192
	v_med3_f32 v13, v13, s55, v192
	v_med3_f32 v17, v17, s55, v192
	v_med3_f32 v20, v20, s55, v192
	v_med3_f32 v24, v24, s55, v192
	v_med3_f32 v21, v21, s55, v192
	v_med3_f32 v25, v25, s55, v192
	v_cvt_pk_fp8_f32 v4, v12, v13 op_sel:[0,0,1]
	v_cvt_pk_fp8_f32 v5, v16, v17 op_sel:[0,0,1]
	v_cvt_pk_fp8_f32 v6, v20, v21 op_sel:[0,0,1]
	v_cvt_pk_fp8_f32 v7, v24, v25 op_sel:[0,0,1]
	v_add_co_u32_e32 v10, vcc, s0, v0
	s_mov_b32 s0, 0x28000
	s_nop 0
	v_addc_co_u32_e32 v11, vcc, 0, v1, vcc
	global_store_dwordx2 v[10:11], v[4:5], off
	global_store_dwordx2 v[8:9], v[6:7], off offset:128
	v_mov_b32_e32 v4, 0
	v_mov_b32_e32 v5, 0
	v_mov_b32_e32 v6, 0
	v_mov_b32_e32 v7, 0
	v_lshl_add_u64 v[8:9], v[0:1], 0, s[2:3]
	s_mov_b64 s[2:3], s[20:21]
	v_mul_f32_e32 v10, 0x3d000000, v199
	v_mul_f32_e32 v10, 0x42000000, v10
	v_pk_mul_f32 v[14:15], v[60:61], v[10:11] op_sel_hi:[1,0]
	v_pk_mul_f32 v[18:19], v[56:57], v[10:11] op_sel_hi:[1,0]
	v_pk_mul_f32 v[12:13], v[62:63], v[10:11] op_sel_hi:[1,0]
	v_pk_mul_f32 v[16:17], v[58:59], v[10:11] op_sel_hi:[1,0]
	v_pk_mul_f32 v[20:21], v[54:55], v[10:11] op_sel_hi:[1,0]
	v_pk_mul_f32 v[22:23], v[52:53], v[10:11] op_sel_hi:[1,0]
	v_pk_mul_f32 v[24:25], v[50:51], v[10:11] op_sel_hi:[1,0]
	v_pk_mul_f32 v[10:11], v[48:49], v[10:11] op_sel_hi:[1,0]
	v_med3_f32 v14, v14, s55, v192
	v_med3_f32 v18, v18, s55, v192
	v_med3_f32 v15, v15, s55, v192
	v_med3_f32 v19, v19, s55, v192
	v_med3_f32 v22, v22, s55, v192
	v_med3_f32 v10, v10, s55, v192
	v_med3_f32 v23, v23, s55, v192
	v_med3_f32 v11, v11, s55, v192
	v_cvt_pk_fp8_f32 v4, v14, v15
	v_cvt_pk_fp8_f32 v5, v18, v19
	v_cvt_pk_fp8_f32 v6, v22, v23
	v_cvt_pk_fp8_f32 v7, v10, v11
	v_med3_f32 v12, v12, s55, v192
	v_med3_f32 v16, v16, s55, v192
	v_med3_f32 v13, v13, s55, v192
	v_med3_f32 v17, v17, s55, v192
	v_med3_f32 v20, v20, s55, v192
	v_med3_f32 v24, v24, s55, v192
	v_med3_f32 v21, v21, s55, v192
	v_med3_f32 v25, v25, s55, v192
	v_cvt_pk_fp8_f32 v4, v12, v13 op_sel:[0,0,1]
	v_cvt_pk_fp8_f32 v5, v16, v17 op_sel:[0,0,1]
	v_cvt_pk_fp8_f32 v6, v20, v21 op_sel:[0,0,1]
	v_cvt_pk_fp8_f32 v7, v24, v25 op_sel:[0,0,1]
	v_add_co_u32_e32 v10, vcc, s0, v0
	s_mov_b32 s0, s18
	s_nop 0
	v_addc_co_u32_e32 v11, vcc, 0, v1, vcc
	global_store_dwordx2 v[10:11], v[4:5], off
	global_store_dwordx2 v[8:9], v[6:7], off offset:128
	v_mov_b32_e32 v2, 0
	v_mov_b32_e32 v3, 0
	v_mov_b32_e32 v4, 0
	v_mov_b32_e32 v5, 0
	v_lshl_add_u64 v[6:7], v[0:1], 0, s[6:7]
	v_add_co_u32_e64 v0, s[6:7], s13, v0
	s_and_b64 vcc, exec, s[14:15]
	s_nop 0
	v_addc_co_u32_e64 v1, s[6:7], 0, v1, s[6:7]
	v_mul_f32_e32 v8, 0x3d000000, v200
	v_mul_f32_e32 v8, 0x42000000, v8
	v_pk_mul_f32 v[12:13], v[44:45], v[8:9] op_sel_hi:[1,0]
	v_pk_mul_f32 v[16:17], v[40:41], v[8:9] op_sel_hi:[1,0]
	v_pk_mul_f32 v[10:11], v[46:47], v[8:9] op_sel_hi:[1,0]
	v_pk_mul_f32 v[14:15], v[42:43], v[8:9] op_sel_hi:[1,0]
	v_pk_mul_f32 v[18:19], v[38:39], v[8:9] op_sel_hi:[1,0]
	v_pk_mul_f32 v[20:21], v[36:37], v[8:9] op_sel_hi:[1,0]
	v_pk_mul_f32 v[22:23], v[34:35], v[8:9] op_sel_hi:[1,0]
	v_pk_mul_f32 v[8:9], v[32:33], v[8:9] op_sel_hi:[1,0]
	v_med3_f32 v12, v12, s55, v192
	v_med3_f32 v16, v16, s55, v192
	v_med3_f32 v13, v13, s55, v192
	v_med3_f32 v17, v17, s55, v192
	v_med3_f32 v20, v20, s55, v192
	v_med3_f32 v8, v8, s55, v192
	v_med3_f32 v21, v21, s55, v192
	v_med3_f32 v9, v9, s55, v192
	v_cvt_pk_fp8_f32 v2, v12, v13
	v_cvt_pk_fp8_f32 v3, v16, v17
	v_cvt_pk_fp8_f32 v4, v20, v21
	v_cvt_pk_fp8_f32 v5, v8, v9
	v_med3_f32 v10, v10, s55, v192
	v_med3_f32 v14, v14, s55, v192
	v_med3_f32 v11, v11, s55, v192
	v_med3_f32 v15, v15, s55, v192
	v_med3_f32 v18, v18, s55, v192
	v_med3_f32 v22, v22, s55, v192
	v_med3_f32 v19, v19, s55, v192
	v_med3_f32 v23, v23, s55, v192
	v_cvt_pk_fp8_f32 v2, v10, v11 op_sel:[0,0,1]
	v_cvt_pk_fp8_f32 v3, v14, v15 op_sel:[0,0,1]
	v_cvt_pk_fp8_f32 v4, v18, v19 op_sel:[0,0,1]
	v_cvt_pk_fp8_f32 v5, v22, v23 op_sel:[0,0,1]
	global_store_dwordx2 v[0:1], v[2:3], off
	global_store_dwordx2 v[6:7], v[4:5], off offset:128
	s_cbranch_vccz .LBB0_2056
	s_waitcnt vmcnt(0)
	v_readlane_b32 s54, v242, 34
	s_cmpk_gt_u32 s34, 0xff
	v_readlane_b32 s55, v242, 35
	s_cbranch_scc1 .LBB0_2063
	s_barrier

.LBB0_2200:
	s_add_u32 s30, s28, 0x100
	ds_read_b128 v[158:161], v141
	ds_read_b128 v[162:165], v142
	ds_read_b128 v[166:169], v149
	ds_read_b128 v[170:173], v150
	s_addc_u32 s31, s29, 0
	s_and_b32 s62, s30, 0x700
	s_add_u32 s63, s12, s62
	s_addc_u32 s64, s13, 0
	s_cmp_eq_u32 s61, 12
	s_cselect_b64 s[36:37], -1, 0
	s_and_b64 s[34:35], s[36:37], exec
	s_cselect_b32 s35, s21, s64
	s_cselect_b32 s34, s23, s63
	s_cselect_b32 s63, 0, 0
	s_cselect_b32 s62, 0, s62
	s_add_u32 s28, s18, s28
	s_addc_u32 s29, s19, s29
	s_add_u32 s28, s28, 0x40080
	s_addc_u32 s29, s29, 0
	ds_read_b128 v[174:177], v157
	ds_read_b128 v[178:181], v157 offset:1024
	ds_read_b128 v[182:185], v157 offset:2048
	ds_read_b128 v[186:189], v157 offset:3072
	ds_read_b128 v[190:193], v157 offset:4096
	ds_read_b128 v[194:197], v157 offset:5120
	ds_read_b128 v[198:201], v157 offset:6144
	ds_read_b128 v[202:205], v157 offset:7168
	s_add_i32 m0, s3, 0xc000
	s_nop 0
	global_load_lds_dwordx4 v134, s[28:29]
	s_add_i32 m0, s3, 0xe000
	s_nop 0
	global_load_lds_dwordx4 v130, s[28:29]
	s_waitcnt lgkmcnt(8)
	s_nop 0
	s_barrier
	s_waitcnt lgkmcnt(0)
	s_setprio 1
	s_waitcnt lgkmcnt(0)
	v_mfma_f32_16x16x32_bf16 v[124:127], v[158:161], v[174:177], v[124:127]
	v_mfma_f32_16x16x32_bf16 v[120:123], v[166:169], v[174:177], v[120:123]
	v_mfma_f32_16x16x32_bf16 v[116:119], v[158:161], v[182:185], v[116:119]
	v_mfma_f32_16x16x32_bf16 v[112:115], v[166:169], v[182:185], v[112:115]
	v_mfma_f32_16x16x32_bf16 v[100:103], v[158:161], v[190:193], v[100:103]
	v_mfma_f32_16x16x32_bf16 v[96:99], v[166:169], v[190:193], v[96:99]
	v_mfma_f32_16x16x32_bf16 v[84:87], v[158:161], v[198:201], v[84:87]
	v_mfma_f32_16x16x32_bf16 v[80:83], v[166:169], v[198:201], v[80:83]
	v_mfma_f32_16x16x32_bf16 v[124:127], v[162:165], v[178:181], v[124:127]
	v_mfma_f32_16x16x32_bf16 v[120:123], v[170:173], v[178:181], v[120:123]
	v_mfma_f32_16x16x32_bf16 v[116:119], v[162:165], v[186:189], v[116:119]
	v_mfma_f32_16x16x32_bf16 v[112:115], v[170:173], v[186:189], v[112:115]
	v_mfma_f32_16x16x32_bf16 v[100:103], v[162:165], v[194:197], v[100:103]
	v_mfma_f32_16x16x32_bf16 v[96:99], v[170:173], v[194:197], v[96:99]
	v_mfma_f32_16x16x32_bf16 v[84:87], v[162:165], v[202:205], v[84:87]
	v_mfma_f32_16x16x32_bf16 v[80:83], v[170:173], v[202:205], v[80:83]
	s_setprio 0
	s_barrier
	s_mov_b64 s[28:29], s[34:35]
	s_mov_b32 m0, s44
	ds_read_b128 v[210:213], v143
	ds_read_b128 v[214:217], v144
	ds_read_b128 v[218:221], v151
	ds_read_b128 v[222:225], v152
	s_nop 0
	global_load_lds_dwordx4 v132, s[28:29]
	s_mov_b32 m0, s45
	s_nop 0
	global_load_lds_dwordx4 v128, s[28:29]
	s_nop 0
	s_barrier
	s_waitcnt lgkmcnt(0)
	s_setprio 1
	s_waitcnt lgkmcnt(0)
	v_mfma_f32_16x16x32_bf16 v[108:111], v[210:213], v[174:177], v[108:111]
	v_mfma_f32_16x16x32_bf16 v[104:107], v[218:221], v[174:177], v[104:107]
	v_mfma_f32_16x16x32_bf16 v[92:95], v[210:213], v[182:185], v[92:95]
	v_mfma_f32_16x16x32_bf16 v[88:91], v[218:221], v[182:185], v[88:91]
	v_mfma_f32_16x16x32_bf16 v[76:79], v[210:213], v[190:193], v[76:79]
	v_mfma_f32_16x16x32_bf16 v[72:75], v[218:221], v[190:193], v[72:75]
	v_mfma_f32_16x16x32_bf16 v[68:71], v[210:213], v[198:201], v[68:71]
	v_mfma_f32_16x16x32_bf16 v[64:67], v[218:221], v[198:201], v[64:67]
	v_mfma_f32_16x16x32_bf16 v[108:111], v[214:217], v[178:181], v[108:111]
	v_mfma_f32_16x16x32_bf16 v[104:107], v[222:225], v[178:181], v[104:107]
	v_mfma_f32_16x16x32_bf16 v[92:95], v[214:217], v[186:189], v[92:95]
	v_mfma_f32_16x16x32_bf16 v[88:91], v[222:225], v[186:189], v[88:91]
	v_mfma_f32_16x16x32_bf16 v[76:79], v[214:217], v[194:197], v[76:79]
	v_mfma_f32_16x16x32_bf16 v[72:75], v[222:225], v[194:197], v[72:75]
	v_mfma_f32_16x16x32_bf16 v[68:71], v[214:217], v[202:205], v[68:71]
	v_mfma_f32_16x16x32_bf16 v[64:67], v[222:225], v[202:205], v[64:67]
	s_setprio 0
	s_and_b64 s[28:29], s[16:17], s[36:37]
	s_and_b64 s[28:29], s[28:29], exec
	s_cselect_b32 s28, s24, s18
	s_cselect_b32 s29, s25, s19
	s_add_u32 s28, s28, s62
	s_addc_u32 s29, s29, s63
	s_mov_b64 s[36:37], s[28:29]
	s_mov_b32 m0, s3
	s_barrier
	ds_read_b128 v[174:177], v157 offset:16384
	ds_read_b128 v[178:181], v157 offset:17408
	ds_read_b128 v[182:185], v157 offset:18432
	ds_read_b128 v[186:189], v157 offset:19456
	ds_read_b128 v[190:193], v157 offset:20480
	ds_read_b128 v[194:197], v157 offset:21504
	ds_read_b128 v[198:201], v157 offset:22528
	ds_read_b128 v[202:205], v157 offset:23552
	s_nop 0
	global_load_lds_dwordx4 v134, s[36:37]
	s_mov_b32 m0, s46
	s_nop 0
	global_load_lds_dwordx4 v130, s[36:37]
	s_nop 0
	s_barrier
	s_waitcnt lgkmcnt(0)
	s_setprio 1
	s_waitcnt lgkmcnt(0)
	v_mfma_f32_16x16x32_bf16 v[60:63], v[158:161], v[174:177], v[60:63]
	v_mfma_f32_16x16x32_bf16 v[56:59], v[166:169], v[174:177], v[56:59]
	v_mfma_f32_16x16x32_bf16 v[52:55], v[158:161], v[182:185], v[52:55]
	v_mfma_f32_16x16x32_bf16 v[48:51], v[166:169], v[182:185], v[48:51]
	v_mfma_f32_16x16x32_bf16 v[36:39], v[158:161], v[190:193], v[36:39]
	v_mfma_f32_16x16x32_bf16 v[32:35], v[166:169], v[190:193], v[32:35]
	v_mfma_f32_16x16x32_bf16 v[20:23], v[158:161], v[198:201], v[20:23]
	v_mfma_f32_16x16x32_bf16 v[16:19], v[166:169], v[198:201], v[16:19]
	v_mfma_f32_16x16x32_bf16 v[60:63], v[162:165], v[178:181], v[60:63]
	v_mfma_f32_16x16x32_bf16 v[56:59], v[170:173], v[178:181], v[56:59]
	v_mfma_f32_16x16x32_bf16 v[52:55], v[162:165], v[186:189], v[52:55]
	v_mfma_f32_16x16x32_bf16 v[48:51], v[170:173], v[186:189], v[48:51]
	v_mfma_f32_16x16x32_bf16 v[36:39], v[162:165], v[194:197], v[36:39]
	v_mfma_f32_16x16x32_bf16 v[32:35], v[170:173], v[194:197], v[32:35]
	v_mfma_f32_16x16x32_bf16 v[20:23], v[162:165], v[202:205], v[20:23]
	v_mfma_f32_16x16x32_bf16 v[16:19], v[170:173], v[202:205], v[16:19]
	s_setprio 0
	s_barrier
	s_add_u32 s36, s34, 0x40000
	s_addc_u32 s37, s35, 0
	s_mov_b32 m0, s47
	s_nop 0
	global_load_lds_dwordx4 v132, s[36:37]
	s_mov_b32 m0, s48
	s_nop 0
	global_load_lds_dwordx4 v128, s[36:37]
	s_waitcnt vmcnt(6)
	s_barrier
	s_setprio 1
	v_mfma_f32_16x16x32_bf16 v[44:47], v[210:213], v[174:177], v[44:47]
	v_mfma_f32_16x16x32_bf16 v[40:43], v[218:221], v[174:177], v[40:43]
	v_mfma_f32_16x16x32_bf16 v[28:31], v[210:213], v[182:185], v[28:31]
	v_mfma_f32_16x16x32_bf16 v[24:27], v[218:221], v[182:185], v[24:27]
	v_mfma_f32_16x16x32_bf16 v[12:15], v[210:213], v[190:193], v[12:15]
	v_mfma_f32_16x16x32_bf16 v[8:11], v[218:221], v[190:193], v[8:11]
	v_mfma_f32_16x16x32_bf16 v[4:7], v[210:213], v[198:201], v[4:7]
	v_mfma_f32_16x16x32_bf16 v[0:3], v[218:221], v[198:201], v[0:3]
	v_mfma_f32_16x16x32_bf16 v[44:47], v[214:217], v[178:181], v[44:47]
	v_mfma_f32_16x16x32_bf16 v[40:43], v[222:225], v[178:181], v[40:43]
	v_mfma_f32_16x16x32_bf16 v[28:31], v[214:217], v[186:189], v[28:31]
	v_mfma_f32_16x16x32_bf16 v[24:27], v[222:225], v[186:189], v[24:27]
	v_mfma_f32_16x16x32_bf16 v[12:15], v[214:217], v[194:197], v[12:15]
	v_mfma_f32_16x16x32_bf16 v[8:11], v[222:225], v[194:197], v[8:11]
	v_mfma_f32_16x16x32_bf16 v[4:7], v[214:217], v[202:205], v[4:7]
	v_mfma_f32_16x16x32_bf16 v[0:3], v[222:225], v[202:205], v[0:3]
	s_setprio 0
	s_barrier
	ds_read_b128 v[158:161], v145
	ds_read_b128 v[162:165], v146
	ds_read_b128 v[166:169], v153
	ds_read_b128 v[170:173], v154
	s_add_u32 s36, s28, 0x40000
	s_addc_u32 s37, s29, 0
	s_mov_b32 m0, s49
	ds_read_b128 v[174:177], v157 offset:32768
	ds_read_b128 v[178:181], v157 offset:33792
	ds_read_b128 v[182:185], v157 offset:34816
	ds_read_b128 v[186:189], v157 offset:35840
	ds_read_b128 v[190:193], v157 offset:36864
	ds_read_b128 v[194:197], v157 offset:37888
	ds_read_b128 v[198:201], v157 offset:38912
	ds_read_b128 v[202:205], v157 offset:39936
	s_nop 0
	global_load_lds_dwordx4 v134, s[36:37]
	s_mov_b32 m0, s50
	s_nop 0
	global_load_lds_dwordx4 v130, s[36:37]
	s_waitcnt lgkmcnt(8)
	s_barrier
	s_waitcnt lgkmcnt(0)
	s_setprio 1
	s_waitcnt lgkmcnt(0)
	v_mfma_f32_16x16x32_bf16 v[124:127], v[158:161], v[174:177], v[124:127]
	v_mfma_f32_16x16x32_bf16 v[120:123], v[166:169], v[174:177], v[120:123]
	v_mfma_f32_16x16x32_bf16 v[116:119], v[158:161], v[182:185], v[116:119]
	v_mfma_f32_16x16x32_bf16 v[112:115], v[166:169], v[182:185], v[112:115]
	v_mfma_f32_16x16x32_bf16 v[100:103], v[158:161], v[190:193], v[100:103]
	v_mfma_f32_16x16x32_bf16 v[96:99], v[166:169], v[190:193], v[96:99]
	v_mfma_f32_16x16x32_bf16 v[84:87], v[158:161], v[198:201], v[84:87]
	v_mfma_f32_16x16x32_bf16 v[80:83], v[166:169], v[198:201], v[80:83]
	v_mfma_f32_16x16x32_bf16 v[124:127], v[162:165], v[178:181], v[124:127]
	v_mfma_f32_16x16x32_bf16 v[120:123], v[170:173], v[178:181], v[120:123]
	v_mfma_f32_16x16x32_bf16 v[116:119], v[162:165], v[186:189], v[116:119]
	v_mfma_f32_16x16x32_bf16 v[112:115], v[170:173], v[186:189], v[112:115]
	v_mfma_f32_16x16x32_bf16 v[100:103], v[162:165], v[194:197], v[100:103]
	v_mfma_f32_16x16x32_bf16 v[96:99], v[170:173], v[194:197], v[96:99]
	v_mfma_f32_16x16x32_bf16 v[84:87], v[162:165], v[202:205], v[84:87]
	v_mfma_f32_16x16x32_bf16 v[80:83], v[170:173], v[202:205], v[80:83]
	s_setprio 0
	s_barrier
	s_add_u32 s36, s34, 0x80
	s_addc_u32 s37, s35, 0
	s_mov_b32 m0, s52
	ds_read_b128 v[210:213], v147
	ds_read_b128 v[214:217], v148
	ds_read_b128 v[218:221], v155
	ds_read_b128 v[222:225], v156
	s_nop 0
	global_load_lds_dwordx4 v132, s[36:37]
	s_mov_b32 m0, s53
	s_nop 0
	global_load_lds_dwordx4 v128, s[36:37]
	s_nop 0
	s_barrier
	s_waitcnt lgkmcnt(0)
	s_setprio 1
	s_waitcnt lgkmcnt(0)
	v_mfma_f32_16x16x32_bf16 v[108:111], v[210:213], v[174:177], v[108:111]
	v_mfma_f32_16x16x32_bf16 v[104:107], v[218:221], v[174:177], v[104:107]
	v_mfma_f32_16x16x32_bf16 v[92:95], v[210:213], v[182:185], v[92:95]
	v_mfma_f32_16x16x32_bf16 v[88:91], v[218:221], v[182:185], v[88:91]
	v_mfma_f32_16x16x32_bf16 v[76:79], v[210:213], v[190:193], v[76:79]
	v_mfma_f32_16x16x32_bf16 v[72:75], v[218:221], v[190:193], v[72:75]
	v_mfma_f32_16x16x32_bf16 v[68:71], v[210:213], v[198:201], v[68:71]
	v_mfma_f32_16x16x32_bf16 v[64:67], v[218:221], v[198:201], v[64:67]
	v_mfma_f32_16x16x32_bf16 v[108:111], v[214:217], v[178:181], v[108:111]
	v_mfma_f32_16x16x32_bf16 v[104:107], v[222:225], v[178:181], v[104:107]
	v_mfma_f32_16x16x32_bf16 v[92:95], v[214:217], v[186:189], v[92:95]
	v_mfma_f32_16x16x32_bf16 v[88:91], v[222:225], v[186:189], v[88:91]
	v_mfma_f32_16x16x32_bf16 v[76:79], v[214:217], v[194:197], v[76:79]
	v_mfma_f32_16x16x32_bf16 v[72:75], v[222:225], v[194:197], v[72:75]
	v_mfma_f32_16x16x32_bf16 v[68:71], v[214:217], v[202:205], v[68:71]
	v_mfma_f32_16x16x32_bf16 v[64:67], v[222:225], v[202:205], v[64:67]
	s_setprio 0
	s_add_u32 s28, s28, 0x80
	s_addc_u32 s29, s29, 0
	s_mov_b32 m0, s54
	s_barrier
	ds_read_b128 v[174:177], v157 offset:49152
	ds_read_b128 v[178:181], v157 offset:50176
	ds_read_b128 v[182:185], v157 offset:51200
	ds_read_b128 v[186:189], v157 offset:52224
	ds_read_b128 v[190:193], v157 offset:53248
	ds_read_b128 v[194:197], v157 offset:54272
	ds_read_b128 v[198:201], v157 offset:55296
	ds_read_b128 v[202:205], v157 offset:56320
	s_nop 0
	global_load_lds_dwordx4 v134, s[28:29]
	s_mov_b32 m0, s55
	s_nop 0
	global_load_lds_dwordx4 v130, s[28:29]
	s_nop 0
	s_barrier
	s_waitcnt lgkmcnt(0)
	s_setprio 1
	s_waitcnt lgkmcnt(0)
	v_mfma_f32_16x16x32_bf16 v[60:63], v[158:161], v[174:177], v[60:63]
	v_mfma_f32_16x16x32_bf16 v[56:59], v[166:169], v[174:177], v[56:59]
	v_mfma_f32_16x16x32_bf16 v[52:55], v[158:161], v[182:185], v[52:55]
	v_mfma_f32_16x16x32_bf16 v[48:51], v[166:169], v[182:185], v[48:51]
	v_mfma_f32_16x16x32_bf16 v[36:39], v[158:161], v[190:193], v[36:39]
	v_mfma_f32_16x16x32_bf16 v[32:35], v[166:169], v[190:193], v[32:35]
	v_mfma_f32_16x16x32_bf16 v[20:23], v[158:161], v[198:201], v[20:23]
	v_mfma_f32_16x16x32_bf16 v[16:19], v[166:169], v[198:201], v[16:19]
	v_mfma_f32_16x16x32_bf16 v[60:63], v[162:165], v[178:181], v[60:63]
	v_mfma_f32_16x16x32_bf16 v[56:59], v[170:173], v[178:181], v[56:59]
	v_mfma_f32_16x16x32_bf16 v[52:55], v[162:165], v[186:189], v[52:55]
	v_mfma_f32_16x16x32_bf16 v[48:51], v[170:173], v[186:189], v[48:51]
	v_mfma_f32_16x16x32_bf16 v[36:39], v[162:165], v[194:197], v[36:39]
	v_mfma_f32_16x16x32_bf16 v[32:35], v[170:173], v[194:197], v[32:35]
	v_mfma_f32_16x16x32_bf16 v[20:23], v[162:165], v[202:205], v[20:23]
	v_mfma_f32_16x16x32_bf16 v[16:19], v[170:173], v[202:205], v[16:19]
	s_setprio 0
	s_barrier
	s_add_u32 s28, s34, 0x40080
	s_addc_u32 s29, s35, 0
	s_mov_b32 m0, s56
	s_nop 0
	global_load_lds_dwordx4 v132, s[28:29]
	s_mov_b32 m0, s57
	s_nop 0
	global_load_lds_dwordx4 v128, s[28:29]
	s_waitcnt vmcnt(6)
	s_barrier
	s_setprio 1
	v_mfma_f32_16x16x32_bf16 v[44:47], v[210:213], v[174:177], v[44:47]
	v_mfma_f32_16x16x32_bf16 v[40:43], v[218:221], v[174:177], v[40:43]
	v_mfma_f32_16x16x32_bf16 v[28:31], v[210:213], v[182:185], v[28:31]
	v_mfma_f32_16x16x32_bf16 v[24:27], v[218:221], v[182:185], v[24:27]
	v_mfma_f32_16x16x32_bf16 v[12:15], v[210:213], v[190:193], v[12:15]
	v_mfma_f32_16x16x32_bf16 v[8:11], v[218:221], v[190:193], v[8:11]
	v_mfma_f32_16x16x32_bf16 v[4:7], v[210:213], v[198:201], v[4:7]
	v_mfma_f32_16x16x32_bf16 v[0:3], v[218:221], v[198:201], v[0:3]
	v_mfma_f32_16x16x32_bf16 v[44:47], v[214:217], v[178:181], v[44:47]
	v_mfma_f32_16x16x32_bf16 v[40:43], v[222:225], v[178:181], v[40:43]
	v_mfma_f32_16x16x32_bf16 v[28:31], v[214:217], v[186:189], v[28:31]
	v_mfma_f32_16x16x32_bf16 v[24:27], v[222:225], v[186:189], v[24:27]
	v_mfma_f32_16x16x32_bf16 v[12:15], v[214:217], v[194:197], v[12:15]
	v_mfma_f32_16x16x32_bf16 v[8:11], v[222:225], v[194:197], v[8:11]
	v_mfma_f32_16x16x32_bf16 v[4:7], v[214:217], v[202:205], v[4:7]
	v_mfma_f32_16x16x32_bf16 v[0:3], v[222:225], v[202:205], v[0:3]
	s_setprio 0
	s_add_i32 s61, s61, 2
	s_cmp_gt_u32 s61, 13
	s_mov_b64 s[28:29], s[30:31]
	s_barrier
	s_cbranch_scc0 .LBB0_2200
	v_mov_b32_e32 v158, v140
	v_mov_b64_e32 v[160:161], s[0:1]
	v_ashrrev_i32_e32 v159, 2, v158
	v_and_b32_e32 v159, 0xffffffc0, v159
	v_lshl_add_u32 v159, s2, 8, v159
	v_and_or_b32 v164, v158, 15, v159
	v_lshrrev_b32_e32 v158, 1, v158
	v_and_b32_e32 v158, 0x78, v158
	v_lshl_or_b32 v158, s60, 8, v158
	v_ashrrev_i32_e32 v159, 31, v158
	v_cvt_pk_bf16_f32 v68, v68, v69
	v_cvt_pk_bf16_f32 v69, v70, v71
	v_cvt_pk_bf16_f32 v70, v64, v65
	v_add_u32_e32 v64, 0x80, v164
	v_mad_i64_i32 v[162:163], s[12:13], v164, s59, v[160:161]
	v_lshlrev_b64 v[158:159], 1, v[158:159]
	v_cvt_pk_bf16_f32 v108, v108, v109
	v_cvt_pk_bf16_f32 v109, v110, v111
	v_cvt_pk_bf16_f32 v110, v104, v105
	v_or_b32_e32 v104, 16, v164
	v_mad_i64_i32 v[64:65], s[12:13], v64, s59, v[160:161]
	v_cvt_pk_bf16_f32 v44, v44, v45
	v_cvt_pk_bf16_f32 v45, v46, v47
	v_cvt_pk_bf16_f32 v46, v40, v41
	v_add_u32_e32 v40, 0x90, v164
	v_lshl_add_u64 v[162:163], v[162:163], 0, v[158:159]
	v_cvt_pk_bf16_f32 v111, v106, v107
	v_mad_i64_i32 v[104:105], s[12:13], v104, s59, v[160:161]
	v_cvt_pk_bf16_f32 v92, v92, v93
	v_cvt_pk_bf16_f32 v93, v94, v95
	v_cvt_pk_bf16_f32 v94, v88, v89
	v_or_b32_e32 v88, 32, v164
	v_lshl_add_u64 v[64:65], v[64:65], 0, v[158:159]
	v_cvt_pk_bf16_f32 v47, v42, v43
	v_mad_i64_i32 v[40:41], s[12:13], v40, s59, v[160:161]
	v_cvt_pk_bf16_f32 v28, v28, v29
	v_cvt_pk_bf16_f32 v29, v30, v31
	v_cvt_pk_bf16_f32 v30, v24, v25
	v_add_u32_e32 v24, 0xa0, v164
	global_store_dwordx4 v[162:163], v[108:111], off offset:256
	v_cvt_pk_bf16_f32 v95, v90, v91
	v_mad_i64_i32 v[88:89], s[12:13], v88, s59, v[160:161]
	v_lshl_add_u64 v[108:109], v[104:105], 0, v[158:159]
	v_cvt_pk_bf16_f32 v76, v76, v77
	v_cvt_pk_bf16_f32 v77, v78, v79
	v_cvt_pk_bf16_f32 v78, v72, v73
	v_or_b32_e32 v72, 48, v164
	global_store_dwordx4 v[64:65], v[44:47], off offset:256
	v_cvt_pk_bf16_f32 v31, v26, v27
	v_mad_i64_i32 v[24:25], s[12:13], v24, s59, v[160:161]
	v_lshl_add_u64 v[44:45], v[40:41], 0, v[158:159]
	v_cvt_pk_bf16_f32 v12, v12, v13
	v_cvt_pk_bf16_f32 v13, v14, v15
	v_cvt_pk_bf16_f32 v14, v8, v9
	v_add_u32_e32 v8, 0xb0, v164
	global_store_dwordx4 v[108:109], v[92:95], off offset:256
	v_cvt_pk_bf16_f32 v79, v74, v75
	v_mad_i64_i32 v[72:73], s[12:13], v72, s59, v[160:161]
	v_lshl_add_u64 v[92:93], v[88:89], 0, v[158:159]
	global_store_dwordx4 v[44:45], v[28:31], off offset:256
	v_cvt_pk_bf16_f32 v15, v10, v11
	v_mad_i64_i32 v[8:9], s[12:13], v8, s59, v[160:161]
	v_lshl_add_u64 v[28:29], v[24:25], 0, v[158:159]
	v_cvt_pk_bf16_f32 v124, v124, v125
	v_cvt_pk_bf16_f32 v125, v126, v127
	v_cvt_pk_bf16_f32 v126, v120, v121
	v_cvt_pk_bf16_f32 v127, v122, v123
	v_cvt_pk_bf16_f32 v104, v116, v117
	v_cvt_pk_bf16_f32 v105, v118, v119
	v_cvt_pk_bf16_f32 v106, v112, v113
	v_cvt_pk_bf16_f32 v107, v114, v115
	v_cvt_pk_bf16_f32 v88, v100, v101
	v_cvt_pk_bf16_f32 v89, v102, v103
	v_cvt_pk_bf16_f32 v90, v96, v97
	v_cvt_pk_bf16_f32 v91, v98, v99
	global_store_dwordx4 v[92:93], v[76:79], off offset:256
	v_cvt_pk_bf16_f32 v74, v80, v81
	v_cvt_pk_bf16_f32 v75, v82, v83
	v_lshl_add_u64 v[76:77], v[72:73], 0, v[158:159]
	v_cvt_pk_bf16_f32 v72, v84, v85
	v_cvt_pk_bf16_f32 v73, v86, v87
	v_cvt_pk_bf16_f32 v71, v66, v67
	v_cvt_pk_bf16_f32 v60, v60, v61
	v_cvt_pk_bf16_f32 v61, v62, v63
	v_cvt_pk_bf16_f32 v62, v56, v57
	v_cvt_pk_bf16_f32 v63, v58, v59
	v_cvt_pk_bf16_f32 v40, v52, v53
	v_cvt_pk_bf16_f32 v41, v54, v55
	v_cvt_pk_bf16_f32 v42, v48, v49
	v_cvt_pk_bf16_f32 v43, v50, v51
	v_cvt_pk_bf16_f32 v24, v36, v37
	v_cvt_pk_bf16_f32 v25, v38, v39
	v_cvt_pk_bf16_f32 v26, v32, v33
	v_cvt_pk_bf16_f32 v27, v34, v35
	global_store_dwordx4 v[28:29], v[12:15], off offset:256
	v_cvt_pk_bf16_f32 v10, v16, v17
	v_cvt_pk_bf16_f32 v11, v18, v19
	v_lshl_add_u64 v[12:13], v[8:9], 0, v[158:159]
	v_cvt_pk_bf16_f32 v8, v20, v21
	v_cvt_pk_bf16_f32 v9, v22, v23
	v_cvt_pk_bf16_f32 v4, v4, v5
	v_cvt_pk_bf16_f32 v5, v6, v7
	v_cvt_pk_bf16_f32 v6, v0, v1
	v_cvt_pk_bf16_f32 v7, v2, v3
	s_and_b64 vcc, exec, s[14:15]
	s_mov_b32 s60, s20
	s_mov_b32 s2, s22
	s_mov_b64 s[12:13], s[26:27]
	s_mov_b64 s[18:19], s[24:25]
	global_store_dwordx4 v[162:163], v[124:127], off
	global_store_dwordx4 v[108:109], v[104:107], off
	global_store_dwordx4 v[92:93], v[88:91], off
	global_store_dwordx4 v[76:77], v[72:75], off
	global_store_dwordx4 v[76:77], v[68:71], off offset:256
	global_store_dwordx4 v[64:65], v[60:63], off
	global_store_dwordx4 v[44:45], v[40:43], off
	global_store_dwordx4 v[28:29], v[24:27], off
	global_store_dwordx4 v[12:13], v[8:11], off
	global_store_dwordx4 v[12:13], v[4:7], off offset:256
	s_cbranch_vccz .LBB0_2197
	s_waitcnt vmcnt(0)
	v_readlane_b32 s54, v242, 34
	s_cmpk_gt_u32 s33, 0xff
	v_readlane_b32 s55, v242, 35
	s_cbranch_scc1 .LBB0_2204
	s_barrier

.LBB0_2526:
	s_add_u32 s36, s34, 0x100
	ds_read_b128 v[92:95], v165
	ds_read_b128 v[100:103], v166
	ds_read_b128 v[104:107], v173
	ds_read_b128 v[108:111], v174
	s_addc_u32 s37, s35, 0
	s_and_b32 s27, s36, 0x700
	s_add_u32 s33, s2, s27
	s_addc_u32 s65, s3, 0
	s_cmp_eq_u32 s25, 12
	s_cselect_b64 s[40:41], -1, 0
	s_and_b64 s[38:39], s[40:41], exec
	s_cselect_b32 s39, s1, s65
	s_cselect_b32 s38, s20, s33
	s_cselect_b32 s33, 0, 0
	s_cselect_b32 s27, 0, s27
	s_add_u32 s34, s4, s34
	s_addc_u32 s35, s5, s35
	s_add_u32 s34, s34, 0x40080
	s_addc_u32 s35, s35, 0
	ds_read_b128 v[158:161], v181
	ds_read_b128 v[182:185], v181 offset:1024
	ds_read_b128 v[186:189], v181 offset:2048
	ds_read_b128 v[190:193], v181 offset:3072
	ds_read_b128 v[194:197], v181 offset:4096
	ds_read_b128 v[198:201], v181 offset:5120
	ds_read_b128 v[202:205], v181 offset:6144
	ds_read_b128 v[210:213], v181 offset:7168
	s_add_i32 m0, s13, 0xc000
	s_nop 0
	global_load_lds_dwordx4 v144, s[34:35]
	s_add_i32 m0, s13, 0xe000
	s_nop 0
	global_load_lds_dwordx4 v148, s[34:35]
	s_waitcnt lgkmcnt(8)
	s_barrier
	s_waitcnt lgkmcnt(0)
	s_setprio 1
	s_waitcnt lgkmcnt(0)
	v_mfma_f32_16x16x32_bf16 v[140:143], v[92:95], v[158:161], v[140:143]
	v_mfma_f32_16x16x32_bf16 v[136:139], v[104:107], v[158:161], v[136:139]
	v_mfma_f32_16x16x32_bf16 v[124:127], v[92:95], v[186:189], v[124:127]
	v_mfma_f32_16x16x32_bf16 v[120:123], v[104:107], v[186:189], v[120:123]
	v_mfma_f32_16x16x32_bf16 v[96:99], v[92:95], v[194:197], v[96:99]
	v_mfma_f32_16x16x32_bf16 v[88:91], v[104:107], v[194:197], v[88:91]
	v_mfma_f32_16x16x32_bf16 v[76:79], v[92:95], v[202:205], v[76:79]
	v_mfma_f32_16x16x32_bf16 v[72:75], v[104:107], v[202:205], v[72:75]
	v_mfma_f32_16x16x32_bf16 v[140:143], v[100:103], v[182:185], v[140:143]
	v_mfma_f32_16x16x32_bf16 v[136:139], v[108:111], v[182:185], v[136:139]
	v_mfma_f32_16x16x32_bf16 v[124:127], v[100:103], v[190:193], v[124:127]
	v_mfma_f32_16x16x32_bf16 v[120:123], v[108:111], v[190:193], v[120:123]
	v_mfma_f32_16x16x32_bf16 v[96:99], v[100:103], v[198:201], v[96:99]
	v_mfma_f32_16x16x32_bf16 v[88:91], v[108:111], v[198:201], v[88:91]
	v_mfma_f32_16x16x32_bf16 v[76:79], v[100:103], v[210:213], v[76:79]
	v_mfma_f32_16x16x32_bf16 v[72:75], v[108:111], v[210:213], v[72:75]
	s_setprio 0
	s_barrier
	s_mov_b64 s[34:35], s[38:39]
	s_mov_b32 m0, s47
	ds_read_b128 v[214:217], v167
	ds_read_b128 v[218:221], v168
	ds_read_b128 v[222:225], v175
	ds_read_b128 v[226:229], v176
	s_nop 0
	global_load_lds_dwordx4 v146, s[34:35]
	s_mov_b32 m0, s48
	s_nop 0
	global_load_lds_dwordx4 v150, s[34:35]
	s_nop 0
	s_barrier
	s_waitcnt lgkmcnt(0)
	s_setprio 1
	s_waitcnt lgkmcnt(0)
	v_mfma_f32_16x16x32_bf16 v[132:135], v[214:217], v[158:161], v[132:135]
	v_mfma_f32_16x16x32_bf16 v[128:131], v[222:225], v[158:161], v[128:131]
	v_mfma_f32_16x16x32_bf16 v[116:119], v[214:217], v[186:189], v[116:119]
	v_mfma_f32_16x16x32_bf16 v[112:115], v[222:225], v[186:189], v[112:115]
	v_mfma_f32_16x16x32_bf16 v[84:87], v[214:217], v[194:197], v[84:87]
	v_mfma_f32_16x16x32_bf16 v[80:83], v[222:225], v[194:197], v[80:83]
	v_mfma_f32_16x16x32_bf16 v[68:71], v[214:217], v[202:205], v[68:71]
	v_mfma_f32_16x16x32_bf16 v[64:67], v[222:225], v[202:205], v[64:67]
	v_mfma_f32_16x16x32_bf16 v[132:135], v[218:221], v[182:185], v[132:135]
	v_mfma_f32_16x16x32_bf16 v[128:131], v[226:229], v[182:185], v[128:131]
	v_mfma_f32_16x16x32_bf16 v[116:119], v[218:221], v[190:193], v[116:119]
	v_mfma_f32_16x16x32_bf16 v[112:115], v[226:229], v[190:193], v[112:115]
	v_mfma_f32_16x16x32_bf16 v[84:87], v[218:221], v[198:201], v[84:87]
	v_mfma_f32_16x16x32_bf16 v[80:83], v[226:229], v[198:201], v[80:83]
	v_mfma_f32_16x16x32_bf16 v[68:71], v[218:221], v[210:213], v[68:71]
	v_mfma_f32_16x16x32_bf16 v[64:67], v[226:229], v[210:213], v[64:67]
	s_setprio 0
	s_and_b64 s[34:35], s[14:15], s[40:41]
	s_and_b64 s[34:35], s[34:35], exec
	s_cselect_b32 s34, s28, s4
	s_cselect_b32 s35, s29, s5
	s_add_u32 s34, s34, s27
	s_addc_u32 s35, s35, s33
	s_mov_b64 s[40:41], s[34:35]
	s_mov_b32 m0, s13
	s_barrier
	ds_read_b128 v[158:161], v181 offset:16384
	ds_read_b128 v[182:185], v181 offset:17408
	ds_read_b128 v[186:189], v181 offset:18432
	ds_read_b128 v[190:193], v181 offset:19456
	ds_read_b128 v[194:197], v181 offset:20480
	ds_read_b128 v[198:201], v181 offset:21504
	ds_read_b128 v[202:205], v181 offset:22528
	ds_read_b128 v[210:213], v181 offset:23552
	s_nop 0
	global_load_lds_dwordx4 v144, s[40:41]
	s_mov_b32 m0, s49
	s_nop 0
	global_load_lds_dwordx4 v148, s[40:41]
	s_nop 0
	s_barrier
	s_waitcnt lgkmcnt(0)
	s_setprio 1
	s_waitcnt lgkmcnt(0)
	v_mfma_f32_16x16x32_bf16 v[60:63], v[92:95], v[158:161], v[60:63]
	v_mfma_f32_16x16x32_bf16 v[56:59], v[104:107], v[158:161], v[56:59]
	v_mfma_f32_16x16x32_bf16 v[44:47], v[92:95], v[186:189], v[44:47]
	v_mfma_f32_16x16x32_bf16 v[40:43], v[104:107], v[186:189], v[40:43]
	v_mfma_f32_16x16x32_bf16 v[28:31], v[92:95], v[194:197], v[28:31]
	v_mfma_f32_16x16x32_bf16 v[24:27], v[104:107], v[194:197], v[24:27]
	v_mfma_f32_16x16x32_bf16 v[12:15], v[92:95], v[202:205], v[12:15]
	v_mfma_f32_16x16x32_bf16 v[8:11], v[104:107], v[202:205], v[8:11]
	v_mfma_f32_16x16x32_bf16 v[60:63], v[100:103], v[182:185], v[60:63]
	v_mfma_f32_16x16x32_bf16 v[56:59], v[108:111], v[182:185], v[56:59]
	v_mfma_f32_16x16x32_bf16 v[44:47], v[100:103], v[190:193], v[44:47]
	v_mfma_f32_16x16x32_bf16 v[40:43], v[108:111], v[190:193], v[40:43]
	v_mfma_f32_16x16x32_bf16 v[28:31], v[100:103], v[198:201], v[28:31]
	v_mfma_f32_16x16x32_bf16 v[24:27], v[108:111], v[198:201], v[24:27]
	v_mfma_f32_16x16x32_bf16 v[12:15], v[100:103], v[210:213], v[12:15]
	v_mfma_f32_16x16x32_bf16 v[8:11], v[108:111], v[210:213], v[8:11]
	s_setprio 0
	s_barrier
	s_add_u32 s40, s38, 0x40000
	s_addc_u32 s41, s39, 0
	s_mov_b32 m0, s50
	s_nop 0
	global_load_lds_dwordx4 v146, s[40:41]
	s_mov_b32 m0, s51
	s_nop 0
	global_load_lds_dwordx4 v150, s[40:41]
	s_waitcnt vmcnt(6)
	s_barrier
	s_setprio 1
	v_mfma_f32_16x16x32_bf16 v[52:55], v[214:217], v[158:161], v[52:55]
	v_mfma_f32_16x16x32_bf16 v[48:51], v[222:225], v[158:161], v[48:51]
	v_mfma_f32_16x16x32_bf16 v[36:39], v[214:217], v[186:189], v[36:39]
	v_mfma_f32_16x16x32_bf16 v[32:35], v[222:225], v[186:189], v[32:35]
	v_mfma_f32_16x16x32_bf16 v[20:23], v[214:217], v[194:197], v[20:23]
	v_mfma_f32_16x16x32_bf16 v[16:19], v[222:225], v[194:197], v[16:19]
	v_mfma_f32_16x16x32_bf16 v[4:7], v[214:217], v[202:205], v[4:7]
	v_mfma_f32_16x16x32_bf16 v[0:3], v[222:225], v[202:205], v[0:3]
	v_mfma_f32_16x16x32_bf16 v[52:55], v[218:221], v[182:185], v[52:55]
	v_mfma_f32_16x16x32_bf16 v[48:51], v[226:229], v[182:185], v[48:51]
	v_mfma_f32_16x16x32_bf16 v[36:39], v[218:221], v[190:193], v[36:39]
	v_mfma_f32_16x16x32_bf16 v[32:35], v[226:229], v[190:193], v[32:35]
	v_mfma_f32_16x16x32_bf16 v[20:23], v[218:221], v[198:201], v[20:23]
	v_mfma_f32_16x16x32_bf16 v[16:19], v[226:229], v[198:201], v[16:19]
	v_mfma_f32_16x16x32_bf16 v[4:7], v[218:221], v[210:213], v[4:7]
	v_mfma_f32_16x16x32_bf16 v[0:3], v[226:229], v[210:213], v[0:3]
	s_setprio 0
	s_barrier
	ds_read_b128 v[92:95], v169
	ds_read_b128 v[100:103], v170
	ds_read_b128 v[104:107], v177
	ds_read_b128 v[108:111], v178
	s_add_u32 s40, s34, 0x40000
	s_addc_u32 s41, s35, 0
	s_mov_b32 m0, s52
	ds_read_b128 v[158:161], v181 offset:32768
	ds_read_b128 v[182:185], v181 offset:33792
	ds_read_b128 v[186:189], v181 offset:34816
	ds_read_b128 v[190:193], v181 offset:35840
	ds_read_b128 v[194:197], v181 offset:36864
	ds_read_b128 v[198:201], v181 offset:37888
	ds_read_b128 v[202:205], v181 offset:38912
	ds_read_b128 v[210:213], v181 offset:39936
	s_nop 0
	global_load_lds_dwordx4 v144, s[40:41]
	s_mov_b32 m0, s53
	s_nop 0
	global_load_lds_dwordx4 v148, s[40:41]
	s_waitcnt lgkmcnt(8)
	s_barrier
	s_waitcnt lgkmcnt(0)
	s_setprio 1
	s_waitcnt lgkmcnt(0)
	v_mfma_f32_16x16x32_bf16 v[140:143], v[92:95], v[158:161], v[140:143]
	v_mfma_f32_16x16x32_bf16 v[136:139], v[104:107], v[158:161], v[136:139]
	v_mfma_f32_16x16x32_bf16 v[124:127], v[92:95], v[186:189], v[124:127]
	v_mfma_f32_16x16x32_bf16 v[120:123], v[104:107], v[186:189], v[120:123]
	v_mfma_f32_16x16x32_bf16 v[96:99], v[92:95], v[194:197], v[96:99]
	v_mfma_f32_16x16x32_bf16 v[88:91], v[104:107], v[194:197], v[88:91]
	v_mfma_f32_16x16x32_bf16 v[76:79], v[92:95], v[202:205], v[76:79]
	v_mfma_f32_16x16x32_bf16 v[72:75], v[104:107], v[202:205], v[72:75]
	v_mfma_f32_16x16x32_bf16 v[140:143], v[100:103], v[182:185], v[140:143]
	v_mfma_f32_16x16x32_bf16 v[136:139], v[108:111], v[182:185], v[136:139]
	v_mfma_f32_16x16x32_bf16 v[124:127], v[100:103], v[190:193], v[124:127]
	v_mfma_f32_16x16x32_bf16 v[120:123], v[108:111], v[190:193], v[120:123]
	v_mfma_f32_16x16x32_bf16 v[96:99], v[100:103], v[198:201], v[96:99]
	v_mfma_f32_16x16x32_bf16 v[88:91], v[108:111], v[198:201], v[88:91]
	v_mfma_f32_16x16x32_bf16 v[76:79], v[100:103], v[210:213], v[76:79]
	v_mfma_f32_16x16x32_bf16 v[72:75], v[108:111], v[210:213], v[72:75]
	s_setprio 0
	s_barrier
	s_add_u32 s40, s38, 0x80
	s_addc_u32 s41, s39, 0
	s_mov_b32 m0, s56
	ds_read_b128 v[214:217], v171
	ds_read_b128 v[218:221], v172
	ds_read_b128 v[222:225], v179
	ds_read_b128 v[226:229], v180
	s_nop 0
	global_load_lds_dwordx4 v146, s[40:41]
	s_mov_b32 m0, s57
	s_nop 0
	global_load_lds_dwordx4 v150, s[40:41]
	s_nop 0
	s_barrier
	s_waitcnt lgkmcnt(0)
	s_setprio 1
	s_waitcnt lgkmcnt(0)
	v_mfma_f32_16x16x32_bf16 v[132:135], v[214:217], v[158:161], v[132:135]
	v_mfma_f32_16x16x32_bf16 v[128:131], v[222:225], v[158:161], v[128:131]
	v_mfma_f32_16x16x32_bf16 v[116:119], v[214:217], v[186:189], v[116:119]
	v_mfma_f32_16x16x32_bf16 v[112:115], v[222:225], v[186:189], v[112:115]
	v_mfma_f32_16x16x32_bf16 v[84:87], v[214:217], v[194:197], v[84:87]
	v_mfma_f32_16x16x32_bf16 v[80:83], v[222:225], v[194:197], v[80:83]
	v_mfma_f32_16x16x32_bf16 v[68:71], v[214:217], v[202:205], v[68:71]
	v_mfma_f32_16x16x32_bf16 v[64:67], v[222:225], v[202:205], v[64:67]
	v_mfma_f32_16x16x32_bf16 v[132:135], v[218:221], v[182:185], v[132:135]
	v_mfma_f32_16x16x32_bf16 v[128:131], v[226:229], v[182:185], v[128:131]
	v_mfma_f32_16x16x32_bf16 v[116:119], v[218:221], v[190:193], v[116:119]
	v_mfma_f32_16x16x32_bf16 v[112:115], v[226:229], v[190:193], v[112:115]
	v_mfma_f32_16x16x32_bf16 v[84:87], v[218:221], v[198:201], v[84:87]
	v_mfma_f32_16x16x32_bf16 v[80:83], v[226:229], v[198:201], v[80:83]
	v_mfma_f32_16x16x32_bf16 v[68:71], v[218:221], v[210:213], v[68:71]
	v_mfma_f32_16x16x32_bf16 v[64:67], v[226:229], v[210:213], v[64:67]
	s_setprio 0
	s_add_u32 s34, s34, 0x80
	s_addc_u32 s35, s35, 0
	s_mov_b32 m0, s58
	s_barrier
	ds_read_b128 v[158:161], v181 offset:49152
	ds_read_b128 v[182:185], v181 offset:50176
	ds_read_b128 v[186:189], v181 offset:51200
	ds_read_b128 v[190:193], v181 offset:52224
	ds_read_b128 v[194:197], v181 offset:53248
	ds_read_b128 v[198:201], v181 offset:54272
	ds_read_b128 v[202:205], v181 offset:55296
	ds_read_b128 v[210:213], v181 offset:56320
	s_nop 0
	global_load_lds_dwordx4 v144, s[34:35]
	s_mov_b32 m0, s59
	s_nop 0
	global_load_lds_dwordx4 v148, s[34:35]
	s_nop 0
	s_barrier
	s_waitcnt lgkmcnt(0)
	s_setprio 1
	s_waitcnt lgkmcnt(0)
	v_mfma_f32_16x16x32_bf16 v[60:63], v[92:95], v[158:161], v[60:63]
	v_mfma_f32_16x16x32_bf16 v[56:59], v[104:107], v[158:161], v[56:59]
	v_mfma_f32_16x16x32_bf16 v[44:47], v[92:95], v[186:189], v[44:47]
	v_mfma_f32_16x16x32_bf16 v[40:43], v[104:107], v[186:189], v[40:43]
	v_mfma_f32_16x16x32_bf16 v[28:31], v[92:95], v[194:197], v[28:31]
	v_mfma_f32_16x16x32_bf16 v[24:27], v[104:107], v[194:197], v[24:27]
	v_mfma_f32_16x16x32_bf16 v[12:15], v[92:95], v[202:205], v[12:15]
	v_mfma_f32_16x16x32_bf16 v[8:11], v[104:107], v[202:205], v[8:11]
	v_mfma_f32_16x16x32_bf16 v[60:63], v[100:103], v[182:185], v[60:63]
	v_mfma_f32_16x16x32_bf16 v[56:59], v[108:111], v[182:185], v[56:59]
	v_mfma_f32_16x16x32_bf16 v[44:47], v[100:103], v[190:193], v[44:47]
	v_mfma_f32_16x16x32_bf16 v[40:43], v[108:111], v[190:193], v[40:43]
	v_mfma_f32_16x16x32_bf16 v[28:31], v[100:103], v[198:201], v[28:31]
	v_mfma_f32_16x16x32_bf16 v[24:27], v[108:111], v[198:201], v[24:27]
	v_mfma_f32_16x16x32_bf16 v[12:15], v[100:103], v[210:213], v[12:15]
	v_mfma_f32_16x16x32_bf16 v[8:11], v[108:111], v[210:213], v[8:11]
	s_setprio 0
	s_barrier
	s_add_u32 s34, s38, 0x40080
	s_addc_u32 s35, s39, 0
	s_mov_b32 m0, s60
	s_nop 0
	global_load_lds_dwordx4 v146, s[34:35]
	s_mov_b32 m0, s61
	s_nop 0
	global_load_lds_dwordx4 v150, s[34:35]
	s_waitcnt vmcnt(6)
	s_barrier
	s_setprio 1
	v_mfma_f32_16x16x32_bf16 v[52:55], v[214:217], v[158:161], v[52:55]
	v_mfma_f32_16x16x32_bf16 v[48:51], v[222:225], v[158:161], v[48:51]
	v_mfma_f32_16x16x32_bf16 v[36:39], v[214:217], v[186:189], v[36:39]
	v_mfma_f32_16x16x32_bf16 v[32:35], v[222:225], v[186:189], v[32:35]
	v_mfma_f32_16x16x32_bf16 v[20:23], v[214:217], v[194:197], v[20:23]
	v_mfma_f32_16x16x32_bf16 v[16:19], v[222:225], v[194:197], v[16:19]
	v_mfma_f32_16x16x32_bf16 v[4:7], v[214:217], v[202:205], v[4:7]
	v_mfma_f32_16x16x32_bf16 v[0:3], v[222:225], v[202:205], v[0:3]
	v_mfma_f32_16x16x32_bf16 v[52:55], v[218:221], v[182:185], v[52:55]
	v_mfma_f32_16x16x32_bf16 v[48:51], v[226:229], v[182:185], v[48:51]
	v_mfma_f32_16x16x32_bf16 v[36:39], v[218:221], v[190:193], v[36:39]
	v_mfma_f32_16x16x32_bf16 v[32:35], v[226:229], v[190:193], v[32:35]
	v_mfma_f32_16x16x32_bf16 v[20:23], v[218:221], v[198:201], v[20:23]
	v_mfma_f32_16x16x32_bf16 v[16:19], v[226:229], v[198:201], v[16:19]
	v_mfma_f32_16x16x32_bf16 v[4:7], v[218:221], v[210:213], v[4:7]
	v_mfma_f32_16x16x32_bf16 v[0:3], v[226:229], v[210:213], v[0:3]
	s_setprio 0
	s_add_i32 s25, s25, 2
	s_cmp_gt_u32 s25, 13
	s_mov_b64 s[34:35], s[36:37]
	s_barrier
	s_cbranch_scc0 .LBB0_2526
	v_mov_b32_e32 v92, v164
	s_cmpk_gt_i32 s0, 0x7f
	s_mov_b64 s[2:3], 0xc000
	s_cbranch_scc1 .LBB0_2529
	s_ashr_i32 s1, s0, 31
	s_lshr_b32 s1, s1, 28
	s_add_i32 s1, s0, s1
	s_ashr_i32 s1, s1, 4
	s_mul_hi_i32 s3, s1, 0x1800
	s_mul_i32 s2, s1, 0x1800

.LBB0_2958:
	v_mov_b32_e32 v0, v209
	s_mov_b32 s98, 0x44800000
	s_mov_b32 s100, 0xbd38aa3b
	s_ashr_i32 s2, s0, 31
	v_ashrrev_i32_e32 v1, 2, v0
	v_and_b32_e32 v1, 0xffffffc0, v1
	v_lshl_add_u32 v1, s33, 8, v1
	v_and_or_b32 v4, v0, 15, v1
	v_lshrrev_b32_e32 v2, 1, v0
	s_lshr_b32 s2, s2, 29
	s_add_i32 s2, s0, s2
	s_and_b32 s2, s2, 0x1fffff8
	s_sub_i32 s0, s0, s2
	v_and_b32_e32 v2, 0x78, v2
	v_ashrrev_i32_e32 v5, 31, v4
	v_lshl_or_b32 v2, s0, 7, v2
	v_lshlrev_b64 v[0:1], 10, v[4:5]
	v_ashrrev_i32_e32 v3, 31, v2
	v_lshl_add_u64 v[0:1], s[8:9], 0, v[0:1]
	v_lshl_add_u64 v[0:1], v[0:1], 0, v[2:3]
	v_pk_mul_f32 v[10:11], v[188:189], s[100:101] op_sel_hi:[1,0]
	v_pk_mul_f32 v[12:13], v[190:191], s[100:101] op_sel_hi:[1,0]
	v_pk_mul_f32 v[14:15], v[180:181], s[100:101] op_sel_hi:[1,0]
	v_pk_mul_f32 v[16:17], v[182:183], s[100:101] op_sel_hi:[1,0]
	v_exp_f32_e32 v10, v10
	v_exp_f32_e32 v11, v11
	v_exp_f32_e32 v12, v12
	v_exp_f32_e32 v13, v13
	v_exp_f32_e32 v14, v14
	v_exp_f32_e32 v15, v15
	v_exp_f32_e32 v16, v16
	v_exp_f32_e32 v17, v17
	v_pk_fma_f32 v[10:11], v[10:11], s[98:99], s[98:99] op_sel_hi:[1,0,0]
	v_pk_fma_f32 v[12:13], v[12:13], s[98:99], s[98:99] op_sel_hi:[1,0,0]
	v_pk_fma_f32 v[14:15], v[14:15], s[98:99], s[98:99] op_sel_hi:[1,0,0]
	v_pk_fma_f32 v[16:17], v[16:17], s[98:99], s[98:99] op_sel_hi:[1,0,0]
	v_rcp_f32_e32 v10, v10
	v_rcp_f32_e32 v11, v11
	v_rcp_f32_e32 v12, v12
	v_rcp_f32_e32 v13, v13
	v_rcp_f32_e32 v14, v14
	v_rcp_f32_e32 v15, v15
	v_rcp_f32_e32 v16, v16
	v_rcp_f32_e32 v17, v17
	v_pk_mul_f32 v[10:11], v[188:189], v[10:11]
	v_pk_mul_f32 v[12:13], v[190:191], v[12:13]
	v_pk_mul_f32 v[14:15], v[180:181], v[14:15]
	v_pk_mul_f32 v[16:17], v[182:183], v[16:17]
	v_pk_mul_f32 v[10:11], v[10:11], v[184:185]
	v_pk_mul_f32 v[12:13], v[12:13], v[186:187]
	v_pk_mul_f32 v[14:15], v[14:15], v[176:177]
	v_pk_mul_f32 v[16:17], v[16:17], v[178:179]
	v_cvt_pk_fp8_f32 v18, v10, v11
	v_cvt_pk_fp8_f32 v19, v14, v15
	v_cvt_pk_fp8_f32 v18, v12, v13 op_sel:[0,0,1]
	v_cvt_pk_fp8_f32 v19, v16, v17 op_sel:[0,0,1]
	s_nop 0
	global_store_dwordx2 v[0:1], v[18:19], off
	v_or_b32_e32 v8, 16, v4
	v_ashrrev_i32_e32 v9, 31, v8
	v_lshlrev_b64 v[8:9], 10, v[8:9]
	v_lshl_add_u64 v[8:9], s[8:9], 0, v[8:9]
	v_lshl_add_u64 v[8:9], v[8:9], 0, v[2:3]
	v_pk_mul_f32 v[10:11], v[172:173], s[100:101] op_sel_hi:[1,0]
	v_pk_mul_f32 v[12:13], v[174:175], s[100:101] op_sel_hi:[1,0]
	v_pk_mul_f32 v[14:15], v[164:165], s[100:101] op_sel_hi:[1,0]
	v_pk_mul_f32 v[16:17], v[166:167], s[100:101] op_sel_hi:[1,0]
	v_exp_f32_e32 v10, v10
	v_exp_f32_e32 v11, v11
	v_exp_f32_e32 v12, v12
	v_exp_f32_e32 v13, v13
	v_exp_f32_e32 v14, v14
	v_exp_f32_e32 v15, v15
	v_exp_f32_e32 v16, v16
	v_exp_f32_e32 v17, v17
	v_pk_fma_f32 v[10:11], v[10:11], s[98:99], s[98:99] op_sel_hi:[1,0,0]
	v_pk_fma_f32 v[12:13], v[12:13], s[98:99], s[98:99] op_sel_hi:[1,0,0]
	v_pk_fma_f32 v[14:15], v[14:15], s[98:99], s[98:99] op_sel_hi:[1,0,0]
	v_pk_fma_f32 v[16:17], v[16:17], s[98:99], s[98:99] op_sel_hi:[1,0,0]
	v_rcp_f32_e32 v10, v10
	v_rcp_f32_e32 v11, v11
	v_rcp_f32_e32 v12, v12
	v_rcp_f32_e32 v13, v13
	v_rcp_f32_e32 v14, v14
	v_rcp_f32_e32 v15, v15
	v_rcp_f32_e32 v16, v16
	v_rcp_f32_e32 v17, v17
	v_pk_mul_f32 v[10:11], v[172:173], v[10:11]
	v_pk_mul_f32 v[12:13], v[174:175], v[12:13]
	v_pk_mul_f32 v[14:15], v[164:165], v[14:15]
	v_pk_mul_f32 v[16:17], v[166:167], v[16:17]
	v_pk_mul_f32 v[10:11], v[10:11], v[168:169]
	v_pk_mul_f32 v[12:13], v[12:13], v[170:171]
	v_pk_mul_f32 v[14:15], v[14:15], v[160:161]
	v_pk_mul_f32 v[16:17], v[16:17], v[162:163]
	v_cvt_pk_fp8_f32 v18, v10, v11
	v_cvt_pk_fp8_f32 v19, v14, v15
	v_cvt_pk_fp8_f32 v18, v12, v13 op_sel:[0,0,1]
	v_cvt_pk_fp8_f32 v19, v16, v17 op_sel:[0,0,1]
	s_nop 0
	global_store_dwordx2 v[8:9], v[18:19], off
	v_or_b32_e32 v8, 32, v4
	v_ashrrev_i32_e32 v9, 31, v8
	v_or_b32_e32 v4, 48, v4
	v_lshlrev_b64 v[6:7], 10, v[8:9]
	v_lshl_add_u64 v[6:7], s[8:9], 0, v[6:7]
	v_lshl_add_u64 v[6:7], v[6:7], 0, v[2:3]
	v_pk_mul_f32 v[10:11], v[156:157], s[100:101] op_sel_hi:[1,0]
	v_pk_mul_f32 v[12:13], v[158:159], s[100:101] op_sel_hi:[1,0]
	v_pk_mul_f32 v[14:15], v[148:149], s[100:101] op_sel_hi:[1,0]
	v_pk_mul_f32 v[16:17], v[150:151], s[100:101] op_sel_hi:[1,0]
	v_exp_f32_e32 v10, v10
	v_exp_f32_e32 v11, v11
	v_exp_f32_e32 v12, v12
	v_exp_f32_e32 v13, v13
	v_exp_f32_e32 v14, v14
	v_exp_f32_e32 v15, v15
	v_exp_f32_e32 v16, v16
	v_exp_f32_e32 v17, v17
	v_pk_fma_f32 v[10:11], v[10:11], s[98:99], s[98:99] op_sel_hi:[1,0,0]
	v_pk_fma_f32 v[12:13], v[12:13], s[98:99], s[98:99] op_sel_hi:[1,0,0]
	v_pk_fma_f32 v[14:15], v[14:15], s[98:99], s[98:99] op_sel_hi:[1,0,0]
	v_pk_fma_f32 v[16:17], v[16:17], s[98:99], s[98:99] op_sel_hi:[1,0,0]
	v_rcp_f32_e32 v10, v10
	v_rcp_f32_e32 v11, v11
	v_rcp_f32_e32 v12, v12
	v_rcp_f32_e32 v13, v13
	v_rcp_f32_e32 v14, v14
	v_rcp_f32_e32 v15, v15
	v_rcp_f32_e32 v16, v16
	v_rcp_f32_e32 v17, v17
	v_pk_mul_f32 v[10:11], v[156:157], v[10:11]
	v_pk_mul_f32 v[12:13], v[158:159], v[12:13]
	v_pk_mul_f32 v[14:15], v[148:149], v[14:15]
	v_pk_mul_f32 v[16:17], v[150:151], v[16:17]
	v_pk_mul_f32 v[10:11], v[10:11], v[152:153]
	v_pk_mul_f32 v[12:13], v[12:13], v[154:155]
	v_pk_mul_f32 v[14:15], v[14:15], v[144:145]
	v_pk_mul_f32 v[16:17], v[16:17], v[146:147]
	v_cvt_pk_fp8_f32 v18, v10, v11
	v_cvt_pk_fp8_f32 v19, v14, v15
	v_cvt_pk_fp8_f32 v18, v12, v13 op_sel:[0,0,1]
	v_cvt_pk_fp8_f32 v19, v16, v17 op_sel:[0,0,1]
	s_nop 0
	global_store_dwordx2 v[6:7], v[18:19], off
	v_ashrrev_i32_e32 v5, 31, v4
	v_lshlrev_b64 v[4:5], 10, v[4:5]
	v_lshl_add_u64 v[4:5], s[8:9], 0, v[4:5]
	v_lshl_add_u64 v[2:3], v[4:5], 0, v[2:3]
	s_mov_b32 s33, s52
	v_pk_mul_f32 v[10:11], v[140:141], s[100:101] op_sel_hi:[1,0]
	v_pk_mul_f32 v[12:13], v[142:143], s[100:101] op_sel_hi:[1,0]
	v_pk_mul_f32 v[14:15], v[132:133], s[100:101] op_sel_hi:[1,0]
	v_pk_mul_f32 v[16:17], v[134:135], s[100:101] op_sel_hi:[1,0]
	v_exp_f32_e32 v10, v10
	v_exp_f32_e32 v11, v11
	v_exp_f32_e32 v12, v12
	v_exp_f32_e32 v13, v13
	v_exp_f32_e32 v14, v14
	v_exp_f32_e32 v15, v15
	v_exp_f32_e32 v16, v16
	v_exp_f32_e32 v17, v17
	v_pk_fma_f32 v[10:11], v[10:11], s[98:99], s[98:99] op_sel_hi:[1,0,0]
	v_pk_fma_f32 v[12:13], v[12:13], s[98:99], s[98:99] op_sel_hi:[1,0,0]
	v_pk_fma_f32 v[14:15], v[14:15], s[98:99], s[98:99] op_sel_hi:[1,0,0]
	v_pk_fma_f32 v[16:17], v[16:17], s[98:99], s[98:99] op_sel_hi:[1,0,0]
	v_rcp_f32_e32 v10, v10
	v_rcp_f32_e32 v11, v11
	v_rcp_f32_e32 v12, v12
	v_rcp_f32_e32 v13, v13
	v_rcp_f32_e32 v14, v14
	v_rcp_f32_e32 v15, v15
	v_rcp_f32_e32 v16, v16
	v_rcp_f32_e32 v17, v17
	v_pk_mul_f32 v[10:11], v[140:141], v[10:11]
	v_pk_mul_f32 v[12:13], v[142:143], v[12:13]
	v_pk_mul_f32 v[14:15], v[132:133], v[14:15]
	v_pk_mul_f32 v[16:17], v[134:135], v[16:17]
	v_pk_mul_f32 v[10:11], v[10:11], v[136:137]
	v_pk_mul_f32 v[12:13], v[12:13], v[138:139]
	v_pk_mul_f32 v[14:15], v[14:15], v[128:129]
	v_pk_mul_f32 v[16:17], v[16:17], v[130:131]
	v_cvt_pk_fp8_f32 v18, v10, v11
	v_cvt_pk_fp8_f32 v19, v14, v15
	v_cvt_pk_fp8_f32 v18, v12, v13 op_sel:[0,0,1]
	v_cvt_pk_fp8_f32 v19, v16, v17 op_sel:[0,0,1]
	s_nop 0
	global_store_dwordx2 v[2:3], v[18:19], off
	s_mov_b32 s0, s16
	v_add_co_u32_e32 v6, vcc, s49, v0
	v_addc_co_u32_e32 v7, vcc, 0, v1, vcc
	v_pk_mul_f32 v[10:11], v[124:125], s[100:101] op_sel_hi:[1,0]
	v_pk_mul_f32 v[12:13], v[126:127], s[100:101] op_sel_hi:[1,0]
	v_pk_mul_f32 v[14:15], v[116:117], s[100:101] op_sel_hi:[1,0]
	v_pk_mul_f32 v[16:17], v[118:119], s[100:101] op_sel_hi:[1,0]
	v_exp_f32_e32 v10, v10
	v_exp_f32_e32 v11, v11
	v_exp_f32_e32 v12, v12
	v_exp_f32_e32 v13, v13
	v_exp_f32_e32 v14, v14
	v_exp_f32_e32 v15, v15
	v_exp_f32_e32 v16, v16
	v_exp_f32_e32 v17, v17
	v_pk_fma_f32 v[10:11], v[10:11], s[98:99], s[98:99] op_sel_hi:[1,0,0]
	v_pk_fma_f32 v[12:13], v[12:13], s[98:99], s[98:99] op_sel_hi:[1,0,0]
	v_pk_fma_f32 v[14:15], v[14:15], s[98:99], s[98:99] op_sel_hi:[1,0,0]
	v_pk_fma_f32 v[16:17], v[16:17], s[98:99], s[98:99] op_sel_hi:[1,0,0]
	v_rcp_f32_e32 v10, v10
	v_rcp_f32_e32 v11, v11
	v_rcp_f32_e32 v12, v12
	v_rcp_f32_e32 v13, v13
	v_rcp_f32_e32 v14, v14
	v_rcp_f32_e32 v15, v15
	v_rcp_f32_e32 v16, v16
	v_rcp_f32_e32 v17, v17
	v_pk_mul_f32 v[10:11], v[124:125], v[10:11]
	v_pk_mul_f32 v[12:13], v[126:127], v[12:13]
	v_pk_mul_f32 v[14:15], v[116:117], v[14:15]
	v_pk_mul_f32 v[16:17], v[118:119], v[16:17]
	v_pk_mul_f32 v[10:11], v[10:11], v[120:121]
	v_pk_mul_f32 v[12:13], v[12:13], v[122:123]
	v_pk_mul_f32 v[14:15], v[14:15], v[112:113]
	v_pk_mul_f32 v[16:17], v[16:17], v[114:115]
	v_cvt_pk_fp8_f32 v18, v10, v11
	v_cvt_pk_fp8_f32 v19, v14, v15
	v_cvt_pk_fp8_f32 v18, v12, v13 op_sel:[0,0,1]
	v_cvt_pk_fp8_f32 v19, v16, v17 op_sel:[0,0,1]
	s_nop 0
	global_store_dwordx2 v[6:7], v[18:19], off
	v_add_co_u32_e32 v6, vcc, s50, v0
	v_addc_co_u32_e32 v7, vcc, 0, v1, vcc
	v_pk_mul_f32 v[10:11], v[108:109], s[100:101] op_sel_hi:[1,0]
	v_pk_mul_f32 v[12:13], v[110:111], s[100:101] op_sel_hi:[1,0]
	v_pk_mul_f32 v[14:15], v[100:101], s[100:101] op_sel_hi:[1,0]
	v_pk_mul_f32 v[16:17], v[102:103], s[100:101] op_sel_hi:[1,0]
	v_exp_f32_e32 v10, v10
	v_exp_f32_e32 v11, v11
	v_exp_f32_e32 v12, v12
	v_exp_f32_e32 v13, v13
	v_exp_f32_e32 v14, v14
	v_exp_f32_e32 v15, v15
	v_exp_f32_e32 v16, v16
	v_exp_f32_e32 v17, v17
	v_pk_fma_f32 v[10:11], v[10:11], s[98:99], s[98:99] op_sel_hi:[1,0,0]
	v_pk_fma_f32 v[12:13], v[12:13], s[98:99], s[98:99] op_sel_hi:[1,0,0]
	v_pk_fma_f32 v[14:15], v[14:15], s[98:99], s[98:99] op_sel_hi:[1,0,0]
	v_pk_fma_f32 v[16:17], v[16:17], s[98:99], s[98:99] op_sel_hi:[1,0,0]
	v_rcp_f32_e32 v10, v10
	v_rcp_f32_e32 v11, v11
	v_rcp_f32_e32 v12, v12
	v_rcp_f32_e32 v13, v13
	v_rcp_f32_e32 v14, v14
	v_rcp_f32_e32 v15, v15
	v_rcp_f32_e32 v16, v16
	v_rcp_f32_e32 v17, v17
	v_pk_mul_f32 v[10:11], v[108:109], v[10:11]
	v_pk_mul_f32 v[12:13], v[110:111], v[12:13]
	v_pk_mul_f32 v[14:15], v[100:101], v[14:15]
	v_pk_mul_f32 v[16:17], v[102:103], v[16:17]
	v_pk_mul_f32 v[10:11], v[10:11], v[104:105]
	v_pk_mul_f32 v[12:13], v[12:13], v[106:107]
	v_pk_mul_f32 v[14:15], v[14:15], v[96:97]
	v_pk_mul_f32 v[16:17], v[16:17], v[98:99]
	v_cvt_pk_fp8_f32 v18, v10, v11
	v_cvt_pk_fp8_f32 v19, v14, v15
	v_cvt_pk_fp8_f32 v18, v12, v13 op_sel:[0,0,1]
	v_cvt_pk_fp8_f32 v19, v16, v17 op_sel:[0,0,1]
	s_nop 0
	global_store_dwordx2 v[6:7], v[18:19], off
	v_add_co_u32_e32 v6, vcc, s51, v0
	v_addc_co_u32_e32 v7, vcc, 0, v1, vcc
	v_pk_mul_f32 v[10:11], v[92:93], s[100:101] op_sel_hi:[1,0]
	v_pk_mul_f32 v[12:13], v[94:95], s[100:101] op_sel_hi:[1,0]
	v_pk_mul_f32 v[14:15], v[84:85], s[100:101] op_sel_hi:[1,0]
	v_pk_mul_f32 v[16:17], v[86:87], s[100:101] op_sel_hi:[1,0]
	v_exp_f32_e32 v10, v10
	v_exp_f32_e32 v11, v11
	v_exp_f32_e32 v12, v12
	v_exp_f32_e32 v13, v13
	v_exp_f32_e32 v14, v14
	v_exp_f32_e32 v15, v15
	v_exp_f32_e32 v16, v16
	v_exp_f32_e32 v17, v17
	v_pk_fma_f32 v[10:11], v[10:11], s[98:99], s[98:99] op_sel_hi:[1,0,0]
	v_pk_fma_f32 v[12:13], v[12:13], s[98:99], s[98:99] op_sel_hi:[1,0,0]
	v_pk_fma_f32 v[14:15], v[14:15], s[98:99], s[98:99] op_sel_hi:[1,0,0]
	v_pk_fma_f32 v[16:17], v[16:17], s[98:99], s[98:99] op_sel_hi:[1,0,0]
	v_rcp_f32_e32 v10, v10
	v_rcp_f32_e32 v11, v11
	v_rcp_f32_e32 v12, v12
	v_rcp_f32_e32 v13, v13
	v_rcp_f32_e32 v14, v14
	v_rcp_f32_e32 v15, v15
	v_rcp_f32_e32 v16, v16
	v_rcp_f32_e32 v17, v17
	v_pk_mul_f32 v[10:11], v[92:93], v[10:11]
	v_pk_mul_f32 v[12:13], v[94:95], v[12:13]
	v_pk_mul_f32 v[14:15], v[84:85], v[14:15]
	v_pk_mul_f32 v[16:17], v[86:87], v[16:17]
	v_pk_mul_f32 v[10:11], v[10:11], v[88:89]
	v_pk_mul_f32 v[12:13], v[12:13], v[90:91]
	v_pk_mul_f32 v[14:15], v[14:15], v[80:81]
	v_pk_mul_f32 v[16:17], v[16:17], v[82:83]
	v_cvt_pk_fp8_f32 v18, v10, v11
	v_cvt_pk_fp8_f32 v19, v14, v15
	v_cvt_pk_fp8_f32 v18, v12, v13 op_sel:[0,0,1]
	v_cvt_pk_fp8_f32 v19, v16, v17 op_sel:[0,0,1]
	s_nop 0
	global_store_dwordx2 v[6:7], v[18:19], off
	v_add_co_u32_e32 v0, vcc, 0x2c000, v0
	s_mov_b64 s[2:3], s[18:19]
	s_nop 0
	v_addc_co_u32_e32 v1, vcc, 0, v1, vcc
	s_and_b64 vcc, exec, s[10:11]
	v_pk_mul_f32 v[10:11], v[76:77], s[100:101] op_sel_hi:[1,0]
	v_pk_mul_f32 v[12:13], v[78:79], s[100:101] op_sel_hi:[1,0]
	v_pk_mul_f32 v[14:15], v[68:69], s[100:101] op_sel_hi:[1,0]
	v_pk_mul_f32 v[16:17], v[70:71], s[100:101] op_sel_hi:[1,0]
	v_exp_f32_e32 v10, v10
	v_exp_f32_e32 v11, v11
	v_exp_f32_e32 v12, v12
	v_exp_f32_e32 v13, v13
	v_exp_f32_e32 v14, v14
	v_exp_f32_e32 v15, v15
	v_exp_f32_e32 v16, v16
	v_exp_f32_e32 v17, v17
	v_pk_fma_f32 v[10:11], v[10:11], s[98:99], s[98:99] op_sel_hi:[1,0,0]
	v_pk_fma_f32 v[12:13], v[12:13], s[98:99], s[98:99] op_sel_hi:[1,0,0]
	v_pk_fma_f32 v[14:15], v[14:15], s[98:99], s[98:99] op_sel_hi:[1,0,0]
	v_pk_fma_f32 v[16:17], v[16:17], s[98:99], s[98:99] op_sel_hi:[1,0,0]
	v_rcp_f32_e32 v10, v10
	v_rcp_f32_e32 v11, v11
	v_rcp_f32_e32 v12, v12
	v_rcp_f32_e32 v13, v13
	v_rcp_f32_e32 v14, v14
	v_rcp_f32_e32 v15, v15
	v_rcp_f32_e32 v16, v16
	v_rcp_f32_e32 v17, v17
	v_pk_mul_f32 v[10:11], v[76:77], v[10:11]
	v_pk_mul_f32 v[12:13], v[78:79], v[12:13]
	v_pk_mul_f32 v[14:15], v[68:69], v[14:15]
	v_pk_mul_f32 v[16:17], v[70:71], v[16:17]
	v_pk_mul_f32 v[10:11], v[10:11], v[72:73]
	v_pk_mul_f32 v[12:13], v[12:13], v[74:75]
	v_pk_mul_f32 v[14:15], v[14:15], v[64:65]
	v_pk_mul_f32 v[16:17], v[16:17], v[66:67]
	v_cvt_pk_fp8_f32 v18, v10, v11
	v_cvt_pk_fp8_f32 v19, v14, v15
	v_cvt_pk_fp8_f32 v18, v12, v13 op_sel:[0,0,1]
	v_cvt_pk_fp8_f32 v19, v16, v17 op_sel:[0,0,1]
	s_nop 0
	global_store_dwordx2 v[0:1], v[18:19], off
	s_cbranch_vccnz .LBB0_2965

.LBB0_2962:
	s_add_i32 s22, s20, 0xf2401100
	s_and_b32 s55, s22, 0x300
	s_add_u32 s24, s2, s55
	s_addc_u32 s25, s3, 0
	s_and_b64 s[22:23], s[26:27], exec
	s_cselect_b32 s23, s17, s25
	s_cselect_b32 s22, s53, s24
	s_mov_b64 s[24:25], s[22:23]
	s_mov_b32 m0, s34
	ds_read_b128 v[16:19], v217
	ds_read_b128 v[20:23], v218
	ds_read_b128 v[24:27], v225
	ds_read_b128 v[28:31], v226
	v_mov_b32_e32 v203, v197
	global_load_lds_dwordx4 v194, s[24:25]
	v_lshl_add_u64 v[236:237], s[24:25], 0, v[192:193]
	s_mov_b32 m0, s35
	s_add_u32 s24, s22, 0x80
	global_load_lds_dwordx4 v[236:237], off
	s_nop 0
	s_barrier
	s_waitcnt lgkmcnt(0)
	s_addc_u32 s25, s23, 0
	s_and_b64 s[26:27], s[26:27], exec
	s_cselect_b32 s27, 0, 0
	s_cselect_b32 s26, 0, s55
	s_setprio 1
	s_waitcnt lgkmcnt(0)
	v_mfma_scale_f32_16x16x128_f8f6f4 v[184:187], v[16:23], v[56:63], v[184:187], v212, v212 op_sel_hi:[0,0,0]
	v_mfma_scale_f32_16x16x128_f8f6f4 v[176:179], v[24:31], v[56:63], v[176:179], v212, v212 op_sel_hi:[0,0,0]
	v_mfma_scale_f32_16x16x128_f8f6f4 v[168:171], v[16:23], v[48:55], v[168:171], v212, v212 op_sel_hi:[0,0,0]
	v_mfma_scale_f32_16x16x128_f8f6f4 v[160:163], v[24:31], v[48:55], v[160:163], v212, v212 op_sel_hi:[0,0,0]
	v_mfma_scale_f32_16x16x128_f8f6f4 v[152:155], v[16:23], v[40:47], v[152:155], v212, v212 op_sel_hi:[0,0,0]
	v_mfma_scale_f32_16x16x128_f8f6f4 v[144:147], v[24:31], v[40:47], v[144:147], v212, v212 op_sel_hi:[0,0,0]
	v_mfma_scale_f32_16x16x128_f8f6f4 v[136:139], v[16:23], v[32:39], v[136:139], v212, v212 op_sel_hi:[0,0,0]
	v_mfma_scale_f32_16x16x128_f8f6f4 v[128:131], v[24:31], v[32:39], v[128:131], v212, v212 op_sel_hi:[0,0,0]
	s_setprio 0
	s_add_u32 s26, s6, s26
	s_addc_u32 s27, s7, s27
	s_mov_b64 s[56:57], s[26:27]
	s_mov_b32 m0, s1
	s_barrier
	ds_read_b128 v[32:35], v231 offset:16384
	ds_read_b128 v[40:43], v231 offset:18432
	ds_read_b128 v[36:39], v232 offset:16384
	ds_read_b128 v[44:47], v232 offset:18432
	ds_read_b128 v[48:51], v231 offset:20480
	ds_read_b128 v[56:59], v231 offset:22528
	ds_read_b128 v[52:55], v232 offset:20480
	ds_read_b128 v[60:63], v232 offset:22528
	s_nop 0
	global_load_lds_dwordx4 v198, s[56:57]
	s_mov_b32 m0, s36
	s_nop 0
	global_load_lds_dwordx4 v200, s[56:57]
	s_nop 0
	s_barrier
	s_waitcnt lgkmcnt(0)
	s_setprio 1
	s_waitcnt lgkmcnt(0)
	v_mfma_scale_f32_16x16x128_f8f6f4 v[124:127], v[0:7], v[32:39], v[124:127], v212, v212 op_sel_hi:[0,0,0]
	v_mfma_scale_f32_16x16x128_f8f6f4 v[116:119], v[8:15], v[32:39], v[116:119], v212, v212 op_sel_hi:[0,0,0]
	v_mfma_scale_f32_16x16x128_f8f6f4 v[108:111], v[0:7], v[40:47], v[108:111], v212, v212 op_sel_hi:[0,0,0]
	v_mfma_scale_f32_16x16x128_f8f6f4 v[100:103], v[8:15], v[40:47], v[100:103], v212, v212 op_sel_hi:[0,0,0]
	v_mfma_scale_f32_16x16x128_f8f6f4 v[92:95], v[0:7], v[48:55], v[92:95], v212, v212 op_sel_hi:[0,0,0]
	v_mfma_scale_f32_16x16x128_f8f6f4 v[84:87], v[8:15], v[48:55], v[84:87], v212, v212 op_sel_hi:[0,0,0]
	v_mfma_scale_f32_16x16x128_f8f6f4 v[76:79], v[0:7], v[56:63], v[76:79], v212, v212 op_sel_hi:[0,0,0]
	v_mfma_scale_f32_16x16x128_f8f6f4 v[68:71], v[8:15], v[56:63], v[68:71], v212, v212 op_sel_hi:[0,0,0]
	s_setprio 0
	s_barrier
	s_add_u32 s56, s22, 0x20000
	s_addc_u32 s57, s23, 0
	s_mov_b32 m0, s37
	s_nop 0
	global_load_lds_dwordx4 v194, s[56:57]
	s_mov_b32 m0, s38
	s_nop 0
	global_load_lds_dwordx4 v192, s[56:57]
	s_waitcnt vmcnt(6)
	s_barrier
	s_setprio 1
	v_mfma_scale_f32_16x16x128_f8f6f4 v[120:123], v[16:23], v[32:39], v[120:123], v212, v212 op_sel_hi:[0,0,0]
	v_mfma_scale_f32_16x16x128_f8f6f4 v[112:115], v[24:31], v[32:39], v[112:115], v212, v212 op_sel_hi:[0,0,0]
	v_mfma_scale_f32_16x16x128_f8f6f4 v[104:107], v[16:23], v[40:47], v[104:107], v212, v212 op_sel_hi:[0,0,0]
	v_mfma_scale_f32_16x16x128_f8f6f4 v[96:99], v[24:31], v[40:47], v[96:99], v212, v212 op_sel_hi:[0,0,0]
	v_mfma_scale_f32_16x16x128_f8f6f4 v[88:91], v[16:23], v[48:55], v[88:91], v212, v212 op_sel_hi:[0,0,0]
	v_mfma_scale_f32_16x16x128_f8f6f4 v[80:83], v[24:31], v[48:55], v[80:83], v212, v212 op_sel_hi:[0,0,0]
	v_mfma_scale_f32_16x16x128_f8f6f4 v[72:75], v[16:23], v[56:63], v[72:75], v212, v212 op_sel_hi:[0,0,0]
	v_mfma_scale_f32_16x16x128_f8f6f4 v[64:67], v[24:31], v[56:63], v[64:67], v212, v212 op_sel_hi:[0,0,0]
	s_setprio 0
	s_barrier
	ds_read_b128 v[0:3], v219
	ds_read_b128 v[4:7], v220
	ds_read_b128 v[8:11], v227
	ds_read_b128 v[12:15], v228
	s_mov_b64 s[56:57], s[26:27]
	s_mov_b32 m0, s39
	ds_read_b128 v[16:19], v231 offset:32768
	ds_read_b128 v[24:27], v231 offset:34816
	ds_read_b128 v[20:23], v232 offset:32768
	ds_read_b128 v[28:31], v232 offset:34816
	ds_read_b128 v[32:35], v231 offset:36864
	ds_read_b128 v[40:43], v231 offset:38912
	ds_read_b128 v[36:39], v232 offset:36864
	ds_read_b128 v[44:47], v232 offset:38912
	s_nop 0
	global_load_lds_dwordx4 v196, s[56:57]
	s_mov_b32 m0, s40
	s_nop 0
	global_load_lds_dwordx4 v202, s[56:57]
	s_waitcnt lgkmcnt(8)
	s_barrier
	s_waitcnt lgkmcnt(0)
	s_setprio 1
	s_waitcnt lgkmcnt(0)
	v_mfma_scale_f32_16x16x128_f8f6f4 v[188:191], v[0:7], v[16:23], v[188:191], v212, v212 op_sel_hi:[0,0,0]
	v_mfma_scale_f32_16x16x128_f8f6f4 v[180:183], v[8:15], v[16:23], v[180:183], v212, v212 op_sel_hi:[0,0,0]
	v_mfma_scale_f32_16x16x128_f8f6f4 v[172:175], v[0:7], v[24:31], v[172:175], v212, v212 op_sel_hi:[0,0,0]
	v_mfma_scale_f32_16x16x128_f8f6f4 v[164:167], v[8:15], v[24:31], v[164:167], v212, v212 op_sel_hi:[0,0,0]
	v_mfma_scale_f32_16x16x128_f8f6f4 v[156:159], v[0:7], v[32:39], v[156:159], v212, v212 op_sel_hi:[0,0,0]
	v_mfma_scale_f32_16x16x128_f8f6f4 v[148:151], v[8:15], v[32:39], v[148:151], v212, v212 op_sel_hi:[0,0,0]
	v_mfma_scale_f32_16x16x128_f8f6f4 v[140:143], v[0:7], v[40:47], v[140:143], v212, v212 op_sel_hi:[0,0,0]
	v_mfma_scale_f32_16x16x128_f8f6f4 v[132:135], v[8:15], v[40:47], v[132:135], v212, v212 op_sel_hi:[0,0,0]
	s_setprio 0
	s_barrier
	s_mov_b32 m0, s42
	ds_read_b128 v[48:51], v221
	ds_read_b128 v[52:55], v222
	ds_read_b128 v[56:59], v229
	ds_read_b128 v[60:63], v230
	s_nop 0
	global_load_lds_dwordx4 v194, s[24:25]
	s_mov_b32 m0, s43
	s_nop 0
	global_load_lds_dwordx4 v192, s[24:25]
	s_barrier
	s_waitcnt lgkmcnt(0)
	s_setprio 1
	s_waitcnt lgkmcnt(0)
	v_mfma_scale_f32_16x16x128_f8f6f4 v[184:187], v[48:55], v[16:23], v[184:187], v212, v212 op_sel_hi:[0,0,0]
	v_mfma_scale_f32_16x16x128_f8f6f4 v[176:179], v[56:63], v[16:23], v[176:179], v212, v212 op_sel_hi:[0,0,0]
	v_mfma_scale_f32_16x16x128_f8f6f4 v[168:171], v[48:55], v[24:31], v[168:171], v212, v212 op_sel_hi:[0,0,0]
	v_mfma_scale_f32_16x16x128_f8f6f4 v[160:163], v[56:63], v[24:31], v[160:163], v212, v212 op_sel_hi:[0,0,0]
	v_mfma_scale_f32_16x16x128_f8f6f4 v[152:155], v[48:55], v[32:39], v[152:155], v212, v212 op_sel_hi:[0,0,0]
	v_mfma_scale_f32_16x16x128_f8f6f4 v[144:147], v[56:63], v[32:39], v[144:147], v212, v212 op_sel_hi:[0,0,0]
	v_mfma_scale_f32_16x16x128_f8f6f4 v[136:139], v[48:55], v[40:47], v[136:139], v212, v212 op_sel_hi:[0,0,0]
	v_mfma_scale_f32_16x16x128_f8f6f4 v[128:131], v[56:63], v[40:47], v[128:131], v212, v212 op_sel_hi:[0,0,0]
	s_setprio 0
	s_add_u32 s24, s26, 0x80
	s_addc_u32 s25, s27, 0
	s_mov_b32 m0, s44
	s_barrier
	ds_read_b128 v[16:19], v231 offset:49152
	ds_read_b128 v[24:27], v231 offset:51200
	ds_read_b128 v[20:23], v232 offset:49152
	ds_read_b128 v[28:31], v232 offset:51200
	ds_read_b128 v[32:35], v231 offset:53248
	ds_read_b128 v[40:43], v231 offset:55296
	ds_read_b128 v[36:39], v232 offset:53248
	ds_read_b128 v[44:47], v232 offset:55296
	s_nop 0
	global_load_lds_dwordx4 v198, s[24:25]
	s_mov_b32 m0, s45
	s_nop 0
	global_load_lds_dwordx4 v200, s[24:25]
	s_nop 0
	s_barrier
	s_waitcnt lgkmcnt(0)
	s_setprio 1
	s_waitcnt lgkmcnt(0)
	v_mfma_scale_f32_16x16x128_f8f6f4 v[124:127], v[0:7], v[16:23], v[124:127], v212, v212 op_sel_hi:[0,0,0]
	v_mfma_scale_f32_16x16x128_f8f6f4 v[116:119], v[8:15], v[16:23], v[116:119], v212, v212 op_sel_hi:[0,0,0]
	v_mfma_scale_f32_16x16x128_f8f6f4 v[108:111], v[0:7], v[24:31], v[108:111], v212, v212 op_sel_hi:[0,0,0]
	v_mfma_scale_f32_16x16x128_f8f6f4 v[100:103], v[8:15], v[24:31], v[100:103], v212, v212 op_sel_hi:[0,0,0]
	v_mfma_scale_f32_16x16x128_f8f6f4 v[92:95], v[0:7], v[32:39], v[92:95], v212, v212 op_sel_hi:[0,0,0]
	v_mfma_scale_f32_16x16x128_f8f6f4 v[84:87], v[8:15], v[32:39], v[84:87], v212, v212 op_sel_hi:[0,0,0]
	v_mfma_scale_f32_16x16x128_f8f6f4 v[76:79], v[0:7], v[40:47], v[76:79], v212, v212 op_sel_hi:[0,0,0]
	v_mfma_scale_f32_16x16x128_f8f6f4 v[68:71], v[8:15], v[40:47], v[68:71], v212, v212 op_sel_hi:[0,0,0]
	s_setprio 0
	s_barrier
	s_add_u32 s22, s22, 0x20080
	s_addc_u32 s23, s23, 0
	s_mov_b32 m0, s46
	s_nop 0
	global_load_lds_dwordx4 v194, s[22:23]
	s_mov_b32 m0, s47
	s_nop 0
	global_load_lds_dwordx4 v192, s[22:23]
	s_waitcnt vmcnt(6)
	s_barrier
	s_setprio 1
	v_mfma_scale_f32_16x16x128_f8f6f4 v[120:123], v[48:55], v[16:23], v[120:123], v212, v212 op_sel_hi:[0,0,0]
	v_mfma_scale_f32_16x16x128_f8f6f4 v[112:115], v[56:63], v[16:23], v[112:115], v212, v212 op_sel_hi:[0,0,0]
	v_mfma_scale_f32_16x16x128_f8f6f4 v[104:107], v[48:55], v[24:31], v[104:107], v212, v212 op_sel_hi:[0,0,0]
	v_mfma_scale_f32_16x16x128_f8f6f4 v[96:99], v[56:63], v[24:31], v[96:99], v212, v212 op_sel_hi:[0,0,0]
	v_mfma_scale_f32_16x16x128_f8f6f4 v[88:91], v[48:55], v[32:39], v[88:91], v212, v212 op_sel_hi:[0,0,0]
	v_mfma_scale_f32_16x16x128_f8f6f4 v[80:83], v[56:63], v[32:39], v[80:83], v212, v212 op_sel_hi:[0,0,0]
	v_mfma_scale_f32_16x16x128_f8f6f4 v[72:75], v[48:55], v[40:47], v[72:75], v212, v212 op_sel_hi:[0,0,0]
	v_mfma_scale_f32_16x16x128_f8f6f4 v[64:67], v[56:63], v[40:47], v[64:67], v212, v212 op_sel_hi:[0,0,0]
	s_setprio 0
	s_add_i32 s54, s54, 2
	s_add_u32 s20, s20, 0x100
	s_addc_u32 s21, s21, 0
	s_cmp_gt_u32 s54, 5
	s_barrier
	s_cbranch_scc1 .LBB0_2958

.LBB0_3027:
	s_add_u32 s30, s36, 0x100
	ds_read_b128 v[0:3], v174
	ds_read_b128 v[4:7], v175
	ds_read_b128 v[8:11], v182
	ds_read_b128 v[12:15], v183
	s_addc_u32 s31, s37, 0
	s_and_b32 s66, s30, 0x300
	s_add_u32 s65, s26, s66
	s_addc_u32 s67, s27, 0
	s_cmp_eq_u32 s33, 4
	s_cselect_b64 s[38:39], -1, 0
	s_and_b64 s[34:35], s[38:39], exec
	s_cselect_b32 s35, s21, s67
	s_cselect_b32 s34, s23, s65
	s_cselect_b32 s65, 0, 0
	s_cselect_b32 s66, 0, s66
	s_add_u32 s36, s28, s36
	s_addc_u32 s37, s29, s37
	s_add_u32 s36, s36, 0x20080
	s_addc_u32 s37, s37, 0
	ds_read_b128 v[194:197], v190
	ds_read_b128 v[210:213], v190 offset:2048
	ds_read_b128 v[198:201], v191
	ds_read_b128 v[214:217], v191 offset:2048
	ds_read_b128 v[218:221], v190 offset:4096
	ds_read_b128 v[226:229], v190 offset:6144
	ds_read_b128 v[222:225], v191 offset:4096
	ds_read_b128 v[230:233], v191 offset:6144
	s_add_i32 m0, s1, 0xc000
	s_nop 0
	global_load_lds_dwordx4 v166, s[36:37]
	s_add_i32 m0, s1, 0xe000
	s_nop 0
	global_load_lds_dwordx4 v162, s[36:37]
	s_waitcnt lgkmcnt(8)
	s_barrier
	s_waitcnt lgkmcnt(0)
	s_setprio 1
	s_waitcnt lgkmcnt(0)
	v_mfma_scale_f32_16x16x128_f8f6f4 v[156:159], v[0:7], v[194:201], v[156:159], v173, v173 op_sel_hi:[0,0,0]
	v_mfma_scale_f32_16x16x128_f8f6f4 v[152:155], v[8:15], v[194:201], v[152:155], v173, v173 op_sel_hi:[0,0,0]
	v_mfma_scale_f32_16x16x128_f8f6f4 v[140:143], v[0:7], v[210:217], v[140:143], v173, v173 op_sel_hi:[0,0,0]
	v_mfma_scale_f32_16x16x128_f8f6f4 v[136:139], v[8:15], v[210:217], v[136:139], v173, v173 op_sel_hi:[0,0,0]
	v_mfma_scale_f32_16x16x128_f8f6f4 v[124:127], v[0:7], v[218:225], v[124:127], v173, v173 op_sel_hi:[0,0,0]
	v_mfma_scale_f32_16x16x128_f8f6f4 v[120:123], v[8:15], v[218:225], v[120:123], v173, v173 op_sel_hi:[0,0,0]
	v_mfma_scale_f32_16x16x128_f8f6f4 v[108:111], v[0:7], v[226:233], v[108:111], v173, v173 op_sel_hi:[0,0,0]
	v_mfma_scale_f32_16x16x128_f8f6f4 v[104:107], v[8:15], v[226:233], v[104:107], v173, v173 op_sel_hi:[0,0,0]
	s_setprio 0
	s_barrier
	s_mov_b64 s[36:37], s[34:35]
	s_mov_b32 m0, s3
	ds_read_b128 v[16:19], v176
	ds_read_b128 v[20:23], v177
	ds_read_b128 v[24:27], v184
	ds_read_b128 v[28:31], v185
	s_nop 0
	global_load_lds_dwordx4 v164, s[36:37]
	s_mov_b32 m0, s47
	s_nop 0
	global_load_lds_dwordx4 v160, s[36:37]
	s_nop 0
	s_barrier
	s_waitcnt lgkmcnt(0)
	s_setprio 1
	s_waitcnt lgkmcnt(0)
	v_mfma_scale_f32_16x16x128_f8f6f4 v[148:151], v[16:23], v[194:201], v[148:151], v173, v173 op_sel_hi:[0,0,0]
	v_mfma_scale_f32_16x16x128_f8f6f4 v[144:147], v[24:31], v[194:201], v[144:147], v173, v173 op_sel_hi:[0,0,0]
	v_mfma_scale_f32_16x16x128_f8f6f4 v[132:135], v[16:23], v[210:217], v[132:135], v173, v173 op_sel_hi:[0,0,0]
	v_mfma_scale_f32_16x16x128_f8f6f4 v[128:131], v[24:31], v[210:217], v[128:131], v173, v173 op_sel_hi:[0,0,0]
	v_mfma_scale_f32_16x16x128_f8f6f4 v[116:119], v[16:23], v[218:225], v[116:119], v173, v173 op_sel_hi:[0,0,0]
	v_mfma_scale_f32_16x16x128_f8f6f4 v[112:115], v[24:31], v[218:225], v[112:115], v173, v173 op_sel_hi:[0,0,0]
	v_mfma_scale_f32_16x16x128_f8f6f4 v[100:103], v[16:23], v[226:233], v[100:103], v173, v173 op_sel_hi:[0,0,0]
	v_mfma_scale_f32_16x16x128_f8f6f4 v[96:99], v[24:31], v[226:233], v[96:99], v173, v173 op_sel_hi:[0,0,0]
	s_setprio 0
	s_and_b64 s[36:37], s[12:13], s[38:39]
	s_and_b64 s[36:37], s[36:37], exec
	s_cselect_b32 s36, s6, s28
	s_cselect_b32 s37, s7, s29
	s_add_u32 s36, s36, s66
	s_addc_u32 s37, s37, s65
	s_mov_b64 s[38:39], s[36:37]
	s_mov_b32 m0, s1
	s_barrier
	ds_read_b128 v[194:197], v190 offset:16384
	ds_read_b128 v[210:213], v190 offset:18432
	ds_read_b128 v[198:201], v191 offset:16384
	ds_read_b128 v[214:217], v191 offset:18432
	ds_read_b128 v[218:221], v190 offset:20480
	ds_read_b128 v[226:229], v190 offset:22528
	ds_read_b128 v[222:225], v191 offset:20480
	ds_read_b128 v[230:233], v191 offset:22528
	s_nop 0
	global_load_lds_dwordx4 v166, s[38:39]
	s_mov_b32 m0, s48
	s_nop 0
	global_load_lds_dwordx4 v162, s[38:39]
	s_nop 0
	s_barrier
	s_waitcnt lgkmcnt(0)
	s_setprio 1
	s_waitcnt lgkmcnt(0)
	v_mfma_scale_f32_16x16x128_f8f6f4 v[92:95], v[0:7], v[194:201], v[92:95], v173, v173 op_sel_hi:[0,0,0]
	v_mfma_scale_f32_16x16x128_f8f6f4 v[88:91], v[8:15], v[194:201], v[88:91], v173, v173 op_sel_hi:[0,0,0]
	v_mfma_scale_f32_16x16x128_f8f6f4 v[76:79], v[0:7], v[210:217], v[76:79], v173, v173 op_sel_hi:[0,0,0]
	v_mfma_scale_f32_16x16x128_f8f6f4 v[72:75], v[8:15], v[210:217], v[72:75], v173, v173 op_sel_hi:[0,0,0]
	v_mfma_scale_f32_16x16x128_f8f6f4 v[60:63], v[0:7], v[218:225], v[60:63], v173, v173 op_sel_hi:[0,0,0]
	v_mfma_scale_f32_16x16x128_f8f6f4 v[56:59], v[8:15], v[218:225], v[56:59], v173, v173 op_sel_hi:[0,0,0]
	v_mfma_scale_f32_16x16x128_f8f6f4 v[44:47], v[0:7], v[226:233], v[44:47], v173, v173 op_sel_hi:[0,0,0]
	v_mfma_scale_f32_16x16x128_f8f6f4 v[40:43], v[8:15], v[226:233], v[40:43], v173, v173 op_sel_hi:[0,0,0]
	s_setprio 0
	s_barrier
	s_add_u32 s38, s34, 0x20000
	s_addc_u32 s39, s35, 0
	s_mov_b32 m0, s49
	s_nop 0
	global_load_lds_dwordx4 v164, s[38:39]
	s_mov_b32 m0, s50
	s_nop 0
	global_load_lds_dwordx4 v160, s[38:39]
	s_waitcnt vmcnt(6)
	s_barrier
	s_setprio 1
	v_mfma_scale_f32_16x16x128_f8f6f4 v[84:87], v[16:23], v[194:201], v[84:87], v173, v173 op_sel_hi:[0,0,0]
	v_mfma_scale_f32_16x16x128_f8f6f4 v[80:83], v[24:31], v[194:201], v[80:83], v173, v173 op_sel_hi:[0,0,0]
	v_mfma_scale_f32_16x16x128_f8f6f4 v[68:71], v[16:23], v[210:217], v[68:71], v173, v173 op_sel_hi:[0,0,0]
	v_mfma_scale_f32_16x16x128_f8f6f4 v[64:67], v[24:31], v[210:217], v[64:67], v173, v173 op_sel_hi:[0,0,0]
	v_mfma_scale_f32_16x16x128_f8f6f4 v[52:55], v[16:23], v[218:225], v[52:55], v173, v173 op_sel_hi:[0,0,0]
	v_mfma_scale_f32_16x16x128_f8f6f4 v[48:51], v[24:31], v[218:225], v[48:51], v173, v173 op_sel_hi:[0,0,0]
	v_mfma_scale_f32_16x16x128_f8f6f4 v[36:39], v[16:23], v[226:233], v[36:39], v173, v173 op_sel_hi:[0,0,0]
	v_mfma_scale_f32_16x16x128_f8f6f4 v[32:35], v[24:31], v[226:233], v[32:35], v173, v173 op_sel_hi:[0,0,0]
	s_setprio 0
	s_barrier
	ds_read_b128 v[0:3], v178
	ds_read_b128 v[4:7], v179
	ds_read_b128 v[8:11], v186
	ds_read_b128 v[12:15], v187
	s_add_u32 s38, s36, 0x20000
	s_addc_u32 s39, s37, 0
	s_mov_b32 m0, s51
	ds_read_b128 v[16:19], v190 offset:32768
	ds_read_b128 v[24:27], v190 offset:34816
	ds_read_b128 v[20:23], v191 offset:32768
	ds_read_b128 v[28:31], v191 offset:34816
	ds_read_b128 v[194:197], v190 offset:36864
	ds_read_b128 v[210:213], v190 offset:38912
	ds_read_b128 v[198:201], v191 offset:36864
	ds_read_b128 v[214:217], v191 offset:38912
	s_nop 0
	global_load_lds_dwordx4 v166, s[38:39]
	s_mov_b32 m0, s52
	s_nop 0
	global_load_lds_dwordx4 v162, s[38:39]
	s_waitcnt lgkmcnt(8)
	s_barrier
	s_waitcnt lgkmcnt(0)
	s_setprio 1
	s_waitcnt lgkmcnt(0)
	v_mfma_scale_f32_16x16x128_f8f6f4 v[156:159], v[0:7], v[16:23], v[156:159], v173, v173 op_sel_hi:[0,0,0]
	v_mfma_scale_f32_16x16x128_f8f6f4 v[152:155], v[8:15], v[16:23], v[152:155], v173, v173 op_sel_hi:[0,0,0]
	v_mfma_scale_f32_16x16x128_f8f6f4 v[140:143], v[0:7], v[24:31], v[140:143], v173, v173 op_sel_hi:[0,0,0]
	v_mfma_scale_f32_16x16x128_f8f6f4 v[136:139], v[8:15], v[24:31], v[136:139], v173, v173 op_sel_hi:[0,0,0]
	v_mfma_scale_f32_16x16x128_f8f6f4 v[124:127], v[0:7], v[194:201], v[124:127], v173, v173 op_sel_hi:[0,0,0]
	v_mfma_scale_f32_16x16x128_f8f6f4 v[120:123], v[8:15], v[194:201], v[120:123], v173, v173 op_sel_hi:[0,0,0]
	v_mfma_scale_f32_16x16x128_f8f6f4 v[108:111], v[0:7], v[210:217], v[108:111], v173, v173 op_sel_hi:[0,0,0]
	v_mfma_scale_f32_16x16x128_f8f6f4 v[104:107], v[8:15], v[210:217], v[104:107], v173, v173 op_sel_hi:[0,0,0]
	s_setprio 0
	s_barrier
	s_add_u32 s38, s34, 0x80
	s_addc_u32 s39, s35, 0
	s_mov_b32 m0, s54
	ds_read_b128 v[218:221], v180
	ds_read_b128 v[222:225], v181
	ds_read_b128 v[226:229], v188
	ds_read_b128 v[230:233], v189
	s_nop 0
	global_load_lds_dwordx4 v164, s[38:39]
	s_mov_b32 m0, s55
	s_nop 0
	global_load_lds_dwordx4 v160, s[38:39]
	s_nop 0
	s_barrier
	s_waitcnt lgkmcnt(0)
	s_setprio 1
	s_waitcnt lgkmcnt(0)
	v_mfma_scale_f32_16x16x128_f8f6f4 v[148:151], v[218:225], v[16:23], v[148:151], v173, v173 op_sel_hi:[0,0,0]
	v_mfma_scale_f32_16x16x128_f8f6f4 v[144:147], v[226:233], v[16:23], v[144:147], v173, v173 op_sel_hi:[0,0,0]
	v_mfma_scale_f32_16x16x128_f8f6f4 v[132:135], v[218:225], v[24:31], v[132:135], v173, v173 op_sel_hi:[0,0,0]
	v_mfma_scale_f32_16x16x128_f8f6f4 v[128:131], v[226:233], v[24:31], v[128:131], v173, v173 op_sel_hi:[0,0,0]
	v_mfma_scale_f32_16x16x128_f8f6f4 v[116:119], v[218:225], v[194:201], v[116:119], v173, v173 op_sel_hi:[0,0,0]
	v_mfma_scale_f32_16x16x128_f8f6f4 v[112:115], v[226:233], v[194:201], v[112:115], v173, v173 op_sel_hi:[0,0,0]
	v_mfma_scale_f32_16x16x128_f8f6f4 v[100:103], v[218:225], v[210:217], v[100:103], v173, v173 op_sel_hi:[0,0,0]
	v_mfma_scale_f32_16x16x128_f8f6f4 v[96:99], v[226:233], v[210:217], v[96:99], v173, v173 op_sel_hi:[0,0,0]
	s_setprio 0
	s_add_u32 s36, s36, 0x80
	s_addc_u32 s37, s37, 0
	s_mov_b32 m0, s56
	s_barrier
	ds_read_b128 v[16:19], v190 offset:49152
	ds_read_b128 v[24:27], v190 offset:51200
	ds_read_b128 v[20:23], v191 offset:49152
	ds_read_b128 v[28:31], v191 offset:51200
	ds_read_b128 v[194:197], v190 offset:53248
	ds_read_b128 v[210:213], v190 offset:55296
	ds_read_b128 v[198:201], v191 offset:53248
	ds_read_b128 v[214:217], v191 offset:55296
	s_nop 0
	global_load_lds_dwordx4 v166, s[36:37]
	s_mov_b32 m0, s57
	s_nop 0
	global_load_lds_dwordx4 v162, s[36:37]
	s_nop 0
	s_barrier
	s_waitcnt lgkmcnt(0)
	s_setprio 1
	s_waitcnt lgkmcnt(0)
	v_mfma_scale_f32_16x16x128_f8f6f4 v[92:95], v[0:7], v[16:23], v[92:95], v173, v173 op_sel_hi:[0,0,0]
	v_mfma_scale_f32_16x16x128_f8f6f4 v[88:91], v[8:15], v[16:23], v[88:91], v173, v173 op_sel_hi:[0,0,0]
	v_mfma_scale_f32_16x16x128_f8f6f4 v[76:79], v[0:7], v[24:31], v[76:79], v173, v173 op_sel_hi:[0,0,0]
	v_mfma_scale_f32_16x16x128_f8f6f4 v[72:75], v[8:15], v[24:31], v[72:75], v173, v173 op_sel_hi:[0,0,0]
	v_mfma_scale_f32_16x16x128_f8f6f4 v[60:63], v[0:7], v[194:201], v[60:63], v173, v173 op_sel_hi:[0,0,0]
	v_mfma_scale_f32_16x16x128_f8f6f4 v[56:59], v[8:15], v[194:201], v[56:59], v173, v173 op_sel_hi:[0,0,0]
	v_mfma_scale_f32_16x16x128_f8f6f4 v[44:47], v[0:7], v[210:217], v[44:47], v173, v173 op_sel_hi:[0,0,0]
	v_mfma_scale_f32_16x16x128_f8f6f4 v[40:43], v[8:15], v[210:217], v[40:43], v173, v173 op_sel_hi:[0,0,0]
	s_setprio 0
	s_barrier
	s_add_u32 s34, s34, 0x20080
	s_addc_u32 s35, s35, 0
	s_mov_b32 m0, s58
	s_nop 0
	global_load_lds_dwordx4 v164, s[34:35]
	s_mov_b32 m0, s59
	s_nop 0
	global_load_lds_dwordx4 v160, s[34:35]
	s_waitcnt vmcnt(6)
	s_barrier
	s_setprio 1
	v_mfma_scale_f32_16x16x128_f8f6f4 v[84:87], v[218:225], v[16:23], v[84:87], v173, v173 op_sel_hi:[0,0,0]
	v_mfma_scale_f32_16x16x128_f8f6f4 v[80:83], v[226:233], v[16:23], v[80:83], v173, v173 op_sel_hi:[0,0,0]
	v_mfma_scale_f32_16x16x128_f8f6f4 v[68:71], v[218:225], v[24:31], v[68:71], v173, v173 op_sel_hi:[0,0,0]
	v_mfma_scale_f32_16x16x128_f8f6f4 v[64:67], v[226:233], v[24:31], v[64:67], v173, v173 op_sel_hi:[0,0,0]
	v_mfma_scale_f32_16x16x128_f8f6f4 v[52:55], v[218:225], v[194:201], v[52:55], v173, v173 op_sel_hi:[0,0,0]
	v_mfma_scale_f32_16x16x128_f8f6f4 v[48:51], v[226:233], v[194:201], v[48:51], v173, v173 op_sel_hi:[0,0,0]
	v_mfma_scale_f32_16x16x128_f8f6f4 v[36:39], v[218:225], v[210:217], v[36:39], v173, v173 op_sel_hi:[0,0,0]
	v_mfma_scale_f32_16x16x128_f8f6f4 v[32:35], v[226:233], v[210:217], v[32:35], v173, v173 op_sel_hi:[0,0,0]
	s_setprio 0
	s_add_i32 s33, s33, 2
	s_cmp_gt_u32 s33, 5
	s_mov_b64 s[36:37], s[30:31]
	s_barrier
	s_cbranch_scc0 .LBB0_3027
	v_mov_b32_e32 v2, v172
	v_mov_b32_e32 v8, 0
	v_ashrrev_i32_e32 v0, 2, v2
	v_and_b32_e32 v0, 0xffffffc0, v0
	v_lshl_add_u32 v0, s2, 8, v0
	v_and_or_b32 v6, v2, 15, v0
	v_ashrrev_i32_e32 v7, 31, v6
	v_lshl_add_u64 v[0:1], v[6:7], 2, s[4:5]
	global_load_dword v14, v[0:1], off
	global_load_dword v194, v[0:1], off offset:64
	global_load_dword v195, v[0:1], off offset:128
	global_load_dword v196, v[0:1], off offset:192
	global_load_dword v197, v[0:1], off offset:512
	global_load_dword v198, v[0:1], off offset:576
	global_load_dword v199, v[0:1], off offset:640
	global_load_dword v200, v[0:1], off offset:704
	s_ashr_i32 s2, s0, 31
	s_lshr_b32 s2, s2, 30
	s_add_i32 s2, s0, s2
	v_lshrrev_b32_e32 v2, 1, v2
	s_and_b32 s2, s2, 0xfffffc
	v_and_b32_e32 v2, 0x78, v2
	s_sub_i32 s0, s0, s2
	v_lshl_or_b32 v4, s0, 8, v2
	v_lshlrev_b64 v[2:3], 10, v[6:7]
	v_mov_b32_e32 v9, 0
	v_mov_b32_e32 v10, 0
	v_mov_b32_e32 v11, 0
	v_ashrrev_i32_e32 v5, 31, v4
	v_or_b32_e32 v12, 16, v6
	v_lshl_add_u64 v[2:3], s[8:9], 0, v[2:3]
	v_ashrrev_i32_e32 v13, 31, v12
	v_lshl_add_u64 v[2:3], v[2:3], 0, v[4:5]
	s_mov_b32 s0, 0x20000
	s_mov_b64 s[12:13], 0x20000
	s_mov_b64 s[28:29], s[6:7]
	s_mov_b64 s[26:27], s[24:25]
	s_mov_b32 s2, s20
	s_waitcnt vmcnt(0)
	v_mul_f32_e32 v7, 0x3d000000, v14
	v_mul_f32_e32 v14, 0x42000000, v7
	v_pk_mul_f32 v[18:19], v[156:157], v[14:15] op_sel_hi:[1,0]
	v_pk_mul_f32 v[22:23], v[152:153], v[14:15] op_sel_hi:[1,0]
	v_pk_mul_f32 v[16:17], v[158:159], v[14:15] op_sel_hi:[1,0]
	v_pk_mul_f32 v[20:21], v[154:155], v[14:15] op_sel_hi:[1,0]
	v_pk_mul_f32 v[24:25], v[150:151], v[14:15] op_sel_hi:[1,0]
	v_pk_mul_f32 v[26:27], v[148:149], v[14:15] op_sel_hi:[1,0]
	v_pk_mul_f32 v[28:29], v[146:147], v[14:15] op_sel_hi:[1,0]
	v_pk_mul_f32 v[14:15], v[144:145], v[14:15] op_sel_hi:[1,0]
	v_med3_f32 v7, v18, s61, v192
	v_med3_f32 v18, v22, s61, v192
	v_med3_f32 v19, v19, s61, v192
	v_med3_f32 v22, v23, s61, v192
	v_med3_f32 v23, v26, s61, v192
	v_med3_f32 v14, v14, s61, v192
	v_med3_f32 v26, v27, s61, v192
	v_med3_f32 v15, v15, s61, v192
	v_cvt_pk_fp8_f32 v8, v7, v19
	v_cvt_pk_fp8_f32 v9, v18, v22
	v_cvt_pk_fp8_f32 v10, v23, v26
	v_cvt_pk_fp8_f32 v11, v14, v15
	v_med3_f32 v16, v16, s61, v192
	v_med3_f32 v20, v20, s61, v192
	v_med3_f32 v17, v17, s61, v192
	v_med3_f32 v21, v21, s61, v192
	v_med3_f32 v24, v24, s61, v192
	v_med3_f32 v27, v28, s61, v192
	v_med3_f32 v25, v25, s61, v192
	v_med3_f32 v28, v29, s61, v192
	v_cvt_pk_fp8_f32 v8, v16, v17 op_sel:[0,0,1]
	v_cvt_pk_fp8_f32 v9, v20, v21 op_sel:[0,0,1]
	v_cvt_pk_fp8_f32 v10, v24, v25 op_sel:[0,0,1]
	v_cvt_pk_fp8_f32 v11, v27, v28 op_sel:[0,0,1]
	v_lshl_add_u64 v[14:15], v[12:13], 2, s[4:5]
	global_store_dwordx2 v[2:3], v[8:9], off
	global_store_dwordx2 v[2:3], v[10:11], off offset:128
	v_mov_b32_e32 v8, 0
	v_mov_b32_e32 v9, 0
	v_mov_b32_e32 v10, 0
	v_mov_b32_e32 v11, 0
	v_lshlrev_b64 v[12:13], 10, v[12:13]
	v_or_b32_e32 v14, 32, v6
	v_lshl_add_u64 v[12:13], s[8:9], 0, v[12:13]
	v_ashrrev_i32_e32 v15, 31, v14
	v_lshl_add_u64 v[12:13], v[12:13], 0, v[4:5]
	v_lshl_add_u64 v[16:17], v[14:15], 2, s[4:5]
	v_or_b32_e32 v6, 48, v6
	v_mul_f32_e32 v7, 0x3d000000, v194
	v_mul_f32_e32 v18, 0x42000000, v7
	v_pk_mul_f32 v[22:23], v[140:141], v[18:19] op_sel_hi:[1,0]
	v_pk_mul_f32 v[26:27], v[136:137], v[18:19] op_sel_hi:[1,0]
	v_pk_mul_f32 v[20:21], v[142:143], v[18:19] op_sel_hi:[1,0]
	v_pk_mul_f32 v[24:25], v[138:139], v[18:19] op_sel_hi:[1,0]
	v_pk_mul_f32 v[28:29], v[134:135], v[18:19] op_sel_hi:[1,0]
	v_pk_mul_f32 v[30:31], v[132:133], v[18:19] op_sel_hi:[1,0]
	v_pk_mul_f32 v[130:131], v[130:131], v[18:19] op_sel_hi:[1,0]
	v_pk_mul_f32 v[18:19], v[128:129], v[18:19] op_sel_hi:[1,0]
	v_med3_f32 v7, v22, s61, v192
	v_med3_f32 v22, v26, s61, v192
	v_med3_f32 v23, v23, s61, v192
	v_med3_f32 v26, v27, s61, v192
	v_med3_f32 v27, v30, s61, v192
	v_med3_f32 v18, v18, s61, v192
	v_med3_f32 v30, v31, s61, v192
	v_med3_f32 v19, v19, s61, v192
	v_cvt_pk_fp8_f32 v8, v7, v23
	v_cvt_pk_fp8_f32 v9, v22, v26
	v_cvt_pk_fp8_f32 v10, v27, v30
	v_cvt_pk_fp8_f32 v11, v18, v19
	v_med3_f32 v20, v20, s61, v192
	v_med3_f32 v24, v24, s61, v192
	v_med3_f32 v21, v21, s61, v192
	v_med3_f32 v25, v25, s61, v192
	v_med3_f32 v28, v28, s61, v192
	v_med3_f32 v31, v130, s61, v192
	v_med3_f32 v29, v29, s61, v192
	v_med3_f32 v128, v131, s61, v192
	v_cvt_pk_fp8_f32 v8, v20, v21 op_sel:[0,0,1]
	v_cvt_pk_fp8_f32 v9, v24, v25 op_sel:[0,0,1]
	v_cvt_pk_fp8_f32 v10, v28, v29 op_sel:[0,0,1]
	v_cvt_pk_fp8_f32 v11, v31, v128 op_sel:[0,0,1]
	global_store_dwordx2 v[12:13], v[8:9], off
	global_store_dwordx2 v[12:13], v[10:11], off offset:128
	v_mov_b32_e32 v8, 0
	v_mov_b32_e32 v9, 0
	v_mov_b32_e32 v10, 0
	v_mov_b32_e32 v11, 0
	v_lshlrev_b64 v[12:13], 10, v[14:15]
	v_lshl_add_u64 v[12:13], s[8:9], 0, v[12:13]
	v_ashrrev_i32_e32 v7, 31, v6
	v_lshl_add_u64 v[12:13], v[12:13], 0, v[4:5]
	v_lshl_add_u64 v[14:15], v[6:7], 2, s[4:5]
	v_lshlrev_b64 v[6:7], 10, v[6:7]
	v_lshl_add_u64 v[6:7], s[8:9], 0, v[6:7]
	v_lshl_add_u64 v[4:5], v[6:7], 0, v[4:5]
	v_mov_b32_e32 v6, 0
	v_mov_b32_e32 v7, 0
	v_mul_f32_e32 v16, 0x3d000000, v195
	v_mul_f32_e32 v16, 0x42000000, v16
	v_pk_mul_f32 v[20:21], v[124:125], v[16:17] op_sel_hi:[1,0]
	v_pk_mul_f32 v[24:25], v[120:121], v[16:17] op_sel_hi:[1,0]
	v_pk_mul_f32 v[18:19], v[126:127], v[16:17] op_sel_hi:[1,0]
	v_pk_mul_f32 v[22:23], v[122:123], v[16:17] op_sel_hi:[1,0]
	v_pk_mul_f32 v[26:27], v[118:119], v[16:17] op_sel_hi:[1,0]
	v_pk_mul_f32 v[28:29], v[116:117], v[16:17] op_sel_hi:[1,0]
	v_pk_mul_f32 v[30:31], v[114:115], v[16:17] op_sel_hi:[1,0]
	v_pk_mul_f32 v[16:17], v[112:113], v[16:17] op_sel_hi:[1,0]
	v_med3_f32 v20, v20, s61, v192
	v_med3_f32 v24, v24, s61, v192
	v_med3_f32 v21, v21, s61, v192
	v_med3_f32 v25, v25, s61, v192
	v_med3_f32 v28, v28, s61, v192
	v_med3_f32 v16, v16, s61, v192
	v_med3_f32 v29, v29, s61, v192
	v_med3_f32 v17, v17, s61, v192
	v_cvt_pk_fp8_f32 v8, v20, v21
	v_cvt_pk_fp8_f32 v9, v24, v25
	v_cvt_pk_fp8_f32 v10, v28, v29
	v_cvt_pk_fp8_f32 v11, v16, v17
	v_med3_f32 v18, v18, s61, v192
	v_med3_f32 v22, v22, s61, v192
	v_med3_f32 v19, v19, s61, v192
	v_med3_f32 v23, v23, s61, v192
	v_med3_f32 v26, v26, s61, v192
	v_med3_f32 v30, v30, s61, v192
	v_med3_f32 v27, v27, s61, v192
	v_med3_f32 v31, v31, s61, v192
	v_cvt_pk_fp8_f32 v8, v18, v19 op_sel:[0,0,1]
	v_cvt_pk_fp8_f32 v9, v22, v23 op_sel:[0,0,1]
	v_cvt_pk_fp8_f32 v10, v26, v27 op_sel:[0,0,1]
	v_cvt_pk_fp8_f32 v11, v30, v31 op_sel:[0,0,1]
	global_store_dwordx2 v[12:13], v[8:9], off
	global_store_dwordx2 v[12:13], v[10:11], off offset:128
	v_mov_b32_e32 v8, 0
	v_mov_b32_e32 v9, 0
	v_mov_b32_e32 v10, 0
	v_mov_b32_e32 v11, 0
	v_mul_f32_e32 v12, 0x3d000000, v196
	v_mul_f32_e32 v12, 0x42000000, v12
	v_pk_mul_f32 v[16:17], v[108:109], v[12:13] op_sel_hi:[1,0]
	v_pk_mul_f32 v[20:21], v[104:105], v[12:13] op_sel_hi:[1,0]
	v_pk_mul_f32 v[14:15], v[110:111], v[12:13] op_sel_hi:[1,0]
	v_pk_mul_f32 v[18:19], v[106:107], v[12:13] op_sel_hi:[1,0]
	v_pk_mul_f32 v[22:23], v[102:103], v[12:13] op_sel_hi:[1,0]
	v_pk_mul_f32 v[24:25], v[100:101], v[12:13] op_sel_hi:[1,0]
	v_pk_mul_f32 v[26:27], v[98:99], v[12:13] op_sel_hi:[1,0]
	v_pk_mul_f32 v[12:13], v[96:97], v[12:13] op_sel_hi:[1,0]
	v_med3_f32 v16, v16, s61, v192
	v_med3_f32 v20, v20, s61, v192
	v_med3_f32 v17, v17, s61, v192
	v_med3_f32 v21, v21, s61, v192
	v_med3_f32 v24, v24, s61, v192
	v_med3_f32 v12, v12, s61, v192
	v_med3_f32 v25, v25, s61, v192
	v_med3_f32 v13, v13, s61, v192
	v_cvt_pk_fp8_f32 v8, v16, v17
	v_cvt_pk_fp8_f32 v9, v20, v21
	v_cvt_pk_fp8_f32 v10, v24, v25
	v_cvt_pk_fp8_f32 v11, v12, v13
	v_med3_f32 v14, v14, s61, v192
	v_med3_f32 v18, v18, s61, v192
	v_med3_f32 v15, v15, s61, v192
	v_med3_f32 v19, v19, s61, v192
	v_med3_f32 v22, v22, s61, v192
	v_med3_f32 v26, v26, s61, v192
	v_med3_f32 v23, v23, s61, v192
	v_med3_f32 v27, v27, s61, v192
	v_cvt_pk_fp8_f32 v8, v14, v15 op_sel:[0,0,1]
	v_cvt_pk_fp8_f32 v9, v18, v19 op_sel:[0,0,1]
	v_cvt_pk_fp8_f32 v10, v22, v23 op_sel:[0,0,1]
	v_cvt_pk_fp8_f32 v11, v26, v27 op_sel:[0,0,1]
	global_store_dwordx2 v[4:5], v[8:9], off
	global_store_dwordx2 v[4:5], v[10:11], off offset:128
	v_mov_b32_e32 v4, 0
	v_mov_b32_e32 v5, 0
	v_lshl_add_u64 v[8:9], v[2:3], 0, s[12:13]
	v_mul_f32_e32 v10, 0x3d000000, v197
	v_mul_f32_e32 v10, 0x42000000, v10
	v_pk_mul_f32 v[14:15], v[92:93], v[10:11] op_sel_hi:[1,0]
	v_pk_mul_f32 v[18:19], v[88:89], v[10:11] op_sel_hi:[1,0]
	v_pk_mul_f32 v[12:13], v[94:95], v[10:11] op_sel_hi:[1,0]
	v_pk_mul_f32 v[16:17], v[90:91], v[10:11] op_sel_hi:[1,0]
	v_pk_mul_f32 v[20:21], v[86:87], v[10:11] op_sel_hi:[1,0]
	v_pk_mul_f32 v[22:23], v[84:85], v[10:11] op_sel_hi:[1,0]
	v_pk_mul_f32 v[24:25], v[82:83], v[10:11] op_sel_hi:[1,0]
	v_pk_mul_f32 v[10:11], v[80:81], v[10:11] op_sel_hi:[1,0]
	v_med3_f32 v14, v14, s61, v192
	v_med3_f32 v18, v18, s61, v192
	v_med3_f32 v15, v15, s61, v192
	v_med3_f32 v19, v19, s61, v192
	v_med3_f32 v22, v22, s61, v192
	v_med3_f32 v10, v10, s61, v192
	v_med3_f32 v23, v23, s61, v192
	v_med3_f32 v11, v11, s61, v192
	v_cvt_pk_fp8_f32 v4, v14, v15
	v_cvt_pk_fp8_f32 v5, v18, v19
	v_cvt_pk_fp8_f32 v6, v22, v23
	v_cvt_pk_fp8_f32 v7, v10, v11
	v_med3_f32 v12, v12, s61, v192
	v_med3_f32 v16, v16, s61, v192
	v_med3_f32 v13, v13, s61, v192
	v_med3_f32 v17, v17, s61, v192
	v_med3_f32 v20, v20, s61, v192
	v_med3_f32 v24, v24, s61, v192
	v_med3_f32 v21, v21, s61, v192
	v_med3_f32 v25, v25, s61, v192
	v_cvt_pk_fp8_f32 v4, v12, v13 op_sel:[0,0,1]
	v_cvt_pk_fp8_f32 v5, v16, v17 op_sel:[0,0,1]
	v_cvt_pk_fp8_f32 v6, v20, v21 op_sel:[0,0,1]
	v_cvt_pk_fp8_f32 v7, v24, v25 op_sel:[0,0,1]
	v_add_co_u32_e32 v10, vcc, s0, v2
	s_mov_b32 s0, s22
	s_nop 0
	v_addc_co_u32_e32 v11, vcc, 0, v3, vcc
	global_store_dwordx2 v[10:11], v[4:5], off
	global_store_dwordx2 v[8:9], v[6:7], off offset:128
	v_mov_b32_e32 v4, 0
	v_mov_b32_e32 v5, 0
	v_mov_b32_e32 v6, 0
	v_mov_b32_e32 v7, 0
	v_lshl_add_u64 v[8:9], v[2:3], 0, s[14:15]
	v_mul_f32_e32 v10, 0x3d000000, v198
	v_mul_f32_e32 v10, 0x42000000, v10
	v_pk_mul_f32 v[14:15], v[76:77], v[10:11] op_sel_hi:[1,0]
	v_pk_mul_f32 v[18:19], v[72:73], v[10:11] op_sel_hi:[1,0]
	v_pk_mul_f32 v[12:13], v[78:79], v[10:11] op_sel_hi:[1,0]
	v_pk_mul_f32 v[16:17], v[74:75], v[10:11] op_sel_hi:[1,0]
	v_pk_mul_f32 v[20:21], v[70:71], v[10:11] op_sel_hi:[1,0]
	v_pk_mul_f32 v[22:23], v[68:69], v[10:11] op_sel_hi:[1,0]
	v_pk_mul_f32 v[24:25], v[66:67], v[10:11] op_sel_hi:[1,0]
	v_pk_mul_f32 v[10:11], v[64:65], v[10:11] op_sel_hi:[1,0]
	v_med3_f32 v14, v14, s61, v192
	v_med3_f32 v18, v18, s61, v192
	v_med3_f32 v15, v15, s61, v192
	v_med3_f32 v19, v19, s61, v192
	v_med3_f32 v22, v22, s61, v192
	v_med3_f32 v10, v10, s61, v192
	v_med3_f32 v23, v23, s61, v192
	v_med3_f32 v11, v11, s61, v192
	v_cvt_pk_fp8_f32 v4, v14, v15
	v_cvt_pk_fp8_f32 v5, v18, v19
	v_cvt_pk_fp8_f32 v6, v22, v23
	v_cvt_pk_fp8_f32 v7, v10, v11
	v_med3_f32 v12, v12, s61, v192
	v_med3_f32 v16, v16, s61, v192
	v_med3_f32 v13, v13, s61, v192
	v_med3_f32 v17, v17, s61, v192
	v_med3_f32 v20, v20, s61, v192
	v_med3_f32 v24, v24, s61, v192
	v_med3_f32 v21, v21, s61, v192
	v_med3_f32 v25, v25, s61, v192
	v_cvt_pk_fp8_f32 v4, v12, v13 op_sel:[0,0,1]
	v_cvt_pk_fp8_f32 v5, v16, v17 op_sel:[0,0,1]
	v_cvt_pk_fp8_f32 v6, v20, v21 op_sel:[0,0,1]
	v_cvt_pk_fp8_f32 v7, v24, v25 op_sel:[0,0,1]
	v_add_co_u32_e32 v10, vcc, s62, v2
	s_nop 1
	v_addc_co_u32_e32 v11, vcc, 0, v3, vcc
	global_store_dwordx2 v[10:11], v[4:5], off
	global_store_dwordx2 v[8:9], v[6:7], off offset:128
	v_mov_b32_e32 v4, 0
	v_mov_b32_e32 v5, 0
	v_mov_b32_e32 v6, 0
	v_mov_b32_e32 v7, 0
	v_lshl_add_u64 v[8:9], v[2:3], 0, s[16:17]
	v_mul_f32_e32 v10, 0x3d000000, v199
	v_mul_f32_e32 v10, 0x42000000, v10
	v_pk_mul_f32 v[14:15], v[60:61], v[10:11] op_sel_hi:[1,0]
	v_pk_mul_f32 v[18:19], v[56:57], v[10:11] op_sel_hi:[1,0]
	v_pk_mul_f32 v[12:13], v[62:63], v[10:11] op_sel_hi:[1,0]
	v_pk_mul_f32 v[16:17], v[58:59], v[10:11] op_sel_hi:[1,0]
	v_pk_mul_f32 v[20:21], v[54:55], v[10:11] op_sel_hi:[1,0]
	v_pk_mul_f32 v[22:23], v[52:53], v[10:11] op_sel_hi:[1,0]
	v_pk_mul_f32 v[24:25], v[50:51], v[10:11] op_sel_hi:[1,0]
	v_pk_mul_f32 v[10:11], v[48:49], v[10:11] op_sel_hi:[1,0]
	v_med3_f32 v14, v14, s61, v192
	v_med3_f32 v18, v18, s61, v192
	v_med3_f32 v15, v15, s61, v192
	v_med3_f32 v19, v19, s61, v192
	v_med3_f32 v22, v22, s61, v192
	v_med3_f32 v10, v10, s61, v192
	v_med3_f32 v23, v23, s61, v192
	v_med3_f32 v11, v11, s61, v192
	v_cvt_pk_fp8_f32 v4, v14, v15
	v_cvt_pk_fp8_f32 v5, v18, v19
	v_cvt_pk_fp8_f32 v6, v22, v23
	v_cvt_pk_fp8_f32 v7, v10, v11
	v_med3_f32 v12, v12, s61, v192
	v_med3_f32 v16, v16, s61, v192
	v_med3_f32 v13, v13, s61, v192
	v_med3_f32 v17, v17, s61, v192
	v_med3_f32 v20, v20, s61, v192
	v_med3_f32 v24, v24, s61, v192
	v_med3_f32 v21, v21, s61, v192
	v_med3_f32 v25, v25, s61, v192
	v_cvt_pk_fp8_f32 v4, v12, v13 op_sel:[0,0,1]
	v_cvt_pk_fp8_f32 v5, v16, v17 op_sel:[0,0,1]
	v_cvt_pk_fp8_f32 v6, v20, v21 op_sel:[0,0,1]
	v_cvt_pk_fp8_f32 v7, v24, v25 op_sel:[0,0,1]
	v_add_co_u32_e32 v10, vcc, s63, v2
	s_nop 1
	v_addc_co_u32_e32 v11, vcc, 0, v3, vcc
	global_store_dwordx2 v[10:11], v[4:5], off
	global_store_dwordx2 v[8:9], v[6:7], off offset:128
	v_mov_b32_e32 v0, 0
	v_mov_b32_e32 v1, 0
	v_mov_b32_e32 v4, 0
	v_mov_b32_e32 v5, 0
	v_lshl_add_u64 v[6:7], v[2:3], 0, s[18:19]
	v_add_co_u32_e64 v2, s[6:7], s64, v2
	s_and_b64 vcc, exec, s[10:11]
	s_nop 0
	v_addc_co_u32_e64 v3, s[6:7], 0, v3, s[6:7]
	v_mul_f32_e32 v8, 0x3d000000, v200
	v_mul_f32_e32 v8, 0x42000000, v8
	v_pk_mul_f32 v[12:13], v[44:45], v[8:9] op_sel_hi:[1,0]
	v_pk_mul_f32 v[16:17], v[40:41], v[8:9] op_sel_hi:[1,0]
	v_pk_mul_f32 v[10:11], v[46:47], v[8:9] op_sel_hi:[1,0]
	v_pk_mul_f32 v[14:15], v[42:43], v[8:9] op_sel_hi:[1,0]
	v_pk_mul_f32 v[18:19], v[38:39], v[8:9] op_sel_hi:[1,0]
	v_pk_mul_f32 v[20:21], v[36:37], v[8:9] op_sel_hi:[1,0]
	v_pk_mul_f32 v[22:23], v[34:35], v[8:9] op_sel_hi:[1,0]
	v_pk_mul_f32 v[8:9], v[32:33], v[8:9] op_sel_hi:[1,0]
	v_med3_f32 v12, v12, s61, v192
	v_med3_f32 v16, v16, s61, v192
	v_med3_f32 v13, v13, s61, v192
	v_med3_f32 v17, v17, s61, v192
	v_med3_f32 v20, v20, s61, v192
	v_med3_f32 v8, v8, s61, v192
	v_med3_f32 v21, v21, s61, v192
	v_med3_f32 v9, v9, s61, v192
	v_cvt_pk_fp8_f32 v0, v12, v13
	v_cvt_pk_fp8_f32 v1, v16, v17
	v_cvt_pk_fp8_f32 v4, v20, v21
	v_cvt_pk_fp8_f32 v5, v8, v9
	v_med3_f32 v10, v10, s61, v192
	v_med3_f32 v14, v14, s61, v192
	v_med3_f32 v11, v11, s61, v192
	v_med3_f32 v15, v15, s61, v192
	v_med3_f32 v18, v18, s61, v192
	v_med3_f32 v22, v22, s61, v192
	v_med3_f32 v19, v19, s61, v192
	v_med3_f32 v23, v23, s61, v192
	v_cvt_pk_fp8_f32 v0, v10, v11 op_sel:[0,0,1]
	v_cvt_pk_fp8_f32 v1, v14, v15 op_sel:[0,0,1]
	v_cvt_pk_fp8_f32 v4, v18, v19 op_sel:[0,0,1]
	v_cvt_pk_fp8_f32 v5, v22, v23 op_sel:[0,0,1]
	global_store_dwordx2 v[2:3], v[0:1], off
	global_store_dwordx2 v[6:7], v[4:5], off offset:128
	s_cbranch_vccz .LBB0_3024
	s_waitcnt vmcnt(0)
	s_cmpk_gt_u32 s40, 0xff
	v_readlane_b32 s58, v242, 45
	v_readlane_b32 s59, v242, 46
	s_cbranch_scc1 .LBB0_3031
	s_barrier

.LBB0_3168:
	s_add_u32 s36, s34, 0x100
	ds_read_b128 v[158:161], v141
	ds_read_b128 v[162:165], v142
	ds_read_b128 v[166:169], v149
	ds_read_b128 v[170:173], v150
	s_addc_u32 s37, s35, 0
	s_and_b32 s68, s36, 0x700
	s_add_u32 s69, s20, s68
	s_addc_u32 s70, s21, 0
	s_cmp_eq_u32 s67, 12
	s_cselect_b64 s[40:41], -1, 0
	s_and_b64 s[38:39], s[40:41], exec
	s_cselect_b32 s39, s23, s70
	s_cselect_b32 s38, s27, s69
	s_cselect_b32 s69, 0, 0
	s_cselect_b32 s68, 0, s68
	s_add_u32 s34, s24, s34
	s_addc_u32 s35, s25, s35
	s_add_u32 s34, s34, 0x40080
	s_addc_u32 s35, s35, 0
	ds_read_b128 v[174:177], v157
	ds_read_b128 v[178:181], v157 offset:1024
	ds_read_b128 v[182:185], v157 offset:2048
	ds_read_b128 v[186:189], v157 offset:3072
	ds_read_b128 v[190:193], v157 offset:4096
	ds_read_b128 v[194:197], v157 offset:5120
	ds_read_b128 v[198:201], v157 offset:6144
	ds_read_b128 v[202:205], v157 offset:7168
	s_add_i32 m0, s19, 0xc000
	s_nop 0
	global_load_lds_dwordx4 v134, s[34:35]
	s_add_i32 m0, s19, 0xe000
	s_nop 0
	global_load_lds_dwordx4 v130, s[34:35]
	s_waitcnt lgkmcnt(8)
	s_barrier
	s_waitcnt lgkmcnt(0)
	s_setprio 1
	s_waitcnt lgkmcnt(0)
	v_mfma_f32_16x16x32_bf16 v[124:127], v[158:161], v[174:177], v[124:127]
	v_mfma_f32_16x16x32_bf16 v[120:123], v[166:169], v[174:177], v[120:123]
	v_mfma_f32_16x16x32_bf16 v[116:119], v[158:161], v[182:185], v[116:119]
	v_mfma_f32_16x16x32_bf16 v[108:111], v[166:169], v[182:185], v[108:111]
	v_mfma_f32_16x16x32_bf16 v[100:103], v[158:161], v[190:193], v[100:103]
	v_mfma_f32_16x16x32_bf16 v[92:95], v[166:169], v[190:193], v[92:95]
	v_mfma_f32_16x16x32_bf16 v[84:87], v[158:161], v[198:201], v[84:87]
	v_mfma_f32_16x16x32_bf16 v[76:79], v[166:169], v[198:201], v[76:79]
	v_mfma_f32_16x16x32_bf16 v[124:127], v[162:165], v[178:181], v[124:127]
	v_mfma_f32_16x16x32_bf16 v[120:123], v[170:173], v[178:181], v[120:123]
	v_mfma_f32_16x16x32_bf16 v[116:119], v[162:165], v[186:189], v[116:119]
	v_mfma_f32_16x16x32_bf16 v[108:111], v[170:173], v[186:189], v[108:111]
	v_mfma_f32_16x16x32_bf16 v[100:103], v[162:165], v[194:197], v[100:103]
	v_mfma_f32_16x16x32_bf16 v[92:95], v[170:173], v[194:197], v[92:95]
	v_mfma_f32_16x16x32_bf16 v[84:87], v[162:165], v[202:205], v[84:87]
	v_mfma_f32_16x16x32_bf16 v[76:79], v[170:173], v[202:205], v[76:79]
	s_setprio 0
	s_barrier
	s_mov_b64 s[34:35], s[38:39]
	s_mov_b32 m0, s48
	ds_read_b128 v[210:213], v143
	ds_read_b128 v[214:217], v144
	ds_read_b128 v[218:221], v151
	ds_read_b128 v[222:225], v152
	s_nop 0
	global_load_lds_dwordx4 v132, s[34:35]
	s_mov_b32 m0, s49
	s_nop 0
	global_load_lds_dwordx4 v128, s[34:35]
	s_nop 0
	s_barrier
	s_waitcnt lgkmcnt(0)
	s_setprio 1
	s_waitcnt lgkmcnt(0)
	v_mfma_f32_16x16x32_bf16 v[112:115], v[210:213], v[174:177], v[112:115]
	v_mfma_f32_16x16x32_bf16 v[104:107], v[218:221], v[174:177], v[104:107]
	v_mfma_f32_16x16x32_bf16 v[96:99], v[210:213], v[182:185], v[96:99]
	v_mfma_f32_16x16x32_bf16 v[88:91], v[218:221], v[182:185], v[88:91]
	v_mfma_f32_16x16x32_bf16 v[80:83], v[210:213], v[190:193], v[80:83]
	v_mfma_f32_16x16x32_bf16 v[72:75], v[218:221], v[190:193], v[72:75]
	v_mfma_f32_16x16x32_bf16 v[68:71], v[210:213], v[198:201], v[68:71]
	v_mfma_f32_16x16x32_bf16 v[64:67], v[218:221], v[198:201], v[64:67]
	v_mfma_f32_16x16x32_bf16 v[112:115], v[214:217], v[178:181], v[112:115]
	v_mfma_f32_16x16x32_bf16 v[104:107], v[222:225], v[178:181], v[104:107]
	v_mfma_f32_16x16x32_bf16 v[96:99], v[214:217], v[186:189], v[96:99]
	v_mfma_f32_16x16x32_bf16 v[88:91], v[222:225], v[186:189], v[88:91]
	v_mfma_f32_16x16x32_bf16 v[80:83], v[214:217], v[194:197], v[80:83]
	v_mfma_f32_16x16x32_bf16 v[72:75], v[222:225], v[194:197], v[72:75]
	v_mfma_f32_16x16x32_bf16 v[68:71], v[214:217], v[202:205], v[68:71]
	v_mfma_f32_16x16x32_bf16 v[64:67], v[222:225], v[202:205], v[64:67]
	s_setprio 0
	s_and_b64 s[34:35], s[10:11], s[40:41]
	s_and_b64 s[34:35], s[34:35], exec
	s_cselect_b32 s34, s28, s24
	s_cselect_b32 s35, s29, s25
	s_add_u32 s34, s34, s68
	s_addc_u32 s35, s35, s69
	s_mov_b64 s[40:41], s[34:35]
	s_mov_b32 m0, s19
	s_barrier
	ds_read_b128 v[174:177], v157 offset:16384
	ds_read_b128 v[178:181], v157 offset:17408
	ds_read_b128 v[182:185], v157 offset:18432
	ds_read_b128 v[186:189], v157 offset:19456
	ds_read_b128 v[190:193], v157 offset:20480
	ds_read_b128 v[194:197], v157 offset:21504
	ds_read_b128 v[198:201], v157 offset:22528
	ds_read_b128 v[202:205], v157 offset:23552
	s_nop 0
	global_load_lds_dwordx4 v134, s[40:41]
	s_mov_b32 m0, s50
	s_nop 0
	global_load_lds_dwordx4 v130, s[40:41]
	s_nop 0
	s_barrier
	s_waitcnt lgkmcnt(0)
	s_setprio 1
	s_waitcnt lgkmcnt(0)
	v_mfma_f32_16x16x32_bf16 v[60:63], v[158:161], v[174:177], v[60:63]
	v_mfma_f32_16x16x32_bf16 v[56:59], v[166:169], v[174:177], v[56:59]
	v_mfma_f32_16x16x32_bf16 v[52:55], v[158:161], v[182:185], v[52:55]
	v_mfma_f32_16x16x32_bf16 v[48:51], v[166:169], v[182:185], v[48:51]
	v_mfma_f32_16x16x32_bf16 v[36:39], v[158:161], v[190:193], v[36:39]
	v_mfma_f32_16x16x32_bf16 v[32:35], v[166:169], v[190:193], v[32:35]
	v_mfma_f32_16x16x32_bf16 v[20:23], v[158:161], v[198:201], v[20:23]
	v_mfma_f32_16x16x32_bf16 v[16:19], v[166:169], v[198:201], v[16:19]
	v_mfma_f32_16x16x32_bf16 v[60:63], v[162:165], v[178:181], v[60:63]
	v_mfma_f32_16x16x32_bf16 v[56:59], v[170:173], v[178:181], v[56:59]
	v_mfma_f32_16x16x32_bf16 v[52:55], v[162:165], v[186:189], v[52:55]
	v_mfma_f32_16x16x32_bf16 v[48:51], v[170:173], v[186:189], v[48:51]
	v_mfma_f32_16x16x32_bf16 v[36:39], v[162:165], v[194:197], v[36:39]
	v_mfma_f32_16x16x32_bf16 v[32:35], v[170:173], v[194:197], v[32:35]
	v_mfma_f32_16x16x32_bf16 v[20:23], v[162:165], v[202:205], v[20:23]
	v_mfma_f32_16x16x32_bf16 v[16:19], v[170:173], v[202:205], v[16:19]
	s_setprio 0
	s_barrier
	s_add_u32 s40, s38, 0x40000
	s_addc_u32 s41, s39, 0
	s_mov_b32 m0, s51
	s_nop 0
	global_load_lds_dwordx4 v132, s[40:41]
	s_mov_b32 m0, s52
	s_nop 0
	global_load_lds_dwordx4 v128, s[40:41]
	s_waitcnt vmcnt(6)
	s_barrier
	s_setprio 1
	v_mfma_f32_16x16x32_bf16 v[44:47], v[210:213], v[174:177], v[44:47]
	v_mfma_f32_16x16x32_bf16 v[40:43], v[218:221], v[174:177], v[40:43]
	v_mfma_f32_16x16x32_bf16 v[28:31], v[210:213], v[182:185], v[28:31]
	v_mfma_f32_16x16x32_bf16 v[24:27], v[218:221], v[182:185], v[24:27]
	v_mfma_f32_16x16x32_bf16 v[12:15], v[210:213], v[190:193], v[12:15]
	v_mfma_f32_16x16x32_bf16 v[8:11], v[218:221], v[190:193], v[8:11]
	v_mfma_f32_16x16x32_bf16 v[4:7], v[210:213], v[198:201], v[4:7]
	v_mfma_f32_16x16x32_bf16 v[0:3], v[218:221], v[198:201], v[0:3]
	v_mfma_f32_16x16x32_bf16 v[44:47], v[214:217], v[178:181], v[44:47]
	v_mfma_f32_16x16x32_bf16 v[40:43], v[222:225], v[178:181], v[40:43]
	v_mfma_f32_16x16x32_bf16 v[28:31], v[214:217], v[186:189], v[28:31]
	v_mfma_f32_16x16x32_bf16 v[24:27], v[222:225], v[186:189], v[24:27]
	v_mfma_f32_16x16x32_bf16 v[12:15], v[214:217], v[194:197], v[12:15]
	v_mfma_f32_16x16x32_bf16 v[8:11], v[222:225], v[194:197], v[8:11]
	v_mfma_f32_16x16x32_bf16 v[4:7], v[214:217], v[202:205], v[4:7]
	v_mfma_f32_16x16x32_bf16 v[0:3], v[222:225], v[202:205], v[0:3]
	s_setprio 0
	s_barrier
	ds_read_b128 v[158:161], v145
	ds_read_b128 v[162:165], v146
	ds_read_b128 v[166:169], v153
	ds_read_b128 v[170:173], v154
	s_add_u32 s40, s34, 0x40000
	s_addc_u32 s41, s35, 0
	s_mov_b32 m0, s53
	ds_read_b128 v[174:177], v157 offset:32768
	ds_read_b128 v[178:181], v157 offset:33792
	ds_read_b128 v[182:185], v157 offset:34816
	ds_read_b128 v[186:189], v157 offset:35840
	ds_read_b128 v[190:193], v157 offset:36864
	ds_read_b128 v[194:197], v157 offset:37888
	ds_read_b128 v[198:201], v157 offset:38912
	ds_read_b128 v[202:205], v157 offset:39936
	s_nop 0
	global_load_lds_dwordx4 v134, s[40:41]
	s_mov_b32 m0, s54
	s_nop 0
	global_load_lds_dwordx4 v130, s[40:41]
	s_waitcnt lgkmcnt(8)
	s_barrier
	s_waitcnt lgkmcnt(0)
	s_setprio 1
	s_waitcnt lgkmcnt(0)
	v_mfma_f32_16x16x32_bf16 v[124:127], v[158:161], v[174:177], v[124:127]
	v_mfma_f32_16x16x32_bf16 v[120:123], v[166:169], v[174:177], v[120:123]
	v_mfma_f32_16x16x32_bf16 v[116:119], v[158:161], v[182:185], v[116:119]
	v_mfma_f32_16x16x32_bf16 v[108:111], v[166:169], v[182:185], v[108:111]
	v_mfma_f32_16x16x32_bf16 v[100:103], v[158:161], v[190:193], v[100:103]
	v_mfma_f32_16x16x32_bf16 v[92:95], v[166:169], v[190:193], v[92:95]
	v_mfma_f32_16x16x32_bf16 v[84:87], v[158:161], v[198:201], v[84:87]
	v_mfma_f32_16x16x32_bf16 v[76:79], v[166:169], v[198:201], v[76:79]
	v_mfma_f32_16x16x32_bf16 v[124:127], v[162:165], v[178:181], v[124:127]
	v_mfma_f32_16x16x32_bf16 v[120:123], v[170:173], v[178:181], v[120:123]
	v_mfma_f32_16x16x32_bf16 v[116:119], v[162:165], v[186:189], v[116:119]
	v_mfma_f32_16x16x32_bf16 v[108:111], v[170:173], v[186:189], v[108:111]
	v_mfma_f32_16x16x32_bf16 v[100:103], v[162:165], v[194:197], v[100:103]
	v_mfma_f32_16x16x32_bf16 v[92:95], v[170:173], v[194:197], v[92:95]
	v_mfma_f32_16x16x32_bf16 v[84:87], v[162:165], v[202:205], v[84:87]
	v_mfma_f32_16x16x32_bf16 v[76:79], v[170:173], v[202:205], v[76:79]
	s_setprio 0
	s_barrier
	s_add_u32 s40, s38, 0x80
	s_addc_u32 s41, s39, 0
	s_mov_b32 m0, s56
	ds_read_b128 v[210:213], v147
	ds_read_b128 v[214:217], v148
	ds_read_b128 v[218:221], v155
	ds_read_b128 v[222:225], v156
	s_nop 0
	global_load_lds_dwordx4 v132, s[40:41]
	s_mov_b32 m0, s57
	s_nop 0
	global_load_lds_dwordx4 v128, s[40:41]
	s_nop 0
	s_barrier
	s_waitcnt lgkmcnt(0)
	s_setprio 1
	s_waitcnt lgkmcnt(0)
	v_mfma_f32_16x16x32_bf16 v[112:115], v[210:213], v[174:177], v[112:115]
	v_mfma_f32_16x16x32_bf16 v[104:107], v[218:221], v[174:177], v[104:107]
	v_mfma_f32_16x16x32_bf16 v[96:99], v[210:213], v[182:185], v[96:99]
	v_mfma_f32_16x16x32_bf16 v[88:91], v[218:221], v[182:185], v[88:91]
	v_mfma_f32_16x16x32_bf16 v[80:83], v[210:213], v[190:193], v[80:83]
	v_mfma_f32_16x16x32_bf16 v[72:75], v[218:221], v[190:193], v[72:75]
	v_mfma_f32_16x16x32_bf16 v[68:71], v[210:213], v[198:201], v[68:71]
	v_mfma_f32_16x16x32_bf16 v[64:67], v[218:221], v[198:201], v[64:67]
	v_mfma_f32_16x16x32_bf16 v[112:115], v[214:217], v[178:181], v[112:115]
	v_mfma_f32_16x16x32_bf16 v[104:107], v[222:225], v[178:181], v[104:107]
	v_mfma_f32_16x16x32_bf16 v[96:99], v[214:217], v[186:189], v[96:99]
	v_mfma_f32_16x16x32_bf16 v[88:91], v[222:225], v[186:189], v[88:91]
	v_mfma_f32_16x16x32_bf16 v[80:83], v[214:217], v[194:197], v[80:83]
	v_mfma_f32_16x16x32_bf16 v[72:75], v[222:225], v[194:197], v[72:75]
	v_mfma_f32_16x16x32_bf16 v[68:71], v[214:217], v[202:205], v[68:71]
	v_mfma_f32_16x16x32_bf16 v[64:67], v[222:225], v[202:205], v[64:67]
	s_setprio 0
	s_add_u32 s34, s34, 0x80
	s_addc_u32 s35, s35, 0
	s_mov_b32 m0, s58
	s_barrier
	ds_read_b128 v[174:177], v157 offset:49152
	ds_read_b128 v[178:181], v157 offset:50176
	ds_read_b128 v[182:185], v157 offset:51200
	ds_read_b128 v[186:189], v157 offset:52224
	ds_read_b128 v[190:193], v157 offset:53248
	ds_read_b128 v[194:197], v157 offset:54272
	ds_read_b128 v[198:201], v157 offset:55296
	ds_read_b128 v[202:205], v157 offset:56320
	s_nop 0
	global_load_lds_dwordx4 v134, s[34:35]
	s_mov_b32 m0, s59
	s_nop 0
	global_load_lds_dwordx4 v130, s[34:35]
	s_nop 0
	s_barrier
	s_waitcnt lgkmcnt(0)
	s_setprio 1
	s_waitcnt lgkmcnt(0)
	v_mfma_f32_16x16x32_bf16 v[60:63], v[158:161], v[174:177], v[60:63]
	v_mfma_f32_16x16x32_bf16 v[56:59], v[166:169], v[174:177], v[56:59]
	v_mfma_f32_16x16x32_bf16 v[52:55], v[158:161], v[182:185], v[52:55]
	v_mfma_f32_16x16x32_bf16 v[48:51], v[166:169], v[182:185], v[48:51]
	v_mfma_f32_16x16x32_bf16 v[36:39], v[158:161], v[190:193], v[36:39]
	v_mfma_f32_16x16x32_bf16 v[32:35], v[166:169], v[190:193], v[32:35]
	v_mfma_f32_16x16x32_bf16 v[20:23], v[158:161], v[198:201], v[20:23]
	v_mfma_f32_16x16x32_bf16 v[16:19], v[166:169], v[198:201], v[16:19]
	v_mfma_f32_16x16x32_bf16 v[60:63], v[162:165], v[178:181], v[60:63]
	v_mfma_f32_16x16x32_bf16 v[56:59], v[170:173], v[178:181], v[56:59]
	v_mfma_f32_16x16x32_bf16 v[52:55], v[162:165], v[186:189], v[52:55]
	v_mfma_f32_16x16x32_bf16 v[48:51], v[170:173], v[186:189], v[48:51]
	v_mfma_f32_16x16x32_bf16 v[36:39], v[162:165], v[194:197], v[36:39]
	v_mfma_f32_16x16x32_bf16 v[32:35], v[170:173], v[194:197], v[32:35]
	v_mfma_f32_16x16x32_bf16 v[20:23], v[162:165], v[202:205], v[20:23]
	v_mfma_f32_16x16x32_bf16 v[16:19], v[170:173], v[202:205], v[16:19]
	s_setprio 0
	s_barrier
	s_add_u32 s34, s38, 0x40080
	s_addc_u32 s35, s39, 0
	s_mov_b32 m0, s60
	s_nop 0
	global_load_lds_dwordx4 v132, s[34:35]
	s_mov_b32 m0, s61
	s_nop 0
	global_load_lds_dwordx4 v128, s[34:35]
	s_waitcnt vmcnt(6)
	s_barrier
	s_setprio 1
	v_mfma_f32_16x16x32_bf16 v[44:47], v[210:213], v[174:177], v[44:47]
	v_mfma_f32_16x16x32_bf16 v[40:43], v[218:221], v[174:177], v[40:43]
	v_mfma_f32_16x16x32_bf16 v[28:31], v[210:213], v[182:185], v[28:31]
	v_mfma_f32_16x16x32_bf16 v[24:27], v[218:221], v[182:185], v[24:27]
	v_mfma_f32_16x16x32_bf16 v[12:15], v[210:213], v[190:193], v[12:15]
	v_mfma_f32_16x16x32_bf16 v[8:11], v[218:221], v[190:193], v[8:11]
	v_mfma_f32_16x16x32_bf16 v[4:7], v[210:213], v[198:201], v[4:7]
	v_mfma_f32_16x16x32_bf16 v[0:3], v[218:221], v[198:201], v[0:3]
	v_mfma_f32_16x16x32_bf16 v[44:47], v[214:217], v[178:181], v[44:47]
	v_mfma_f32_16x16x32_bf16 v[40:43], v[222:225], v[178:181], v[40:43]
	v_mfma_f32_16x16x32_bf16 v[28:31], v[214:217], v[186:189], v[28:31]
	v_mfma_f32_16x16x32_bf16 v[24:27], v[222:225], v[186:189], v[24:27]
	v_mfma_f32_16x16x32_bf16 v[12:15], v[214:217], v[194:197], v[12:15]
	v_mfma_f32_16x16x32_bf16 v[8:11], v[222:225], v[194:197], v[8:11]
	v_mfma_f32_16x16x32_bf16 v[4:7], v[214:217], v[202:205], v[4:7]
	v_mfma_f32_16x16x32_bf16 v[0:3], v[222:225], v[202:205], v[0:3]
	s_setprio 0
	s_add_i32 s67, s67, 2
	s_cmp_gt_u32 s67, 13
	s_mov_b64 s[34:35], s[36:37]
	s_barrier
	s_cbranch_scc0 .LBB0_3168
	v_mov_b32_e32 v159, v140
	s_mov_b64 s[10:11], 0x80000
	v_ashrrev_i32_e32 v158, 2, v159
	v_and_b32_e32 v158, 0xffffffc0, v158
	v_lshl_add_u32 v158, s18, 8, v158
	v_and_or_b32 v158, v159, 15, v158
	v_lshrrev_b32_e32 v159, 1, v159
	v_and_b32_e32 v159, 0x78, v159
	v_lshl_or_b32 v160, s66, 8, v159
	v_ashrrev_i32_e32 v159, 31, v158
	v_ashrrev_i32_e32 v161, 31, v160
	v_lshlrev_b64 v[162:163], 12, v[158:159]
	v_lshl_add_u64 v[162:163], s[2:3], 0, v[162:163]
	v_lshlrev_b64 v[160:161], 1, v[160:161]
	v_lshl_add_u64 v[162:163], v[162:163], 0, v[160:161]
	v_cvt_pk_bf16_f32 v68, v68, v69
	v_cvt_pk_bf16_f32 v69, v70, v71
	v_cvt_pk_bf16_f32 v70, v64, v65
	v_lshl_add_u64 v[64:65], v[162:163], 0, s[10:11]
	s_mov_b32 s10, 0x80000
	v_cvt_pk_bf16_f32 v60, v60, v61
	v_cvt_pk_bf16_f32 v61, v62, v63
	v_cvt_pk_bf16_f32 v62, v56, v57
	v_add_co_u32_e32 v56, vcc, s10, v162
	v_cvt_pk_bf16_f32 v44, v44, v45
	s_nop 0
	v_addc_co_u32_e32 v57, vcc, 0, v163, vcc
	v_cvt_pk_bf16_f32 v45, v46, v47
	v_cvt_pk_bf16_f32 v46, v40, v41
	v_cvt_pk_bf16_f32 v47, v42, v43
	v_cvt_pk_bf16_f32 v112, v112, v113
	v_cvt_pk_bf16_f32 v113, v114, v115
	v_cvt_pk_bf16_f32 v114, v104, v105
	v_or_b32_e32 v104, 16, v158
	global_store_dwordx4 v[64:65], v[44:47], off offset:256
	s_mov_b64 s[10:11], 0x90000
	v_ashrrev_i32_e32 v105, 31, v104
	v_add_co_u32_e32 v46, vcc, s63, v162
	v_cvt_pk_bf16_f32 v96, v96, v97
	v_cvt_pk_bf16_f32 v97, v98, v99
	v_cvt_pk_bf16_f32 v98, v88, v89
	v_or_b32_e32 v88, 32, v158
	v_lshl_add_u64 v[44:45], v[162:163], 0, s[10:11]
	v_addc_co_u32_e32 v47, vcc, 0, v163, vcc
	v_cvt_pk_bf16_f32 v28, v28, v29
	v_cvt_pk_bf16_f32 v29, v30, v31
	v_cvt_pk_bf16_f32 v30, v24, v25
	v_cvt_pk_bf16_f32 v31, v26, v27
	v_lshlrev_b64 v[104:105], 12, v[104:105]
	v_ashrrev_i32_e32 v89, 31, v88
	v_cvt_pk_bf16_f32 v80, v80, v81
	v_cvt_pk_bf16_f32 v81, v82, v83
	v_cvt_pk_bf16_f32 v82, v72, v73
	v_or_b32_e32 v72, 48, v158
	global_store_dwordx4 v[44:45], v[28:31], off offset:256
	v_cvt_pk_bf16_f32 v115, v106, v107
	v_lshl_add_u64 v[104:105], s[2:3], 0, v[104:105]
	v_add_co_u32_e32 v30, vcc, s64, v162
	v_lshlrev_b64 v[88:89], 12, v[88:89]
	v_ashrrev_i32_e32 v73, 31, v72
	v_lshl_add_u64 v[28:29], v[162:163], 0, s[6:7]
	v_addc_co_u32_e32 v31, vcc, 0, v163, vcc
	v_cvt_pk_bf16_f32 v12, v12, v13
	v_cvt_pk_bf16_f32 v13, v14, v15
	v_cvt_pk_bf16_f32 v14, v8, v9
	v_cvt_pk_bf16_f32 v15, v10, v11
	global_store_dwordx4 v[162:163], v[112:115], off offset:256
	v_cvt_pk_bf16_f32 v99, v90, v91
	v_lshl_add_u64 v[88:89], s[2:3], 0, v[88:89]
	v_lshl_add_u64 v[112:113], v[104:105], 0, v[160:161]
	v_lshlrev_b64 v[72:73], 12, v[72:73]
	global_store_dwordx4 v[28:29], v[12:15], off offset:256
	global_store_dwordx4 v[112:113], v[96:99], off offset:256
	v_cvt_pk_bf16_f32 v83, v74, v75
	v_add_co_u32_e32 v14, vcc, s65, v162
	v_lshl_add_u64 v[96:97], v[88:89], 0, v[160:161]
	v_lshl_add_u64 v[72:73], s[2:3], 0, v[72:73]
	v_addc_co_u32_e32 v15, vcc, 0, v163, vcc
	v_cvt_pk_bf16_f32 v124, v124, v125
	v_cvt_pk_bf16_f32 v125, v126, v127
	v_cvt_pk_bf16_f32 v126, v120, v121
	v_cvt_pk_bf16_f32 v127, v122, v123
	v_cvt_pk_bf16_f32 v104, v116, v117
	v_cvt_pk_bf16_f32 v105, v118, v119
	v_cvt_pk_bf16_f32 v106, v108, v109
	v_cvt_pk_bf16_f32 v107, v110, v111
	v_cvt_pk_bf16_f32 v88, v100, v101
	v_cvt_pk_bf16_f32 v89, v102, v103
	v_cvt_pk_bf16_f32 v90, v92, v93
	v_cvt_pk_bf16_f32 v91, v94, v95
	global_store_dwordx4 v[96:97], v[80:83], off offset:256
	v_cvt_pk_bf16_f32 v74, v76, v77
	v_cvt_pk_bf16_f32 v75, v78, v79
	v_lshl_add_u64 v[80:81], v[72:73], 0, v[160:161]
	v_cvt_pk_bf16_f32 v72, v84, v85
	v_cvt_pk_bf16_f32 v73, v86, v87
	v_cvt_pk_bf16_f32 v71, v66, v67
	v_cvt_pk_bf16_f32 v63, v58, v59
	v_cvt_pk_bf16_f32 v40, v52, v53
	v_cvt_pk_bf16_f32 v41, v54, v55
	v_cvt_pk_bf16_f32 v42, v48, v49
	v_cvt_pk_bf16_f32 v43, v50, v51
	v_cvt_pk_bf16_f32 v24, v36, v37
	v_cvt_pk_bf16_f32 v25, v38, v39
	v_cvt_pk_bf16_f32 v26, v32, v33
	v_cvt_pk_bf16_f32 v27, v34, v35
	v_lshl_add_u64 v[12:13], v[162:163], 0, s[16:17]
	v_cvt_pk_bf16_f32 v8, v20, v21
	v_cvt_pk_bf16_f32 v9, v22, v23
	v_cvt_pk_bf16_f32 v10, v16, v17
	v_cvt_pk_bf16_f32 v11, v18, v19
	v_cvt_pk_bf16_f32 v4, v4, v5
	v_cvt_pk_bf16_f32 v5, v6, v7
	v_cvt_pk_bf16_f32 v6, v0, v1
	v_cvt_pk_bf16_f32 v7, v2, v3
	s_and_b64 vcc, exec, s[8:9]
	s_mov_b32 s66, s22
	s_mov_b32 s18, s26
	s_mov_b64 s[20:21], s[30:31]
	s_mov_b64 s[24:25], s[28:29]
	global_store_dwordx4 v[162:163], v[124:127], off
	global_store_dwordx4 v[112:113], v[104:107], off
	global_store_dwordx4 v[96:97], v[88:91], off
	global_store_dwordx4 v[80:81], v[72:75], off
	global_store_dwordx4 v[80:81], v[68:71], off offset:256
	global_store_dwordx4 v[56:57], v[60:63], off
	global_store_dwordx4 v[46:47], v[40:43], off
	global_store_dwordx4 v[30:31], v[24:27], off
	global_store_dwordx4 v[14:15], v[8:11], off
	global_store_dwordx4 v[12:13], v[4:7], off offset:256
	s_cbranch_vccz .LBB0_3165
	s_waitcnt vmcnt(0)
	s_cmpk_gt_u32 s33, 0xff
	v_readlane_b32 s58, v242, 45
	v_readlane_b32 s59, v242, 46
	s_cbranch_scc1 .LBB0_3172
	s_barrier

.LBB0_3521:
	s_add_u32 s46, s44, 0x100
	ds_read_b128 v[80:83], v163
	ds_read_b128 v[84:87], v164
	ds_read_b128 v[88:91], v171
	ds_read_b128 v[92:95], v172
	s_addc_u32 s47, s45, 0
	s_and_b32 s31, s46, 0x700
	s_add_u32 s33, s40, s31
	s_addc_u32 s35, s41, 0
	s_cmp_eq_u32 s16, 12
	s_cselect_b64 s[50:51], -1, 0
	s_and_b64 s[48:49], s[50:51], exec
	s_cselect_b32 s49, s1, s35
	s_cselect_b32 s48, s3, s33
	s_cselect_b32 s33, 0, 0
	s_cselect_b32 s31, 0, s31
	s_add_u32 s35, s42, s44
	s_addc_u32 s45, s43, s45
	s_add_u32 s44, s35, 0x40080
	s_addc_u32 s45, s45, 0
	ds_read_b128 v[158:161], v179
	ds_read_b128 v[180:183], v179 offset:1024
	ds_read_b128 v[184:187], v179 offset:2048
	ds_read_b128 v[188:191], v179 offset:3072
	ds_read_b128 v[192:195], v179 offset:4096
	ds_read_b128 v[196:199], v179 offset:5120
	ds_read_b128 v[200:203], v179 offset:6144
	ds_read_b128 v[204:207], v179 offset:7168
	s_add_i32 m0, s57, 0xc000
	s_nop 0
	global_load_lds_dwordx4 v144, s[44:45]
	s_add_i32 m0, s57, 0xe000
	s_nop 0
	global_load_lds_dwordx4 v148, s[44:45]
	s_waitcnt lgkmcnt(8)
	s_barrier
	s_waitcnt lgkmcnt(0)
	s_setprio 1
	s_waitcnt lgkmcnt(0)
	v_mfma_f32_16x16x32_bf16 v[140:143], v[80:83], v[158:161], v[140:143]
	v_mfma_f32_16x16x32_bf16 v[136:139], v[88:91], v[158:161], v[136:139]
	v_mfma_f32_16x16x32_bf16 v[124:127], v[80:83], v[184:187], v[124:127]
	v_mfma_f32_16x16x32_bf16 v[120:123], v[88:91], v[184:187], v[120:123]
	v_mfma_f32_16x16x32_bf16 v[108:111], v[80:83], v[192:195], v[108:111]
	v_mfma_f32_16x16x32_bf16 v[104:107], v[88:91], v[192:195], v[104:107]
	v_mfma_f32_16x16x32_bf16 v[76:79], v[80:83], v[200:203], v[76:79]
	v_mfma_f32_16x16x32_bf16 v[72:75], v[88:91], v[200:203], v[72:75]
	v_mfma_f32_16x16x32_bf16 v[140:143], v[84:87], v[180:183], v[140:143]
	v_mfma_f32_16x16x32_bf16 v[136:139], v[92:95], v[180:183], v[136:139]
	v_mfma_f32_16x16x32_bf16 v[124:127], v[84:87], v[188:191], v[124:127]
	v_mfma_f32_16x16x32_bf16 v[120:123], v[92:95], v[188:191], v[120:123]
	v_mfma_f32_16x16x32_bf16 v[108:111], v[84:87], v[196:199], v[108:111]
	v_mfma_f32_16x16x32_bf16 v[104:107], v[92:95], v[196:199], v[104:107]
	v_mfma_f32_16x16x32_bf16 v[76:79], v[84:87], v[204:207], v[76:79]
	v_mfma_f32_16x16x32_bf16 v[72:75], v[92:95], v[204:207], v[72:75]
	s_setprio 0
	s_barrier
	s_mov_b64 s[44:45], s[48:49]
	s_mov_b32 m0, s58
	ds_read_b128 v[210:213], v165
	ds_read_b128 v[214:217], v166
	ds_read_b128 v[218:221], v173
	ds_read_b128 v[222:225], v174
	s_nop 0
	global_load_lds_dwordx4 v146, s[44:45]
	s_mov_b32 m0, s59
	s_nop 0
	global_load_lds_dwordx4 v150, s[44:45]
	s_nop 0
	s_barrier
	s_waitcnt lgkmcnt(0)
	s_setprio 1
	s_waitcnt lgkmcnt(0)
	v_mfma_f32_16x16x32_bf16 v[132:135], v[210:213], v[158:161], v[132:135]
	v_mfma_f32_16x16x32_bf16 v[128:131], v[218:221], v[158:161], v[128:131]
	v_mfma_f32_16x16x32_bf16 v[116:119], v[210:213], v[184:187], v[116:119]
	v_mfma_f32_16x16x32_bf16 v[112:115], v[218:221], v[184:187], v[112:115]
	v_mfma_f32_16x16x32_bf16 v[100:103], v[210:213], v[192:195], v[100:103]
	v_mfma_f32_16x16x32_bf16 v[96:99], v[218:221], v[192:195], v[96:99]
	v_mfma_f32_16x16x32_bf16 v[68:71], v[210:213], v[200:203], v[68:71]
	v_mfma_f32_16x16x32_bf16 v[64:67], v[218:221], v[200:203], v[64:67]
	v_mfma_f32_16x16x32_bf16 v[132:135], v[214:217], v[180:183], v[132:135]
	v_mfma_f32_16x16x32_bf16 v[128:131], v[222:225], v[180:183], v[128:131]
	v_mfma_f32_16x16x32_bf16 v[116:119], v[214:217], v[188:191], v[116:119]
	v_mfma_f32_16x16x32_bf16 v[112:115], v[222:225], v[188:191], v[112:115]
	v_mfma_f32_16x16x32_bf16 v[100:103], v[214:217], v[196:199], v[100:103]
	v_mfma_f32_16x16x32_bf16 v[96:99], v[222:225], v[196:199], v[96:99]
	v_mfma_f32_16x16x32_bf16 v[68:71], v[214:217], v[204:207], v[68:71]
	v_mfma_f32_16x16x32_bf16 v[64:67], v[222:225], v[204:207], v[64:67]
	s_setprio 0
	s_and_b64 s[44:45], s[6:7], s[50:51]
	s_and_b64 s[44:45], s[44:45], exec
	s_cselect_b32 s44, s36, s42
	s_cselect_b32 s35, s37, s43
	s_add_u32 s44, s44, s31
	s_addc_u32 s45, s35, s33
	s_mov_b64 s[50:51], s[44:45]
	s_mov_b32 m0, s57
	s_barrier
	ds_read_b128 v[158:161], v179 offset:16384
	ds_read_b128 v[180:183], v179 offset:17408
	ds_read_b128 v[184:187], v179 offset:18432
	ds_read_b128 v[188:191], v179 offset:19456
	ds_read_b128 v[192:195], v179 offset:20480
	ds_read_b128 v[196:199], v179 offset:21504
	ds_read_b128 v[200:203], v179 offset:22528
	ds_read_b128 v[204:207], v179 offset:23552
	s_nop 0
	global_load_lds_dwordx4 v144, s[50:51]
	s_mov_b32 m0, s60
	s_nop 0
	global_load_lds_dwordx4 v148, s[50:51]
	s_nop 0
	s_barrier
	s_waitcnt lgkmcnt(0)
	s_setprio 1
	s_waitcnt lgkmcnt(0)
	v_mfma_f32_16x16x32_bf16 v[60:63], v[80:83], v[158:161], v[60:63]
	v_mfma_f32_16x16x32_bf16 v[56:59], v[88:91], v[158:161], v[56:59]
	v_mfma_f32_16x16x32_bf16 v[44:47], v[80:83], v[184:187], v[44:47]
	v_mfma_f32_16x16x32_bf16 v[40:43], v[88:91], v[184:187], v[40:43]
	v_mfma_f32_16x16x32_bf16 v[28:31], v[80:83], v[192:195], v[28:31]
	v_mfma_f32_16x16x32_bf16 v[24:27], v[88:91], v[192:195], v[24:27]
	v_mfma_f32_16x16x32_bf16 v[12:15], v[80:83], v[200:203], v[12:15]
	v_mfma_f32_16x16x32_bf16 v[8:11], v[88:91], v[200:203], v[8:11]
	v_mfma_f32_16x16x32_bf16 v[60:63], v[84:87], v[180:183], v[60:63]
	v_mfma_f32_16x16x32_bf16 v[56:59], v[92:95], v[180:183], v[56:59]
	v_mfma_f32_16x16x32_bf16 v[44:47], v[84:87], v[188:191], v[44:47]
	v_mfma_f32_16x16x32_bf16 v[40:43], v[92:95], v[188:191], v[40:43]
	v_mfma_f32_16x16x32_bf16 v[28:31], v[84:87], v[196:199], v[28:31]
	v_mfma_f32_16x16x32_bf16 v[24:27], v[92:95], v[196:199], v[24:27]
	v_mfma_f32_16x16x32_bf16 v[12:15], v[84:87], v[204:207], v[12:15]
	v_mfma_f32_16x16x32_bf16 v[8:11], v[92:95], v[204:207], v[8:11]
	s_setprio 0
	s_barrier
	s_add_u32 s50, s48, 0x40000
	s_addc_u32 s51, s49, 0
	s_mov_b32 m0, s61
	s_nop 0
	global_load_lds_dwordx4 v146, s[50:51]
	s_mov_b32 m0, s62
	s_nop 0
	global_load_lds_dwordx4 v150, s[50:51]
	s_waitcnt vmcnt(6)
	s_barrier
	s_setprio 1
	v_mfma_f32_16x16x32_bf16 v[52:55], v[210:213], v[158:161], v[52:55]
	v_mfma_f32_16x16x32_bf16 v[48:51], v[218:221], v[158:161], v[48:51]
	v_mfma_f32_16x16x32_bf16 v[36:39], v[210:213], v[184:187], v[36:39]
	v_mfma_f32_16x16x32_bf16 v[32:35], v[218:221], v[184:187], v[32:35]
	v_mfma_f32_16x16x32_bf16 v[20:23], v[210:213], v[192:195], v[20:23]
	v_mfma_f32_16x16x32_bf16 v[16:19], v[218:221], v[192:195], v[16:19]
	v_mfma_f32_16x16x32_bf16 v[4:7], v[210:213], v[200:203], v[4:7]
	v_mfma_f32_16x16x32_bf16 v[0:3], v[218:221], v[200:203], v[0:3]
	v_mfma_f32_16x16x32_bf16 v[52:55], v[214:217], v[180:183], v[52:55]
	v_mfma_f32_16x16x32_bf16 v[48:51], v[222:225], v[180:183], v[48:51]
	v_mfma_f32_16x16x32_bf16 v[36:39], v[214:217], v[188:191], v[36:39]
	v_mfma_f32_16x16x32_bf16 v[32:35], v[222:225], v[188:191], v[32:35]
	v_mfma_f32_16x16x32_bf16 v[20:23], v[214:217], v[196:199], v[20:23]
	v_mfma_f32_16x16x32_bf16 v[16:19], v[222:225], v[196:199], v[16:19]
	v_mfma_f32_16x16x32_bf16 v[4:7], v[214:217], v[204:207], v[4:7]
	v_mfma_f32_16x16x32_bf16 v[0:3], v[222:225], v[204:207], v[0:3]
	s_setprio 0
	s_barrier
	ds_read_b128 v[80:83], v167
	ds_read_b128 v[84:87], v168
	ds_read_b128 v[88:91], v175
	ds_read_b128 v[92:95], v176
	s_add_u32 s50, s44, 0x40000
	s_addc_u32 s51, s45, 0
	s_mov_b32 m0, s63
	ds_read_b128 v[158:161], v179 offset:32768
	ds_read_b128 v[180:183], v179 offset:33792
	ds_read_b128 v[184:187], v179 offset:34816
	ds_read_b128 v[188:191], v179 offset:35840
	ds_read_b128 v[192:195], v179 offset:36864
	ds_read_b128 v[196:199], v179 offset:37888
	ds_read_b128 v[200:203], v179 offset:38912
	ds_read_b128 v[204:207], v179 offset:39936
	s_nop 0
	global_load_lds_dwordx4 v144, s[50:51]
	s_mov_b32 m0, s64
	s_nop 0
	global_load_lds_dwordx4 v148, s[50:51]
	s_waitcnt lgkmcnt(8)
	s_barrier
	s_waitcnt lgkmcnt(0)
	s_setprio 1
	s_waitcnt lgkmcnt(0)
	v_mfma_f32_16x16x32_bf16 v[140:143], v[80:83], v[158:161], v[140:143]
	v_mfma_f32_16x16x32_bf16 v[136:139], v[88:91], v[158:161], v[136:139]
	v_mfma_f32_16x16x32_bf16 v[124:127], v[80:83], v[184:187], v[124:127]
	v_mfma_f32_16x16x32_bf16 v[120:123], v[88:91], v[184:187], v[120:123]
	v_mfma_f32_16x16x32_bf16 v[108:111], v[80:83], v[192:195], v[108:111]
	v_mfma_f32_16x16x32_bf16 v[104:107], v[88:91], v[192:195], v[104:107]
	v_mfma_f32_16x16x32_bf16 v[76:79], v[80:83], v[200:203], v[76:79]
	v_mfma_f32_16x16x32_bf16 v[72:75], v[88:91], v[200:203], v[72:75]
	v_mfma_f32_16x16x32_bf16 v[140:143], v[84:87], v[180:183], v[140:143]
	v_mfma_f32_16x16x32_bf16 v[136:139], v[92:95], v[180:183], v[136:139]
	v_mfma_f32_16x16x32_bf16 v[124:127], v[84:87], v[188:191], v[124:127]
	v_mfma_f32_16x16x32_bf16 v[120:123], v[92:95], v[188:191], v[120:123]
	v_mfma_f32_16x16x32_bf16 v[108:111], v[84:87], v[196:199], v[108:111]
	v_mfma_f32_16x16x32_bf16 v[104:107], v[92:95], v[196:199], v[104:107]
	v_mfma_f32_16x16x32_bf16 v[76:79], v[84:87], v[204:207], v[76:79]
	v_mfma_f32_16x16x32_bf16 v[72:75], v[92:95], v[204:207], v[72:75]
	s_setprio 0
	s_barrier
	s_add_u32 s50, s48, 0x80
	s_addc_u32 s51, s49, 0
	s_mov_b32 m0, s67
	ds_read_b128 v[210:213], v169
	ds_read_b128 v[214:217], v170
	ds_read_b128 v[218:221], v177
	ds_read_b128 v[222:225], v178
	s_nop 0
	global_load_lds_dwordx4 v146, s[50:51]
	s_mov_b32 m0, s68
	s_nop 0
	global_load_lds_dwordx4 v150, s[50:51]
	s_nop 0
	s_barrier
	s_waitcnt lgkmcnt(0)
	s_setprio 1
	s_waitcnt lgkmcnt(0)
	v_mfma_f32_16x16x32_bf16 v[132:135], v[210:213], v[158:161], v[132:135]
	v_mfma_f32_16x16x32_bf16 v[128:131], v[218:221], v[158:161], v[128:131]
	v_mfma_f32_16x16x32_bf16 v[116:119], v[210:213], v[184:187], v[116:119]
	v_mfma_f32_16x16x32_bf16 v[112:115], v[218:221], v[184:187], v[112:115]
	v_mfma_f32_16x16x32_bf16 v[100:103], v[210:213], v[192:195], v[100:103]
	v_mfma_f32_16x16x32_bf16 v[96:99], v[218:221], v[192:195], v[96:99]
	v_mfma_f32_16x16x32_bf16 v[68:71], v[210:213], v[200:203], v[68:71]
	v_mfma_f32_16x16x32_bf16 v[64:67], v[218:221], v[200:203], v[64:67]
	v_mfma_f32_16x16x32_bf16 v[132:135], v[214:217], v[180:183], v[132:135]
	v_mfma_f32_16x16x32_bf16 v[128:131], v[222:225], v[180:183], v[128:131]
	v_mfma_f32_16x16x32_bf16 v[116:119], v[214:217], v[188:191], v[116:119]
	v_mfma_f32_16x16x32_bf16 v[112:115], v[222:225], v[188:191], v[112:115]
	v_mfma_f32_16x16x32_bf16 v[100:103], v[214:217], v[196:199], v[100:103]
	v_mfma_f32_16x16x32_bf16 v[96:99], v[222:225], v[196:199], v[96:99]
	v_mfma_f32_16x16x32_bf16 v[68:71], v[214:217], v[204:207], v[68:71]
	v_mfma_f32_16x16x32_bf16 v[64:67], v[222:225], v[204:207], v[64:67]
	s_setprio 0
	s_add_u32 s44, s44, 0x80
	s_addc_u32 s45, s45, 0
	s_mov_b32 m0, s69
	s_barrier
	ds_read_b128 v[158:161], v179 offset:49152
	ds_read_b128 v[180:183], v179 offset:50176
	ds_read_b128 v[184:187], v179 offset:51200
	ds_read_b128 v[188:191], v179 offset:52224
	ds_read_b128 v[192:195], v179 offset:53248
	ds_read_b128 v[196:199], v179 offset:54272
	ds_read_b128 v[200:203], v179 offset:55296
	ds_read_b128 v[204:207], v179 offset:56320
	s_nop 0
	global_load_lds_dwordx4 v144, s[44:45]
	s_mov_b32 m0, s70
	s_nop 0
	global_load_lds_dwordx4 v148, s[44:45]
	s_nop 0
	s_barrier
	s_waitcnt lgkmcnt(0)
	s_setprio 1
	s_waitcnt lgkmcnt(0)
	v_mfma_f32_16x16x32_bf16 v[60:63], v[80:83], v[158:161], v[60:63]
	v_mfma_f32_16x16x32_bf16 v[56:59], v[88:91], v[158:161], v[56:59]
	v_mfma_f32_16x16x32_bf16 v[44:47], v[80:83], v[184:187], v[44:47]
	v_mfma_f32_16x16x32_bf16 v[40:43], v[88:91], v[184:187], v[40:43]
	v_mfma_f32_16x16x32_bf16 v[28:31], v[80:83], v[192:195], v[28:31]
	v_mfma_f32_16x16x32_bf16 v[24:27], v[88:91], v[192:195], v[24:27]
	v_mfma_f32_16x16x32_bf16 v[12:15], v[80:83], v[200:203], v[12:15]
	v_mfma_f32_16x16x32_bf16 v[8:11], v[88:91], v[200:203], v[8:11]
	v_mfma_f32_16x16x32_bf16 v[60:63], v[84:87], v[180:183], v[60:63]
	v_mfma_f32_16x16x32_bf16 v[56:59], v[92:95], v[180:183], v[56:59]
	v_mfma_f32_16x16x32_bf16 v[44:47], v[84:87], v[188:191], v[44:47]
	v_mfma_f32_16x16x32_bf16 v[40:43], v[92:95], v[188:191], v[40:43]
	v_mfma_f32_16x16x32_bf16 v[28:31], v[84:87], v[196:199], v[28:31]
	v_mfma_f32_16x16x32_bf16 v[24:27], v[92:95], v[196:199], v[24:27]
	v_mfma_f32_16x16x32_bf16 v[12:15], v[84:87], v[204:207], v[12:15]
	v_mfma_f32_16x16x32_bf16 v[8:11], v[92:95], v[204:207], v[8:11]
	s_setprio 0
	s_barrier
	s_add_u32 s44, s48, 0x40080
	s_addc_u32 s45, s49, 0
	s_mov_b32 m0, s71
	s_nop 0
	global_load_lds_dwordx4 v146, s[44:45]
	s_mov_b32 m0, s72
	s_nop 0
	global_load_lds_dwordx4 v150, s[44:45]
	s_waitcnt vmcnt(6)
	s_barrier
	s_setprio 1
	v_mfma_f32_16x16x32_bf16 v[52:55], v[210:213], v[158:161], v[52:55]
	v_mfma_f32_16x16x32_bf16 v[48:51], v[218:221], v[158:161], v[48:51]
	v_mfma_f32_16x16x32_bf16 v[36:39], v[210:213], v[184:187], v[36:39]
	v_mfma_f32_16x16x32_bf16 v[32:35], v[218:221], v[184:187], v[32:35]
	v_mfma_f32_16x16x32_bf16 v[20:23], v[210:213], v[192:195], v[20:23]
	v_mfma_f32_16x16x32_bf16 v[16:19], v[218:221], v[192:195], v[16:19]
	v_mfma_f32_16x16x32_bf16 v[4:7], v[210:213], v[200:203], v[4:7]
	v_mfma_f32_16x16x32_bf16 v[0:3], v[218:221], v[200:203], v[0:3]
	v_mfma_f32_16x16x32_bf16 v[52:55], v[214:217], v[180:183], v[52:55]
	v_mfma_f32_16x16x32_bf16 v[48:51], v[222:225], v[180:183], v[48:51]
	v_mfma_f32_16x16x32_bf16 v[36:39], v[214:217], v[188:191], v[36:39]
	v_mfma_f32_16x16x32_bf16 v[32:35], v[222:225], v[188:191], v[32:35]
	v_mfma_f32_16x16x32_bf16 v[20:23], v[214:217], v[196:199], v[20:23]
	v_mfma_f32_16x16x32_bf16 v[16:19], v[222:225], v[196:199], v[16:19]
	v_mfma_f32_16x16x32_bf16 v[4:7], v[214:217], v[204:207], v[4:7]
	v_mfma_f32_16x16x32_bf16 v[0:3], v[222:225], v[204:207], v[0:3]
	s_setprio 0
	s_add_i32 s16, s16, 2
	s_cmp_gt_u32 s16, 13
	s_mov_b64 s[44:45], s[46:47]
	s_barrier
	s_cbranch_scc0 .LBB0_3521
	v_mov_b32_e32 v80, v162
	s_cmpk_gt_i32 s2, 0x7f
	s_mov_b64 s[6:7], 0xc000
	s_cbranch_scc1 .LBB0_3524
	s_ashr_i32 s1, s2, 31
	s_lshr_b32 s1, s1, 28
	s_add_i32 s1, s2, s1
	s_ashr_i32 s1, s1, 4
	s_mul_hi_i32 s7, s1, 0x1800
	s_mul_i32 s6, s1, 0x1800

.LBB0_3910:
	v_mov_b32_e32 v0, v209
	s_mov_b32 s98, 0x44800000
	s_mov_b32 s100, 0xbd38aa3b
	s_ashr_i32 s2, s0, 31
	v_ashrrev_i32_e32 v1, 2, v0
	v_and_b32_e32 v1, 0xffffffc0, v1
	v_lshl_add_u32 v1, s33, 8, v1
	v_and_or_b32 v4, v0, 15, v1
	v_lshrrev_b32_e32 v2, 1, v0
	s_lshr_b32 s2, s2, 29
	s_add_i32 s2, s0, s2
	s_and_b32 s2, s2, 0x1fffff8
	s_sub_i32 s0, s0, s2
	v_and_b32_e32 v2, 0x78, v2
	v_ashrrev_i32_e32 v5, 31, v4
	v_lshl_or_b32 v2, s0, 7, v2
	v_lshlrev_b64 v[0:1], 10, v[4:5]
	v_ashrrev_i32_e32 v3, 31, v2
	v_lshl_add_u64 v[0:1], s[12:13], 0, v[0:1]
	v_lshl_add_u64 v[0:1], v[0:1], 0, v[2:3]
	v_pk_mul_f32 v[10:11], v[188:189], s[100:101] op_sel_hi:[1,0]
	v_pk_mul_f32 v[12:13], v[190:191], s[100:101] op_sel_hi:[1,0]
	v_pk_mul_f32 v[14:15], v[180:181], s[100:101] op_sel_hi:[1,0]
	v_pk_mul_f32 v[16:17], v[182:183], s[100:101] op_sel_hi:[1,0]
	v_exp_f32_e32 v10, v10
	v_exp_f32_e32 v11, v11
	v_exp_f32_e32 v12, v12
	v_exp_f32_e32 v13, v13
	v_exp_f32_e32 v14, v14
	v_exp_f32_e32 v15, v15
	v_exp_f32_e32 v16, v16
	v_exp_f32_e32 v17, v17
	v_pk_fma_f32 v[10:11], v[10:11], s[98:99], s[98:99] op_sel_hi:[1,0,0]
	v_pk_fma_f32 v[12:13], v[12:13], s[98:99], s[98:99] op_sel_hi:[1,0,0]
	v_pk_fma_f32 v[14:15], v[14:15], s[98:99], s[98:99] op_sel_hi:[1,0,0]
	v_pk_fma_f32 v[16:17], v[16:17], s[98:99], s[98:99] op_sel_hi:[1,0,0]
	v_rcp_f32_e32 v10, v10
	v_rcp_f32_e32 v11, v11
	v_rcp_f32_e32 v12, v12
	v_rcp_f32_e32 v13, v13
	v_rcp_f32_e32 v14, v14
	v_rcp_f32_e32 v15, v15
	v_rcp_f32_e32 v16, v16
	v_rcp_f32_e32 v17, v17
	v_pk_mul_f32 v[10:11], v[188:189], v[10:11]
	v_pk_mul_f32 v[12:13], v[190:191], v[12:13]
	v_pk_mul_f32 v[14:15], v[180:181], v[14:15]
	v_pk_mul_f32 v[16:17], v[182:183], v[16:17]
	v_pk_mul_f32 v[10:11], v[10:11], v[184:185]
	v_pk_mul_f32 v[12:13], v[12:13], v[186:187]
	v_pk_mul_f32 v[14:15], v[14:15], v[176:177]
	v_pk_mul_f32 v[16:17], v[16:17], v[178:179]
	v_cvt_pk_fp8_f32 v18, v10, v11
	v_cvt_pk_fp8_f32 v19, v14, v15
	v_cvt_pk_fp8_f32 v18, v12, v13 op_sel:[0,0,1]
	v_cvt_pk_fp8_f32 v19, v16, v17 op_sel:[0,0,1]
	s_nop 0
	global_store_dwordx2 v[0:1], v[18:19], off
	v_or_b32_e32 v8, 16, v4
	v_ashrrev_i32_e32 v9, 31, v8
	v_lshlrev_b64 v[8:9], 10, v[8:9]
	v_lshl_add_u64 v[8:9], s[12:13], 0, v[8:9]
	v_lshl_add_u64 v[8:9], v[8:9], 0, v[2:3]
	v_pk_mul_f32 v[10:11], v[172:173], s[100:101] op_sel_hi:[1,0]
	v_pk_mul_f32 v[12:13], v[174:175], s[100:101] op_sel_hi:[1,0]
	v_pk_mul_f32 v[14:15], v[164:165], s[100:101] op_sel_hi:[1,0]
	v_pk_mul_f32 v[16:17], v[166:167], s[100:101] op_sel_hi:[1,0]
	v_exp_f32_e32 v10, v10
	v_exp_f32_e32 v11, v11
	v_exp_f32_e32 v12, v12
	v_exp_f32_e32 v13, v13
	v_exp_f32_e32 v14, v14
	v_exp_f32_e32 v15, v15
	v_exp_f32_e32 v16, v16
	v_exp_f32_e32 v17, v17
	v_pk_fma_f32 v[10:11], v[10:11], s[98:99], s[98:99] op_sel_hi:[1,0,0]
	v_pk_fma_f32 v[12:13], v[12:13], s[98:99], s[98:99] op_sel_hi:[1,0,0]
	v_pk_fma_f32 v[14:15], v[14:15], s[98:99], s[98:99] op_sel_hi:[1,0,0]
	v_pk_fma_f32 v[16:17], v[16:17], s[98:99], s[98:99] op_sel_hi:[1,0,0]
	v_rcp_f32_e32 v10, v10
	v_rcp_f32_e32 v11, v11
	v_rcp_f32_e32 v12, v12
	v_rcp_f32_e32 v13, v13
	v_rcp_f32_e32 v14, v14
	v_rcp_f32_e32 v15, v15
	v_rcp_f32_e32 v16, v16
	v_rcp_f32_e32 v17, v17
	v_pk_mul_f32 v[10:11], v[172:173], v[10:11]
	v_pk_mul_f32 v[12:13], v[174:175], v[12:13]
	v_pk_mul_f32 v[14:15], v[164:165], v[14:15]
	v_pk_mul_f32 v[16:17], v[166:167], v[16:17]
	v_pk_mul_f32 v[10:11], v[10:11], v[168:169]
	v_pk_mul_f32 v[12:13], v[12:13], v[170:171]
	v_pk_mul_f32 v[14:15], v[14:15], v[160:161]
	v_pk_mul_f32 v[16:17], v[16:17], v[162:163]
	v_cvt_pk_fp8_f32 v18, v10, v11
	v_cvt_pk_fp8_f32 v19, v14, v15
	v_cvt_pk_fp8_f32 v18, v12, v13 op_sel:[0,0,1]
	v_cvt_pk_fp8_f32 v19, v16, v17 op_sel:[0,0,1]
	s_nop 0
	global_store_dwordx2 v[8:9], v[18:19], off
	v_or_b32_e32 v8, 32, v4
	v_ashrrev_i32_e32 v9, 31, v8
	v_or_b32_e32 v4, 48, v4
	v_lshlrev_b64 v[6:7], 10, v[8:9]
	v_lshl_add_u64 v[6:7], s[12:13], 0, v[6:7]
	v_lshl_add_u64 v[6:7], v[6:7], 0, v[2:3]
	v_pk_mul_f32 v[10:11], v[156:157], s[100:101] op_sel_hi:[1,0]
	v_pk_mul_f32 v[12:13], v[158:159], s[100:101] op_sel_hi:[1,0]
	v_pk_mul_f32 v[14:15], v[148:149], s[100:101] op_sel_hi:[1,0]
	v_pk_mul_f32 v[16:17], v[150:151], s[100:101] op_sel_hi:[1,0]
	v_exp_f32_e32 v10, v10
	v_exp_f32_e32 v11, v11
	v_exp_f32_e32 v12, v12
	v_exp_f32_e32 v13, v13
	v_exp_f32_e32 v14, v14
	v_exp_f32_e32 v15, v15
	v_exp_f32_e32 v16, v16
	v_exp_f32_e32 v17, v17
	v_pk_fma_f32 v[10:11], v[10:11], s[98:99], s[98:99] op_sel_hi:[1,0,0]
	v_pk_fma_f32 v[12:13], v[12:13], s[98:99], s[98:99] op_sel_hi:[1,0,0]
	v_pk_fma_f32 v[14:15], v[14:15], s[98:99], s[98:99] op_sel_hi:[1,0,0]
	v_pk_fma_f32 v[16:17], v[16:17], s[98:99], s[98:99] op_sel_hi:[1,0,0]
	v_rcp_f32_e32 v10, v10
	v_rcp_f32_e32 v11, v11
	v_rcp_f32_e32 v12, v12
	v_rcp_f32_e32 v13, v13
	v_rcp_f32_e32 v14, v14
	v_rcp_f32_e32 v15, v15
	v_rcp_f32_e32 v16, v16
	v_rcp_f32_e32 v17, v17
	v_pk_mul_f32 v[10:11], v[156:157], v[10:11]
	v_pk_mul_f32 v[12:13], v[158:159], v[12:13]
	v_pk_mul_f32 v[14:15], v[148:149], v[14:15]
	v_pk_mul_f32 v[16:17], v[150:151], v[16:17]
	v_pk_mul_f32 v[10:11], v[10:11], v[152:153]
	v_pk_mul_f32 v[12:13], v[12:13], v[154:155]
	v_pk_mul_f32 v[14:15], v[14:15], v[144:145]
	v_pk_mul_f32 v[16:17], v[16:17], v[146:147]
	v_cvt_pk_fp8_f32 v18, v10, v11
	v_cvt_pk_fp8_f32 v19, v14, v15
	v_cvt_pk_fp8_f32 v18, v12, v13 op_sel:[0,0,1]
	v_cvt_pk_fp8_f32 v19, v16, v17 op_sel:[0,0,1]
	s_nop 0
	global_store_dwordx2 v[6:7], v[18:19], off
	v_ashrrev_i32_e32 v5, 31, v4
	v_lshlrev_b64 v[4:5], 10, v[4:5]
	v_lshl_add_u64 v[4:5], s[12:13], 0, v[4:5]
	v_lshl_add_u64 v[2:3], v[4:5], 0, v[2:3]
	s_mov_b32 s33, s52
	v_pk_mul_f32 v[10:11], v[140:141], s[100:101] op_sel_hi:[1,0]
	v_pk_mul_f32 v[12:13], v[142:143], s[100:101] op_sel_hi:[1,0]
	v_pk_mul_f32 v[14:15], v[132:133], s[100:101] op_sel_hi:[1,0]
	v_pk_mul_f32 v[16:17], v[134:135], s[100:101] op_sel_hi:[1,0]
	v_exp_f32_e32 v10, v10
	v_exp_f32_e32 v11, v11
	v_exp_f32_e32 v12, v12
	v_exp_f32_e32 v13, v13
	v_exp_f32_e32 v14, v14
	v_exp_f32_e32 v15, v15
	v_exp_f32_e32 v16, v16
	v_exp_f32_e32 v17, v17
	v_pk_fma_f32 v[10:11], v[10:11], s[98:99], s[98:99] op_sel_hi:[1,0,0]
	v_pk_fma_f32 v[12:13], v[12:13], s[98:99], s[98:99] op_sel_hi:[1,0,0]
	v_pk_fma_f32 v[14:15], v[14:15], s[98:99], s[98:99] op_sel_hi:[1,0,0]
	v_pk_fma_f32 v[16:17], v[16:17], s[98:99], s[98:99] op_sel_hi:[1,0,0]
	v_rcp_f32_e32 v10, v10
	v_rcp_f32_e32 v11, v11
	v_rcp_f32_e32 v12, v12
	v_rcp_f32_e32 v13, v13
	v_rcp_f32_e32 v14, v14
	v_rcp_f32_e32 v15, v15
	v_rcp_f32_e32 v16, v16
	v_rcp_f32_e32 v17, v17
	v_pk_mul_f32 v[10:11], v[140:141], v[10:11]
	v_pk_mul_f32 v[12:13], v[142:143], v[12:13]
	v_pk_mul_f32 v[14:15], v[132:133], v[14:15]
	v_pk_mul_f32 v[16:17], v[134:135], v[16:17]
	v_pk_mul_f32 v[10:11], v[10:11], v[136:137]
	v_pk_mul_f32 v[12:13], v[12:13], v[138:139]
	v_pk_mul_f32 v[14:15], v[14:15], v[128:129]
	v_pk_mul_f32 v[16:17], v[16:17], v[130:131]
	v_cvt_pk_fp8_f32 v18, v10, v11
	v_cvt_pk_fp8_f32 v19, v14, v15
	v_cvt_pk_fp8_f32 v18, v12, v13 op_sel:[0,0,1]
	v_cvt_pk_fp8_f32 v19, v16, v17 op_sel:[0,0,1]
	s_nop 0
	global_store_dwordx2 v[2:3], v[18:19], off
	s_mov_b32 s0, s16
	v_add_co_u32_e32 v6, vcc, s49, v0
	v_addc_co_u32_e32 v7, vcc, 0, v1, vcc
	v_pk_mul_f32 v[10:11], v[124:125], s[100:101] op_sel_hi:[1,0]
	v_pk_mul_f32 v[12:13], v[126:127], s[100:101] op_sel_hi:[1,0]
	v_pk_mul_f32 v[14:15], v[116:117], s[100:101] op_sel_hi:[1,0]
	v_pk_mul_f32 v[16:17], v[118:119], s[100:101] op_sel_hi:[1,0]
	v_exp_f32_e32 v10, v10
	v_exp_f32_e32 v11, v11
	v_exp_f32_e32 v12, v12
	v_exp_f32_e32 v13, v13
	v_exp_f32_e32 v14, v14
	v_exp_f32_e32 v15, v15
	v_exp_f32_e32 v16, v16
	v_exp_f32_e32 v17, v17
	v_pk_fma_f32 v[10:11], v[10:11], s[98:99], s[98:99] op_sel_hi:[1,0,0]
	v_pk_fma_f32 v[12:13], v[12:13], s[98:99], s[98:99] op_sel_hi:[1,0,0]
	v_pk_fma_f32 v[14:15], v[14:15], s[98:99], s[98:99] op_sel_hi:[1,0,0]
	v_pk_fma_f32 v[16:17], v[16:17], s[98:99], s[98:99] op_sel_hi:[1,0,0]
	v_rcp_f32_e32 v10, v10
	v_rcp_f32_e32 v11, v11
	v_rcp_f32_e32 v12, v12
	v_rcp_f32_e32 v13, v13
	v_rcp_f32_e32 v14, v14
	v_rcp_f32_e32 v15, v15
	v_rcp_f32_e32 v16, v16
	v_rcp_f32_e32 v17, v17
	v_pk_mul_f32 v[10:11], v[124:125], v[10:11]
	v_pk_mul_f32 v[12:13], v[126:127], v[12:13]
	v_pk_mul_f32 v[14:15], v[116:117], v[14:15]
	v_pk_mul_f32 v[16:17], v[118:119], v[16:17]
	v_pk_mul_f32 v[10:11], v[10:11], v[120:121]
	v_pk_mul_f32 v[12:13], v[12:13], v[122:123]
	v_pk_mul_f32 v[14:15], v[14:15], v[112:113]
	v_pk_mul_f32 v[16:17], v[16:17], v[114:115]
	v_cvt_pk_fp8_f32 v18, v10, v11
	v_cvt_pk_fp8_f32 v19, v14, v15
	v_cvt_pk_fp8_f32 v18, v12, v13 op_sel:[0,0,1]
	v_cvt_pk_fp8_f32 v19, v16, v17 op_sel:[0,0,1]
	s_nop 0
	global_store_dwordx2 v[6:7], v[18:19], off
	v_add_co_u32_e32 v6, vcc, s50, v0
	v_addc_co_u32_e32 v7, vcc, 0, v1, vcc
	v_pk_mul_f32 v[10:11], v[108:109], s[100:101] op_sel_hi:[1,0]
	v_pk_mul_f32 v[12:13], v[110:111], s[100:101] op_sel_hi:[1,0]
	v_pk_mul_f32 v[14:15], v[100:101], s[100:101] op_sel_hi:[1,0]
	v_pk_mul_f32 v[16:17], v[102:103], s[100:101] op_sel_hi:[1,0]
	v_exp_f32_e32 v10, v10
	v_exp_f32_e32 v11, v11
	v_exp_f32_e32 v12, v12
	v_exp_f32_e32 v13, v13
	v_exp_f32_e32 v14, v14
	v_exp_f32_e32 v15, v15
	v_exp_f32_e32 v16, v16
	v_exp_f32_e32 v17, v17
	v_pk_fma_f32 v[10:11], v[10:11], s[98:99], s[98:99] op_sel_hi:[1,0,0]
	v_pk_fma_f32 v[12:13], v[12:13], s[98:99], s[98:99] op_sel_hi:[1,0,0]
	v_pk_fma_f32 v[14:15], v[14:15], s[98:99], s[98:99] op_sel_hi:[1,0,0]
	v_pk_fma_f32 v[16:17], v[16:17], s[98:99], s[98:99] op_sel_hi:[1,0,0]
	v_rcp_f32_e32 v10, v10
	v_rcp_f32_e32 v11, v11
	v_rcp_f32_e32 v12, v12
	v_rcp_f32_e32 v13, v13
	v_rcp_f32_e32 v14, v14
	v_rcp_f32_e32 v15, v15
	v_rcp_f32_e32 v16, v16
	v_rcp_f32_e32 v17, v17
	v_pk_mul_f32 v[10:11], v[108:109], v[10:11]
	v_pk_mul_f32 v[12:13], v[110:111], v[12:13]
	v_pk_mul_f32 v[14:15], v[100:101], v[14:15]
	v_pk_mul_f32 v[16:17], v[102:103], v[16:17]
	v_pk_mul_f32 v[10:11], v[10:11], v[104:105]
	v_pk_mul_f32 v[12:13], v[12:13], v[106:107]
	v_pk_mul_f32 v[14:15], v[14:15], v[96:97]
	v_pk_mul_f32 v[16:17], v[16:17], v[98:99]
	v_cvt_pk_fp8_f32 v18, v10, v11
	v_cvt_pk_fp8_f32 v19, v14, v15
	v_cvt_pk_fp8_f32 v18, v12, v13 op_sel:[0,0,1]
	v_cvt_pk_fp8_f32 v19, v16, v17 op_sel:[0,0,1]
	s_nop 0
	global_store_dwordx2 v[6:7], v[18:19], off
	v_add_co_u32_e32 v6, vcc, s51, v0
	v_addc_co_u32_e32 v7, vcc, 0, v1, vcc
	v_pk_mul_f32 v[10:11], v[92:93], s[100:101] op_sel_hi:[1,0]
	v_pk_mul_f32 v[12:13], v[94:95], s[100:101] op_sel_hi:[1,0]
	v_pk_mul_f32 v[14:15], v[84:85], s[100:101] op_sel_hi:[1,0]
	v_pk_mul_f32 v[16:17], v[86:87], s[100:101] op_sel_hi:[1,0]
	v_exp_f32_e32 v10, v10
	v_exp_f32_e32 v11, v11
	v_exp_f32_e32 v12, v12
	v_exp_f32_e32 v13, v13
	v_exp_f32_e32 v14, v14
	v_exp_f32_e32 v15, v15
	v_exp_f32_e32 v16, v16
	v_exp_f32_e32 v17, v17
	v_pk_fma_f32 v[10:11], v[10:11], s[98:99], s[98:99] op_sel_hi:[1,0,0]
	v_pk_fma_f32 v[12:13], v[12:13], s[98:99], s[98:99] op_sel_hi:[1,0,0]
	v_pk_fma_f32 v[14:15], v[14:15], s[98:99], s[98:99] op_sel_hi:[1,0,0]
	v_pk_fma_f32 v[16:17], v[16:17], s[98:99], s[98:99] op_sel_hi:[1,0,0]
	v_rcp_f32_e32 v10, v10
	v_rcp_f32_e32 v11, v11
	v_rcp_f32_e32 v12, v12
	v_rcp_f32_e32 v13, v13
	v_rcp_f32_e32 v14, v14
	v_rcp_f32_e32 v15, v15
	v_rcp_f32_e32 v16, v16
	v_rcp_f32_e32 v17, v17
	v_pk_mul_f32 v[10:11], v[92:93], v[10:11]
	v_pk_mul_f32 v[12:13], v[94:95], v[12:13]
	v_pk_mul_f32 v[14:15], v[84:85], v[14:15]
	v_pk_mul_f32 v[16:17], v[86:87], v[16:17]
	v_pk_mul_f32 v[10:11], v[10:11], v[88:89]
	v_pk_mul_f32 v[12:13], v[12:13], v[90:91]
	v_pk_mul_f32 v[14:15], v[14:15], v[80:81]
	v_pk_mul_f32 v[16:17], v[16:17], v[82:83]
	v_cvt_pk_fp8_f32 v18, v10, v11
	v_cvt_pk_fp8_f32 v19, v14, v15
	v_cvt_pk_fp8_f32 v18, v12, v13 op_sel:[0,0,1]
	v_cvt_pk_fp8_f32 v19, v16, v17 op_sel:[0,0,1]
	s_nop 0
	global_store_dwordx2 v[6:7], v[18:19], off
	v_add_co_u32_e32 v0, vcc, 0x2c000, v0
	s_mov_b64 s[2:3], s[18:19]
	s_nop 0
	v_addc_co_u32_e32 v1, vcc, 0, v1, vcc
	s_and_b64 vcc, exec, s[4:5]
	v_pk_mul_f32 v[10:11], v[76:77], s[100:101] op_sel_hi:[1,0]
	v_pk_mul_f32 v[12:13], v[78:79], s[100:101] op_sel_hi:[1,0]
	v_pk_mul_f32 v[14:15], v[68:69], s[100:101] op_sel_hi:[1,0]
	v_pk_mul_f32 v[16:17], v[70:71], s[100:101] op_sel_hi:[1,0]
	v_exp_f32_e32 v10, v10
	v_exp_f32_e32 v11, v11
	v_exp_f32_e32 v12, v12
	v_exp_f32_e32 v13, v13
	v_exp_f32_e32 v14, v14
	v_exp_f32_e32 v15, v15
	v_exp_f32_e32 v16, v16
	v_exp_f32_e32 v17, v17
	v_pk_fma_f32 v[10:11], v[10:11], s[98:99], s[98:99] op_sel_hi:[1,0,0]
	v_pk_fma_f32 v[12:13], v[12:13], s[98:99], s[98:99] op_sel_hi:[1,0,0]
	v_pk_fma_f32 v[14:15], v[14:15], s[98:99], s[98:99] op_sel_hi:[1,0,0]
	v_pk_fma_f32 v[16:17], v[16:17], s[98:99], s[98:99] op_sel_hi:[1,0,0]
	v_rcp_f32_e32 v10, v10
	v_rcp_f32_e32 v11, v11
	v_rcp_f32_e32 v12, v12
	v_rcp_f32_e32 v13, v13
	v_rcp_f32_e32 v14, v14
	v_rcp_f32_e32 v15, v15
	v_rcp_f32_e32 v16, v16
	v_rcp_f32_e32 v17, v17
	v_pk_mul_f32 v[10:11], v[76:77], v[10:11]
	v_pk_mul_f32 v[12:13], v[78:79], v[12:13]
	v_pk_mul_f32 v[14:15], v[68:69], v[14:15]
	v_pk_mul_f32 v[16:17], v[70:71], v[16:17]
	v_pk_mul_f32 v[10:11], v[10:11], v[72:73]
	v_pk_mul_f32 v[12:13], v[12:13], v[74:75]
	v_pk_mul_f32 v[14:15], v[14:15], v[64:65]
	v_pk_mul_f32 v[16:17], v[16:17], v[66:67]
	v_cvt_pk_fp8_f32 v18, v10, v11
	v_cvt_pk_fp8_f32 v19, v14, v15
	v_cvt_pk_fp8_f32 v18, v12, v13 op_sel:[0,0,1]
	v_cvt_pk_fp8_f32 v19, v16, v17 op_sel:[0,0,1]
	s_nop 0
	global_store_dwordx2 v[0:1], v[18:19], off
	s_cbranch_vccnz .LBB0_3917

.LBB0_3914:
	s_add_i32 s22, s20, 0xf2401100
	s_and_b32 s55, s22, 0x300
	s_add_u32 s24, s2, s55
	s_addc_u32 s25, s3, 0
	s_and_b64 s[22:23], s[26:27], exec
	s_cselect_b32 s23, s17, s25
	s_cselect_b32 s22, s53, s24
	s_mov_b64 s[24:25], s[22:23]
	s_mov_b32 m0, s34
	ds_read_b128 v[16:19], v217
	ds_read_b128 v[20:23], v218
	ds_read_b128 v[24:27], v225
	ds_read_b128 v[28:31], v226
	v_mov_b32_e32 v203, v197
	global_load_lds_dwordx4 v194, s[24:25]
	v_lshl_add_u64 v[236:237], s[24:25], 0, v[192:193]
	s_mov_b32 m0, s35
	s_add_u32 s24, s22, 0x80
	global_load_lds_dwordx4 v[236:237], off
	s_nop 0
	s_barrier
	s_waitcnt lgkmcnt(0)
	s_addc_u32 s25, s23, 0
	s_and_b64 s[26:27], s[26:27], exec
	s_cselect_b32 s27, 0, 0
	s_cselect_b32 s26, 0, s55
	s_setprio 1
	s_waitcnt lgkmcnt(0)
	v_mfma_scale_f32_16x16x128_f8f6f4 v[184:187], v[16:23], v[56:63], v[184:187], v212, v212 op_sel_hi:[0,0,0]
	v_mfma_scale_f32_16x16x128_f8f6f4 v[176:179], v[24:31], v[56:63], v[176:179], v212, v212 op_sel_hi:[0,0,0]
	v_mfma_scale_f32_16x16x128_f8f6f4 v[168:171], v[16:23], v[48:55], v[168:171], v212, v212 op_sel_hi:[0,0,0]
	v_mfma_scale_f32_16x16x128_f8f6f4 v[160:163], v[24:31], v[48:55], v[160:163], v212, v212 op_sel_hi:[0,0,0]
	v_mfma_scale_f32_16x16x128_f8f6f4 v[152:155], v[16:23], v[40:47], v[152:155], v212, v212 op_sel_hi:[0,0,0]
	v_mfma_scale_f32_16x16x128_f8f6f4 v[144:147], v[24:31], v[40:47], v[144:147], v212, v212 op_sel_hi:[0,0,0]
	v_mfma_scale_f32_16x16x128_f8f6f4 v[136:139], v[16:23], v[32:39], v[136:139], v212, v212 op_sel_hi:[0,0,0]
	v_mfma_scale_f32_16x16x128_f8f6f4 v[128:131], v[24:31], v[32:39], v[128:131], v212, v212 op_sel_hi:[0,0,0]
	s_setprio 0
	s_add_u32 s26, s10, s26
	s_addc_u32 s27, s11, s27
	s_mov_b64 s[56:57], s[26:27]
	s_mov_b32 m0, s1
	s_barrier
	ds_read_b128 v[32:35], v231 offset:16384
	ds_read_b128 v[40:43], v231 offset:18432
	ds_read_b128 v[36:39], v232 offset:16384
	ds_read_b128 v[44:47], v232 offset:18432
	ds_read_b128 v[48:51], v231 offset:20480
	ds_read_b128 v[56:59], v231 offset:22528
	ds_read_b128 v[52:55], v232 offset:20480
	ds_read_b128 v[60:63], v232 offset:22528
	s_nop 0
	global_load_lds_dwordx4 v198, s[56:57]
	s_mov_b32 m0, s36
	s_nop 0
	global_load_lds_dwordx4 v200, s[56:57]
	s_nop 0
	s_barrier
	s_waitcnt lgkmcnt(0)
	s_setprio 1
	s_waitcnt lgkmcnt(0)
	v_mfma_scale_f32_16x16x128_f8f6f4 v[124:127], v[0:7], v[32:39], v[124:127], v212, v212 op_sel_hi:[0,0,0]
	v_mfma_scale_f32_16x16x128_f8f6f4 v[116:119], v[8:15], v[32:39], v[116:119], v212, v212 op_sel_hi:[0,0,0]
	v_mfma_scale_f32_16x16x128_f8f6f4 v[108:111], v[0:7], v[40:47], v[108:111], v212, v212 op_sel_hi:[0,0,0]
	v_mfma_scale_f32_16x16x128_f8f6f4 v[100:103], v[8:15], v[40:47], v[100:103], v212, v212 op_sel_hi:[0,0,0]
	v_mfma_scale_f32_16x16x128_f8f6f4 v[92:95], v[0:7], v[48:55], v[92:95], v212, v212 op_sel_hi:[0,0,0]
	v_mfma_scale_f32_16x16x128_f8f6f4 v[84:87], v[8:15], v[48:55], v[84:87], v212, v212 op_sel_hi:[0,0,0]
	v_mfma_scale_f32_16x16x128_f8f6f4 v[76:79], v[0:7], v[56:63], v[76:79], v212, v212 op_sel_hi:[0,0,0]
	v_mfma_scale_f32_16x16x128_f8f6f4 v[68:71], v[8:15], v[56:63], v[68:71], v212, v212 op_sel_hi:[0,0,0]
	s_setprio 0
	s_barrier
	s_add_u32 s56, s22, 0x20000
	s_addc_u32 s57, s23, 0
	s_mov_b32 m0, s37
	s_nop 0
	global_load_lds_dwordx4 v194, s[56:57]
	s_mov_b32 m0, s38
	s_nop 0
	global_load_lds_dwordx4 v192, s[56:57]
	s_waitcnt vmcnt(6)
	s_barrier
	s_setprio 1
	v_mfma_scale_f32_16x16x128_f8f6f4 v[120:123], v[16:23], v[32:39], v[120:123], v212, v212 op_sel_hi:[0,0,0]
	v_mfma_scale_f32_16x16x128_f8f6f4 v[112:115], v[24:31], v[32:39], v[112:115], v212, v212 op_sel_hi:[0,0,0]
	v_mfma_scale_f32_16x16x128_f8f6f4 v[104:107], v[16:23], v[40:47], v[104:107], v212, v212 op_sel_hi:[0,0,0]
	v_mfma_scale_f32_16x16x128_f8f6f4 v[96:99], v[24:31], v[40:47], v[96:99], v212, v212 op_sel_hi:[0,0,0]
	v_mfma_scale_f32_16x16x128_f8f6f4 v[88:91], v[16:23], v[48:55], v[88:91], v212, v212 op_sel_hi:[0,0,0]
	v_mfma_scale_f32_16x16x128_f8f6f4 v[80:83], v[24:31], v[48:55], v[80:83], v212, v212 op_sel_hi:[0,0,0]
	v_mfma_scale_f32_16x16x128_f8f6f4 v[72:75], v[16:23], v[56:63], v[72:75], v212, v212 op_sel_hi:[0,0,0]
	v_mfma_scale_f32_16x16x128_f8f6f4 v[64:67], v[24:31], v[56:63], v[64:67], v212, v212 op_sel_hi:[0,0,0]
	s_setprio 0
	s_barrier
	ds_read_b128 v[0:3], v219
	ds_read_b128 v[4:7], v220
	ds_read_b128 v[8:11], v227
	ds_read_b128 v[12:15], v228
	s_mov_b64 s[56:57], s[26:27]
	s_mov_b32 m0, s39
	ds_read_b128 v[16:19], v231 offset:32768
	ds_read_b128 v[24:27], v231 offset:34816
	ds_read_b128 v[20:23], v232 offset:32768
	ds_read_b128 v[28:31], v232 offset:34816
	ds_read_b128 v[32:35], v231 offset:36864
	ds_read_b128 v[40:43], v231 offset:38912
	ds_read_b128 v[36:39], v232 offset:36864
	ds_read_b128 v[44:47], v232 offset:38912
	s_nop 0
	global_load_lds_dwordx4 v196, s[56:57]
	s_mov_b32 m0, s40
	s_nop 0
	global_load_lds_dwordx4 v202, s[56:57]
	s_waitcnt lgkmcnt(8)
	s_barrier
	s_waitcnt lgkmcnt(0)
	s_setprio 1
	s_waitcnt lgkmcnt(0)
	v_mfma_scale_f32_16x16x128_f8f6f4 v[188:191], v[0:7], v[16:23], v[188:191], v212, v212 op_sel_hi:[0,0,0]
	v_mfma_scale_f32_16x16x128_f8f6f4 v[180:183], v[8:15], v[16:23], v[180:183], v212, v212 op_sel_hi:[0,0,0]
	v_mfma_scale_f32_16x16x128_f8f6f4 v[172:175], v[0:7], v[24:31], v[172:175], v212, v212 op_sel_hi:[0,0,0]
	v_mfma_scale_f32_16x16x128_f8f6f4 v[164:167], v[8:15], v[24:31], v[164:167], v212, v212 op_sel_hi:[0,0,0]
	v_mfma_scale_f32_16x16x128_f8f6f4 v[156:159], v[0:7], v[32:39], v[156:159], v212, v212 op_sel_hi:[0,0,0]
	v_mfma_scale_f32_16x16x128_f8f6f4 v[148:151], v[8:15], v[32:39], v[148:151], v212, v212 op_sel_hi:[0,0,0]
	v_mfma_scale_f32_16x16x128_f8f6f4 v[140:143], v[0:7], v[40:47], v[140:143], v212, v212 op_sel_hi:[0,0,0]
	v_mfma_scale_f32_16x16x128_f8f6f4 v[132:135], v[8:15], v[40:47], v[132:135], v212, v212 op_sel_hi:[0,0,0]
	s_setprio 0
	s_barrier
	s_mov_b32 m0, s42
	ds_read_b128 v[48:51], v221
	ds_read_b128 v[52:55], v222
	ds_read_b128 v[56:59], v229
	ds_read_b128 v[60:63], v230
	s_nop 0
	global_load_lds_dwordx4 v194, s[24:25]
	s_mov_b32 m0, s43
	s_nop 0
	global_load_lds_dwordx4 v192, s[24:25]
	s_barrier
	s_waitcnt lgkmcnt(0)
	s_setprio 1
	s_waitcnt lgkmcnt(0)
	v_mfma_scale_f32_16x16x128_f8f6f4 v[184:187], v[48:55], v[16:23], v[184:187], v212, v212 op_sel_hi:[0,0,0]
	v_mfma_scale_f32_16x16x128_f8f6f4 v[176:179], v[56:63], v[16:23], v[176:179], v212, v212 op_sel_hi:[0,0,0]
	v_mfma_scale_f32_16x16x128_f8f6f4 v[168:171], v[48:55], v[24:31], v[168:171], v212, v212 op_sel_hi:[0,0,0]
	v_mfma_scale_f32_16x16x128_f8f6f4 v[160:163], v[56:63], v[24:31], v[160:163], v212, v212 op_sel_hi:[0,0,0]
	v_mfma_scale_f32_16x16x128_f8f6f4 v[152:155], v[48:55], v[32:39], v[152:155], v212, v212 op_sel_hi:[0,0,0]
	v_mfma_scale_f32_16x16x128_f8f6f4 v[144:147], v[56:63], v[32:39], v[144:147], v212, v212 op_sel_hi:[0,0,0]
	v_mfma_scale_f32_16x16x128_f8f6f4 v[136:139], v[48:55], v[40:47], v[136:139], v212, v212 op_sel_hi:[0,0,0]
	v_mfma_scale_f32_16x16x128_f8f6f4 v[128:131], v[56:63], v[40:47], v[128:131], v212, v212 op_sel_hi:[0,0,0]
	s_setprio 0
	s_add_u32 s24, s26, 0x80
	s_addc_u32 s25, s27, 0
	s_mov_b32 m0, s44
	s_barrier
	ds_read_b128 v[16:19], v231 offset:49152
	ds_read_b128 v[24:27], v231 offset:51200
	ds_read_b128 v[20:23], v232 offset:49152
	ds_read_b128 v[28:31], v232 offset:51200
	ds_read_b128 v[32:35], v231 offset:53248
	ds_read_b128 v[40:43], v231 offset:55296
	ds_read_b128 v[36:39], v232 offset:53248
	ds_read_b128 v[44:47], v232 offset:55296
	s_nop 0
	global_load_lds_dwordx4 v198, s[24:25]
	s_mov_b32 m0, s45
	s_nop 0
	global_load_lds_dwordx4 v200, s[24:25]
	s_nop 0
	s_barrier
	s_waitcnt lgkmcnt(0)
	s_setprio 1
	s_waitcnt lgkmcnt(0)
	v_mfma_scale_f32_16x16x128_f8f6f4 v[124:127], v[0:7], v[16:23], v[124:127], v212, v212 op_sel_hi:[0,0,0]
	v_mfma_scale_f32_16x16x128_f8f6f4 v[116:119], v[8:15], v[16:23], v[116:119], v212, v212 op_sel_hi:[0,0,0]
	v_mfma_scale_f32_16x16x128_f8f6f4 v[108:111], v[0:7], v[24:31], v[108:111], v212, v212 op_sel_hi:[0,0,0]
	v_mfma_scale_f32_16x16x128_f8f6f4 v[100:103], v[8:15], v[24:31], v[100:103], v212, v212 op_sel_hi:[0,0,0]
	v_mfma_scale_f32_16x16x128_f8f6f4 v[92:95], v[0:7], v[32:39], v[92:95], v212, v212 op_sel_hi:[0,0,0]
	v_mfma_scale_f32_16x16x128_f8f6f4 v[84:87], v[8:15], v[32:39], v[84:87], v212, v212 op_sel_hi:[0,0,0]
	v_mfma_scale_f32_16x16x128_f8f6f4 v[76:79], v[0:7], v[40:47], v[76:79], v212, v212 op_sel_hi:[0,0,0]
	v_mfma_scale_f32_16x16x128_f8f6f4 v[68:71], v[8:15], v[40:47], v[68:71], v212, v212 op_sel_hi:[0,0,0]
	s_setprio 0
	s_barrier
	s_add_u32 s22, s22, 0x20080
	s_addc_u32 s23, s23, 0
	s_mov_b32 m0, s46
	s_nop 0
	global_load_lds_dwordx4 v194, s[22:23]
	s_mov_b32 m0, s47
	s_nop 0
	global_load_lds_dwordx4 v192, s[22:23]
	s_waitcnt vmcnt(6)
	s_barrier
	s_setprio 1
	v_mfma_scale_f32_16x16x128_f8f6f4 v[120:123], v[48:55], v[16:23], v[120:123], v212, v212 op_sel_hi:[0,0,0]
	v_mfma_scale_f32_16x16x128_f8f6f4 v[112:115], v[56:63], v[16:23], v[112:115], v212, v212 op_sel_hi:[0,0,0]
	v_mfma_scale_f32_16x16x128_f8f6f4 v[104:107], v[48:55], v[24:31], v[104:107], v212, v212 op_sel_hi:[0,0,0]
	v_mfma_scale_f32_16x16x128_f8f6f4 v[96:99], v[56:63], v[24:31], v[96:99], v212, v212 op_sel_hi:[0,0,0]
	v_mfma_scale_f32_16x16x128_f8f6f4 v[88:91], v[48:55], v[32:39], v[88:91], v212, v212 op_sel_hi:[0,0,0]
	v_mfma_scale_f32_16x16x128_f8f6f4 v[80:83], v[56:63], v[32:39], v[80:83], v212, v212 op_sel_hi:[0,0,0]
	v_mfma_scale_f32_16x16x128_f8f6f4 v[72:75], v[48:55], v[40:47], v[72:75], v212, v212 op_sel_hi:[0,0,0]
	v_mfma_scale_f32_16x16x128_f8f6f4 v[64:67], v[56:63], v[40:47], v[64:67], v212, v212 op_sel_hi:[0,0,0]
	s_setprio 0
	s_add_i32 s54, s54, 2
	s_add_u32 s20, s20, 0x100
	s_addc_u32 s21, s21, 0
	s_cmp_gt_u32 s54, 5
	s_barrier
	s_cbranch_scc1 .LBB0_3910

.LBB0_3979:
	s_add_u32 s34, s38, 0x100
	ds_read_b128 v[0:3], v174
	ds_read_b128 v[4:7], v175
	ds_read_b128 v[8:11], v182
	ds_read_b128 v[12:15], v183
	s_addc_u32 s35, s39, 0
	s_and_b32 s69, s34, 0x300
	s_add_u32 s68, s28, s69
	s_addc_u32 s70, s29, 0
	s_cmp_eq_u32 s33, 4
	s_cselect_b64 s[40:41], -1, 0
	s_and_b64 s[36:37], s[40:41], exec
	s_cselect_b32 s37, s21, s70
	s_cselect_b32 s36, s23, s68
	s_cselect_b32 s68, 0, 0
	s_cselect_b32 s69, 0, s69
	s_add_u32 s38, s30, s38
	s_addc_u32 s39, s31, s39
	s_add_u32 s38, s38, 0x20080
	s_addc_u32 s39, s39, 0
	ds_read_b128 v[194:197], v190
	ds_read_b128 v[210:213], v190 offset:2048
	ds_read_b128 v[198:201], v191
	ds_read_b128 v[214:217], v191 offset:2048
	ds_read_b128 v[218:221], v190 offset:4096
	ds_read_b128 v[226:229], v190 offset:6144
	ds_read_b128 v[222:225], v191 offset:4096
	ds_read_b128 v[230:233], v191 offset:6144
	s_add_i32 m0, s1, 0xc000
	s_nop 0
	global_load_lds_dwordx4 v166, s[38:39]
	s_add_i32 m0, s1, 0xe000
	s_nop 0
	global_load_lds_dwordx4 v162, s[38:39]
	s_waitcnt lgkmcnt(8)
	s_nop 0
	s_barrier
	s_waitcnt lgkmcnt(0)
	s_setprio 1
	s_waitcnt lgkmcnt(0)
	v_mfma_scale_f32_16x16x128_f8f6f4 v[156:159], v[0:7], v[194:201], v[156:159], v173, v173 op_sel_hi:[0,0,0]
	v_mfma_scale_f32_16x16x128_f8f6f4 v[152:155], v[8:15], v[194:201], v[152:155], v173, v173 op_sel_hi:[0,0,0]
	v_mfma_scale_f32_16x16x128_f8f6f4 v[140:143], v[0:7], v[210:217], v[140:143], v173, v173 op_sel_hi:[0,0,0]
	v_mfma_scale_f32_16x16x128_f8f6f4 v[136:139], v[8:15], v[210:217], v[136:139], v173, v173 op_sel_hi:[0,0,0]
	v_mfma_scale_f32_16x16x128_f8f6f4 v[124:127], v[0:7], v[218:225], v[124:127], v173, v173 op_sel_hi:[0,0,0]
	v_mfma_scale_f32_16x16x128_f8f6f4 v[120:123], v[8:15], v[218:225], v[120:123], v173, v173 op_sel_hi:[0,0,0]
	v_mfma_scale_f32_16x16x128_f8f6f4 v[108:111], v[0:7], v[226:233], v[108:111], v173, v173 op_sel_hi:[0,0,0]
	v_mfma_scale_f32_16x16x128_f8f6f4 v[104:107], v[8:15], v[226:233], v[104:107], v173, v173 op_sel_hi:[0,0,0]
	s_setprio 0
	s_barrier
	s_mov_b64 s[38:39], s[36:37]
	s_mov_b32 m0, s3
	ds_read_b128 v[16:19], v176
	ds_read_b128 v[20:23], v177
	ds_read_b128 v[24:27], v184
	ds_read_b128 v[28:31], v185
	s_nop 0
	global_load_lds_dwordx4 v164, s[38:39]
	s_mov_b32 m0, s49
	s_nop 0
	global_load_lds_dwordx4 v160, s[38:39]
	s_nop 0
	s_barrier
	s_waitcnt lgkmcnt(0)
	s_setprio 1
	s_waitcnt lgkmcnt(0)
	v_mfma_scale_f32_16x16x128_f8f6f4 v[148:151], v[16:23], v[194:201], v[148:151], v173, v173 op_sel_hi:[0,0,0]
	v_mfma_scale_f32_16x16x128_f8f6f4 v[144:147], v[24:31], v[194:201], v[144:147], v173, v173 op_sel_hi:[0,0,0]
	v_mfma_scale_f32_16x16x128_f8f6f4 v[132:135], v[16:23], v[210:217], v[132:135], v173, v173 op_sel_hi:[0,0,0]
	v_mfma_scale_f32_16x16x128_f8f6f4 v[128:131], v[24:31], v[210:217], v[128:131], v173, v173 op_sel_hi:[0,0,0]
	v_mfma_scale_f32_16x16x128_f8f6f4 v[116:119], v[16:23], v[218:225], v[116:119], v173, v173 op_sel_hi:[0,0,0]
	v_mfma_scale_f32_16x16x128_f8f6f4 v[112:115], v[24:31], v[218:225], v[112:115], v173, v173 op_sel_hi:[0,0,0]
	v_mfma_scale_f32_16x16x128_f8f6f4 v[100:103], v[16:23], v[226:233], v[100:103], v173, v173 op_sel_hi:[0,0,0]
	v_mfma_scale_f32_16x16x128_f8f6f4 v[96:99], v[24:31], v[226:233], v[96:99], v173, v173 op_sel_hi:[0,0,0]
	s_setprio 0
	s_and_b64 s[38:39], s[6:7], s[40:41]
	s_and_b64 s[38:39], s[38:39], exec
	s_cselect_b32 s38, s24, s30
	s_cselect_b32 s39, s25, s31
	s_add_u32 s38, s38, s69
	s_addc_u32 s39, s39, s68
	s_mov_b64 s[40:41], s[38:39]
	s_mov_b32 m0, s1
	s_barrier
	ds_read_b128 v[194:197], v190 offset:16384
	ds_read_b128 v[210:213], v190 offset:18432
	ds_read_b128 v[198:201], v191 offset:16384
	ds_read_b128 v[214:217], v191 offset:18432
	ds_read_b128 v[218:221], v190 offset:20480
	ds_read_b128 v[226:229], v190 offset:22528
	ds_read_b128 v[222:225], v191 offset:20480
	ds_read_b128 v[230:233], v191 offset:22528
	s_nop 0
	global_load_lds_dwordx4 v166, s[40:41]
	s_mov_b32 m0, s50
	s_nop 0
	global_load_lds_dwordx4 v162, s[40:41]
	s_nop 0
	s_barrier
	s_waitcnt lgkmcnt(0)
	s_setprio 1
	s_waitcnt lgkmcnt(0)
	v_mfma_scale_f32_16x16x128_f8f6f4 v[92:95], v[0:7], v[194:201], v[92:95], v173, v173 op_sel_hi:[0,0,0]
	v_mfma_scale_f32_16x16x128_f8f6f4 v[88:91], v[8:15], v[194:201], v[88:91], v173, v173 op_sel_hi:[0,0,0]
	v_mfma_scale_f32_16x16x128_f8f6f4 v[76:79], v[0:7], v[210:217], v[76:79], v173, v173 op_sel_hi:[0,0,0]
	v_mfma_scale_f32_16x16x128_f8f6f4 v[72:75], v[8:15], v[210:217], v[72:75], v173, v173 op_sel_hi:[0,0,0]
	v_mfma_scale_f32_16x16x128_f8f6f4 v[60:63], v[0:7], v[218:225], v[60:63], v173, v173 op_sel_hi:[0,0,0]
	v_mfma_scale_f32_16x16x128_f8f6f4 v[56:59], v[8:15], v[218:225], v[56:59], v173, v173 op_sel_hi:[0,0,0]
	v_mfma_scale_f32_16x16x128_f8f6f4 v[44:47], v[0:7], v[226:233], v[44:47], v173, v173 op_sel_hi:[0,0,0]
	v_mfma_scale_f32_16x16x128_f8f6f4 v[40:43], v[8:15], v[226:233], v[40:43], v173, v173 op_sel_hi:[0,0,0]
	s_setprio 0
	s_barrier
	s_add_u32 s40, s36, 0x20000
	s_addc_u32 s41, s37, 0
	s_mov_b32 m0, s51
	s_nop 0
	global_load_lds_dwordx4 v164, s[40:41]
	s_mov_b32 m0, s52
	s_nop 0
	global_load_lds_dwordx4 v160, s[40:41]
	s_waitcnt vmcnt(6)
	s_barrier
	s_setprio 1
	v_mfma_scale_f32_16x16x128_f8f6f4 v[84:87], v[16:23], v[194:201], v[84:87], v173, v173 op_sel_hi:[0,0,0]
	v_mfma_scale_f32_16x16x128_f8f6f4 v[80:83], v[24:31], v[194:201], v[80:83], v173, v173 op_sel_hi:[0,0,0]
	v_mfma_scale_f32_16x16x128_f8f6f4 v[68:71], v[16:23], v[210:217], v[68:71], v173, v173 op_sel_hi:[0,0,0]
	v_mfma_scale_f32_16x16x128_f8f6f4 v[64:67], v[24:31], v[210:217], v[64:67], v173, v173 op_sel_hi:[0,0,0]
	v_mfma_scale_f32_16x16x128_f8f6f4 v[52:55], v[16:23], v[218:225], v[52:55], v173, v173 op_sel_hi:[0,0,0]
	v_mfma_scale_f32_16x16x128_f8f6f4 v[48:51], v[24:31], v[218:225], v[48:51], v173, v173 op_sel_hi:[0,0,0]
	v_mfma_scale_f32_16x16x128_f8f6f4 v[36:39], v[16:23], v[226:233], v[36:39], v173, v173 op_sel_hi:[0,0,0]
	v_mfma_scale_f32_16x16x128_f8f6f4 v[32:35], v[24:31], v[226:233], v[32:35], v173, v173 op_sel_hi:[0,0,0]
	s_setprio 0
	s_barrier
	ds_read_b128 v[0:3], v178
	ds_read_b128 v[4:7], v179
	ds_read_b128 v[8:11], v186
	ds_read_b128 v[12:15], v187
	s_add_u32 s40, s38, 0x20000
	s_addc_u32 s41, s39, 0
	s_mov_b32 m0, s53
	ds_read_b128 v[16:19], v190 offset:32768
	ds_read_b128 v[24:27], v190 offset:34816
	ds_read_b128 v[20:23], v191 offset:32768
	ds_read_b128 v[28:31], v191 offset:34816
	ds_read_b128 v[194:197], v190 offset:36864
	ds_read_b128 v[210:213], v190 offset:38912
	ds_read_b128 v[198:201], v191 offset:36864
	ds_read_b128 v[214:217], v191 offset:38912
	s_nop 0
	global_load_lds_dwordx4 v166, s[40:41]
	s_mov_b32 m0, s54
	s_nop 0
	global_load_lds_dwordx4 v162, s[40:41]
	s_waitcnt lgkmcnt(8)
	s_barrier
	s_waitcnt lgkmcnt(0)
	s_setprio 1
	s_waitcnt lgkmcnt(0)
	v_mfma_scale_f32_16x16x128_f8f6f4 v[156:159], v[0:7], v[16:23], v[156:159], v173, v173 op_sel_hi:[0,0,0]
	v_mfma_scale_f32_16x16x128_f8f6f4 v[152:155], v[8:15], v[16:23], v[152:155], v173, v173 op_sel_hi:[0,0,0]
	v_mfma_scale_f32_16x16x128_f8f6f4 v[140:143], v[0:7], v[24:31], v[140:143], v173, v173 op_sel_hi:[0,0,0]
	v_mfma_scale_f32_16x16x128_f8f6f4 v[136:139], v[8:15], v[24:31], v[136:139], v173, v173 op_sel_hi:[0,0,0]
	v_mfma_scale_f32_16x16x128_f8f6f4 v[124:127], v[0:7], v[194:201], v[124:127], v173, v173 op_sel_hi:[0,0,0]
	v_mfma_scale_f32_16x16x128_f8f6f4 v[120:123], v[8:15], v[194:201], v[120:123], v173, v173 op_sel_hi:[0,0,0]
	v_mfma_scale_f32_16x16x128_f8f6f4 v[108:111], v[0:7], v[210:217], v[108:111], v173, v173 op_sel_hi:[0,0,0]
	v_mfma_scale_f32_16x16x128_f8f6f4 v[104:107], v[8:15], v[210:217], v[104:107], v173, v173 op_sel_hi:[0,0,0]
	s_setprio 0
	s_barrier
	s_add_u32 s40, s36, 0x80
	s_addc_u32 s41, s37, 0
	s_mov_b32 m0, s56
	ds_read_b128 v[218:221], v180
	ds_read_b128 v[222:225], v181
	ds_read_b128 v[226:229], v188
	ds_read_b128 v[230:233], v189
	s_nop 0
	global_load_lds_dwordx4 v164, s[40:41]
	s_mov_b32 m0, s57
	s_nop 0
	global_load_lds_dwordx4 v160, s[40:41]
	s_nop 0
	s_barrier
	s_waitcnt lgkmcnt(0)
	s_setprio 1
	s_waitcnt lgkmcnt(0)
	v_mfma_scale_f32_16x16x128_f8f6f4 v[148:151], v[218:225], v[16:23], v[148:151], v173, v173 op_sel_hi:[0,0,0]
	v_mfma_scale_f32_16x16x128_f8f6f4 v[144:147], v[226:233], v[16:23], v[144:147], v173, v173 op_sel_hi:[0,0,0]
	v_mfma_scale_f32_16x16x128_f8f6f4 v[132:135], v[218:225], v[24:31], v[132:135], v173, v173 op_sel_hi:[0,0,0]
	v_mfma_scale_f32_16x16x128_f8f6f4 v[128:131], v[226:233], v[24:31], v[128:131], v173, v173 op_sel_hi:[0,0,0]
	v_mfma_scale_f32_16x16x128_f8f6f4 v[116:119], v[218:225], v[194:201], v[116:119], v173, v173 op_sel_hi:[0,0,0]
	v_mfma_scale_f32_16x16x128_f8f6f4 v[112:115], v[226:233], v[194:201], v[112:115], v173, v173 op_sel_hi:[0,0,0]
	v_mfma_scale_f32_16x16x128_f8f6f4 v[100:103], v[218:225], v[210:217], v[100:103], v173, v173 op_sel_hi:[0,0,0]
	v_mfma_scale_f32_16x16x128_f8f6f4 v[96:99], v[226:233], v[210:217], v[96:99], v173, v173 op_sel_hi:[0,0,0]
	s_setprio 0
	s_add_u32 s38, s38, 0x80
	s_addc_u32 s39, s39, 0
	s_mov_b32 m0, s58
	s_barrier
	ds_read_b128 v[16:19], v190 offset:49152
	ds_read_b128 v[24:27], v190 offset:51200
	ds_read_b128 v[20:23], v191 offset:49152
	ds_read_b128 v[28:31], v191 offset:51200
	ds_read_b128 v[194:197], v190 offset:53248
	ds_read_b128 v[210:213], v190 offset:55296
	ds_read_b128 v[198:201], v191 offset:53248
	ds_read_b128 v[214:217], v191 offset:55296
	s_nop 0
	global_load_lds_dwordx4 v166, s[38:39]
	s_mov_b32 m0, s59
	s_nop 0
	global_load_lds_dwordx4 v162, s[38:39]
	s_nop 0
	s_barrier
	s_waitcnt lgkmcnt(0)
	s_setprio 1
	s_waitcnt lgkmcnt(0)
	v_mfma_scale_f32_16x16x128_f8f6f4 v[92:95], v[0:7], v[16:23], v[92:95], v173, v173 op_sel_hi:[0,0,0]
	v_mfma_scale_f32_16x16x128_f8f6f4 v[88:91], v[8:15], v[16:23], v[88:91], v173, v173 op_sel_hi:[0,0,0]
	v_mfma_scale_f32_16x16x128_f8f6f4 v[76:79], v[0:7], v[24:31], v[76:79], v173, v173 op_sel_hi:[0,0,0]
	v_mfma_scale_f32_16x16x128_f8f6f4 v[72:75], v[8:15], v[24:31], v[72:75], v173, v173 op_sel_hi:[0,0,0]
	v_mfma_scale_f32_16x16x128_f8f6f4 v[60:63], v[0:7], v[194:201], v[60:63], v173, v173 op_sel_hi:[0,0,0]
	v_mfma_scale_f32_16x16x128_f8f6f4 v[56:59], v[8:15], v[194:201], v[56:59], v173, v173 op_sel_hi:[0,0,0]
	v_mfma_scale_f32_16x16x128_f8f6f4 v[44:47], v[0:7], v[210:217], v[44:47], v173, v173 op_sel_hi:[0,0,0]
	v_mfma_scale_f32_16x16x128_f8f6f4 v[40:43], v[8:15], v[210:217], v[40:43], v173, v173 op_sel_hi:[0,0,0]
	s_setprio 0
	s_barrier
	s_add_u32 s36, s36, 0x20080
	s_addc_u32 s37, s37, 0
	s_mov_b32 m0, s60
	s_nop 0
	global_load_lds_dwordx4 v164, s[36:37]
	s_mov_b32 m0, s61
	s_nop 0
	global_load_lds_dwordx4 v160, s[36:37]
	s_waitcnt vmcnt(6)
	s_barrier
	s_setprio 1
	v_mfma_scale_f32_16x16x128_f8f6f4 v[84:87], v[218:225], v[16:23], v[84:87], v173, v173 op_sel_hi:[0,0,0]
	v_mfma_scale_f32_16x16x128_f8f6f4 v[80:83], v[226:233], v[16:23], v[80:83], v173, v173 op_sel_hi:[0,0,0]
	v_mfma_scale_f32_16x16x128_f8f6f4 v[68:71], v[218:225], v[24:31], v[68:71], v173, v173 op_sel_hi:[0,0,0]
	v_mfma_scale_f32_16x16x128_f8f6f4 v[64:67], v[226:233], v[24:31], v[64:67], v173, v173 op_sel_hi:[0,0,0]
	v_mfma_scale_f32_16x16x128_f8f6f4 v[52:55], v[218:225], v[194:201], v[52:55], v173, v173 op_sel_hi:[0,0,0]
	v_mfma_scale_f32_16x16x128_f8f6f4 v[48:51], v[226:233], v[194:201], v[48:51], v173, v173 op_sel_hi:[0,0,0]
	v_mfma_scale_f32_16x16x128_f8f6f4 v[36:39], v[218:225], v[210:217], v[36:39], v173, v173 op_sel_hi:[0,0,0]
	v_mfma_scale_f32_16x16x128_f8f6f4 v[32:35], v[226:233], v[210:217], v[32:35], v173, v173 op_sel_hi:[0,0,0]
	s_setprio 0
	s_add_i32 s33, s33, 2
	s_cmp_gt_u32 s33, 5
	s_mov_b64 s[38:39], s[34:35]
	s_barrier
	s_cbranch_scc0 .LBB0_3979
	v_mov_b32_e32 v2, v172
	v_mov_b32_e32 v8, 0
	v_ashrrev_i32_e32 v0, 2, v2
	v_and_b32_e32 v0, 0xffffffc0, v0
	v_lshl_add_u32 v0, s2, 8, v0
	v_and_or_b32 v6, v2, 15, v0
	v_ashrrev_i32_e32 v7, 31, v6
	v_lshl_add_u64 v[0:1], v[6:7], 2, s[10:11]
	global_load_dword v14, v[0:1], off
	global_load_dword v194, v[0:1], off offset:64
	global_load_dword v195, v[0:1], off offset:128
	global_load_dword v196, v[0:1], off offset:192
	global_load_dword v197, v[0:1], off offset:512
	global_load_dword v198, v[0:1], off offset:576
	global_load_dword v199, v[0:1], off offset:640
	global_load_dword v200, v[0:1], off offset:704
	s_ashr_i32 s2, s0, 31
	s_lshr_b32 s2, s2, 30
	s_add_i32 s2, s0, s2
	v_lshrrev_b32_e32 v2, 1, v2
	s_and_b32 s2, s2, 0xfffffc
	v_and_b32_e32 v2, 0x78, v2
	s_sub_i32 s0, s0, s2
	v_lshl_or_b32 v4, s0, 8, v2
	v_lshlrev_b64 v[2:3], 10, v[6:7]
	v_mov_b32_e32 v9, 0
	v_mov_b32_e32 v10, 0
	v_mov_b32_e32 v11, 0
	v_ashrrev_i32_e32 v5, 31, v4
	v_or_b32_e32 v12, 16, v6
	v_lshl_add_u64 v[2:3], s[12:13], 0, v[2:3]
	v_ashrrev_i32_e32 v13, 31, v12
	v_lshl_add_u64 v[2:3], v[2:3], 0, v[4:5]
	s_mov_b64 s[28:29], s[26:27]
	s_mov_b64 s[30:31], s[24:25]
	s_mov_b32 s0, s22
	s_mov_b32 s2, s20
	s_waitcnt vmcnt(0)
	v_mul_f32_e32 v7, 0x3d000000, v14
	v_mul_f32_e32 v14, 0x42000000, v7
	v_pk_mul_f32 v[18:19], v[156:157], v[14:15] op_sel_hi:[1,0]
	v_pk_mul_f32 v[22:23], v[152:153], v[14:15] op_sel_hi:[1,0]
	v_pk_mul_f32 v[16:17], v[158:159], v[14:15] op_sel_hi:[1,0]
	v_pk_mul_f32 v[20:21], v[154:155], v[14:15] op_sel_hi:[1,0]
	v_pk_mul_f32 v[24:25], v[150:151], v[14:15] op_sel_hi:[1,0]
	v_pk_mul_f32 v[26:27], v[148:149], v[14:15] op_sel_hi:[1,0]
	v_pk_mul_f32 v[28:29], v[146:147], v[14:15] op_sel_hi:[1,0]
	v_pk_mul_f32 v[14:15], v[144:145], v[14:15] op_sel_hi:[1,0]
	v_med3_f32 v7, v18, s63, v192
	v_med3_f32 v18, v22, s63, v192
	v_med3_f32 v19, v19, s63, v192
	v_med3_f32 v22, v23, s63, v192
	v_med3_f32 v23, v26, s63, v192
	v_med3_f32 v14, v14, s63, v192
	v_med3_f32 v26, v27, s63, v192
	v_med3_f32 v15, v15, s63, v192
	v_cvt_pk_fp8_f32 v8, v7, v19
	v_cvt_pk_fp8_f32 v9, v18, v22
	v_cvt_pk_fp8_f32 v10, v23, v26
	v_cvt_pk_fp8_f32 v11, v14, v15
	v_med3_f32 v16, v16, s63, v192
	v_med3_f32 v20, v20, s63, v192
	v_med3_f32 v17, v17, s63, v192
	v_med3_f32 v21, v21, s63, v192
	v_med3_f32 v24, v24, s63, v192
	v_med3_f32 v27, v28, s63, v192
	v_med3_f32 v25, v25, s63, v192
	v_med3_f32 v28, v29, s63, v192
	v_cvt_pk_fp8_f32 v8, v16, v17 op_sel:[0,0,1]
	v_cvt_pk_fp8_f32 v9, v20, v21 op_sel:[0,0,1]
	v_cvt_pk_fp8_f32 v10, v24, v25 op_sel:[0,0,1]
	v_cvt_pk_fp8_f32 v11, v27, v28 op_sel:[0,0,1]
	v_lshl_add_u64 v[14:15], v[12:13], 2, s[10:11]
	global_store_dwordx2 v[2:3], v[8:9], off
	global_store_dwordx2 v[2:3], v[10:11], off offset:128
	v_mov_b32_e32 v8, 0
	v_mov_b32_e32 v9, 0
	v_mov_b32_e32 v10, 0
	v_mov_b32_e32 v11, 0
	v_lshlrev_b64 v[12:13], 10, v[12:13]
	v_or_b32_e32 v14, 32, v6
	v_lshl_add_u64 v[12:13], s[12:13], 0, v[12:13]
	v_ashrrev_i32_e32 v15, 31, v14
	v_lshl_add_u64 v[12:13], v[12:13], 0, v[4:5]
	v_lshl_add_u64 v[16:17], v[14:15], 2, s[10:11]
	v_or_b32_e32 v6, 48, v6
	v_mul_f32_e32 v7, 0x3d000000, v194
	v_mul_f32_e32 v18, 0x42000000, v7
	v_pk_mul_f32 v[22:23], v[140:141], v[18:19] op_sel_hi:[1,0]
	v_pk_mul_f32 v[26:27], v[136:137], v[18:19] op_sel_hi:[1,0]
	v_pk_mul_f32 v[20:21], v[142:143], v[18:19] op_sel_hi:[1,0]
	v_pk_mul_f32 v[24:25], v[138:139], v[18:19] op_sel_hi:[1,0]
	v_pk_mul_f32 v[28:29], v[134:135], v[18:19] op_sel_hi:[1,0]
	v_pk_mul_f32 v[30:31], v[132:133], v[18:19] op_sel_hi:[1,0]
	v_pk_mul_f32 v[130:131], v[130:131], v[18:19] op_sel_hi:[1,0]
	v_pk_mul_f32 v[18:19], v[128:129], v[18:19] op_sel_hi:[1,0]
	v_med3_f32 v7, v22, s63, v192
	v_med3_f32 v22, v26, s63, v192
	v_med3_f32 v23, v23, s63, v192
	v_med3_f32 v26, v27, s63, v192
	v_med3_f32 v27, v30, s63, v192
	v_med3_f32 v18, v18, s63, v192
	v_med3_f32 v30, v31, s63, v192
	v_med3_f32 v19, v19, s63, v192
	v_cvt_pk_fp8_f32 v8, v7, v23
	v_cvt_pk_fp8_f32 v9, v22, v26
	v_cvt_pk_fp8_f32 v10, v27, v30
	v_cvt_pk_fp8_f32 v11, v18, v19
	v_med3_f32 v20, v20, s63, v192
	v_med3_f32 v24, v24, s63, v192
	v_med3_f32 v21, v21, s63, v192
	v_med3_f32 v25, v25, s63, v192
	v_med3_f32 v28, v28, s63, v192
	v_med3_f32 v31, v130, s63, v192
	v_med3_f32 v29, v29, s63, v192
	v_med3_f32 v128, v131, s63, v192
	v_cvt_pk_fp8_f32 v8, v20, v21 op_sel:[0,0,1]
	v_cvt_pk_fp8_f32 v9, v24, v25 op_sel:[0,0,1]
	v_cvt_pk_fp8_f32 v10, v28, v29 op_sel:[0,0,1]
	v_cvt_pk_fp8_f32 v11, v31, v128 op_sel:[0,0,1]
	global_store_dwordx2 v[12:13], v[8:9], off
	global_store_dwordx2 v[12:13], v[10:11], off offset:128
	v_mov_b32_e32 v8, 0
	v_mov_b32_e32 v9, 0
	v_mov_b32_e32 v10, 0
	v_mov_b32_e32 v11, 0
	v_lshlrev_b64 v[12:13], 10, v[14:15]
	v_lshl_add_u64 v[12:13], s[12:13], 0, v[12:13]
	v_ashrrev_i32_e32 v7, 31, v6
	v_lshl_add_u64 v[12:13], v[12:13], 0, v[4:5]
	v_lshl_add_u64 v[14:15], v[6:7], 2, s[10:11]
	v_lshlrev_b64 v[6:7], 10, v[6:7]
	v_lshl_add_u64 v[6:7], s[12:13], 0, v[6:7]
	v_lshl_add_u64 v[4:5], v[6:7], 0, v[4:5]
	v_mov_b32_e32 v6, 0
	v_mov_b32_e32 v7, 0
	v_mul_f32_e32 v16, 0x3d000000, v195
	v_mul_f32_e32 v16, 0x42000000, v16
	v_pk_mul_f32 v[20:21], v[124:125], v[16:17] op_sel_hi:[1,0]
	v_pk_mul_f32 v[24:25], v[120:121], v[16:17] op_sel_hi:[1,0]
	v_pk_mul_f32 v[18:19], v[126:127], v[16:17] op_sel_hi:[1,0]
	v_pk_mul_f32 v[22:23], v[122:123], v[16:17] op_sel_hi:[1,0]
	v_pk_mul_f32 v[26:27], v[118:119], v[16:17] op_sel_hi:[1,0]
	v_pk_mul_f32 v[28:29], v[116:117], v[16:17] op_sel_hi:[1,0]
	v_pk_mul_f32 v[30:31], v[114:115], v[16:17] op_sel_hi:[1,0]
	v_pk_mul_f32 v[16:17], v[112:113], v[16:17] op_sel_hi:[1,0]
	v_med3_f32 v20, v20, s63, v192
	v_med3_f32 v24, v24, s63, v192
	v_med3_f32 v21, v21, s63, v192
	v_med3_f32 v25, v25, s63, v192
	v_med3_f32 v28, v28, s63, v192
	v_med3_f32 v16, v16, s63, v192
	v_med3_f32 v29, v29, s63, v192
	v_med3_f32 v17, v17, s63, v192
	v_cvt_pk_fp8_f32 v8, v20, v21
	v_cvt_pk_fp8_f32 v9, v24, v25
	v_cvt_pk_fp8_f32 v10, v28, v29
	v_cvt_pk_fp8_f32 v11, v16, v17
	v_med3_f32 v18, v18, s63, v192
	v_med3_f32 v22, v22, s63, v192
	v_med3_f32 v19, v19, s63, v192
	v_med3_f32 v23, v23, s63, v192
	v_med3_f32 v26, v26, s63, v192
	v_med3_f32 v30, v30, s63, v192
	v_med3_f32 v27, v27, s63, v192
	v_med3_f32 v31, v31, s63, v192
	v_cvt_pk_fp8_f32 v8, v18, v19 op_sel:[0,0,1]
	v_cvt_pk_fp8_f32 v9, v22, v23 op_sel:[0,0,1]
	v_cvt_pk_fp8_f32 v10, v26, v27 op_sel:[0,0,1]
	v_cvt_pk_fp8_f32 v11, v30, v31 op_sel:[0,0,1]
	global_store_dwordx2 v[12:13], v[8:9], off
	global_store_dwordx2 v[12:13], v[10:11], off offset:128
	v_mov_b32_e32 v8, 0
	v_mov_b32_e32 v9, 0
	v_mov_b32_e32 v10, 0
	v_mov_b32_e32 v11, 0
	v_mul_f32_e32 v12, 0x3d000000, v196
	v_mul_f32_e32 v12, 0x42000000, v12
	v_pk_mul_f32 v[16:17], v[108:109], v[12:13] op_sel_hi:[1,0]
	v_pk_mul_f32 v[20:21], v[104:105], v[12:13] op_sel_hi:[1,0]
	v_pk_mul_f32 v[14:15], v[110:111], v[12:13] op_sel_hi:[1,0]
	v_pk_mul_f32 v[18:19], v[106:107], v[12:13] op_sel_hi:[1,0]
	v_pk_mul_f32 v[22:23], v[102:103], v[12:13] op_sel_hi:[1,0]
	v_pk_mul_f32 v[24:25], v[100:101], v[12:13] op_sel_hi:[1,0]
	v_pk_mul_f32 v[26:27], v[98:99], v[12:13] op_sel_hi:[1,0]
	v_pk_mul_f32 v[12:13], v[96:97], v[12:13] op_sel_hi:[1,0]
	v_med3_f32 v16, v16, s63, v192
	v_med3_f32 v20, v20, s63, v192
	v_med3_f32 v17, v17, s63, v192
	v_med3_f32 v21, v21, s63, v192
	v_med3_f32 v24, v24, s63, v192
	v_med3_f32 v12, v12, s63, v192
	v_med3_f32 v25, v25, s63, v192
	v_med3_f32 v13, v13, s63, v192
	v_cvt_pk_fp8_f32 v8, v16, v17
	v_cvt_pk_fp8_f32 v9, v20, v21
	v_cvt_pk_fp8_f32 v10, v24, v25
	v_cvt_pk_fp8_f32 v11, v12, v13
	v_med3_f32 v14, v14, s63, v192
	v_med3_f32 v18, v18, s63, v192
	v_med3_f32 v15, v15, s63, v192
	v_med3_f32 v19, v19, s63, v192
	v_med3_f32 v22, v22, s63, v192
	v_med3_f32 v26, v26, s63, v192
	v_med3_f32 v23, v23, s63, v192
	v_med3_f32 v27, v27, s63, v192
	v_cvt_pk_fp8_f32 v8, v14, v15 op_sel:[0,0,1]
	v_cvt_pk_fp8_f32 v9, v18, v19 op_sel:[0,0,1]
	v_cvt_pk_fp8_f32 v10, v22, v23 op_sel:[0,0,1]
	v_cvt_pk_fp8_f32 v11, v26, v27 op_sel:[0,0,1]
	global_store_dwordx2 v[4:5], v[8:9], off
	global_store_dwordx2 v[4:5], v[10:11], off offset:128
	v_mov_b32_e32 v4, 0
	v_mov_b32_e32 v5, 0
	v_lshl_add_u64 v[8:9], v[2:3], 0, s[8:9]
	v_mul_f32_e32 v10, 0x3d000000, v197
	v_mul_f32_e32 v10, 0x42000000, v10
	v_pk_mul_f32 v[14:15], v[92:93], v[10:11] op_sel_hi:[1,0]
	v_pk_mul_f32 v[18:19], v[88:89], v[10:11] op_sel_hi:[1,0]
	v_pk_mul_f32 v[12:13], v[94:95], v[10:11] op_sel_hi:[1,0]
	v_pk_mul_f32 v[16:17], v[90:91], v[10:11] op_sel_hi:[1,0]
	v_pk_mul_f32 v[20:21], v[86:87], v[10:11] op_sel_hi:[1,0]
	v_pk_mul_f32 v[22:23], v[84:85], v[10:11] op_sel_hi:[1,0]
	v_pk_mul_f32 v[24:25], v[82:83], v[10:11] op_sel_hi:[1,0]
	v_pk_mul_f32 v[10:11], v[80:81], v[10:11] op_sel_hi:[1,0]
	v_med3_f32 v14, v14, s63, v192
	v_med3_f32 v18, v18, s63, v192
	v_med3_f32 v15, v15, s63, v192
	v_med3_f32 v19, v19, s63, v192
	v_med3_f32 v22, v22, s63, v192
	v_med3_f32 v10, v10, s63, v192
	v_med3_f32 v23, v23, s63, v192
	v_med3_f32 v11, v11, s63, v192
	v_cvt_pk_fp8_f32 v4, v14, v15
	v_cvt_pk_fp8_f32 v5, v18, v19
	v_cvt_pk_fp8_f32 v6, v22, v23
	v_cvt_pk_fp8_f32 v7, v10, v11
	v_med3_f32 v12, v12, s63, v192
	v_med3_f32 v16, v16, s63, v192
	v_med3_f32 v13, v13, s63, v192
	v_med3_f32 v17, v17, s63, v192
	v_med3_f32 v20, v20, s63, v192
	v_med3_f32 v24, v24, s63, v192
	v_med3_f32 v21, v21, s63, v192
	v_med3_f32 v25, v25, s63, v192
	v_cvt_pk_fp8_f32 v4, v12, v13 op_sel:[0,0,1]
	v_cvt_pk_fp8_f32 v5, v16, v17 op_sel:[0,0,1]
	v_cvt_pk_fp8_f32 v6, v20, v21 op_sel:[0,0,1]
	v_cvt_pk_fp8_f32 v7, v24, v25 op_sel:[0,0,1]
	v_add_co_u32_e32 v10, vcc, s64, v2
	s_nop 1
	v_addc_co_u32_e32 v11, vcc, 0, v3, vcc
	global_store_dwordx2 v[10:11], v[4:5], off
	global_store_dwordx2 v[8:9], v[6:7], off offset:128
	v_mov_b32_e32 v4, 0
	v_mov_b32_e32 v5, 0
	v_mov_b32_e32 v6, 0
	v_mov_b32_e32 v7, 0
	v_lshl_add_u64 v[8:9], v[2:3], 0, s[14:15]
	v_mul_f32_e32 v10, 0x3d000000, v198
	v_mul_f32_e32 v10, 0x42000000, v10
	v_pk_mul_f32 v[14:15], v[76:77], v[10:11] op_sel_hi:[1,0]
	v_pk_mul_f32 v[18:19], v[72:73], v[10:11] op_sel_hi:[1,0]
	v_pk_mul_f32 v[12:13], v[78:79], v[10:11] op_sel_hi:[1,0]
	v_pk_mul_f32 v[16:17], v[74:75], v[10:11] op_sel_hi:[1,0]
	v_pk_mul_f32 v[20:21], v[70:71], v[10:11] op_sel_hi:[1,0]
	v_pk_mul_f32 v[22:23], v[68:69], v[10:11] op_sel_hi:[1,0]
	v_pk_mul_f32 v[24:25], v[66:67], v[10:11] op_sel_hi:[1,0]
	v_pk_mul_f32 v[10:11], v[64:65], v[10:11] op_sel_hi:[1,0]
	v_med3_f32 v14, v14, s63, v192
	v_med3_f32 v18, v18, s63, v192
	v_med3_f32 v15, v15, s63, v192
	v_med3_f32 v19, v19, s63, v192
	v_med3_f32 v22, v22, s63, v192
	v_med3_f32 v10, v10, s63, v192
	v_med3_f32 v23, v23, s63, v192
	v_med3_f32 v11, v11, s63, v192
	v_cvt_pk_fp8_f32 v4, v14, v15
	v_cvt_pk_fp8_f32 v5, v18, v19
	v_cvt_pk_fp8_f32 v6, v22, v23
	v_cvt_pk_fp8_f32 v7, v10, v11
	v_med3_f32 v12, v12, s63, v192
	v_med3_f32 v16, v16, s63, v192
	v_med3_f32 v13, v13, s63, v192
	v_med3_f32 v17, v17, s63, v192
	v_med3_f32 v20, v20, s63, v192
	v_med3_f32 v24, v24, s63, v192
	v_med3_f32 v21, v21, s63, v192
	v_med3_f32 v25, v25, s63, v192
	v_cvt_pk_fp8_f32 v4, v12, v13 op_sel:[0,0,1]
	v_cvt_pk_fp8_f32 v5, v16, v17 op_sel:[0,0,1]
	v_cvt_pk_fp8_f32 v6, v20, v21 op_sel:[0,0,1]
	v_cvt_pk_fp8_f32 v7, v24, v25 op_sel:[0,0,1]
	v_add_co_u32_e32 v10, vcc, s65, v2
	s_nop 1
	v_addc_co_u32_e32 v11, vcc, 0, v3, vcc
	global_store_dwordx2 v[10:11], v[4:5], off
	global_store_dwordx2 v[8:9], v[6:7], off offset:128
	v_mov_b32_e32 v4, 0
	v_mov_b32_e32 v5, 0
	v_mov_b32_e32 v6, 0
	v_mov_b32_e32 v7, 0
	v_lshl_add_u64 v[8:9], v[2:3], 0, s[16:17]
	v_mul_f32_e32 v10, 0x3d000000, v199
	v_mul_f32_e32 v10, 0x42000000, v10
	v_pk_mul_f32 v[14:15], v[60:61], v[10:11] op_sel_hi:[1,0]
	v_pk_mul_f32 v[18:19], v[56:57], v[10:11] op_sel_hi:[1,0]
	v_pk_mul_f32 v[12:13], v[62:63], v[10:11] op_sel_hi:[1,0]
	v_pk_mul_f32 v[16:17], v[58:59], v[10:11] op_sel_hi:[1,0]
	v_pk_mul_f32 v[20:21], v[54:55], v[10:11] op_sel_hi:[1,0]
	v_pk_mul_f32 v[22:23], v[52:53], v[10:11] op_sel_hi:[1,0]
	v_pk_mul_f32 v[24:25], v[50:51], v[10:11] op_sel_hi:[1,0]
	v_pk_mul_f32 v[10:11], v[48:49], v[10:11] op_sel_hi:[1,0]
	v_med3_f32 v14, v14, s63, v192
	v_med3_f32 v18, v18, s63, v192
	v_med3_f32 v15, v15, s63, v192
	v_med3_f32 v19, v19, s63, v192
	v_med3_f32 v22, v22, s63, v192
	v_med3_f32 v10, v10, s63, v192
	v_med3_f32 v23, v23, s63, v192
	v_med3_f32 v11, v11, s63, v192
	v_cvt_pk_fp8_f32 v4, v14, v15
	v_cvt_pk_fp8_f32 v5, v18, v19
	v_cvt_pk_fp8_f32 v6, v22, v23
	v_cvt_pk_fp8_f32 v7, v10, v11
	v_med3_f32 v12, v12, s63, v192
	v_med3_f32 v16, v16, s63, v192
	v_med3_f32 v13, v13, s63, v192
	v_med3_f32 v17, v17, s63, v192
	v_med3_f32 v20, v20, s63, v192
	v_med3_f32 v24, v24, s63, v192
	v_med3_f32 v21, v21, s63, v192
	v_med3_f32 v25, v25, s63, v192
	v_cvt_pk_fp8_f32 v4, v12, v13 op_sel:[0,0,1]
	v_cvt_pk_fp8_f32 v5, v16, v17 op_sel:[0,0,1]
	v_cvt_pk_fp8_f32 v6, v20, v21 op_sel:[0,0,1]
	v_cvt_pk_fp8_f32 v7, v24, v25 op_sel:[0,0,1]
	v_add_co_u32_e32 v10, vcc, s66, v2
	s_nop 1
	v_addc_co_u32_e32 v11, vcc, 0, v3, vcc
	global_store_dwordx2 v[10:11], v[4:5], off
	global_store_dwordx2 v[8:9], v[6:7], off offset:128
	v_mov_b32_e32 v0, 0
	v_mov_b32_e32 v1, 0
	v_mov_b32_e32 v4, 0
	v_mov_b32_e32 v5, 0
	s_and_b64 vcc, exec, s[4:5]
	v_lshl_add_u64 v[6:7], v[2:3], 0, s[18:19]
	v_add_co_u32_e64 v2, s[4:5], s67, v2
	v_mul_f32_e32 v8, 0x3d000000, v200
	v_mul_f32_e32 v8, 0x42000000, v8
	v_pk_mul_f32 v[12:13], v[44:45], v[8:9] op_sel_hi:[1,0]
	v_pk_mul_f32 v[16:17], v[40:41], v[8:9] op_sel_hi:[1,0]
	v_pk_mul_f32 v[10:11], v[46:47], v[8:9] op_sel_hi:[1,0]
	v_pk_mul_f32 v[14:15], v[42:43], v[8:9] op_sel_hi:[1,0]
	v_pk_mul_f32 v[18:19], v[38:39], v[8:9] op_sel_hi:[1,0]
	v_pk_mul_f32 v[20:21], v[36:37], v[8:9] op_sel_hi:[1,0]
	v_pk_mul_f32 v[22:23], v[34:35], v[8:9] op_sel_hi:[1,0]
	v_pk_mul_f32 v[8:9], v[32:33], v[8:9] op_sel_hi:[1,0]
	v_med3_f32 v12, v12, s63, v192
	v_med3_f32 v16, v16, s63, v192
	v_med3_f32 v13, v13, s63, v192
	v_med3_f32 v17, v17, s63, v192
	v_med3_f32 v20, v20, s63, v192
	v_med3_f32 v8, v8, s63, v192
	v_med3_f32 v21, v21, s63, v192
	v_med3_f32 v9, v9, s63, v192
	v_cvt_pk_fp8_f32 v0, v12, v13
	v_cvt_pk_fp8_f32 v1, v16, v17
	v_cvt_pk_fp8_f32 v4, v20, v21
	v_cvt_pk_fp8_f32 v5, v8, v9
	v_med3_f32 v10, v10, s63, v192
	v_med3_f32 v14, v14, s63, v192
	v_med3_f32 v11, v11, s63, v192
	v_med3_f32 v15, v15, s63, v192
	v_med3_f32 v18, v18, s63, v192
	v_med3_f32 v22, v22, s63, v192
	v_med3_f32 v19, v19, s63, v192
	v_med3_f32 v23, v23, s63, v192
	v_cvt_pk_fp8_f32 v0, v10, v11 op_sel:[0,0,1]
	v_cvt_pk_fp8_f32 v1, v14, v15 op_sel:[0,0,1]
	v_cvt_pk_fp8_f32 v4, v18, v19 op_sel:[0,0,1]
	v_cvt_pk_fp8_f32 v5, v22, v23 op_sel:[0,0,1]
	v_addc_co_u32_e64 v3, s[4:5], 0, v3, s[4:5]
	global_store_dwordx2 v[2:3], v[0:1], off
	global_store_dwordx2 v[6:7], v[4:5], off offset:128
	s_cbranch_vccz .LBB0_3976
	s_waitcnt vmcnt(0)
	s_cmpk_gt_u32 s42, 0xff
	s_cbranch_scc1 .LBB0_3983
	s_barrier
